# attention window mask: one signed compare per element with rotating mask registers (vcc, s98..s101) instead of add + unsigned compare; pads removed
# speedup vs baseline: 1.0012x; 1.0012x over previous
; __device__ __forceinline__ unsigned cvt_pk_bf16(float lo, float hi) { unsigned r; asm volatile("v_cvt_pk_bf16_f32 %0, %1, %2" : "=v"(r) : "v"(lo), "v"(hi)); return r; }
; #define LAS __attribute__((address_space(3)))
; #define MFMA32(a, b, c) __builtin_amdgcn_mfma_f32_32x32x16_bf16((a), (b), (c), 0, 0, 0)
; template <int STAGE, int OFF> __device__ __forceinline__ void attn32_unit(const bf16* base, bf16* yrow0, int blk0, int u, LAS unsigned char* xtab, LAS unsigned char* kbuf, LAS unsigned char* vbuf, int lane, ...
;     ...
;         for (int c = 0; c < 4; ++c) { *(LAS v4u*)(kbuf + (8 * c + lrow) * 144 + lch * 16) = kr[set][c]; *(LAS v4u*)(vbuf + (8 * c + lrow) * 160 + lch * 16) = vr[set][c]; }
;         if (pp + 2 < 5) { ATT32_LOAD(set, pp + 2, t0, SH); }
;         else { const bf16* base_ = base; { const bf16* base = nbase; ATT32_LOAD(set, pp + 2 - 5, nt0, nsh); } (void)base_; }
;         f32x16 sc;
; #pragma unroll
;         for (int i = 0; i < 16; ++i) sc[i] = 0.f;
; #pragma unroll
;         for (int ks = 0; ks < 4; ++ks) { const bf16x8 ka = *(const LAS bf16x8*)(kbuf + qi * 144 + 32 * ks + 16 * h); sc = MFMA32(ka, qb[ks], sc); }
;         if (pp == 4) {
; #pragma unroll
;             for (int ks = 0; ks < 4; ++ks) qb[ks] = *(const bf16x8*)(nbase + (size_t)min(nt0 + (qi << nsh), SEQ - 1) * 1536 + 16 * ks + 8 * h);
;         }
;         const int mbase = n0 + 4 * h - lo; float mx = -INFINITY;
; #pragma unroll
;         for (int rg = 0; rg < 16; ++rg) { sc[rg] = ((unsigned)(mbase + (rg & 3) + 8 * (rg >> 2)) <= mspan) ? sc[rg] : -INFINITY; mx = fmaxf(mx, sc[rg]); }
;         mx = fmaxf(mx, __shfl_xor(mx, 32));
;         if (__any(mx > m)) {
;             const float mn = fmaxf(m, mx), alpha = __builtin_amdgcn_exp2f(m - mn); m = mn; l *= alpha;
; #pragma unroll
;             for (int i = 0; i < 16; ++i) { o[0][i] *= alpha; o[1][i] *= alpha; }
;         }
;         float ps = 0.f;
; #pragma unroll
;         for (int rg = 0; rg < 16; ++rg) { sc[rg] = __builtin_amdgcn_exp2f(sc[rg] - m); ps += sc[rg]; }
;         l += ps;
;         bf16x8 pb[2];
; #pragma unroll
;         for (int s2 = 0; s2 < 2; ++s2) { v4u w; w.x = pg8::cvt_pk_bf16(sc[8 * s2], sc[8 * s2 + 1]); w.y = pg8::cvt_pk_bf16(sc[8 * s2 + 2], sc[8 * s2 + 3]); w.z = pg8::cvt_pk_bf16(sc[8 * s2 + 4], sc[8 * s2 + 5]); w.w = pg8::cvt_pk_bf16(sc[8 * s2 + 6], sc[8 * s2 + 7]); pb[s2] = __builtin_bit_cast(bf16x8, w); }
.LBB0_360:
	s_waitcnt vmcnt(0)
	ds_write_b128 v231, v[74:77]
	ds_write_b128 v232, v[82:85] offset:4608
	ds_write_b128 v231, v[78:81] offset:1152
	ds_write_b128 v232, v[94:97] offset:5888
	ds_write_b128 v231, v[86:89] offset:2304
	ds_write_b128 v232, v[98:101] offset:7168
	ds_write_b128 v231, v[90:93] offset:3456
	ds_write_b128 v232, v[102:105] offset:8448
	ds_read_b128 v[2:5], v177
	ds_read_b128 v[18:21], v177 offset:32
	s_ashr_i32 s12, s9, 8
	s_lshl_b32 s0, s9, 9
	s_and_b32 s13, s0, 0x3e00
	s_mul_i32 s1, s12, 0x3000000
	s_mul_hi_i32 s0, s12, 0x3000000
	s_add_u32 s1, s16, s1
	s_addc_u32 s0, s17, s0
	s_waitcnt lgkmcnt(0)
	v_mfma_f32_32x32x16_bf16 v[2:17], v[2:5], v[66:69], 0
	s_lshl_b32 s8, s9, 1
	s_and_b32 s8, s8, 0x1c0
	s_lshl_b32 s39, s8, 1
	s_add_u32 s8, s1, s39
	s_addc_u32 s9, s0, 0
	s_add_i32 s10, s13, s23
	s_sub_i32 s0, 0, s10
	v_mfma_f32_32x32x16_bf16 v[2:17], v[18:21], v[62:65], v[2:17]
	v_max_i32_e32 v22, s0, v175
	v_add_u32_e32 v168, s10, v174
	v_sub_u32_e32 v171, v1, v22
	v_sub_u32_e32 v173, v178, v22
	v_med3_i32 v22, v168, 0, v233
	v_mul_u32_u24_e32 v30, 0xc00, v22
	ds_read_b128 v[22:25], v177 offset:96
	ds_read_b128 v[26:29], v177 offset:64
	s_waitcnt lgkmcnt(0)
	v_mfma_f32_32x32x16_bf16 v[2:17], v[26:29], v[58:61], v[2:17]
	v_or_b32_e32 v18, v30, v176
	global_load_dwordx4 v[70:73], v18, s[8:9] offset:1024
	global_load_dwordx4 v[138:141], v18, s[8:9] offset:2048
	v_or_b32_e32 v18, 8, v168
	v_med3_i32 v18, v18, 0, v233
	v_mul_u32_u24_e32 v18, 0xc00, v18
	v_or_b32_e32 v18, v18, v176
	global_load_dwordx4 v[142:145], v18, s[8:9] offset:1024
	global_load_dwordx4 v[146:149], v18, s[8:9] offset:2048
	v_mfma_f32_32x32x16_bf16 v[2:17], v[22:25], v[54:57], v[2:17]
	v_or_b32_e32 v18, 16, v168
	v_med3_i32 v18, v18, 0, v233
	v_mul_u32_u24_e32 v18, 0xc00, v18
	v_or_b32_e32 v18, v18, v176
	global_load_dwordx4 v[150:153], v18, s[8:9] offset:1024
	global_load_dwordx4 v[154:157], v18, s[8:9] offset:2048
	s_nop 2
	v_add_u32_e32 v253, 27, v173
	v_cmp_le_i32_e32 vcc, 27, v253
	v_cmp_le_i32_e64 s[98:99], 26, v253
	v_cmp_le_i32_e64 s[100:101], 25, v253
	v_cndmask_b32_e32 v2, v234, v2, vcc
	v_or_b32_e32 v20, 24, v168
	v_med3_i32 v20, v20, 0, v233
	v_cmp_le_i32_e32 vcc, 24, v253
	v_cndmask_b32_e64 v3, v234, v3, s[98:99]
	v_max3_f32 v18, v2, s31, v3
	v_cmp_le_i32_e64 s[98:99], 19, v253
	v_cndmask_b32_e64 v4, v234, v4, s[100:101]
	v_mul_u32_u24_e32 v20, 0xc00, v20
	v_cmp_le_i32_e64 s[100:101], 18, v253
	v_cndmask_b32_e32 v5, v234, v5, vcc
	v_max3_f32 v18, v18, v4, v5
	v_cmp_le_i32_e32 vcc, 17, v253
	v_cndmask_b32_e64 v6, v234, v6, s[98:99]
	v_or_b32_e32 v20, v20, v176
	v_cmp_le_i32_e64 s[98:99], 16, v253
	v_cndmask_b32_e64 v7, v234, v7, s[100:101]
	v_max3_f32 v18, v18, v6, v7
	v_cmp_le_i32_e64 s[100:101], 11, v253
	v_cndmask_b32_e32 v8, v234, v8, vcc
	global_load_dwordx4 v[158:161], v20, s[8:9] offset:1024
	global_load_dwordx4 v[162:165], v20, s[8:9] offset:2048
	v_cmp_le_i32_e32 vcc, 10, v253
	v_cndmask_b32_e64 v9, v234, v9, s[98:99]
	v_max3_f32 v18, v18, v8, v9
	v_cmp_le_i32_e64 s[98:99], 9, v253
	v_cndmask_b32_e64 v10, v234, v10, s[100:101]
	v_cmp_le_i32_e64 s[100:101], 8, v253
	v_cndmask_b32_e32 v11, v234, v11, vcc
	v_max3_f32 v18, v18, v10, v11
	v_cmp_le_i32_e32 vcc, 3, v253
	v_cndmask_b32_e64 v12, v234, v12, s[98:99]
	v_cmp_le_i32_e64 s[98:99], 2, v253
	v_cndmask_b32_e64 v13, v234, v13, s[100:101]
	v_max3_f32 v18, v18, v12, v13
	v_cmp_le_i32_e64 s[100:101], 1, v253
	v_cndmask_b32_e32 v14, v234, v14, vcc
	v_cmp_le_i32_e32 vcc, 0, v253
	v_cndmask_b32_e64 v15, v234, v15, s[98:99]
	v_max3_f32 v18, v18, v14, v15
	v_cndmask_b32_e64 v16, v234, v16, s[100:101]
	v_cndmask_b32_e32 v17, v234, v17, vcc
	v_max3_f32 v18, v18, v16, v17
	ds_bpermute_b32 v19, v179, v18
	s_waitcnt lgkmcnt(0)
	v_max_f32_e32 v19, v19, v19
	v_max_f32_e32 v18, v18, v19
	v_cmp_lt_f32_e32 vcc, s34, v18
	s_cmp_eq_u64 vcc, 0
	v_max_f32_e32 v19, 0xf149f2ca, v18
	s_cselect_b64 vcc, -1, 0
	v_cndmask_b32_e32 v172, v19, v235, vcc
	v_sub_f32_e32 v2, v2, v172
	v_exp_f32_e32 v50, v2
	v_sub_f32_e32 v2, v3, v172
	v_exp_f32_e32 v51, v2
	v_sub_f32_e32 v2, v4, v172
	v_exp_f32_e32 v82, v2
	v_sub_f32_e32 v2, v5, v172
	v_exp_f32_e32 v83, v2
	v_sub_f32_e32 v2, v6, v172
	v_exp_f32_e32 v6, v2
	v_sub_f32_e32 v2, v7, v172
	v_exp_f32_e32 v7, v2
	v_sub_f32_e32 v2, v8, v172
	v_exp_f32_e32 v8, v2
	v_sub_f32_e32 v2, v9, v172
	v_exp_f32_e32 v9, v2
	v_sub_f32_e32 v2, v10, v172
	v_exp_f32_e32 v237, v2
	v_sub_f32_e32 v2, v11, v172
	v_exp_f32_e32 v246, v2
	v_sub_f32_e32 v2, v12, v172
	v_exp_f32_e32 v247, v2
	v_sub_f32_e32 v2, v13, v172
	v_exp_f32_e32 v248, v2
	v_sub_f32_e32 v2, v14, v172
	v_sub_f32_e32 v21, 0xf149f2ca, v19
	v_exp_f32_e32 v249, v2
	v_sub_f32_e32 v2, v15, v172
	v_exp_f32_e32 v21, v21
	v_exp_f32_e32 v250, v2
	v_sub_f32_e32 v2, v16, v172
	v_exp_f32_e32 v251, v2
	v_sub_f32_e32 v2, v17, v172
	v_exp_f32_e32 v252, v2
	v_cvt_pk_bf16_f32 v74, v50, v51
	v_cvt_pk_bf16_f32 v75, v82, v83
	v_cvt_pk_bf16_f32 v76, v6, v7
	v_cvt_pk_bf16_f32 v77, v8, v9
	v_cvt_pk_bf16_f32 v238, v237, v246
	v_cvt_pk_bf16_f32 v239, v247, v248
	v_cvt_pk_bf16_f32 v240, v249, v250
	v_cvt_pk_bf16_f32 v241, v251, v252
	ds_read_b64_tr_b16 v[2:3], v181 offset:4608
	ds_read_b64_tr_b16 v[4:5], v181 offset:5888
	v_mul_f32_e32 v18, 0, v21
	v_cndmask_b32_e64 v34, v18, 0, vcc
	v_mov_b32_e32 v35, v34
	v_mov_b32_e32 v36, v34
	v_mov_b32_e32 v37, v34
	v_mov_b32_e32 v38, v34
	v_mov_b32_e32 v39, v34
	v_mov_b32_e32 v40, v34
	v_mov_b32_e32 v41, v34
	v_mov_b32_e32 v42, v34
	v_mov_b32_e32 v43, v34
	v_mov_b32_e32 v44, v34
	v_mov_b32_e32 v45, v34
	v_mov_b32_e32 v46, v34
	v_mov_b32_e32 v47, v34
	v_mov_b32_e32 v48, v34
	v_mov_b32_e32 v49, v34
	ds_read_b64_tr_b16 v[80:81], v181 offset:5952
	ds_read_b64_tr_b16 v[78:79], v181 offset:4672
	s_waitcnt lgkmcnt(2)
; #define LAS __attribute__((address_space(3)))
; template <int STAGE, int OFF> __device__ __forceinline__ void attn32_unit(const bf16* base, bf16* yrow0, int blk0, int u, LAS unsigned char* xtab, LAS unsigned char* kbuf, LAS unsigned char* vbuf, int lane, ...
;     ...
;         for (int c = 0; c < 4; ++c) { *(LAS v4u*)(kbuf + (8 * c + lrow) * 144 + lch * 16) = kr[set][c]; *(LAS v4u*)(vbuf + (8 * c + lrow) * 160 + lch * 16) = vr[set][c]; }
;         if (pp + 2 < 5) { ATT32_LOAD(set, pp + 2, t0, SH); }
;         else { const bf16* base_ = base; { const bf16* base = nbase; ATT32_LOAD(set, pp + 2 - 5, nt0, nsh); } (void)base_; }
;         f32x16 sc;
; #pragma unroll
;         for (int i = 0; i < 16; ++i) sc[i] = 0.f;
; #pragma unroll
;         for (int ks = 0; ks < 4; ++ks) { const bf16x8 ka = *(const LAS bf16x8*)(kbuf + qi * 144 + 32 * ks + 16 * h); sc = MFMA32(ka, qb[ks], sc); }
;         if (pp == 4) {
; #pragma unroll
;             for (int ks = 0; ks < 4; ++ks) qb[ks] = *(const bf16x8*)(nbase + (size_t)min(nt0 + (qi << nsh), SEQ - 1) * 1536 + 16 * ks + 8 * h);
;         }
;         const int mbase = n0 + 4 * h - lo; float mx = -INFINITY;
; #pragma unroll
;         for (int rg = 0; rg < 16; ++rg) { sc[rg] = ((unsigned)(mbase + (rg & 3) + 8 * (rg >> 2)) <= mspan) ? sc[rg] : -INFINITY; mx = fmaxf(mx, sc[rg]); }
;         mx = fmaxf(mx, __shfl_xor(mx, 32));
;         if (__any(mx > m)) {
;             const float mn = fmaxf(m, mx), alpha = __builtin_amdgcn_exp2f(m - mn); m = mn; l *= alpha;
; #pragma unroll
;             for (int i = 0; i < 16; ++i) { o[0][i] *= alpha; o[1][i] *= alpha; }
;         }
;         float ps = 0.f;
; #pragma unroll
;         for (int rg = 0; rg < 16; ++rg) { sc[rg] = __builtin_amdgcn_exp2f(sc[rg] - m); ps += sc[rg]; }
;         l += ps;
;         bf16x8 pb[2];
; #pragma unroll
;         for (int s2 = 0; s2 < 2; ++s2) { v4u w; w.x = pg8::cvt_pk_bf16(sc[8 * s2], sc[8 * s2 + 1]); w.y = pg8::cvt_pk_bf16(sc[8 * s2 + 2], sc[8 * s2 + 3]); w.z = pg8::cvt_pk_bf16(sc[8 * s2 + 4], sc[8 * s2 + 5]); w.w = pg8::cvt_pk_bf16(sc[8 * s2 + 6], sc[8 * s2 + 7]); pb[s2] = __builtin_bit_cast(bf16x8, w); }
; #pragma unroll
;         for (int mb = 0; mb < 2; ++mb)
; #pragma unroll
;             for (int s2 = 0; s2 < 2; ++s2) {
;                 LAS unsigned char* vp = vbuf + tr_off + (16 * s2) * 160 + 64 * mb;
	v_mfma_f32_32x32x16_bf16 v[18:33], v[2:5], v[74:77], v[34:49]
	ds_read_b64_tr_b16 v[2:3], v181 offset:7168
	ds_read_b64_tr_b16 v[4:5], v181 offset:8448
	v_add_f32_e32 v10, 0, v50
	v_add_f32_e32 v10, v51, v10
	ds_read_b64_tr_b16 v[244:245], v181 offset:8512
	ds_read_b64_tr_b16 v[242:243], v181 offset:7232
	ds_write_b128 v231, v[106:109]
	ds_write_b128 v232, v[122:125] offset:4608
	ds_write_b128 v231, v[110:113] offset:1152
	ds_write_b128 v232, v[126:129] offset:5888
	ds_write_b128 v231, v[114:117] offset:2304
	ds_write_b128 v232, v[130:133] offset:7168
	ds_write_b128 v231, v[118:121] offset:3456
	ds_write_b128 v232, v[134:137] offset:8448
	s_waitcnt lgkmcnt(10)
	v_mfma_f32_32x32x16_bf16 v[18:33], v[2:5], v[238:241], v[18:33]
	v_add_f32_e32 v2, v82, v10
	v_add_f32_e32 v2, v83, v2
	v_add_f32_e32 v2, v6, v2
	v_add_f32_e32 v2, v7, v2
	v_add_f32_e32 v2, v8, v2
	v_add_f32_e32 v253, v9, v2
	v_mov_b64_e32 v[2:3], v[34:35]
	v_mov_b64_e32 v[4:5], v[36:37]
	v_mov_b64_e32 v[6:7], v[38:39]
	v_mov_b64_e32 v[8:9], v[40:41]
	v_mov_b64_e32 v[10:11], v[42:43]
	v_mov_b64_e32 v[12:13], v[44:45]
	v_mov_b64_e32 v[14:15], v[46:47]
	v_mov_b64_e32 v[16:17], v[48:49]
	ds_read_b128 v[36:39], v177
	v_or_b32_e32 v35, 32, v168
	v_med3_i32 v35, v35, 0, v233
	v_mul_u32_u24_e32 v35, 0xc00, v35
	v_or_b32_e32 v35, v35, v176
	v_mfma_f32_32x32x16_bf16 v[2:17], v[78:81], v[74:77], v[2:17]
	global_load_dwordx4 v[74:77], v35, s[8:9] offset:1024
	global_load_dwordx4 v[78:81], v35, s[8:9] offset:2048
	ds_read_b128 v[90:93], v177 offset:32
	v_or_b32_e32 v35, 40, v168
	v_med3_i32 v35, v35, 0, v233
	v_mul_u32_u24_e32 v35, 0xc00, v35
	v_or_b32_e32 v35, v35, v176
	global_load_dwordx4 v[82:85], v35, s[8:9] offset:1024
	global_load_dwordx4 v[86:89], v35, s[8:9] offset:2048
	s_waitcnt lgkmcnt(1)
	v_mfma_f32_32x32x16_bf16 v[36:51], v[36:39], v[66:69], 0
	v_or_b32_e32 v35, 48, v168
	v_med3_i32 v35, v35, 0, v233
	v_mul_u32_u24_e32 v35, 0xc00, v35
	v_or_b32_e32 v35, v35, v176
	ds_read_b128 v[106:109], v177 offset:96
	ds_read_b128 v[110:113], v177 offset:64
	s_waitcnt lgkmcnt(2)
	v_mfma_f32_32x32x16_bf16 v[36:51], v[90:93], v[62:65], v[36:51]
	global_load_dwordx4 v[90:93], v35, s[8:9] offset:1024
	global_load_dwordx4 v[94:97], v35, s[8:9] offset:2048
	v_or_b32_e32 v35, 56, v168
	v_med3_i32 v35, v35, 0, v233
	v_mul_u32_u24_e32 v35, 0xc00, v35
	v_or_b32_e32 v35, v35, v176
	global_load_dwordx4 v[98:101], v35, s[8:9] offset:1024
	global_load_dwordx4 v[102:105], v35, s[8:9] offset:2048
	v_add_f32_e32 v35, v237, v253
	s_waitcnt lgkmcnt(0)
	v_mfma_f32_32x32x16_bf16 v[36:51], v[110:113], v[58:61], v[36:51]
	v_add_f32_e32 v35, v246, v35
	v_add_f32_e32 v35, v247, v35
	v_add_f32_e32 v35, v248, v35
	v_add_f32_e32 v35, v249, v35
	v_add_f32_e32 v35, v250, v35
	v_add_f32_e32 v110, v251, v35
	v_mfma_f32_32x32x16_bf16 v[36:51], v[106:109], v[54:57], v[36:51]
	v_mfma_f32_32x32x16_bf16 v[2:17], v[242:245], v[238:241], v[2:17]
	s_nop 9
	v_add_u32_e32 v253, 59, v173
	v_cmp_le_i32_e32 vcc, 27, v253
	v_cmp_le_i32_e64 s[98:99], 26, v253
	v_cmp_le_i32_e64 s[100:101], 25, v253
	v_cndmask_b32_e32 v35, v234, v36, vcc
	v_cmp_le_i32_e32 vcc, 24, v253
	v_cndmask_b32_e64 v36, v234, v37, s[98:99]
	v_max3_f32 v106, v35, s31, v36
	v_cmp_le_i32_e64 s[98:99], 19, v253
	v_cndmask_b32_e64 v37, v234, v38, s[100:101]
	v_cmp_le_i32_e64 s[100:101], 18, v253
	v_cndmask_b32_e32 v38, v234, v39, vcc
	v_max3_f32 v106, v106, v37, v38
	v_cmp_le_i32_e32 vcc, 17, v253
	v_cndmask_b32_e64 v39, v234, v40, s[98:99]
	v_cmp_le_i32_e64 s[98:99], 16, v253
	v_cndmask_b32_e64 v40, v234, v41, s[100:101]
	v_max3_f32 v106, v106, v39, v40
	v_cmp_le_i32_e64 s[100:101], 11, v253
	v_cndmask_b32_e32 v41, v234, v42, vcc
	v_cmp_le_i32_e32 vcc, 10, v253
	v_cndmask_b32_e64 v42, v234, v43, s[98:99]
	v_max3_f32 v106, v106, v41, v42
	v_cmp_le_i32_e64 s[98:99], 9, v253
	v_cndmask_b32_e64 v43, v234, v44, s[100:101]
	v_cmp_le_i32_e64 s[100:101], 8, v253
	v_cndmask_b32_e32 v44, v234, v45, vcc
	v_max3_f32 v106, v106, v43, v44
	v_cmp_le_i32_e32 vcc, 3, v253
	v_cndmask_b32_e64 v45, v234, v46, s[98:99]
	v_cmp_le_i32_e64 s[98:99], 2, v253
	v_cndmask_b32_e64 v46, v234, v47, s[100:101]
	v_max3_f32 v106, v106, v45, v46
	v_cmp_le_i32_e64 s[100:101], 1, v253
	v_cndmask_b32_e32 v47, v234, v48, vcc
	v_cmp_le_i32_e32 vcc, 0, v253
	v_cndmask_b32_e64 v48, v234, v49, s[98:99]
	v_max3_f32 v106, v106, v47, v48
	v_cndmask_b32_e64 v49, v234, v50, s[100:101]
	v_add_f32_e32 v50, v252, v110
	v_add_f32_e32 v50, v34, v50
	v_cndmask_b32_e32 v51, v234, v51, vcc
	v_max3_f32 v106, v106, v49, v51
	ds_bpermute_b32 v107, v179, v106
	s_waitcnt lgkmcnt(0)
	v_max_f32_e32 v34, v107, v107
	v_max_f32_e32 v34, v106, v34
	v_cmp_gt_f32_e32 vcc, v34, v172
	s_cbranch_vccz .LBB0_362
	v_max_f32_e32 v34, v34, v34
	v_max_f32_e32 v106, v172, v172
	v_max_f32_e32 v106, v106, v34
	v_sub_f32_e32 v34, v172, v106
	v_exp_f32_e32 v34, v34
	v_mov_b32_e32 v172, v106
	v_pk_mul_f32 v[32:33], v[32:33], v[34:35] op_sel_hi:[1,0]
	v_pk_mul_f32 v[30:31], v[30:31], v[34:35] op_sel_hi:[1,0]
	v_pk_mul_f32 v[28:29], v[28:29], v[34:35] op_sel_hi:[1,0]
	v_pk_mul_f32 v[26:27], v[26:27], v[34:35] op_sel_hi:[1,0]
	v_pk_mul_f32 v[24:25], v[24:25], v[34:35] op_sel_hi:[1,0]
	v_pk_mul_f32 v[22:23], v[22:23], v[34:35] op_sel_hi:[1,0]
	v_pk_mul_f32 v[20:21], v[20:21], v[34:35] op_sel_hi:[1,0]
	v_pk_mul_f32 v[18:19], v[18:19], v[34:35] op_sel_hi:[1,0]
	v_pk_mul_f32 v[16:17], v[16:17], v[34:35] op_sel_hi:[1,0]
	v_pk_mul_f32 v[14:15], v[14:15], v[34:35] op_sel_hi:[1,0]
	v_pk_mul_f32 v[12:13], v[12:13], v[34:35] op_sel_hi:[1,0]
	v_pk_mul_f32 v[10:11], v[10:11], v[34:35] op_sel_hi:[1,0]
	v_pk_mul_f32 v[8:9], v[8:9], v[34:35] op_sel_hi:[1,0]
	v_pk_mul_f32 v[6:7], v[6:7], v[34:35] op_sel_hi:[1,0]
	v_pk_mul_f32 v[4:5], v[4:5], v[34:35] op_sel_hi:[1,0]
	v_pk_mul_f32 v[2:3], v[2:3], v[34:35] op_sel_hi:[1,0]
	v_mul_f32_e32 v50, v50, v34
; #define LAS __attribute__((address_space(3)))
; template <int STAGE, int OFF> __device__ __forceinline__ void attn32_unit(const bf16* base, bf16* yrow0, int blk0, int u, LAS unsigned char* xtab, LAS unsigned char* kbuf, LAS unsigned char* vbuf, int lane, ...
;     ...
;         for (int c = 0; c < 4; ++c) { *(LAS v4u*)(kbuf + (8 * c + lrow) * 144 + lch * 16) = kr[set][c]; *(LAS v4u*)(vbuf + (8 * c + lrow) * 160 + lch * 16) = vr[set][c]; }
;         if (pp + 2 < 5) { ATT32_LOAD(set, pp + 2, t0, SH); }
;         else { const bf16* base_ = base; { const bf16* base = nbase; ATT32_LOAD(set, pp + 2 - 5, nt0, nsh); } (void)base_; }
;         f32x16 sc;
; #pragma unroll
;         for (int i = 0; i < 16; ++i) sc[i] = 0.f;
; #pragma unroll
;         for (int ks = 0; ks < 4; ++ks) { const bf16x8 ka = *(const LAS bf16x8*)(kbuf + qi * 144 + 32 * ks + 16 * h); sc = MFMA32(ka, qb[ks], sc); }
;         if (pp == 4) {
; #pragma unroll
;             for (int ks = 0; ks < 4; ++ks) qb[ks] = *(const bf16x8*)(nbase + (size_t)min(nt0 + (qi << nsh), SEQ - 1) * 1536 + 16 * ks + 8 * h);
;         }
;         const int mbase = n0 + 4 * h - lo; float mx = -INFINITY;
; #pragma unroll
;         for (int rg = 0; rg < 16; ++rg) { sc[rg] = ((unsigned)(mbase + (rg & 3) + 8 * (rg >> 2)) <= mspan) ? sc[rg] : -INFINITY; mx = fmaxf(mx, sc[rg]); }
;         mx = fmaxf(mx, __shfl_xor(mx, 32));
;         if (__any(mx > m)) {
;             const float mn = fmaxf(m, mx), alpha = __builtin_amdgcn_exp2f(m - mn); m = mn; l *= alpha;
; #pragma unroll
;             for (int i = 0; i < 16; ++i) { o[0][i] *= alpha; o[1][i] *= alpha; }
;         }
;         float ps = 0.f;
; #pragma unroll
;         for (int rg = 0; rg < 16; ++rg) { sc[rg] = __builtin_amdgcn_exp2f(sc[rg] - m); ps += sc[rg]; }
;         l += ps;
;         bf16x8 pb[2];
; #pragma unroll
;         for (int s2 = 0; s2 < 2; ++s2) { v4u w; w.x = pg8::cvt_pk_bf16(sc[8 * s2], sc[8 * s2 + 1]); w.y = pg8::cvt_pk_bf16(sc[8 * s2 + 2], sc[8 * s2 + 3]); w.z = pg8::cvt_pk_bf16(sc[8 * s2 + 4], sc[8 * s2 + 5]); w.w = pg8::cvt_pk_bf16(sc[8 * s2 + 6], sc[8 * s2 + 7]); pb[s2] = __builtin_bit_cast(bf16x8, w); }
; #pragma unroll
;         for (int mb = 0; mb < 2; ++mb)
; #pragma unroll
;             for (int s2 = 0; s2 < 2; ++s2) {
;                 LAS unsigned char* vp = vbuf + tr_off + (16 * s2) * 160 + 64 * mb;
.LBB0_362:
	v_sub_f32_e32 v34, v35, v172
	v_exp_f32_e32 v106, v34
	v_sub_f32_e32 v34, v36, v172
	v_exp_f32_e32 v107, v34
	v_sub_f32_e32 v34, v37, v172
	v_exp_f32_e32 v108, v34
	v_sub_f32_e32 v34, v38, v172
	v_exp_f32_e32 v109, v34
	v_sub_f32_e32 v34, v39, v172
	v_exp_f32_e32 v110, v34
	v_sub_f32_e32 v34, v40, v172
	v_exp_f32_e32 v111, v34
	v_sub_f32_e32 v34, v41, v172
	v_exp_f32_e32 v112, v34
	v_sub_f32_e32 v34, v42, v172
	v_exp_f32_e32 v113, v34
	v_sub_f32_e32 v34, v43, v172
	v_exp_f32_e32 v237, v34
	v_sub_f32_e32 v34, v44, v172
	v_exp_f32_e32 v242, v34
	v_sub_f32_e32 v34, v45, v172
	v_exp_f32_e32 v243, v34
	v_sub_f32_e32 v34, v46, v172
	v_exp_f32_e32 v244, v34
	v_sub_f32_e32 v34, v47, v172
	v_exp_f32_e32 v245, v34
	v_sub_f32_e32 v34, v48, v172
	v_exp_f32_e32 v246, v34
	v_sub_f32_e32 v34, v49, v172
	v_exp_f32_e32 v247, v34
	v_sub_f32_e32 v34, v51, v172
	v_exp_f32_e32 v51, v34
	v_cvt_pk_bf16_f32 v34, v106, v107
	v_cvt_pk_bf16_f32 v35, v108, v109
	v_cvt_pk_bf16_f32 v36, v110, v111
	v_cvt_pk_bf16_f32 v37, v112, v113
	v_cvt_pk_bf16_f32 v134, v237, v242
	v_cvt_pk_bf16_f32 v135, v243, v244
	v_cvt_pk_bf16_f32 v136, v245, v246
	v_cvt_pk_bf16_f32 v137, v247, v51
	ds_read_b64_tr_b16 v[38:39], v181 offset:4608
	ds_read_b64_tr_b16 v[40:41], v181 offset:5888
	ds_read_b64_tr_b16 v[44:45], v181 offset:5952
	ds_read_b64_tr_b16 v[42:43], v181 offset:4672
	s_waitcnt lgkmcnt(2)
	v_mfma_f32_32x32x16_bf16 v[18:33], v[38:41], v[34:37], v[18:33]
	ds_read_b64_tr_b16 v[38:39], v181 offset:7168
	ds_read_b64_tr_b16 v[40:41], v181 offset:8448
	v_add_f32_e32 v46, 0, v106
	ds_read_b64_tr_b16 v[240:241], v181 offset:8512
	ds_read_b64_tr_b16 v[238:239], v181 offset:7232
	s_waitcnt vmcnt(15)
	ds_write_b128 v231, v[70:73]
	s_waitcnt vmcnt(14)
	ds_write_b128 v232, v[138:141] offset:4608
	s_waitcnt vmcnt(13)
	ds_write_b128 v231, v[142:145] offset:1152
	s_waitcnt vmcnt(12)
	ds_write_b128 v232, v[146:149] offset:5888
	s_waitcnt vmcnt(11)
	ds_write_b128 v231, v[150:153] offset:2304
	s_waitcnt vmcnt(10)
	ds_write_b128 v232, v[154:157] offset:7168
	s_waitcnt vmcnt(9)
	ds_write_b128 v231, v[158:161] offset:3456
	s_waitcnt vmcnt(8)
	ds_write_b128 v232, v[162:165] offset:8448
	v_add_u32_e32 v122, 0x50, v168
	v_add_u32_e32 v126, 0x58, v168
	s_waitcnt lgkmcnt(10)
	v_mfma_f32_32x32x16_bf16 v[18:33], v[38:41], v[134:137], v[18:33]
	v_add_f32_e32 v38, v107, v46
	v_add_f32_e32 v38, v108, v38
	v_add_f32_e32 v38, v109, v38
	v_add_f32_e32 v38, v110, v38
	v_add_f32_e32 v38, v111, v38
	v_add_f32_e32 v38, v112, v38
	v_add_f32_e32 v248, v113, v38
	v_mfma_f32_32x32x16_bf16 v[2:17], v[42:45], v[34:37], v[2:17]
	v_or_b32_e32 v34, s10, v53
	v_min_u32_e32 v34, 0x3fff, v34
	v_mul_u32_u24_e32 v38, 0xc00, v34
	ds_read_b128 v[34:37], v177
	v_or_b32_e32 v38, v38, v176
	global_load_dwordx4 v[70:73], v38, s[8:9] offset:1024
	global_load_dwordx4 v[106:109], v38, s[8:9] offset:2048
	v_add_u32_e32 v38, 0x48, v168
	v_med3_i32 v38, v38, 0, v233
	v_mul_u32_u24_e32 v38, 0xc00, v38
	ds_read_b128 v[118:121], v177 offset:32
	v_or_b32_e32 v114, v38, v176
	s_waitcnt lgkmcnt(1)
	v_mfma_f32_32x32x16_bf16 v[34:49], v[34:37], v[66:69], 0
	v_med3_i32 v122, v122, 0, v233
	v_med3_i32 v126, v126, 0, v233
	v_mul_u32_u24_e32 v122, 0xc00, v122
	v_mul_u32_u24_e32 v126, 0xc00, v126
	v_or_b32_e32 v122, v122, v176
	v_or_b32_e32 v130, v126, v176
	global_load_dwordx4 v[110:113], v114, s[8:9] offset:1024
	s_nop 0
	global_load_dwordx4 v[114:117], v114, s[8:9] offset:2048
	ds_read_b128 v[138:141], v177 offset:96
	ds_read_b128 v[142:145], v177 offset:64
	s_waitcnt lgkmcnt(2)
	v_mfma_f32_32x32x16_bf16 v[34:49], v[118:121], v[62:65], v[34:49]
	global_load_dwordx4 v[118:121], v122, s[8:9] offset:1024
	s_nop 0
	global_load_dwordx4 v[122:125], v122, s[8:9] offset:2048
	s_nop 0
	global_load_dwordx4 v[126:129], v130, s[8:9] offset:1024
	s_nop 0
	global_load_dwordx4 v[130:133], v130, s[8:9] offset:2048
	s_waitcnt lgkmcnt(0)
	v_mfma_f32_32x32x16_bf16 v[34:49], v[142:145], v[58:61], v[34:49]
	v_add_f32_e32 v142, v237, v248
	v_add_f32_e32 v142, v242, v142
	v_add_f32_e32 v142, v243, v142
	v_add_f32_e32 v142, v244, v142
	v_add_f32_e32 v142, v245, v142
	v_add_f32_e32 v142, v246, v142
	v_add_f32_e32 v142, v247, v142
	v_mfma_f32_32x32x16_bf16 v[34:49], v[138:141], v[54:57], v[34:49]
	v_add_f32_e32 v51, v51, v142
	v_add_f32_e32 v51, v50, v51
	s_nop 5
	v_add_u32_e32 v253, 91, v173
	v_cmp_le_i32_e32 vcc, 27, v253
	v_cmp_le_i32_e64 s[98:99], 26, v253
	v_cmp_le_i32_e64 s[100:101], 25, v253
	v_cndmask_b32_e32 v34, v234, v34, vcc
	v_mfma_f32_32x32x16_bf16 v[2:17], v[238:241], v[134:137], v[2:17]
	v_cmp_le_i32_e32 vcc, 24, v253
	v_cndmask_b32_e64 v35, v234, v35, s[98:99]
	v_max3_f32 v138, v34, s31, v35
	v_cmp_le_i32_e64 s[98:99], 19, v253
	v_cndmask_b32_e64 v36, v234, v36, s[100:101]
	v_cmp_le_i32_e64 s[100:101], 18, v253
	v_cndmask_b32_e32 v37, v234, v37, vcc
	v_max3_f32 v138, v138, v36, v37
	v_cmp_le_i32_e32 vcc, 17, v253
	v_cndmask_b32_e64 v38, v234, v38, s[98:99]
	v_cmp_le_i32_e64 s[98:99], 16, v253
	v_cndmask_b32_e64 v39, v234, v39, s[100:101]
	v_max3_f32 v138, v138, v38, v39
	v_cmp_le_i32_e64 s[100:101], 11, v253
	v_cndmask_b32_e32 v40, v234, v40, vcc
	v_cmp_le_i32_e32 vcc, 10, v253
	v_cndmask_b32_e64 v41, v234, v41, s[98:99]
	v_max3_f32 v138, v138, v40, v41
	v_cmp_le_i32_e64 s[98:99], 9, v253
	v_cndmask_b32_e64 v42, v234, v42, s[100:101]
	v_cmp_le_i32_e64 s[100:101], 8, v253
	v_cndmask_b32_e32 v43, v234, v43, vcc
	v_max3_f32 v138, v138, v42, v43
	v_cmp_le_i32_e32 vcc, 3, v253
	v_cndmask_b32_e64 v44, v234, v44, s[98:99]
	v_cmp_le_i32_e64 s[98:99], 2, v253
	v_cndmask_b32_e64 v45, v234, v45, s[100:101]
	v_max3_f32 v138, v138, v44, v45
	v_cmp_le_i32_e64 s[100:101], 1, v253
	v_cndmask_b32_e32 v46, v234, v46, vcc
	v_cmp_le_i32_e32 vcc, 0, v253
	v_cndmask_b32_e64 v47, v234, v47, s[98:99]
	v_max3_f32 v138, v138, v46, v47
	v_cndmask_b32_e64 v48, v234, v48, s[100:101]
	v_cndmask_b32_e32 v49, v234, v49, vcc
	v_max3_f32 v138, v138, v48, v49
	ds_bpermute_b32 v139, v179, v138
	s_waitcnt lgkmcnt(0)
	v_max_f32_e32 v50, v139, v139
	v_max_f32_e32 v50, v138, v50
	v_cmp_gt_f32_e32 vcc, v50, v172
	s_cbranch_vccz .LBB0_364
; #define LAS __attribute__((address_space(3)))
; template <int STAGE, int OFF> __device__ __forceinline__ void attn32_unit(const bf16* base, bf16* yrow0, int blk0, int u, LAS unsigned char* xtab, LAS unsigned char* kbuf, LAS unsigned char* vbuf, int lane, ...
;     ...
;         for (int c = 0; c < 4; ++c) { *(LAS v4u*)(kbuf + (8 * c + lrow) * 144 + lch * 16) = kr[set][c]; *(LAS v4u*)(vbuf + (8 * c + lrow) * 160 + lch * 16) = vr[set][c]; }
;         if (pp + 2 < 5) { ATT32_LOAD(set, pp + 2, t0, SH); }
;         else { const bf16* base_ = base; { const bf16* base = nbase; ATT32_LOAD(set, pp + 2 - 5, nt0, nsh); } (void)base_; }
;         f32x16 sc;
; #pragma unroll
;         for (int i = 0; i < 16; ++i) sc[i] = 0.f;
; #pragma unroll
;         for (int ks = 0; ks < 4; ++ks) { const bf16x8 ka = *(const LAS bf16x8*)(kbuf + qi * 144 + 32 * ks + 16 * h); sc = MFMA32(ka, qb[ks], sc); }
;         if (pp == 4) {
; #pragma unroll
;             for (int ks = 0; ks < 4; ++ks) qb[ks] = *(const bf16x8*)(nbase + (size_t)min(nt0 + (qi << nsh), SEQ - 1) * 1536 + 16 * ks + 8 * h);
;         }
;         const int mbase = n0 + 4 * h - lo; float mx = -INFINITY;
; #pragma unroll
;         for (int rg = 0; rg < 16; ++rg) { sc[rg] = ((unsigned)(mbase + (rg & 3) + 8 * (rg >> 2)) <= mspan) ? sc[rg] : -INFINITY; mx = fmaxf(mx, sc[rg]); }
;         mx = fmaxf(mx, __shfl_xor(mx, 32));
;         if (__any(mx > m)) {
;             const float mn = fmaxf(m, mx), alpha = __builtin_amdgcn_exp2f(m - mn); m = mn; l *= alpha;
; #pragma unroll
;             for (int i = 0; i < 16; ++i) { o[0][i] *= alpha; o[1][i] *= alpha; }
;         }
;         float ps = 0.f;
; #pragma unroll
;         for (int rg = 0; rg < 16; ++rg) { sc[rg] = __builtin_amdgcn_exp2f(sc[rg] - m); ps += sc[rg]; }
;         l += ps;
;         bf16x8 pb[2];
; #pragma unroll
;         for (int s2 = 0; s2 < 2; ++s2) { v4u w; w.x = pg8::cvt_pk_bf16(sc[8 * s2], sc[8 * s2 + 1]); w.y = pg8::cvt_pk_bf16(sc[8 * s2 + 2], sc[8 * s2 + 3]); w.z = pg8::cvt_pk_bf16(sc[8 * s2 + 4], sc[8 * s2 + 5]); w.w = pg8::cvt_pk_bf16(sc[8 * s2 + 6], sc[8 * s2 + 7]); pb[s2] = __builtin_bit_cast(bf16x8, w); }
; #pragma unroll
;         for (int mb = 0; mb < 2; ++mb)
; #pragma unroll
;             for (int s2 = 0; s2 < 2; ++s2) {
;                 LAS unsigned char* vp = vbuf + tr_off + (16 * s2) * 160 + 64 * mb;
	v_max_f32_e32 v50, v50, v50
	v_max_f32_e32 v134, v172, v172
	v_max_f32_e32 v134, v134, v50
	v_sub_f32_e32 v50, v172, v134
	v_exp_f32_e32 v50, v50
	v_mov_b32_e32 v172, v134
	v_pk_mul_f32 v[32:33], v[32:33], v[50:51] op_sel_hi:[1,0]
	v_pk_mul_f32 v[30:31], v[30:31], v[50:51] op_sel_hi:[1,0]
	v_pk_mul_f32 v[28:29], v[28:29], v[50:51] op_sel_hi:[1,0]
	v_pk_mul_f32 v[26:27], v[26:27], v[50:51] op_sel_hi:[1,0]
	v_pk_mul_f32 v[24:25], v[24:25], v[50:51] op_sel_hi:[1,0]
	v_pk_mul_f32 v[22:23], v[22:23], v[50:51] op_sel_hi:[1,0]
	v_pk_mul_f32 v[20:21], v[20:21], v[50:51] op_sel_hi:[1,0]
	v_pk_mul_f32 v[18:19], v[18:19], v[50:51] op_sel_hi:[1,0]
	v_pk_mul_f32 v[16:17], v[16:17], v[50:51] op_sel_hi:[1,0]
	v_pk_mul_f32 v[14:15], v[14:15], v[50:51] op_sel_hi:[1,0]
	v_pk_mul_f32 v[12:13], v[12:13], v[50:51] op_sel_hi:[1,0]
	v_pk_mul_f32 v[10:11], v[10:11], v[50:51] op_sel_hi:[1,0]
	v_pk_mul_f32 v[8:9], v[8:9], v[50:51] op_sel_hi:[1,0]
	v_pk_mul_f32 v[6:7], v[6:7], v[50:51] op_sel_hi:[1,0]
	v_pk_mul_f32 v[4:5], v[4:5], v[50:51] op_sel_hi:[1,0]
	v_pk_mul_f32 v[2:3], v[2:3], v[50:51] op_sel_hi:[1,0]
	v_mul_f32_e32 v51, v51, v50
.LBB0_364:
	v_sub_f32_e32 v34, v34, v172
	v_exp_f32_e32 v138, v34
	v_sub_f32_e32 v34, v35, v172
	v_exp_f32_e32 v142, v34
	v_sub_f32_e32 v34, v36, v172
	v_exp_f32_e32 v143, v34
	v_sub_f32_e32 v34, v37, v172
	v_exp_f32_e32 v144, v34
	v_sub_f32_e32 v34, v38, v172
	v_exp_f32_e32 v145, v34
	v_sub_f32_e32 v34, v39, v172
	v_exp_f32_e32 v146, v34
	v_sub_f32_e32 v34, v40, v172
	v_exp_f32_e32 v147, v34
	v_sub_f32_e32 v34, v41, v172
	v_exp_f32_e32 v148, v34
	v_sub_f32_e32 v34, v42, v172
	v_exp_f32_e32 v150, v34
	v_sub_f32_e32 v34, v43, v172
	v_exp_f32_e32 v151, v34
	v_sub_f32_e32 v34, v44, v172
	v_exp_f32_e32 v152, v34
	v_sub_f32_e32 v34, v45, v172
	v_exp_f32_e32 v153, v34
	v_sub_f32_e32 v34, v46, v172
	v_exp_f32_e32 v154, v34
	v_sub_f32_e32 v34, v47, v172
	v_exp_f32_e32 v155, v34
	v_sub_f32_e32 v34, v48, v172
	v_exp_f32_e32 v156, v34
	v_sub_f32_e32 v34, v49, v172
	v_exp_f32_e32 v157, v34
	v_cvt_pk_bf16_f32 v34, v138, v142
	v_cvt_pk_bf16_f32 v35, v143, v144
	v_cvt_pk_bf16_f32 v36, v145, v146
	v_cvt_pk_bf16_f32 v37, v147, v148
	v_cvt_pk_bf16_f32 v134, v150, v151
	v_cvt_pk_bf16_f32 v135, v152, v153
	v_cvt_pk_bf16_f32 v136, v154, v155
	v_cvt_pk_bf16_f32 v137, v156, v157
	ds_read_b64_tr_b16 v[38:39], v181 offset:4608
	ds_read_b64_tr_b16 v[40:41], v181 offset:5888
	ds_read_b64_tr_b16 v[44:45], v181 offset:5952
	ds_read_b64_tr_b16 v[42:43], v181 offset:4672
	s_waitcnt lgkmcnt(2)
	v_mfma_f32_32x32x16_bf16 v[18:33], v[38:41], v[34:37], v[18:33]
	ds_read_b64_tr_b16 v[38:39], v181 offset:7168
	ds_read_b64_tr_b16 v[40:41], v181 offset:8448
	s_add_i32 s10, s13, s22
	v_add_u32_e32 v50, s10, v180
	v_add_f32_e32 v46, 0, v138
	ds_read_b64_tr_b16 v[140:141], v181 offset:8512
	ds_read_b64_tr_b16 v[138:139], v181 offset:7232
	s_waitcnt vmcnt(15)
	ds_write_b128 v231, v[74:77]
	s_waitcnt vmcnt(14)
	ds_write_b128 v232, v[78:81] offset:4608
	s_waitcnt vmcnt(13)
	ds_write_b128 v231, v[82:85] offset:1152
	s_waitcnt vmcnt(12)
	ds_write_b128 v232, v[86:89] offset:5888
	s_waitcnt vmcnt(11)
	ds_write_b128 v231, v[90:93] offset:2304
	s_waitcnt vmcnt(10)
	ds_write_b128 v232, v[94:97] offset:7168
	s_waitcnt vmcnt(9)
	ds_write_b128 v231, v[98:101] offset:3456
	s_waitcnt vmcnt(8)
	ds_write_b128 v232, v[102:105] offset:8448
	s_waitcnt lgkmcnt(10)
	v_mfma_f32_32x32x16_bf16 v[18:33], v[38:41], v[134:137], v[18:33]
	v_add_f32_e32 v38, v142, v46
	v_add_f32_e32 v38, v143, v38
	v_add_f32_e32 v38, v144, v38
	v_add_f32_e32 v38, v145, v38
	v_add_f32_e32 v38, v146, v38
	v_add_f32_e32 v38, v147, v38
	v_add_f32_e32 v158, v148, v38
	v_mfma_f32_32x32x16_bf16 v[2:17], v[42:45], v[34:37], v[2:17]
	v_max_i32_e32 v34, 0xffffffa0, v50
	v_add_u32_e32 v34, 0x60, v34
	v_min_u32_e32 v34, 0x3fff, v34
	v_mul_u32_u24_e32 v34, 0xc00, v34
	v_or_b32_e32 v34, v34, v176
	global_load_dwordx4 v[74:77], v34, s[8:9] offset:1024
	global_load_dwordx4 v[78:81], v34, s[8:9] offset:2048
	v_max_i32_e32 v34, 0xffffff98, v50
	v_add_u32_e32 v38, 0x68, v34
	ds_read_b128 v[34:37], v177
	v_min_u32_e32 v38, 0x3fff, v38
	v_mul_u32_u24_e32 v38, 0xc00, v38
	v_or_b32_e32 v38, v38, v176
	global_load_dwordx4 v[82:85], v38, s[8:9] offset:1024
	global_load_dwordx4 v[86:89], v38, s[8:9] offset:2048
	v_max_i32_e32 v38, 0xffffff90, v50
	ds_read_b128 v[98:101], v177 offset:32
	v_add_u32_e32 v90, 0x70, v38
	s_waitcnt lgkmcnt(1)
	v_mfma_f32_32x32x16_bf16 v[34:49], v[34:37], v[66:69], 0
	v_min_u32_e32 v90, 0x3fff, v90
	v_mul_u32_u24_e32 v90, 0xc00, v90
	v_or_b32_e32 v94, v90, v176
	global_load_dwordx4 v[90:93], v94, s[8:9] offset:1024
	s_nop 0
	global_load_dwordx4 v[94:97], v94, s[8:9] offset:2048
	ds_read_b128 v[142:145], v177 offset:96
	ds_read_b128 v[146:149], v177 offset:64
	s_waitcnt lgkmcnt(2)
	v_mfma_f32_32x32x16_bf16 v[34:49], v[98:101], v[62:65], v[34:49]
	v_max_i32_e32 v98, 0xffffff88, v50
	v_add_u32_e32 v98, 0x78, v98
	v_min_u32_e32 v98, 0x3fff, v98
	v_mul_u32_u24_e32 v98, 0xc00, v98
	v_or_b32_e32 v102, v98, v176
	global_load_dwordx4 v[98:101], v102, s[8:9] offset:1024
	s_nop 0
	global_load_dwordx4 v[102:105], v102, s[8:9] offset:2048
	s_waitcnt lgkmcnt(0)
; __device__ __forceinline__ unsigned cvt_pk_bf16(float lo, float hi) { unsigned r; asm volatile("v_cvt_pk_bf16_f32 %0, %1, %2" : "=v"(r) : "v"(lo), "v"(hi)); return r; }
; #define LAS __attribute__((address_space(3)))
; template <int STAGE, int OFF> __device__ __forceinline__ void attn32_unit(const bf16* base, bf16* yrow0, int blk0, int u, LAS unsigned char* xtab, LAS unsigned char* kbuf, LAS unsigned char* vbuf, int lane, ...
;     ...
; #pragma unroll
;         for (int ks = 0; ks < 4; ++ks) { const bf16x8 ka = *(const LAS bf16x8*)(kbuf + qi * 144 + 32 * ks + 16 * h); sc = MFMA32(ka, qb[ks], sc); }
;         if (pp == 4) {
; #pragma unroll
;             for (int ks = 0; ks < 4; ++ks) qb[ks] = *(const bf16x8*)(nbase + (size_t)min(nt0 + (qi << nsh), SEQ - 1) * 1536 + 16 * ks + 8 * h);
;         }
;         const int mbase = n0 + 4 * h - lo; float mx = -INFINITY;
; #pragma unroll
;         for (int rg = 0; rg < 16; ++rg) { sc[rg] = ((unsigned)(mbase + (rg & 3) + 8 * (rg >> 2)) <= mspan) ? sc[rg] : -INFINITY; mx = fmaxf(mx, sc[rg]); }
;         mx = fmaxf(mx, __shfl_xor(mx, 32));
;         if (__any(mx > m)) {
;             const float mn = fmaxf(m, mx), alpha = __builtin_amdgcn_exp2f(m - mn); m = mn; l *= alpha;
; #pragma unroll
;             for (int i = 0; i < 16; ++i) { o[0][i] *= alpha; o[1][i] *= alpha; }
;         }
;         float ps = 0.f;
; #pragma unroll
;         for (int rg = 0; rg < 16; ++rg) { sc[rg] = __builtin_amdgcn_exp2f(sc[rg] - m); ps += sc[rg]; }
;         l += ps;
;         bf16x8 pb[2];
; #pragma unroll
;         for (int s2 = 0; s2 < 2; ++s2) { v4u w; w.x = pg8::cvt_pk_bf16(sc[8 * s2], sc[8 * s2 + 1]); w.y = pg8::cvt_pk_bf16(sc[8 * s2 + 2], sc[8 * s2 + 3]); w.z = pg8::cvt_pk_bf16(sc[8 * s2 + 4], sc[8 * s2 + 5]); w.w = pg8::cvt_pk_bf16(sc[8 * s2 + 6], sc[8 * s2 + 7]); pb[s2] = __builtin_bit_cast(bf16x8, w); }
; #pragma unroll
;         for (int mb = 0; mb < 2; ++mb)
; #pragma unroll
;             for (int s2 = 0; s2 < 2; ++s2) {
;                 LAS unsigned char* vp = vbuf + tr_off + (16 * s2) * 160 + 64 * mb;
;                 const v4i16 a0 = __builtin_amdgcn_ds_read_tr16_b64_v4i16((LAS v4i16*)vp), a1 = __builtin_amdgcn_ds_read_tr16_b64_v4i16((LAS v4i16*)(vp + 8 * 160));
;                 const bf16x8 va = __builtin_shufflevector(a0, a1, 0, 1, 2, 3, 4, 5, 6, 7);
;                 o[mb] = MFMA32(va, pb[s2], o[mb]);
;             }
	v_mfma_f32_32x32x16_bf16 v[34:49], v[146:149], v[58:61], v[34:49]
	v_add_f32_e32 v146, v150, v158
	v_add_f32_e32 v146, v151, v146
	v_add_f32_e32 v146, v152, v146
	v_add_f32_e32 v146, v153, v146
	v_add_f32_e32 v146, v154, v146
	v_add_f32_e32 v146, v155, v146
	v_add_f32_e32 v146, v156, v146
	v_mfma_f32_32x32x16_bf16 v[34:49], v[142:145], v[54:57], v[34:49]
	v_add_f32_e32 v144, v157, v146
	v_add_f32_e32 v51, v51, v144
	s_nop 5
	v_add_u32_e32 v253, 123, v173
	v_cmp_le_i32_e32 vcc, 27, v253
	v_cmp_le_i32_e64 s[98:99], 26, v253
	v_cmp_le_i32_e64 s[100:101], 25, v253
	v_cndmask_b32_e32 v34, v234, v34, vcc
	v_mfma_f32_32x32x16_bf16 v[2:17], v[138:141], v[134:137], v[2:17]
	v_cmp_le_i32_e32 vcc, 24, v253
	v_cndmask_b32_e64 v35, v234, v35, s[98:99]
	v_max3_f32 v142, v34, s31, v35
	v_cmp_le_i32_e64 s[98:99], 19, v253
	v_cndmask_b32_e64 v36, v234, v36, s[100:101]
	v_cmp_le_i32_e64 s[100:101], 18, v253
	v_cndmask_b32_e32 v37, v234, v37, vcc
	v_max3_f32 v142, v142, v36, v37
	v_cmp_le_i32_e32 vcc, 17, v253
	v_cndmask_b32_e64 v38, v234, v38, s[98:99]
	v_cmp_le_i32_e64 s[98:99], 16, v253
	v_cndmask_b32_e64 v39, v234, v39, s[100:101]
	v_max3_f32 v142, v142, v38, v39
	v_cmp_le_i32_e64 s[100:101], 11, v253
	v_cndmask_b32_e32 v40, v234, v40, vcc
	v_cmp_le_i32_e32 vcc, 10, v253
	v_cndmask_b32_e64 v41, v234, v41, s[98:99]
	v_max3_f32 v142, v142, v40, v41
	v_cmp_le_i32_e64 s[98:99], 9, v253
	v_cndmask_b32_e64 v42, v234, v42, s[100:101]
	v_cmp_le_i32_e64 s[100:101], 8, v253
	v_cndmask_b32_e32 v43, v234, v43, vcc
	v_max3_f32 v142, v142, v42, v43
	v_cmp_le_i32_e32 vcc, 3, v253
	v_cndmask_b32_e64 v44, v234, v44, s[98:99]
	v_cmp_le_i32_e64 s[98:99], 2, v253
	v_cndmask_b32_e64 v45, v234, v45, s[100:101]
	v_max3_f32 v142, v142, v44, v45
	v_cmp_le_i32_e64 s[100:101], 1, v253
	v_cndmask_b32_e32 v46, v234, v46, vcc
	v_cmp_le_i32_e32 vcc, 0, v253
	v_cndmask_b32_e64 v47, v234, v47, s[98:99]
	v_max3_f32 v142, v142, v46, v47
	v_cndmask_b32_e64 v48, v234, v48, s[100:101]
	v_cndmask_b32_e32 v49, v234, v49, vcc
	v_max3_f32 v142, v142, v48, v49
	ds_bpermute_b32 v143, v179, v142
	s_waitcnt lgkmcnt(0)
	v_max_f32_e32 v134, v143, v143
	v_max_f32_e32 v134, v142, v134
	v_cmp_gt_f32_e32 vcc, v134, v172
	s_cbranch_vccz .LBB0_366
	v_max_f32_e32 v134, v134, v134
	v_max_f32_e32 v135, v172, v172
	v_max_f32_e32 v135, v135, v134
	v_sub_f32_e32 v134, v172, v135
	v_exp_f32_e32 v134, v134
	v_mov_b32_e32 v172, v135
	v_pk_mul_f32 v[32:33], v[32:33], v[134:135] op_sel_hi:[1,0]
	v_pk_mul_f32 v[30:31], v[30:31], v[134:135] op_sel_hi:[1,0]
	v_pk_mul_f32 v[28:29], v[28:29], v[134:135] op_sel_hi:[1,0]
	v_pk_mul_f32 v[26:27], v[26:27], v[134:135] op_sel_hi:[1,0]
	v_pk_mul_f32 v[24:25], v[24:25], v[134:135] op_sel_hi:[1,0]
	v_pk_mul_f32 v[22:23], v[22:23], v[134:135] op_sel_hi:[1,0]
	v_pk_mul_f32 v[20:21], v[20:21], v[134:135] op_sel_hi:[1,0]
	v_pk_mul_f32 v[18:19], v[18:19], v[134:135] op_sel_hi:[1,0]
	v_pk_mul_f32 v[16:17], v[16:17], v[134:135] op_sel_hi:[1,0]
	v_pk_mul_f32 v[14:15], v[14:15], v[134:135] op_sel_hi:[1,0]
	v_pk_mul_f32 v[12:13], v[12:13], v[134:135] op_sel_hi:[1,0]
	v_pk_mul_f32 v[10:11], v[10:11], v[134:135] op_sel_hi:[1,0]
	v_pk_mul_f32 v[8:9], v[8:9], v[134:135] op_sel_hi:[1,0]
	v_pk_mul_f32 v[6:7], v[6:7], v[134:135] op_sel_hi:[1,0]
	v_pk_mul_f32 v[4:5], v[4:5], v[134:135] op_sel_hi:[1,0]
	v_pk_mul_f32 v[2:3], v[2:3], v[134:135] op_sel_hi:[1,0]
	v_mul_f32_e32 v51, v51, v134
.LBB0_366:
	v_sub_f32_e32 v34, v34, v172
	v_exp_f32_e32 v134, v34
	v_sub_f32_e32 v34, v35, v172
	v_exp_f32_e32 v135, v34
	v_sub_f32_e32 v34, v36, v172
	v_exp_f32_e32 v136, v34
	v_sub_f32_e32 v34, v37, v172
	v_exp_f32_e32 v137, v34
	v_sub_f32_e32 v34, v38, v172
	v_exp_f32_e32 v146, v34
	v_sub_f32_e32 v34, v39, v172
	v_exp_f32_e32 v147, v34
	v_sub_f32_e32 v34, v40, v172
	v_exp_f32_e32 v148, v34
	v_sub_f32_e32 v34, v41, v172
	v_exp_f32_e32 v149, v34
	v_sub_f32_e32 v34, v42, v172
	v_exp_f32_e32 v152, v34
	v_sub_f32_e32 v34, v43, v172
	v_exp_f32_e32 v153, v34
	v_sub_f32_e32 v34, v44, v172
	v_exp_f32_e32 v154, v34
	v_sub_f32_e32 v34, v45, v172
	v_exp_f32_e32 v155, v34
	v_sub_f32_e32 v34, v46, v172
	v_exp_f32_e32 v156, v34
	v_sub_f32_e32 v34, v47, v172
	v_exp_f32_e32 v157, v34
	v_sub_f32_e32 v34, v48, v172
	v_exp_f32_e32 v158, v34
	v_sub_f32_e32 v34, v49, v172
	v_exp_f32_e32 v159, v34
	v_cvt_pk_bf16_f32 v34, v134, v135
	v_cvt_pk_bf16_f32 v35, v136, v137
	v_cvt_pk_bf16_f32 v36, v146, v147
	v_cvt_pk_bf16_f32 v37, v148, v149
	v_cvt_pk_bf16_f32 v138, v152, v153
	v_cvt_pk_bf16_f32 v139, v154, v155
	v_cvt_pk_bf16_f32 v140, v156, v157
	v_cvt_pk_bf16_f32 v141, v158, v159
	ds_read_b64_tr_b16 v[38:39], v181 offset:4608
	ds_read_b64_tr_b16 v[40:41], v181 offset:5888
	v_or_b32_e32 v42, s10, v1
	v_min_i32_e32 v142, 0x3fff, v42
	ds_read_b64_tr_b16 v[42:43], v181 offset:7168
	ds_read_b64_tr_b16 v[44:45], v181 offset:8448
	ds_read_b64_tr_b16 v[48:49], v181 offset:5952
	ds_read_b64_tr_b16 v[46:47], v181 offset:4672
	v_mul_u32_u24_e32 v168, 0xc00, v142
	s_waitcnt lgkmcnt(4)
	v_mfma_f32_32x32x16_bf16 v[18:33], v[38:41], v[34:37], v[18:33]
	v_lshl_add_u64 v[38:39], s[8:9], 0, v[168:169]
	v_lshlrev_b32_e32 v168, 1, v166
	v_lshl_add_u64 v[150:151], v[38:39], 0, v[168:169]
	v_add_f32_e32 v38, 0, v134
	v_add_f32_e32 v38, v135, v38
	v_add_f32_e32 v38, v136, v38
	v_add_f32_e32 v38, v137, v38
	s_waitcnt lgkmcnt(0)
	v_mfma_f32_32x32x16_bf16 v[2:17], v[46:49], v[34:37], v[2:17]
	v_max_i32_e32 v34, 0xffffff80, v50
	v_add_u32_e32 v34, 0x80, v34
	v_min_u32_e32 v34, 0x3fff, v34
	v_add_f32_e32 v38, v146, v38
	v_mul_u32_u24_e32 v34, 0xc00, v34
	ds_read_b64_tr_b16 v[144:145], v181 offset:8512
	ds_read_b64_tr_b16 v[142:143], v181 offset:7232
	v_add_f32_e32 v38, v147, v38
	s_waitcnt vmcnt(15)
; #define LAS __attribute__((address_space(3)))
; template <int STAGE, int OFF> __device__ __forceinline__ void attn32_unit(const bf16* base, bf16* yrow0, int blk0, int u, LAS unsigned char* xtab, LAS unsigned char* kbuf, LAS unsigned char* vbuf, int lane, ...
;     ...
;         for (int c = 0; c < 4; ++c) { *(LAS v4u*)(kbuf + (8 * c + lrow) * 144 + lch * 16) = kr[set][c]; *(LAS v4u*)(vbuf + (8 * c + lrow) * 160 + lch * 16) = vr[set][c]; }
;         if (pp + 2 < 5) { ATT32_LOAD(set, pp + 2, t0, SH); }
;         else { const bf16* base_ = base; { const bf16* base = nbase; ATT32_LOAD(set, pp + 2 - 5, nt0, nsh); } (void)base_; }
;         f32x16 sc;
; #pragma unroll
;         for (int i = 0; i < 16; ++i) sc[i] = 0.f;
; #pragma unroll
;         for (int ks = 0; ks < 4; ++ks) { const bf16x8 ka = *(const LAS bf16x8*)(kbuf + qi * 144 + 32 * ks + 16 * h); sc = MFMA32(ka, qb[ks], sc); }
;         if (pp == 4) {
; #pragma unroll
;             for (int ks = 0; ks < 4; ++ks) qb[ks] = *(const bf16x8*)(nbase + (size_t)min(nt0 + (qi << nsh), SEQ - 1) * 1536 + 16 * ks + 8 * h);
;         }
;         const int mbase = n0 + 4 * h - lo; float mx = -INFINITY;
; #pragma unroll
;         for (int rg = 0; rg < 16; ++rg) { sc[rg] = ((unsigned)(mbase + (rg & 3) + 8 * (rg >> 2)) <= mspan) ? sc[rg] : -INFINITY; mx = fmaxf(mx, sc[rg]); }
;         mx = fmaxf(mx, __shfl_xor(mx, 32));
;         if (__any(mx > m)) {
;             const float mn = fmaxf(m, mx), alpha = __builtin_amdgcn_exp2f(m - mn); m = mn; l *= alpha;
; #pragma unroll
;             for (int i = 0; i < 16; ++i) { o[0][i] *= alpha; o[1][i] *= alpha; }
;         }
;         float ps = 0.f;
; #pragma unroll
;         for (int rg = 0; rg < 16; ++rg) { sc[rg] = __builtin_amdgcn_exp2f(sc[rg] - m); ps += sc[rg]; }
;         l += ps;
;         bf16x8 pb[2];
; #pragma unroll
;         for (int s2 = 0; s2 < 2; ++s2) { v4u w; w.x = pg8::cvt_pk_bf16(sc[8 * s2], sc[8 * s2 + 1]); w.y = pg8::cvt_pk_bf16(sc[8 * s2 + 2], sc[8 * s2 + 3]); w.z = pg8::cvt_pk_bf16(sc[8 * s2 + 4], sc[8 * s2 + 5]); w.w = pg8::cvt_pk_bf16(sc[8 * s2 + 6], sc[8 * s2 + 7]); pb[s2] = __builtin_bit_cast(bf16x8, w); }
; #pragma unroll
;         for (int mb = 0; mb < 2; ++mb)
; #pragma unroll
;             for (int s2 = 0; s2 < 2; ++s2) {
;                 LAS unsigned char* vp = vbuf + tr_off + (16 * s2) * 160 + 64 * mb;
	ds_write_b128 v231, v[70:73]
	s_waitcnt vmcnt(14)
	ds_write_b128 v232, v[106:109] offset:4608
	s_waitcnt vmcnt(13)
	ds_write_b128 v231, v[110:113] offset:1152
	s_waitcnt vmcnt(12)
	ds_write_b128 v232, v[114:117] offset:5888
	s_waitcnt vmcnt(11)
	ds_write_b128 v231, v[118:121] offset:2304
	s_waitcnt vmcnt(10)
	ds_write_b128 v232, v[122:125] offset:7168
	s_waitcnt vmcnt(9)
	ds_write_b128 v231, v[126:129] offset:3456
	s_waitcnt vmcnt(8)
	ds_write_b128 v232, v[130:133] offset:8448
	v_or_b32_e32 v34, v34, v176
	v_add_f32_e32 v38, v148, v38
	global_load_dwordx4 v[106:109], v34, s[8:9] offset:1024
	global_load_dwordx4 v[110:113], v34, s[8:9] offset:2048
	v_max_i32_e32 v34, 0xffffff78, v50
	v_add_f32_e32 v160, v149, v38
	v_add_u32_e32 v38, 0x88, v34
	ds_read_b128 v[34:37], v177
	v_min_u32_e32 v38, 0x3fff, v38
	v_mul_u32_u24_e32 v38, 0xc00, v38
	v_or_b32_e32 v38, v38, v176
	global_load_dwordx4 v[114:117], v38, s[8:9] offset:1024
	global_load_dwordx4 v[118:121], v38, s[8:9] offset:2048
	v_max_i32_e32 v38, 0xffffff70, v50
	ds_read_b128 v[70:73], v177 offset:32
	v_mfma_f32_32x32x16_bf16 v[18:33], v[42:45], v[138:141], v[18:33]
	v_add_u32_e32 v122, 0x90, v38
	v_max_i32_e32 v50, 0xffffff68, v50
	v_add_u32_e32 v50, 0x98, v50
	v_min_u32_e32 v50, 0x3fff, v50
	v_mul_u32_u24_e32 v50, 0xc00, v50
	v_or_b32_e32 v50, v50, v176
	s_waitcnt lgkmcnt(1)
	v_mfma_f32_32x32x16_bf16 v[34:49], v[34:37], v[66:69], 0
	v_min_u32_e32 v66, 0x3fff, v122
	v_mul_u32_u24_e32 v66, 0xc00, v66
	v_or_b32_e32 v66, v66, v176
	global_load_dwordx4 v[122:125], v66, s[8:9] offset:1024
	global_load_dwordx4 v[126:129], v66, s[8:9] offset:2048
	ds_read_b128 v[146:149], v177 offset:96
	ds_read_b128 v[66:69], v177 offset:64
	global_load_dwordx4 v[130:133], v50, s[8:9] offset:1024
	global_load_dwordx4 v[134:137], v50, s[8:9] offset:2048
	v_add_f32_e32 v50, v152, v160
	s_waitcnt lgkmcnt(2)
	v_mfma_f32_32x32x16_bf16 v[34:49], v[70:73], v[62:65], v[34:49]
	v_add_f32_e32 v50, v153, v50
	v_add_f32_e32 v50, v154, v50
	v_add_f32_e32 v50, v155, v50
	v_add_f32_e32 v50, v156, v50
	v_add_f32_e32 v50, v157, v50
	s_waitcnt lgkmcnt(0)
	v_mfma_f32_32x32x16_bf16 v[34:49], v[66:69], v[58:61], v[34:49]
	global_load_dwordx4 v[66:69], v[150:151], off
	global_load_dwordx4 v[62:65], v[150:151], off offset:32
	global_load_dwordx4 v[58:61], v[150:151], off offset:64
	global_load_dwordx4 v[70:73], v[150:151], off offset:96
	v_add_f32_e32 v150, v158, v50
	v_mfma_f32_32x32x16_bf16 v[34:49], v[146:149], v[54:57], v[34:49]
	v_mfma_f32_32x32x16_bf16 v[2:17], v[142:145], v[138:141], v[2:17]
	s_nop 9
	v_sub_u32_e32 v253, v171, v173
	v_subrev_u32_e32 v253, 0x80, v253
	v_cmp_le_i32_e32 vcc, 0, v253
	v_cmp_le_i32_e64 s[98:99], 1, v253
	v_cmp_le_i32_e64 s[100:101], 2, v253
	v_cndmask_b32_e32 v50, v234, v34, vcc
	v_cmp_le_i32_e32 vcc, 3, v253
	v_cndmask_b32_e64 v35, v234, v35, s[98:99]
	v_max3_f32 v34, v50, s31, v35
	v_cmp_le_i32_e64 s[98:99], 8, v253
	v_cndmask_b32_e64 v36, v234, v36, s[100:101]
	v_cmp_le_i32_e64 s[100:101], 9, v253
	v_cndmask_b32_e32 v37, v234, v37, vcc
	v_max3_f32 v34, v34, v36, v37
	v_cmp_le_i32_e32 vcc, 10, v253
	v_cndmask_b32_e64 v38, v234, v38, s[98:99]
	v_cmp_le_i32_e64 s[98:99], 11, v253
	v_cndmask_b32_e64 v39, v234, v39, s[100:101]
	v_max3_f32 v34, v34, v38, v39
	v_cmp_le_i32_e64 s[100:101], 16, v253
	v_cndmask_b32_e32 v40, v234, v40, vcc
	v_cmp_le_i32_e32 vcc, 17, v253
	v_cndmask_b32_e64 v41, v234, v41, s[98:99]
	v_max3_f32 v34, v34, v40, v41
	v_cmp_le_i32_e64 s[98:99], 18, v253
	v_cndmask_b32_e64 v42, v234, v42, s[100:101]
	v_cmp_le_i32_e64 s[100:101], 19, v253
	v_cndmask_b32_e32 v43, v234, v43, vcc
	v_max3_f32 v34, v34, v42, v43
	v_cmp_le_i32_e32 vcc, 24, v253
	v_cndmask_b32_e64 v44, v234, v44, s[98:99]
	v_cmp_le_i32_e64 s[98:99], 25, v253
	v_cndmask_b32_e64 v45, v234, v45, s[100:101]
	v_max3_f32 v34, v34, v44, v45
	v_cmp_le_i32_e64 s[100:101], 26, v253
	v_cndmask_b32_e32 v46, v234, v46, vcc
	v_cmp_le_i32_e32 vcc, 27, v253
	v_cndmask_b32_e64 v47, v234, v47, s[98:99]
	v_max3_f32 v34, v34, v46, v47
	v_cndmask_b32_e64 v48, v234, v48, s[100:101]
	v_cndmask_b32_e32 v49, v234, v49, vcc
	v_max3_f32 v54, v34, v48, v49
	ds_bpermute_b32 v55, v179, v54
	v_add_f32_e32 v34, v159, v150
	v_add_f32_e32 v34, v51, v34
	s_waitcnt lgkmcnt(0)
	v_max_f32_e32 v51, v55, v55
	v_max_f32_e32 v51, v54, v51
	v_cmp_gt_f32_e32 vcc, v51, v172
	s_cbranch_vccz .LBB0_368
	v_max_f32_e32 v51, v51, v51
	v_max_f32_e32 v54, v172, v172
	v_max_f32_e32 v51, v54, v51
	v_sub_f32_e32 v54, v172, v51
	v_exp_f32_e32 v54, v54
	v_mov_b32_e32 v172, v51
	v_pk_mul_f32 v[32:33], v[32:33], v[54:55] op_sel_hi:[1,0]
	v_pk_mul_f32 v[30:31], v[30:31], v[54:55] op_sel_hi:[1,0]
	v_pk_mul_f32 v[28:29], v[28:29], v[54:55] op_sel_hi:[1,0]
	v_pk_mul_f32 v[26:27], v[26:27], v[54:55] op_sel_hi:[1,0]
	v_pk_mul_f32 v[24:25], v[24:25], v[54:55] op_sel_hi:[1,0]
	v_pk_mul_f32 v[22:23], v[22:23], v[54:55] op_sel_hi:[1,0]
	v_pk_mul_f32 v[20:21], v[20:21], v[54:55] op_sel_hi:[1,0]
	v_pk_mul_f32 v[18:19], v[18:19], v[54:55] op_sel_hi:[1,0]
	v_pk_mul_f32 v[16:17], v[16:17], v[54:55] op_sel_hi:[1,0]
	v_pk_mul_f32 v[14:15], v[14:15], v[54:55] op_sel_hi:[1,0]
	v_pk_mul_f32 v[12:13], v[12:13], v[54:55] op_sel_hi:[1,0]
	v_pk_mul_f32 v[10:11], v[10:11], v[54:55] op_sel_hi:[1,0]
	v_pk_mul_f32 v[8:9], v[8:9], v[54:55] op_sel_hi:[1,0]
	v_pk_mul_f32 v[6:7], v[6:7], v[54:55] op_sel_hi:[1,0]
	v_pk_mul_f32 v[4:5], v[4:5], v[54:55] op_sel_hi:[1,0]
	v_pk_mul_f32 v[2:3], v[2:3], v[54:55] op_sel_hi:[1,0]
	v_mul_f32_e32 v34, v34, v54

; template <int STAGE, int OFF> __device__ __forceinline__ void attn32_unit(const bf16* base, bf16* yrow0, int blk0, int u, LAS unsigned char* xtab, LAS unsigned char* kbuf, LAS unsigned char* vbuf, int lane, ...
;     ...
;     if (STAGE == 0) {
; #pragma unroll
;         for (int i = 0; i < 16; ++i) { o[0][i] = 0.f; o[1][i] = 0.f; }
;         m = -1e30f; l = 0.f;
;     } else {
; #pragma unroll
;         for (int mb = 0; mb < 2; ++mb)
; #pragma unroll
;             for (int gq = 0; gq < 4; ++gq) { const v2u w = *(const LAS v2u*)(xrow + 2 * (32 * mb + 8 * gq + 4 * h)); o[mb][4 * gq] = bf_lo(w.x); o[mb][4 * gq + 1] = bf_hi(w.x); o[mb][4 * gq + 2] = bf_lo(w.y); o[mb][4 * gq + 3] = bf_hi(w.y); }
;         m = *(const LAS float*)(xrow + 128); l = h == 0 ? *(const LAS float*)(xrow + 132) : 0.f;
;     }
;     const int hi = qi, lo = max(qi - 128, -(t0 >> SH));
;     const unsigned mspan = (unsigned)(hi - lo);
; #pragma unroll
;     for (int pp = 0; pp < 5; ++pp) {
;         constexpr int dummy = 0; (void)dummy;
;         const int set = (pp + OFF) % 2, n0 = -128 + 32 * pp;
; #pragma unroll
;         for (int c = 0; c < 4; ++c) { *(LAS v4u*)(kbuf + (8 * c + lrow) * 144 + lch * 16) = kr[set][c]; *(LAS v4u*)(vbuf + (8 * c + lrow) * 160 + lch * 16) = vr[set][c]; }
;         if (pp + 2 < 5) { ATT32_LOAD(set, pp + 2, t0, SH); }
;         else { const bf16* base_ = base; { const bf16* base = nbase; ATT32_LOAD(set, pp + 2 - 5, nt0, nsh); } (void)base_; }
;         f32x16 sc;
; #pragma unroll
;         for (int i = 0; i < 16; ++i) sc[i] = 0.f;
; #pragma unroll
;         for (int ks = 0; ks < 4; ++ks) { const bf16x8 ka = *(const LAS bf16x8*)(kbuf + qi * 144 + 32 * ks + 16 * h); sc = MFMA32(ka, qb[ks], sc); }
;         if (pp == 4) {
; #pragma unroll
;             for (int ks = 0; ks < 4; ++ks) qb[ks] = *(const bf16x8*)(nbase + (size_t)min(nt0 + (qi << nsh), SEQ - 1) * 1536 + 16 * ks + 8 * h);
;         }
;         const int mbase = n0 + 4 * h - lo; float mx = -INFINITY;
; #pragma unroll
;         for (int rg = 0; rg < 16; ++rg) { sc[rg] = ((unsigned)(mbase + (rg & 3) + 8 * (rg >> 2)) <= mspan) ? sc[rg] : -INFINITY; mx = fmaxf(mx, sc[rg]); }
;         mx = fmaxf(mx, __shfl_xor(mx, 32));
;         if (__any(mx > m)) {
;             const float mn = fmaxf(m, mx), alpha = __builtin_amdgcn_exp2f(m - mn); m = mn; l *= alpha;
; #pragma unroll
.LBB0_370:
	s_or_b64 exec, exec, s[14:15]
	s_waitcnt vmcnt(19)
	ds_write_b128 v231, v[74:77]
	s_waitcnt vmcnt(18)
	ds_write_b128 v232, v[78:81] offset:4608
	s_waitcnt vmcnt(17)
	ds_write_b128 v231, v[82:85] offset:1152
	s_waitcnt vmcnt(16)
	ds_write_b128 v232, v[86:89] offset:5888
	s_waitcnt vmcnt(15)
	ds_write_b128 v231, v[90:93] offset:2304
	s_waitcnt vmcnt(14)
	ds_write_b128 v232, v[94:97] offset:7168
	s_waitcnt vmcnt(13)
	ds_write_b128 v231, v[98:101] offset:3456
	s_waitcnt vmcnt(12)
	ds_write_b128 v232, v[102:105] offset:8448
	ds_read_b128 v[2:5], v177
	ds_read_b128 v[18:21], v177 offset:32
	s_sub_i32 s0, 0, s10
	v_max_i32_e32 v22, s0, v175
	v_add_u32_e32 v153, s10, v174
	v_sub_u32_e32 v151, v1, v22
	v_sub_u32_e32 v152, v178, v22
	v_med3_i32 v22, v153, 0, v233
	v_mul_u32_u24_e32 v22, 0xc00, v22
	s_waitcnt vmcnt(3) lgkmcnt(1)
	v_mfma_f32_32x32x16_bf16 v[2:17], v[2:5], v[66:69], 0
	v_or_b32_e32 v30, v22, v176
	ds_read_b128 v[22:25], v177 offset:96
	ds_read_b128 v[26:29], v177 offset:64
	global_load_dwordx4 v[78:81], v30, s[8:9] offset:1024
	global_load_dwordx4 v[82:85], v30, s[8:9] offset:2048
	s_waitcnt vmcnt(4) lgkmcnt(2)
	v_mfma_f32_32x32x16_bf16 v[2:17], v[18:21], v[62:65], v[2:17]
	v_or_b32_e32 v18, 8, v153
	v_med3_i32 v18, v18, 0, v233
	v_mul_u32_u24_e32 v18, 0xc00, v18
	v_or_b32_e32 v18, v18, v176
	global_load_dwordx4 v[86:89], v18, s[8:9] offset:1024
	global_load_dwordx4 v[90:93], v18, s[8:9] offset:2048
	v_or_b32_e32 v18, 16, v153
	v_med3_i32 v18, v18, 0, v233
	s_waitcnt vmcnt(5) lgkmcnt(0)
	v_mfma_f32_32x32x16_bf16 v[2:17], v[26:29], v[58:61], v[2:17]
	v_mul_u32_u24_e32 v18, 0xc00, v18
	v_or_b32_e32 v18, v18, v176
	global_load_dwordx4 v[102:105], v18, s[8:9] offset:1024
	global_load_dwordx4 v[138:141], v18, s[8:9] offset:2048
	v_or_b32_e32 v20, 24, v153
	v_med3_i32 v20, v20, 0, v233
	s_waitcnt vmcnt(6)
	v_mfma_f32_32x32x16_bf16 v[2:17], v[22:25], v[70:73], v[2:17]
	v_mul_u32_u24_e32 v20, 0xc00, v20
	v_or_b32_e32 v20, v20, v176
	global_load_dwordx4 v[142:145], v20, s[8:9] offset:1024
	global_load_dwordx4 v[146:149], v20, s[8:9] offset:2048
	s_nop 7
	v_add_u32_e32 v253, 27, v152
	v_cmp_le_i32_e32 vcc, 27, v253
	v_cmp_le_i32_e64 s[98:99], 26, v253
	v_cmp_le_i32_e64 s[100:101], 25, v253
	v_cndmask_b32_e32 v2, v234, v2, vcc
	v_cmp_le_i32_e32 vcc, 24, v253
	v_cndmask_b32_e64 v3, v234, v3, s[98:99]
	v_max3_f32 v18, v2, s31, v3
	v_cmp_le_i32_e64 s[98:99], 19, v253
	v_cndmask_b32_e64 v4, v234, v4, s[100:101]
	v_cmp_le_i32_e64 s[100:101], 18, v253
	v_cndmask_b32_e32 v5, v234, v5, vcc
	v_max3_f32 v18, v18, v4, v5
	v_cmp_le_i32_e32 vcc, 17, v253
	v_cndmask_b32_e64 v6, v234, v6, s[98:99]
	v_cmp_le_i32_e64 s[98:99], 16, v253
	v_cndmask_b32_e64 v7, v234, v7, s[100:101]
	v_max3_f32 v18, v18, v6, v7
	v_cmp_le_i32_e64 s[100:101], 11, v253
	v_cndmask_b32_e32 v8, v234, v8, vcc
	v_cmp_le_i32_e32 vcc, 10, v253
	v_cndmask_b32_e64 v9, v234, v9, s[98:99]
	v_max3_f32 v18, v18, v8, v9
	v_cmp_le_i32_e64 s[98:99], 9, v253
	v_cndmask_b32_e64 v10, v234, v10, s[100:101]
	v_cmp_le_i32_e64 s[100:101], 8, v253
	v_cndmask_b32_e32 v11, v234, v11, vcc
	v_max3_f32 v18, v18, v10, v11
	v_cmp_le_i32_e32 vcc, 3, v253
	v_cndmask_b32_e64 v12, v234, v12, s[98:99]
	v_cmp_le_i32_e64 s[98:99], 2, v253
	v_cndmask_b32_e64 v13, v234, v13, s[100:101]
	v_max3_f32 v18, v18, v12, v13
	v_cmp_le_i32_e64 s[100:101], 1, v253
	v_cndmask_b32_e32 v14, v234, v14, vcc
	v_cmp_le_i32_e32 vcc, 0, v253
	v_cndmask_b32_e64 v15, v234, v15, s[98:99]
	v_max3_f32 v18, v18, v14, v15
	v_cndmask_b32_e64 v16, v234, v16, s[100:101]
	v_cndmask_b32_e32 v17, v234, v17, vcc
	v_max3_f32 v18, v18, v16, v17
	ds_bpermute_b32 v19, v179, v18
	s_waitcnt lgkmcnt(0)
	v_max_f32_e32 v19, v19, v19
	v_max_f32_e32 v18, v18, v19
	v_cmp_lt_f32_e32 vcc, s34, v18
	s_cmp_eq_u64 vcc, 0
	v_max_f32_e32 v19, 0xf149f2ca, v18
	s_cselect_b64 vcc, -1, 0
	v_cndmask_b32_e32 v150, v19, v235, vcc
	v_sub_f32_e32 v2, v2, v150
	v_exp_f32_e32 v50, v2
	v_sub_f32_e32 v2, v3, v150
	v_exp_f32_e32 v51, v2
	v_sub_f32_e32 v2, v4, v150
	v_exp_f32_e32 v94, v2
	v_sub_f32_e32 v2, v5, v150
	v_exp_f32_e32 v95, v2
	v_sub_f32_e32 v2, v6, v150
	v_exp_f32_e32 v6, v2
	v_sub_f32_e32 v2, v7, v150
	v_exp_f32_e32 v7, v2
	v_sub_f32_e32 v2, v8, v150
	v_exp_f32_e32 v8, v2
	v_sub_f32_e32 v2, v9, v150
	v_exp_f32_e32 v9, v2
	v_sub_f32_e32 v2, v10, v150
	v_exp_f32_e32 v162, v2
	v_sub_f32_e32 v2, v11, v150
	v_exp_f32_e32 v163, v2
	v_sub_f32_e32 v2, v12, v150
	v_exp_f32_e32 v164, v2
	v_sub_f32_e32 v2, v13, v150
	v_exp_f32_e32 v165, v2
	v_sub_f32_e32 v2, v14, v150
	v_sub_f32_e32 v21, 0xf149f2ca, v19
	v_exp_f32_e32 v171, v2
	v_sub_f32_e32 v2, v15, v150
	v_exp_f32_e32 v21, v21
	v_exp_f32_e32 v172, v2
	v_sub_f32_e32 v2, v16, v150
	v_exp_f32_e32 v173, v2
	v_sub_f32_e32 v2, v17, v150
	v_exp_f32_e32 v237, v2
	v_cvt_pk_bf16_f32 v54, v50, v51
	v_cvt_pk_bf16_f32 v55, v94, v95
	v_cvt_pk_bf16_f32 v56, v6, v7
	v_cvt_pk_bf16_f32 v57, v8, v9
	v_cvt_pk_bf16_f32 v154, v162, v163
	v_cvt_pk_bf16_f32 v155, v164, v165
	v_cvt_pk_bf16_f32 v156, v171, v172
	v_cvt_pk_bf16_f32 v157, v173, v237
	ds_read_b64_tr_b16 v[2:3], v181 offset:4608
	ds_read_b64_tr_b16 v[4:5], v181 offset:5888
	v_mul_f32_e32 v18, 0, v21
	v_cndmask_b32_e64 v34, v18, 0, vcc
	v_mov_b32_e32 v35, v34
	v_mov_b32_e32 v36, v34
	v_mov_b32_e32 v37, v34
	v_mov_b32_e32 v38, v34
	v_mov_b32_e32 v39, v34
	v_mov_b32_e32 v40, v34
	v_mov_b32_e32 v41, v34
	v_mov_b32_e32 v42, v34
	v_mov_b32_e32 v43, v34
	v_mov_b32_e32 v44, v34
	v_mov_b32_e32 v45, v34
	v_mov_b32_e32 v46, v34
	v_mov_b32_e32 v47, v34
	v_mov_b32_e32 v48, v34
	v_mov_b32_e32 v49, v34
	ds_read_b64_tr_b16 v[76:77], v181 offset:5952
	ds_read_b64_tr_b16 v[74:75], v181 offset:4672
	s_waitcnt lgkmcnt(2)
; #define LAS __attribute__((address_space(3)))
; template <int STAGE, int OFF> __device__ __forceinline__ void attn32_unit(const bf16* base, bf16* yrow0, int blk0, int u, LAS unsigned char* xtab, LAS unsigned char* kbuf, LAS unsigned char* vbuf, int lane, ...
;     ...
;         for (int c = 0; c < 4; ++c) { *(LAS v4u*)(kbuf + (8 * c + lrow) * 144 + lch * 16) = kr[set][c]; *(LAS v4u*)(vbuf + (8 * c + lrow) * 160 + lch * 16) = vr[set][c]; }
;         if (pp + 2 < 5) { ATT32_LOAD(set, pp + 2, t0, SH); }
;         else { const bf16* base_ = base; { const bf16* base = nbase; ATT32_LOAD(set, pp + 2 - 5, nt0, nsh); } (void)base_; }
;         f32x16 sc;
; #pragma unroll
;         for (int i = 0; i < 16; ++i) sc[i] = 0.f;
; #pragma unroll
;         for (int ks = 0; ks < 4; ++ks) { const bf16x8 ka = *(const LAS bf16x8*)(kbuf + qi * 144 + 32 * ks + 16 * h); sc = MFMA32(ka, qb[ks], sc); }
;         if (pp == 4) {
; #pragma unroll
;             for (int ks = 0; ks < 4; ++ks) qb[ks] = *(const bf16x8*)(nbase + (size_t)min(nt0 + (qi << nsh), SEQ - 1) * 1536 + 16 * ks + 8 * h);
;         }
;         const int mbase = n0 + 4 * h - lo; float mx = -INFINITY;
; #pragma unroll
;         for (int rg = 0; rg < 16; ++rg) { sc[rg] = ((unsigned)(mbase + (rg & 3) + 8 * (rg >> 2)) <= mspan) ? sc[rg] : -INFINITY; mx = fmaxf(mx, sc[rg]); }
;         mx = fmaxf(mx, __shfl_xor(mx, 32));
;         if (__any(mx > m)) {
;             const float mn = fmaxf(m, mx), alpha = __builtin_amdgcn_exp2f(m - mn); m = mn; l *= alpha;
; #pragma unroll
;             for (int i = 0; i < 16; ++i) { o[0][i] *= alpha; o[1][i] *= alpha; }
;         }
;         float ps = 0.f;
; #pragma unroll
;         for (int rg = 0; rg < 16; ++rg) { sc[rg] = __builtin_amdgcn_exp2f(sc[rg] - m); ps += sc[rg]; }
;         l += ps;
;         bf16x8 pb[2];
; #pragma unroll
;         for (int s2 = 0; s2 < 2; ++s2) { v4u w; w.x = pg8::cvt_pk_bf16(sc[8 * s2], sc[8 * s2 + 1]); w.y = pg8::cvt_pk_bf16(sc[8 * s2 + 2], sc[8 * s2 + 3]); w.z = pg8::cvt_pk_bf16(sc[8 * s2 + 4], sc[8 * s2 + 5]); w.w = pg8::cvt_pk_bf16(sc[8 * s2 + 6], sc[8 * s2 + 7]); pb[s2] = __builtin_bit_cast(bf16x8, w); }
; #pragma unroll
;         for (int mb = 0; mb < 2; ++mb)
; #pragma unroll
;             for (int s2 = 0; s2 < 2; ++s2) {
;                 LAS unsigned char* vp = vbuf + tr_off + (16 * s2) * 160 + 64 * mb;
	v_mfma_f32_32x32x16_bf16 v[18:33], v[2:5], v[54:57], v[34:49]
	ds_read_b64_tr_b16 v[2:3], v181 offset:7168
	ds_read_b64_tr_b16 v[4:5], v181 offset:8448
	v_add_f32_e32 v10, 0, v50
	v_add_f32_e32 v10, v51, v10
	ds_read_b64_tr_b16 v[160:161], v181 offset:8512
	ds_read_b64_tr_b16 v[158:159], v181 offset:7232
	ds_write_b128 v231, v[106:109]
	ds_write_b128 v232, v[110:113] offset:4608
	ds_write_b128 v231, v[114:117] offset:1152
	ds_write_b128 v232, v[118:121] offset:5888
	ds_write_b128 v231, v[122:125] offset:2304
	ds_write_b128 v232, v[126:129] offset:7168
	ds_write_b128 v231, v[130:133] offset:3456
	ds_write_b128 v232, v[134:137] offset:8448
	s_waitcnt lgkmcnt(10)
	v_mfma_f32_32x32x16_bf16 v[18:33], v[2:5], v[154:157], v[18:33]
	v_add_f32_e32 v2, v94, v10
	v_add_f32_e32 v2, v95, v2
	v_add_f32_e32 v2, v6, v2
	v_add_f32_e32 v2, v7, v2
	v_add_f32_e32 v2, v8, v2
	v_add_f32_e32 v238, v9, v2
	v_mov_b64_e32 v[2:3], v[34:35]
	v_mov_b64_e32 v[4:5], v[36:37]
	v_mov_b64_e32 v[6:7], v[38:39]
	v_mov_b64_e32 v[8:9], v[40:41]
	v_mov_b64_e32 v[10:11], v[42:43]
	v_mov_b64_e32 v[12:13], v[44:45]
	v_mov_b64_e32 v[14:15], v[46:47]
	v_mov_b64_e32 v[16:17], v[48:49]
	v_max_i32_e32 v35, 0xffffffe0, v153
	v_add_u32_e32 v35, 32, v35
	v_min_u32_e32 v35, 0x3fff, v35
	v_mul_u32_u24_e32 v35, 0xc00, v35
	v_or_b32_e32 v35, v35, v176
	v_mfma_f32_32x32x16_bf16 v[2:17], v[74:77], v[54:57], v[2:17]
	global_load_dwordx4 v[54:57], v35, s[8:9] offset:1024
	global_load_dwordx4 v[74:77], v35, s[8:9] offset:2048
	ds_read_b128 v[36:39], v177
	v_max_i32_e32 v35, 0xffffffd8, v153
	v_add_u32_e32 v35, 40, v35
	v_min_u32_e32 v35, 0x3fff, v35
	v_mul_u32_u24_e32 v35, 0xc00, v35
	v_or_b32_e32 v35, v35, v176
	global_load_dwordx4 v[94:97], v35, s[8:9] offset:1024
	global_load_dwordx4 v[98:101], v35, s[8:9] offset:2048
	v_max_i32_e32 v35, 0xffffffd0, v153
	v_add_u32_e32 v35, 48, v35
	ds_read_b128 v[114:117], v177 offset:32
	s_waitcnt lgkmcnt(1)
	v_mfma_f32_32x32x16_bf16 v[36:51], v[36:39], v[66:69], 0
	v_min_u32_e32 v35, 0x3fff, v35
	v_mul_u32_u24_e32 v35, 0xc00, v35
	v_or_b32_e32 v35, v35, v176
	global_load_dwordx4 v[106:109], v35, s[8:9] offset:1024
	global_load_dwordx4 v[110:113], v35, s[8:9] offset:2048
	v_max_i32_e32 v35, 0xffffffc8, v153
	v_add_u32_e32 v35, 56, v35
	v_min_u32_e32 v35, 0x3fff, v35
	v_mul_u32_u24_e32 v35, 0xc00, v35
	v_or_b32_e32 v35, v35, v176
	ds_read_b128 v[122:125], v177 offset:96
	ds_read_b128 v[126:129], v177 offset:64
	s_waitcnt lgkmcnt(2)
	v_mfma_f32_32x32x16_bf16 v[36:51], v[114:117], v[62:65], v[36:51]
	global_load_dwordx4 v[114:117], v35, s[8:9] offset:1024
	global_load_dwordx4 v[118:121], v35, s[8:9] offset:2048
	v_add_f32_e32 v35, v162, v238
	v_add_f32_e32 v35, v163, v35
	v_add_f32_e32 v35, v164, v35
	v_add_f32_e32 v35, v165, v35
	v_add_f32_e32 v35, v171, v35
	v_add_f32_e32 v35, v172, v35
	s_waitcnt lgkmcnt(0)
	v_mfma_f32_32x32x16_bf16 v[36:51], v[126:129], v[58:61], v[36:51]
	v_add_f32_e32 v126, v173, v35
	v_mfma_f32_32x32x16_bf16 v[36:51], v[122:125], v[70:73], v[36:51]
	v_mfma_f32_32x32x16_bf16 v[2:17], v[158:161], v[154:157], v[2:17]
	s_nop 10
	v_add_u32_e32 v253, 59, v152
	v_cmp_le_i32_e32 vcc, 27, v253
	v_cmp_le_i32_e64 s[98:99], 26, v253
	v_cmp_le_i32_e64 s[100:101], 25, v253
	v_cndmask_b32_e32 v35, v234, v36, vcc
	v_cmp_le_i32_e32 vcc, 24, v253
	v_cndmask_b32_e64 v36, v234, v37, s[98:99]
	v_max3_f32 v122, v35, s31, v36
	v_cmp_le_i32_e64 s[98:99], 19, v253
	v_cndmask_b32_e64 v37, v234, v38, s[100:101]
	v_cmp_le_i32_e64 s[100:101], 18, v253
	v_cndmask_b32_e32 v38, v234, v39, vcc
	v_max3_f32 v122, v122, v37, v38
	v_cmp_le_i32_e32 vcc, 17, v253
	v_cndmask_b32_e64 v39, v234, v40, s[98:99]
	v_cmp_le_i32_e64 s[98:99], 16, v253
	v_cndmask_b32_e64 v40, v234, v41, s[100:101]
	v_max3_f32 v122, v122, v39, v40
	v_cmp_le_i32_e64 s[100:101], 11, v253
	v_cndmask_b32_e32 v41, v234, v42, vcc
	v_cmp_le_i32_e32 vcc, 10, v253
	v_cndmask_b32_e64 v42, v234, v43, s[98:99]
	v_max3_f32 v122, v122, v41, v42
	v_cmp_le_i32_e64 s[98:99], 9, v253
	v_cndmask_b32_e64 v43, v234, v44, s[100:101]
	v_cmp_le_i32_e64 s[100:101], 8, v253
	v_cndmask_b32_e32 v44, v234, v45, vcc
	v_max3_f32 v122, v122, v43, v44
	v_cmp_le_i32_e32 vcc, 3, v253
	v_cndmask_b32_e64 v45, v234, v46, s[98:99]
	v_cmp_le_i32_e64 s[98:99], 2, v253
	v_cndmask_b32_e64 v46, v234, v47, s[100:101]
	v_max3_f32 v122, v122, v45, v46
	v_cmp_le_i32_e64 s[100:101], 1, v253
	v_cndmask_b32_e32 v47, v234, v48, vcc
	v_cmp_le_i32_e32 vcc, 0, v253
	v_cndmask_b32_e64 v48, v234, v49, s[98:99]
	v_max3_f32 v122, v122, v47, v48
	v_cndmask_b32_e64 v49, v234, v50, s[100:101]
	v_add_f32_e32 v50, v237, v126
	v_add_f32_e32 v50, v34, v50
	v_cndmask_b32_e32 v51, v234, v51, vcc
	v_max3_f32 v122, v122, v49, v51
	ds_bpermute_b32 v123, v179, v122
	s_waitcnt lgkmcnt(0)
	v_max_f32_e32 v34, v123, v123
	v_max_f32_e32 v34, v122, v34
	v_cmp_gt_f32_e32 vcc, v34, v150
	s_cbranch_vccz .LBB0_372
	v_max_f32_e32 v34, v34, v34
	v_max_f32_e32 v122, v150, v150
	v_max_f32_e32 v122, v122, v34
	v_sub_f32_e32 v34, v150, v122
	v_exp_f32_e32 v34, v34
	v_mov_b32_e32 v150, v122
	v_pk_mul_f32 v[32:33], v[32:33], v[34:35] op_sel_hi:[1,0]
	v_pk_mul_f32 v[30:31], v[30:31], v[34:35] op_sel_hi:[1,0]
	v_pk_mul_f32 v[28:29], v[28:29], v[34:35] op_sel_hi:[1,0]
	v_pk_mul_f32 v[26:27], v[26:27], v[34:35] op_sel_hi:[1,0]
	v_pk_mul_f32 v[24:25], v[24:25], v[34:35] op_sel_hi:[1,0]
	v_pk_mul_f32 v[22:23], v[22:23], v[34:35] op_sel_hi:[1,0]
	v_pk_mul_f32 v[20:21], v[20:21], v[34:35] op_sel_hi:[1,0]
	v_pk_mul_f32 v[18:19], v[18:19], v[34:35] op_sel_hi:[1,0]
	v_pk_mul_f32 v[16:17], v[16:17], v[34:35] op_sel_hi:[1,0]
	v_pk_mul_f32 v[14:15], v[14:15], v[34:35] op_sel_hi:[1,0]
	v_pk_mul_f32 v[12:13], v[12:13], v[34:35] op_sel_hi:[1,0]
	v_pk_mul_f32 v[10:11], v[10:11], v[34:35] op_sel_hi:[1,0]
	v_pk_mul_f32 v[8:9], v[8:9], v[34:35] op_sel_hi:[1,0]
	v_pk_mul_f32 v[6:7], v[6:7], v[34:35] op_sel_hi:[1,0]
	v_pk_mul_f32 v[4:5], v[4:5], v[34:35] op_sel_hi:[1,0]
	v_pk_mul_f32 v[2:3], v[2:3], v[34:35] op_sel_hi:[1,0]
	v_mul_f32_e32 v50, v50, v34
; #define LAS __attribute__((address_space(3)))
; template <int STAGE, int OFF> __device__ __forceinline__ void attn32_unit(const bf16* base, bf16* yrow0, int blk0, int u, LAS unsigned char* xtab, LAS unsigned char* kbuf, LAS unsigned char* vbuf, int lane, ...
;     ...
;         for (int c = 0; c < 4; ++c) { *(LAS v4u*)(kbuf + (8 * c + lrow) * 144 + lch * 16) = kr[set][c]; *(LAS v4u*)(vbuf + (8 * c + lrow) * 160 + lch * 16) = vr[set][c]; }
;         if (pp + 2 < 5) { ATT32_LOAD(set, pp + 2, t0, SH); }
;         else { const bf16* base_ = base; { const bf16* base = nbase; ATT32_LOAD(set, pp + 2 - 5, nt0, nsh); } (void)base_; }
;         f32x16 sc;
; #pragma unroll
;         for (int i = 0; i < 16; ++i) sc[i] = 0.f;
; #pragma unroll
;         for (int ks = 0; ks < 4; ++ks) { const bf16x8 ka = *(const LAS bf16x8*)(kbuf + qi * 144 + 32 * ks + 16 * h); sc = MFMA32(ka, qb[ks], sc); }
;         if (pp == 4) {
; #pragma unroll
;             for (int ks = 0; ks < 4; ++ks) qb[ks] = *(const bf16x8*)(nbase + (size_t)min(nt0 + (qi << nsh), SEQ - 1) * 1536 + 16 * ks + 8 * h);
;         }
;         const int mbase = n0 + 4 * h - lo; float mx = -INFINITY;
; #pragma unroll
;         for (int rg = 0; rg < 16; ++rg) { sc[rg] = ((unsigned)(mbase + (rg & 3) + 8 * (rg >> 2)) <= mspan) ? sc[rg] : -INFINITY; mx = fmaxf(mx, sc[rg]); }
;         mx = fmaxf(mx, __shfl_xor(mx, 32));
;         if (__any(mx > m)) {
;             const float mn = fmaxf(m, mx), alpha = __builtin_amdgcn_exp2f(m - mn); m = mn; l *= alpha;
; #pragma unroll
;             for (int i = 0; i < 16; ++i) { o[0][i] *= alpha; o[1][i] *= alpha; }
;         }
;         float ps = 0.f;
; #pragma unroll
;         for (int rg = 0; rg < 16; ++rg) { sc[rg] = __builtin_amdgcn_exp2f(sc[rg] - m); ps += sc[rg]; }
;         l += ps;
;         bf16x8 pb[2];
; #pragma unroll
;         for (int s2 = 0; s2 < 2; ++s2) { v4u w; w.x = pg8::cvt_pk_bf16(sc[8 * s2], sc[8 * s2 + 1]); w.y = pg8::cvt_pk_bf16(sc[8 * s2 + 2], sc[8 * s2 + 3]); w.z = pg8::cvt_pk_bf16(sc[8 * s2 + 4], sc[8 * s2 + 5]); w.w = pg8::cvt_pk_bf16(sc[8 * s2 + 6], sc[8 * s2 + 7]); pb[s2] = __builtin_bit_cast(bf16x8, w); }
; #pragma unroll
;         for (int mb = 0; mb < 2; ++mb)
; #pragma unroll
;             for (int s2 = 0; s2 < 2; ++s2) {
;                 LAS unsigned char* vp = vbuf + tr_off + (16 * s2) * 160 + 64 * mb;
.LBB0_372:
	v_sub_f32_e32 v34, v35, v150
	v_exp_f32_e32 v126, v34
	v_sub_f32_e32 v34, v36, v150
	v_exp_f32_e32 v130, v34
	v_sub_f32_e32 v34, v37, v150
	v_exp_f32_e32 v131, v34
	v_sub_f32_e32 v34, v38, v150
	v_exp_f32_e32 v132, v34
	v_sub_f32_e32 v34, v39, v150
	v_exp_f32_e32 v133, v34
	v_sub_f32_e32 v34, v40, v150
	v_exp_f32_e32 v134, v34
	v_sub_f32_e32 v34, v41, v150
	v_exp_f32_e32 v135, v34
	v_sub_f32_e32 v34, v42, v150
	v_exp_f32_e32 v136, v34
	v_sub_f32_e32 v34, v43, v150
	v_exp_f32_e32 v154, v34
	v_sub_f32_e32 v34, v44, v150
	v_exp_f32_e32 v155, v34
	v_sub_f32_e32 v34, v45, v150
	v_exp_f32_e32 v156, v34
	v_sub_f32_e32 v34, v46, v150
	v_exp_f32_e32 v157, v34
	v_sub_f32_e32 v34, v47, v150
	v_exp_f32_e32 v158, v34
	v_sub_f32_e32 v34, v48, v150
	v_exp_f32_e32 v159, v34
	v_sub_f32_e32 v34, v49, v150
	v_exp_f32_e32 v160, v34
	v_sub_f32_e32 v34, v51, v150
	v_exp_f32_e32 v51, v34
	v_cvt_pk_bf16_f32 v34, v126, v130
	v_cvt_pk_bf16_f32 v35, v131, v132
	v_cvt_pk_bf16_f32 v36, v133, v134
	v_cvt_pk_bf16_f32 v37, v135, v136
	v_cvt_pk_bf16_f32 v122, v154, v155
	v_cvt_pk_bf16_f32 v123, v156, v157
	v_cvt_pk_bf16_f32 v124, v158, v159
	v_cvt_pk_bf16_f32 v125, v160, v51
	ds_read_b64_tr_b16 v[38:39], v181 offset:4608
	ds_read_b64_tr_b16 v[40:41], v181 offset:5888
	ds_read_b64_tr_b16 v[44:45], v181 offset:5952
	ds_read_b64_tr_b16 v[42:43], v181 offset:4672
	s_waitcnt lgkmcnt(2)
	v_mfma_f32_32x32x16_bf16 v[18:33], v[38:41], v[34:37], v[18:33]
	ds_read_b64_tr_b16 v[38:39], v181 offset:7168
	ds_read_b64_tr_b16 v[40:41], v181 offset:8448
	v_add_f32_e32 v46, 0, v126
	ds_read_b64_tr_b16 v[128:129], v181 offset:8512
	ds_read_b64_tr_b16 v[126:127], v181 offset:7232
	s_waitcnt vmcnt(15)
	ds_write_b128 v231, v[78:81]
	s_waitcnt vmcnt(14)
	ds_write_b128 v232, v[82:85] offset:4608
	s_waitcnt vmcnt(13)
	ds_write_b128 v231, v[86:89] offset:1152
	s_waitcnt vmcnt(12)
	ds_write_b128 v232, v[90:93] offset:5888
	s_waitcnt vmcnt(11)
	ds_write_b128 v231, v[102:105] offset:2304
	s_waitcnt vmcnt(10)
	ds_write_b128 v232, v[138:141] offset:7168
	s_waitcnt vmcnt(9)
	ds_write_b128 v231, v[142:145] offset:3456
	s_waitcnt vmcnt(8)
	ds_write_b128 v232, v[146:149] offset:8448
	v_add_u32_e32 v142, 0x58, v153
	v_med3_i32 v142, v142, 0, v233
	s_waitcnt lgkmcnt(10)
	v_mfma_f32_32x32x16_bf16 v[18:33], v[38:41], v[122:125], v[18:33]
	v_add_f32_e32 v38, v130, v46
	v_add_f32_e32 v38, v131, v38
	v_add_f32_e32 v38, v132, v38
	v_add_f32_e32 v38, v133, v38
	v_add_f32_e32 v38, v134, v38
	v_add_f32_e32 v38, v135, v38
	v_add_f32_e32 v161, v136, v38
	v_mfma_f32_32x32x16_bf16 v[2:17], v[42:45], v[34:37], v[2:17]
	v_or_b32_e32 v34, s10, v53
	v_min_u32_e32 v34, 0x3fff, v34
	v_mul_u32_u24_e32 v38, 0xc00, v34
	ds_read_b128 v[34:37], v177
	v_or_b32_e32 v38, v38, v176
	global_load_dwordx4 v[78:81], v38, s[8:9] offset:1024
	global_load_dwordx4 v[82:85], v38, s[8:9] offset:2048
	v_add_u32_e32 v38, 0x48, v153
	v_med3_i32 v38, v38, 0, v233
	v_mul_u32_u24_e32 v38, 0xc00, v38
	ds_read_b128 v[102:105], v177 offset:32
	v_or_b32_e32 v90, v38, v176
	s_waitcnt lgkmcnt(1)
	v_mfma_f32_32x32x16_bf16 v[34:49], v[34:37], v[66:69], 0
	v_add_u32_e32 v130, 0x50, v153
	v_med3_i32 v130, v130, 0, v233
	v_mul_u32_u24_e32 v130, 0xc00, v130
	v_mul_u32_u24_e32 v142, 0xc00, v142
	v_or_b32_e32 v138, v130, v176
	v_or_b32_e32 v146, v142, v176
	global_load_dwordx4 v[86:89], v90, s[8:9] offset:1024
	s_nop 0
	global_load_dwordx4 v[90:93], v90, s[8:9] offset:2048
	ds_read_b128 v[130:133], v177 offset:96
	ds_read_b128 v[134:137], v177 offset:64
	s_waitcnt lgkmcnt(2)
	v_mfma_f32_32x32x16_bf16 v[34:49], v[102:105], v[62:65], v[34:49]
	global_load_dwordx4 v[102:105], v138, s[8:9] offset:1024
	s_nop 0
	global_load_dwordx4 v[138:141], v138, s[8:9] offset:2048
	s_nop 0
	global_load_dwordx4 v[142:145], v146, s[8:9] offset:1024
	s_nop 0
	global_load_dwordx4 v[146:149], v146, s[8:9] offset:2048
	s_waitcnt lgkmcnt(0)
	v_mfma_f32_32x32x16_bf16 v[34:49], v[134:137], v[58:61], v[34:49]
	v_add_f32_e32 v134, v154, v161
	v_add_f32_e32 v134, v155, v134
	v_add_f32_e32 v134, v156, v134
	v_add_f32_e32 v134, v157, v134
	v_add_f32_e32 v134, v158, v134
	v_add_f32_e32 v134, v159, v134
	v_add_f32_e32 v134, v160, v134
	v_mfma_f32_32x32x16_bf16 v[34:49], v[130:133], v[70:73], v[34:49]
	v_add_f32_e32 v51, v51, v134
	v_add_f32_e32 v50, v50, v51
	s_nop 5
	v_add_u32_e32 v253, 91, v152
	v_cmp_le_i32_e32 vcc, 27, v253
	v_cmp_le_i32_e64 s[98:99], 26, v253
	v_cmp_le_i32_e64 s[100:101], 25, v253
	v_cndmask_b32_e32 v34, v234, v34, vcc
	v_mfma_f32_32x32x16_bf16 v[2:17], v[126:129], v[122:125], v[2:17]
	v_cmp_le_i32_e32 vcc, 24, v253
	v_cndmask_b32_e64 v35, v234, v35, s[98:99]
	v_max3_f32 v130, v34, s31, v35
	v_cmp_le_i32_e64 s[98:99], 19, v253
	v_cndmask_b32_e64 v36, v234, v36, s[100:101]
	v_cmp_le_i32_e64 s[100:101], 18, v253
	v_cndmask_b32_e32 v37, v234, v37, vcc
	v_max3_f32 v130, v130, v36, v37
	v_cmp_le_i32_e32 vcc, 17, v253
	v_cndmask_b32_e64 v38, v234, v38, s[98:99]
	v_cmp_le_i32_e64 s[98:99], 16, v253
	v_cndmask_b32_e64 v39, v234, v39, s[100:101]
	v_max3_f32 v130, v130, v38, v39
	v_cmp_le_i32_e64 s[100:101], 11, v253
	v_cndmask_b32_e32 v40, v234, v40, vcc
	v_cmp_le_i32_e32 vcc, 10, v253
	v_cndmask_b32_e64 v41, v234, v41, s[98:99]
	v_max3_f32 v130, v130, v40, v41
	v_cmp_le_i32_e64 s[98:99], 9, v253
	v_cndmask_b32_e64 v42, v234, v42, s[100:101]
	v_cmp_le_i32_e64 s[100:101], 8, v253
	v_cndmask_b32_e32 v43, v234, v43, vcc
	v_max3_f32 v130, v130, v42, v43
	v_cmp_le_i32_e32 vcc, 3, v253
	v_cndmask_b32_e64 v44, v234, v44, s[98:99]
	v_cmp_le_i32_e64 s[98:99], 2, v253
	v_cndmask_b32_e64 v45, v234, v45, s[100:101]
	v_max3_f32 v130, v130, v44, v45
	v_cmp_le_i32_e64 s[100:101], 1, v253
	v_cndmask_b32_e32 v46, v234, v46, vcc
	v_cmp_le_i32_e32 vcc, 0, v253
	v_cndmask_b32_e64 v47, v234, v47, s[98:99]
	v_max3_f32 v130, v130, v46, v47
	v_cndmask_b32_e64 v48, v234, v48, s[100:101]
	v_cndmask_b32_e32 v49, v234, v49, vcc
	v_max3_f32 v130, v130, v48, v49
	ds_bpermute_b32 v131, v179, v130
	s_waitcnt lgkmcnt(0)
	v_max_f32_e32 v51, v131, v131
	v_max_f32_e32 v51, v130, v51
	v_cmp_gt_f32_e32 vcc, v51, v150
	s_cbranch_vccz .LBB0_374
; #define LAS __attribute__((address_space(3)))
; template <int STAGE, int OFF> __device__ __forceinline__ void attn32_unit(const bf16* base, bf16* yrow0, int blk0, int u, LAS unsigned char* xtab, LAS unsigned char* kbuf, LAS unsigned char* vbuf, int lane, ...
;     ...
;         for (int c = 0; c < 4; ++c) { *(LAS v4u*)(kbuf + (8 * c + lrow) * 144 + lch * 16) = kr[set][c]; *(LAS v4u*)(vbuf + (8 * c + lrow) * 160 + lch * 16) = vr[set][c]; }
;         if (pp + 2 < 5) { ATT32_LOAD(set, pp + 2, t0, SH); }
;         else { const bf16* base_ = base; { const bf16* base = nbase; ATT32_LOAD(set, pp + 2 - 5, nt0, nsh); } (void)base_; }
;         f32x16 sc;
; #pragma unroll
;         for (int i = 0; i < 16; ++i) sc[i] = 0.f;
; #pragma unroll
;         for (int ks = 0; ks < 4; ++ks) { const bf16x8 ka = *(const LAS bf16x8*)(kbuf + qi * 144 + 32 * ks + 16 * h); sc = MFMA32(ka, qb[ks], sc); }
;         if (pp == 4) {
; #pragma unroll
;             for (int ks = 0; ks < 4; ++ks) qb[ks] = *(const bf16x8*)(nbase + (size_t)min(nt0 + (qi << nsh), SEQ - 1) * 1536 + 16 * ks + 8 * h);
;         }
;         const int mbase = n0 + 4 * h - lo; float mx = -INFINITY;
; #pragma unroll
;         for (int rg = 0; rg < 16; ++rg) { sc[rg] = ((unsigned)(mbase + (rg & 3) + 8 * (rg >> 2)) <= mspan) ? sc[rg] : -INFINITY; mx = fmaxf(mx, sc[rg]); }
;         mx = fmaxf(mx, __shfl_xor(mx, 32));
;         if (__any(mx > m)) {
;             const float mn = fmaxf(m, mx), alpha = __builtin_amdgcn_exp2f(m - mn); m = mn; l *= alpha;
; #pragma unroll
;             for (int i = 0; i < 16; ++i) { o[0][i] *= alpha; o[1][i] *= alpha; }
;         }
;         float ps = 0.f;
; #pragma unroll
;         for (int rg = 0; rg < 16; ++rg) { sc[rg] = __builtin_amdgcn_exp2f(sc[rg] - m); ps += sc[rg]; }
;         l += ps;
;         bf16x8 pb[2];
; #pragma unroll
;         for (int s2 = 0; s2 < 2; ++s2) { v4u w; w.x = pg8::cvt_pk_bf16(sc[8 * s2], sc[8 * s2 + 1]); w.y = pg8::cvt_pk_bf16(sc[8 * s2 + 2], sc[8 * s2 + 3]); w.z = pg8::cvt_pk_bf16(sc[8 * s2 + 4], sc[8 * s2 + 5]); w.w = pg8::cvt_pk_bf16(sc[8 * s2 + 6], sc[8 * s2 + 7]); pb[s2] = __builtin_bit_cast(bf16x8, w); }
; #pragma unroll
;         for (int mb = 0; mb < 2; ++mb)
; #pragma unroll
;             for (int s2 = 0; s2 < 2; ++s2) {
;                 LAS unsigned char* vp = vbuf + tr_off + (16 * s2) * 160 + 64 * mb;
	v_max_f32_e32 v51, v51, v51
	v_max_f32_e32 v122, v150, v150
	v_max_f32_e32 v51, v122, v51
	v_sub_f32_e32 v122, v150, v51
	v_exp_f32_e32 v122, v122
	v_mov_b32_e32 v150, v51
	v_pk_mul_f32 v[32:33], v[32:33], v[122:123] op_sel_hi:[1,0]
	v_pk_mul_f32 v[30:31], v[30:31], v[122:123] op_sel_hi:[1,0]
	v_pk_mul_f32 v[28:29], v[28:29], v[122:123] op_sel_hi:[1,0]
	v_pk_mul_f32 v[26:27], v[26:27], v[122:123] op_sel_hi:[1,0]
	v_pk_mul_f32 v[24:25], v[24:25], v[122:123] op_sel_hi:[1,0]
	v_pk_mul_f32 v[22:23], v[22:23], v[122:123] op_sel_hi:[1,0]
	v_pk_mul_f32 v[20:21], v[20:21], v[122:123] op_sel_hi:[1,0]
	v_pk_mul_f32 v[18:19], v[18:19], v[122:123] op_sel_hi:[1,0]
	v_pk_mul_f32 v[16:17], v[16:17], v[122:123] op_sel_hi:[1,0]
	v_pk_mul_f32 v[14:15], v[14:15], v[122:123] op_sel_hi:[1,0]
	v_pk_mul_f32 v[12:13], v[12:13], v[122:123] op_sel_hi:[1,0]
	v_pk_mul_f32 v[10:11], v[10:11], v[122:123] op_sel_hi:[1,0]
	v_pk_mul_f32 v[8:9], v[8:9], v[122:123] op_sel_hi:[1,0]
	v_pk_mul_f32 v[6:7], v[6:7], v[122:123] op_sel_hi:[1,0]
	v_pk_mul_f32 v[4:5], v[4:5], v[122:123] op_sel_hi:[1,0]
	v_pk_mul_f32 v[2:3], v[2:3], v[122:123] op_sel_hi:[1,0]
	v_mul_f32_e32 v50, v50, v122
.LBB0_374:
	v_sub_f32_e32 v34, v34, v150
	v_exp_f32_e32 v51, v34
	v_sub_f32_e32 v34, v35, v150
	v_exp_f32_e32 v122, v34
	v_sub_f32_e32 v34, v36, v150
	v_exp_f32_e32 v123, v34
	v_sub_f32_e32 v34, v37, v150
	v_exp_f32_e32 v124, v34
	v_sub_f32_e32 v34, v38, v150
	v_exp_f32_e32 v125, v34
	v_sub_f32_e32 v34, v39, v150
	v_exp_f32_e32 v126, v34
	v_sub_f32_e32 v34, v40, v150
	v_exp_f32_e32 v127, v34
	v_sub_f32_e32 v34, v41, v150
	v_exp_f32_e32 v128, v34
	v_sub_f32_e32 v34, v42, v150
	v_exp_f32_e32 v153, v34
	v_sub_f32_e32 v34, v43, v150
	v_exp_f32_e32 v162, v34
	v_sub_f32_e32 v34, v44, v150
	v_exp_f32_e32 v163, v34
	v_sub_f32_e32 v34, v45, v150
	v_exp_f32_e32 v164, v34
	v_sub_f32_e32 v34, v46, v150
	v_exp_f32_e32 v165, v34
	v_sub_f32_e32 v34, v47, v150
	v_exp_f32_e32 v171, v34
	v_sub_f32_e32 v34, v48, v150
	v_exp_f32_e32 v172, v34
	v_sub_f32_e32 v34, v49, v150
	v_exp_f32_e32 v173, v34
	v_cvt_pk_bf16_f32 v34, v51, v122
	v_cvt_pk_bf16_f32 v35, v123, v124
	v_cvt_pk_bf16_f32 v36, v125, v126
	v_cvt_pk_bf16_f32 v37, v127, v128
	v_cvt_pk_bf16_f32 v154, v153, v162
	v_cvt_pk_bf16_f32 v155, v163, v164
	v_cvt_pk_bf16_f32 v156, v165, v171
	v_cvt_pk_bf16_f32 v157, v172, v173
	ds_read_b64_tr_b16 v[38:39], v181 offset:4608
	ds_read_b64_tr_b16 v[40:41], v181 offset:5888
	ds_read_b64_tr_b16 v[44:45], v181 offset:5952
	ds_read_b64_tr_b16 v[42:43], v181 offset:4672
	s_waitcnt lgkmcnt(2)
	v_mfma_f32_32x32x16_bf16 v[18:33], v[38:41], v[34:37], v[18:33]
	ds_read_b64_tr_b16 v[38:39], v181 offset:7168
	ds_read_b64_tr_b16 v[40:41], v181 offset:8448
	v_add_f32_e32 v46, 0, v51
	s_add_i32 s10, s13, s24
	ds_read_b64_tr_b16 v[160:161], v181 offset:8512
	ds_read_b64_tr_b16 v[158:159], v181 offset:7232
	s_waitcnt vmcnt(15)
	ds_write_b128 v231, v[54:57]
	s_waitcnt vmcnt(14)
	ds_write_b128 v232, v[74:77] offset:4608
	s_waitcnt vmcnt(13)
	ds_write_b128 v231, v[94:97] offset:1152
	s_waitcnt vmcnt(12)
	ds_write_b128 v232, v[98:101] offset:5888
	s_waitcnt vmcnt(11)
	ds_write_b128 v231, v[106:109] offset:2304
	s_waitcnt vmcnt(10)
	ds_write_b128 v232, v[110:113] offset:7168
	s_waitcnt vmcnt(9)
	ds_write_b128 v231, v[114:117] offset:3456
	s_waitcnt vmcnt(8)
	ds_write_b128 v232, v[118:121] offset:8448
	s_waitcnt lgkmcnt(10)
	v_mfma_f32_32x32x16_bf16 v[18:33], v[38:41], v[154:157], v[18:33]
	v_add_f32_e32 v38, v122, v46
	v_add_f32_e32 v38, v123, v38
	v_add_f32_e32 v38, v124, v38
	v_add_f32_e32 v38, v125, v38
	v_add_f32_e32 v38, v126, v38
	v_add_f32_e32 v38, v127, v38
	v_add_f32_e32 v51, v128, v38
	v_mfma_f32_32x32x16_bf16 v[2:17], v[42:45], v[34:37], v[2:17]
	v_add_u32_e32 v34, s10, v185
	v_med3_i32 v34, v34, 0, v233
	v_mul_u32_u24_e32 v38, 0xc00, v34
	ds_read_b128 v[34:37], v177
	v_or_b32_e32 v38, v38, v176
	global_load_dwordx4 v[106:109], v38, s[8:9] offset:1024
	global_load_dwordx4 v[110:113], v38, s[8:9] offset:2048
	v_add_u32_e32 v38, s10, v186
	v_med3_i32 v38, v38, 0, v233
	v_mul_u32_u24_e32 v38, 0xc00, v38
	ds_read_b128 v[54:57], v177 offset:32
	v_or_b32_e32 v74, v38, v176
	s_waitcnt lgkmcnt(1)
	v_mfma_f32_32x32x16_bf16 v[34:49], v[34:37], v[66:69], 0
	global_load_dwordx4 v[114:117], v74, s[8:9] offset:1024
	global_load_dwordx4 v[118:121], v74, s[8:9] offset:2048
	v_add_u32_e32 v74, s10, v187
	v_med3_i32 v74, v74, 0, v233
	v_mul_u32_u24_e32 v74, 0xc00, v74
	v_or_b32_e32 v98, v74, v176
	ds_read_b128 v[74:77], v177 offset:96
	ds_read_b128 v[94:97], v177 offset:64
	global_load_dwordx4 v[122:125], v98, s[8:9] offset:1024
	global_load_dwordx4 v[126:129], v98, s[8:9] offset:2048
	s_waitcnt lgkmcnt(2)
	v_mfma_f32_32x32x16_bf16 v[34:49], v[54:57], v[62:65], v[34:49]
	v_add_u32_e32 v54, s10, v188
	v_med3_i32 v54, v54, 0, v233
	v_mul_u32_u24_e32 v54, 0xc00, v54
	v_or_b32_e32 v54, v54, v176
	global_load_dwordx4 v[130:133], v54, s[8:9] offset:1024
	global_load_dwordx4 v[134:137], v54, s[8:9] offset:2048
	s_waitcnt lgkmcnt(0)
; __device__ __forceinline__ unsigned cvt_pk_bf16(float lo, float hi) { unsigned r; asm volatile("v_cvt_pk_bf16_f32 %0, %1, %2" : "=v"(r) : "v"(lo), "v"(hi)); return r; }
; #define LAS __attribute__((address_space(3)))
; template <int STAGE, int OFF> __device__ __forceinline__ void attn32_unit(const bf16* base, bf16* yrow0, int blk0, int u, LAS unsigned char* xtab, LAS unsigned char* kbuf, LAS unsigned char* vbuf, int lane, ...
;     ...
; #pragma unroll
;         for (int ks = 0; ks < 4; ++ks) { const bf16x8 ka = *(const LAS bf16x8*)(kbuf + qi * 144 + 32 * ks + 16 * h); sc = MFMA32(ka, qb[ks], sc); }
;         if (pp == 4) {
; #pragma unroll
;             for (int ks = 0; ks < 4; ++ks) qb[ks] = *(const bf16x8*)(nbase + (size_t)min(nt0 + (qi << nsh), SEQ - 1) * 1536 + 16 * ks + 8 * h);
;         }
;         const int mbase = n0 + 4 * h - lo; float mx = -INFINITY;
; #pragma unroll
;         for (int rg = 0; rg < 16; ++rg) { sc[rg] = ((unsigned)(mbase + (rg & 3) + 8 * (rg >> 2)) <= mspan) ? sc[rg] : -INFINITY; mx = fmaxf(mx, sc[rg]); }
;         mx = fmaxf(mx, __shfl_xor(mx, 32));
;         if (__any(mx > m)) {
;             const float mn = fmaxf(m, mx), alpha = __builtin_amdgcn_exp2f(m - mn); m = mn; l *= alpha;
; #pragma unroll
;             for (int i = 0; i < 16; ++i) { o[0][i] *= alpha; o[1][i] *= alpha; }
;         }
;         float ps = 0.f;
; #pragma unroll
;         for (int rg = 0; rg < 16; ++rg) { sc[rg] = __builtin_amdgcn_exp2f(sc[rg] - m); ps += sc[rg]; }
;         l += ps;
;         bf16x8 pb[2];
; #pragma unroll
;         for (int s2 = 0; s2 < 2; ++s2) { v4u w; w.x = pg8::cvt_pk_bf16(sc[8 * s2], sc[8 * s2 + 1]); w.y = pg8::cvt_pk_bf16(sc[8 * s2 + 2], sc[8 * s2 + 3]); w.z = pg8::cvt_pk_bf16(sc[8 * s2 + 4], sc[8 * s2 + 5]); w.w = pg8::cvt_pk_bf16(sc[8 * s2 + 6], sc[8 * s2 + 7]); pb[s2] = __builtin_bit_cast(bf16x8, w); }
; #pragma unroll
;         for (int mb = 0; mb < 2; ++mb)
; #pragma unroll
;             for (int s2 = 0; s2 < 2; ++s2) {
;                 LAS unsigned char* vp = vbuf + tr_off + (16 * s2) * 160 + 64 * mb;
;                 const v4i16 a0 = __builtin_amdgcn_ds_read_tr16_b64_v4i16((LAS v4i16*)vp), a1 = __builtin_amdgcn_ds_read_tr16_b64_v4i16((LAS v4i16*)(vp + 8 * 160));
;                 const bf16x8 va = __builtin_shufflevector(a0, a1, 0, 1, 2, 3, 4, 5, 6, 7);
;                 o[mb] = MFMA32(va, pb[s2], o[mb]);
;             }
	v_mfma_f32_32x32x16_bf16 v[34:49], v[94:97], v[58:61], v[34:49]
	v_add_f32_e32 v51, v153, v51
	v_add_f32_e32 v51, v162, v51
	v_add_f32_e32 v51, v163, v51
	v_add_f32_e32 v51, v164, v51
	v_add_f32_e32 v51, v165, v51
	v_mfma_f32_32x32x16_bf16 v[34:49], v[74:77], v[70:73], v[34:49]
	v_add_f32_e32 v51, v171, v51
	v_add_f32_e32 v51, v172, v51
	v_add_f32_e32 v51, v173, v51
	v_add_f32_e32 v50, v50, v51
	v_mfma_f32_32x32x16_bf16 v[2:17], v[158:161], v[154:157], v[2:17]
	s_nop 6
	v_add_u32_e32 v253, 123, v152
	v_cmp_le_i32_e32 vcc, 27, v253
	v_cmp_le_i32_e64 s[98:99], 26, v253
	v_cmp_le_i32_e64 s[100:101], 25, v253
	v_cndmask_b32_e32 v34, v234, v34, vcc
	v_cmp_le_i32_e32 vcc, 24, v253
	v_cndmask_b32_e64 v35, v234, v35, s[98:99]
	v_max3_f32 v54, v34, s31, v35
	v_cmp_le_i32_e64 s[98:99], 19, v253
	v_cndmask_b32_e64 v36, v234, v36, s[100:101]
	v_cmp_le_i32_e64 s[100:101], 18, v253
	v_cndmask_b32_e32 v37, v234, v37, vcc
	v_max3_f32 v54, v54, v36, v37
	v_cmp_le_i32_e32 vcc, 17, v253
	v_cndmask_b32_e64 v38, v234, v38, s[98:99]
	v_cmp_le_i32_e64 s[98:99], 16, v253
	v_cndmask_b32_e64 v39, v234, v39, s[100:101]
	v_max3_f32 v54, v54, v38, v39
	v_cmp_le_i32_e64 s[100:101], 11, v253
	v_cndmask_b32_e32 v40, v234, v40, vcc
	v_cmp_le_i32_e32 vcc, 10, v253
	v_cndmask_b32_e64 v41, v234, v41, s[98:99]
	v_max3_f32 v54, v54, v40, v41
	v_cmp_le_i32_e64 s[98:99], 9, v253
	v_cndmask_b32_e64 v42, v234, v42, s[100:101]
	v_cmp_le_i32_e64 s[100:101], 8, v253
	v_cndmask_b32_e32 v43, v234, v43, vcc
	v_max3_f32 v54, v54, v42, v43
	v_cmp_le_i32_e32 vcc, 3, v253
	v_cndmask_b32_e64 v44, v234, v44, s[98:99]
	v_cmp_le_i32_e64 s[98:99], 2, v253
	v_cndmask_b32_e64 v45, v234, v45, s[100:101]
	v_max3_f32 v54, v54, v44, v45
	v_cmp_le_i32_e64 s[100:101], 1, v253
	v_cndmask_b32_e32 v46, v234, v46, vcc
	v_cmp_le_i32_e32 vcc, 0, v253
	v_cndmask_b32_e64 v47, v234, v47, s[98:99]
	v_max3_f32 v54, v54, v46, v47
	v_cndmask_b32_e64 v48, v234, v48, s[100:101]
	v_cndmask_b32_e32 v49, v234, v49, vcc
	v_max3_f32 v54, v54, v48, v49
	ds_bpermute_b32 v55, v179, v54
	s_waitcnt lgkmcnt(0)
	v_max_f32_e32 v51, v55, v55
	v_max_f32_e32 v51, v54, v51
	v_cmp_gt_f32_e32 vcc, v51, v150
	s_cbranch_vccz .LBB0_376
	v_max_f32_e32 v51, v51, v51
	v_max_f32_e32 v54, v150, v150
	v_max_f32_e32 v51, v54, v51
	v_sub_f32_e32 v54, v150, v51
	v_exp_f32_e32 v54, v54
	v_mov_b32_e32 v150, v51
	v_pk_mul_f32 v[32:33], v[32:33], v[54:55] op_sel_hi:[1,0]
	v_pk_mul_f32 v[30:31], v[30:31], v[54:55] op_sel_hi:[1,0]
	v_pk_mul_f32 v[28:29], v[28:29], v[54:55] op_sel_hi:[1,0]
	v_pk_mul_f32 v[26:27], v[26:27], v[54:55] op_sel_hi:[1,0]
	v_pk_mul_f32 v[24:25], v[24:25], v[54:55] op_sel_hi:[1,0]
	v_pk_mul_f32 v[22:23], v[22:23], v[54:55] op_sel_hi:[1,0]
	v_pk_mul_f32 v[20:21], v[20:21], v[54:55] op_sel_hi:[1,0]
	v_pk_mul_f32 v[18:19], v[18:19], v[54:55] op_sel_hi:[1,0]
	v_pk_mul_f32 v[16:17], v[16:17], v[54:55] op_sel_hi:[1,0]
	v_pk_mul_f32 v[14:15], v[14:15], v[54:55] op_sel_hi:[1,0]
	v_pk_mul_f32 v[12:13], v[12:13], v[54:55] op_sel_hi:[1,0]
	v_pk_mul_f32 v[10:11], v[10:11], v[54:55] op_sel_hi:[1,0]
	v_pk_mul_f32 v[8:9], v[8:9], v[54:55] op_sel_hi:[1,0]
	v_pk_mul_f32 v[6:7], v[6:7], v[54:55] op_sel_hi:[1,0]
	v_pk_mul_f32 v[4:5], v[4:5], v[54:55] op_sel_hi:[1,0]
	v_pk_mul_f32 v[2:3], v[2:3], v[54:55] op_sel_hi:[1,0]
	v_mul_f32_e32 v50, v50, v54
.LBB0_376:
	v_sub_f32_e32 v34, v34, v150
	v_exp_f32_e32 v51, v34
	v_sub_f32_e32 v34, v35, v150
	v_exp_f32_e32 v54, v34
	v_sub_f32_e32 v34, v36, v150
	v_exp_f32_e32 v55, v34
	v_sub_f32_e32 v34, v37, v150
	v_exp_f32_e32 v56, v34
	v_sub_f32_e32 v34, v38, v150
	v_exp_f32_e32 v57, v34
	v_sub_f32_e32 v34, v39, v150
	v_exp_f32_e32 v74, v34
	v_sub_f32_e32 v34, v40, v150
	v_exp_f32_e32 v75, v34
	v_sub_f32_e32 v34, v41, v150
	v_exp_f32_e32 v76, v34
	v_sub_f32_e32 v34, v42, v150
	v_exp_f32_e32 v153, v34
	v_sub_f32_e32 v34, v43, v150
	v_exp_f32_e32 v164, v34
	v_sub_f32_e32 v34, v44, v150
	v_exp_f32_e32 v165, v34
	v_sub_f32_e32 v34, v45, v150
	v_exp_f32_e32 v171, v34
	v_sub_f32_e32 v34, v46, v150
	v_exp_f32_e32 v172, v34
	v_sub_f32_e32 v34, v47, v150
	v_exp_f32_e32 v173, v34
	v_sub_f32_e32 v34, v48, v150
	v_exp_f32_e32 v237, v34
	v_sub_f32_e32 v34, v49, v150
	v_exp_f32_e32 v238, v34
	v_cvt_pk_bf16_f32 v34, v51, v54
	v_cvt_pk_bf16_f32 v35, v55, v56
	v_cvt_pk_bf16_f32 v36, v57, v74
	v_cvt_pk_bf16_f32 v37, v75, v76
	v_cvt_pk_bf16_f32 v154, v153, v164
	v_cvt_pk_bf16_f32 v155, v165, v171
	v_cvt_pk_bf16_f32 v156, v172, v173
	v_cvt_pk_bf16_f32 v157, v237, v238
	ds_read_b64_tr_b16 v[38:39], v181 offset:4608
	ds_read_b64_tr_b16 v[40:41], v181 offset:5888
	v_or_b32_e32 v42, s10, v183
	v_min_i32_e32 v77, 0x3fff, v42
	s_waitcnt lgkmcnt(0)
	v_mfma_f32_32x32x16_bf16 v[18:33], v[38:41], v[34:37], v[18:33]
	v_mov_b64_e32 v[38:39], s[8:9]
	v_mad_i64_i32 v[38:39], s[14:15], v77, s30, v[38:39]
	ds_read_b64_tr_b16 v[42:43], v181 offset:7168
	ds_read_b64_tr_b16 v[44:45], v181 offset:8448
	ds_read_b64_tr_b16 v[48:49], v181 offset:5952
	ds_read_b64_tr_b16 v[46:47], v181 offset:4672
	v_lshl_add_u64 v[162:163], v[38:39], 0, v[168:169]
	v_add_f32_e32 v38, 0, v51
	v_add_f32_e32 v38, v54, v38
	v_add_f32_e32 v38, v55, v38
	v_add_f32_e32 v38, v56, v38
	v_add_f32_e32 v38, v57, v38
	v_add_f32_e32 v38, v74, v38
	s_waitcnt lgkmcnt(0)
	v_mfma_f32_32x32x16_bf16 v[2:17], v[46:49], v[34:37], v[2:17]
	v_add_u32_e32 v34, s10, v189
	ds_read_b64_tr_b16 v[160:161], v181 offset:8512
	ds_read_b64_tr_b16 v[158:159], v181 offset:7232
	v_add_f32_e32 v38, v75, v38
	s_waitcnt vmcnt(15)
; #define LAS __attribute__((address_space(3)))
; template <int STAGE, int OFF> __device__ __forceinline__ void attn32_unit(const bf16* base, bf16* yrow0, int blk0, int u, LAS unsigned char* xtab, LAS unsigned char* kbuf, LAS unsigned char* vbuf, int lane, ...
;     ...
;         for (int c = 0; c < 4; ++c) { *(LAS v4u*)(kbuf + (8 * c + lrow) * 144 + lch * 16) = kr[set][c]; *(LAS v4u*)(vbuf + (8 * c + lrow) * 160 + lch * 16) = vr[set][c]; }
;         if (pp + 2 < 5) { ATT32_LOAD(set, pp + 2, t0, SH); }
;         else { const bf16* base_ = base; { const bf16* base = nbase; ATT32_LOAD(set, pp + 2 - 5, nt0, nsh); } (void)base_; }
;         f32x16 sc;
; #pragma unroll
;         for (int i = 0; i < 16; ++i) sc[i] = 0.f;
; #pragma unroll
;         for (int ks = 0; ks < 4; ++ks) { const bf16x8 ka = *(const LAS bf16x8*)(kbuf + qi * 144 + 32 * ks + 16 * h); sc = MFMA32(ka, qb[ks], sc); }
;         if (pp == 4) {
; #pragma unroll
;             for (int ks = 0; ks < 4; ++ks) qb[ks] = *(const bf16x8*)(nbase + (size_t)min(nt0 + (qi << nsh), SEQ - 1) * 1536 + 16 * ks + 8 * h);
;         }
;         const int mbase = n0 + 4 * h - lo; float mx = -INFINITY;
; #pragma unroll
;         for (int rg = 0; rg < 16; ++rg) { sc[rg] = ((unsigned)(mbase + (rg & 3) + 8 * (rg >> 2)) <= mspan) ? sc[rg] : -INFINITY; mx = fmaxf(mx, sc[rg]); }
;         mx = fmaxf(mx, __shfl_xor(mx, 32));
;         if (__any(mx > m)) {
;             const float mn = fmaxf(m, mx), alpha = __builtin_amdgcn_exp2f(m - mn); m = mn; l *= alpha;
; #pragma unroll
;             for (int i = 0; i < 16; ++i) { o[0][i] *= alpha; o[1][i] *= alpha; }
;         }
;         float ps = 0.f;
; #pragma unroll
;         for (int rg = 0; rg < 16; ++rg) { sc[rg] = __builtin_amdgcn_exp2f(sc[rg] - m); ps += sc[rg]; }
;         l += ps;
;         bf16x8 pb[2];
; #pragma unroll
;         for (int s2 = 0; s2 < 2; ++s2) { v4u w; w.x = pg8::cvt_pk_bf16(sc[8 * s2], sc[8 * s2 + 1]); w.y = pg8::cvt_pk_bf16(sc[8 * s2 + 2], sc[8 * s2 + 3]); w.z = pg8::cvt_pk_bf16(sc[8 * s2 + 4], sc[8 * s2 + 5]); w.w = pg8::cvt_pk_bf16(sc[8 * s2 + 6], sc[8 * s2 + 7]); pb[s2] = __builtin_bit_cast(bf16x8, w); }
; #pragma unroll
;         for (int mb = 0; mb < 2; ++mb)
; #pragma unroll
;             for (int s2 = 0; s2 < 2; ++s2) {
;                 LAS unsigned char* vp = vbuf + tr_off + (16 * s2) * 160 + 64 * mb;
	ds_write_b128 v231, v[78:81]
	s_waitcnt vmcnt(14)
	ds_write_b128 v232, v[82:85] offset:4608
	s_waitcnt vmcnt(13)
	ds_write_b128 v231, v[86:89] offset:1152
	s_waitcnt vmcnt(12)
	ds_write_b128 v232, v[90:93] offset:5888
	s_waitcnt vmcnt(11)
	ds_write_b128 v231, v[102:105] offset:2304
	s_waitcnt vmcnt(10)
	ds_write_b128 v232, v[138:141] offset:7168
	s_waitcnt vmcnt(9)
	ds_write_b128 v231, v[142:145] offset:3456
	s_waitcnt vmcnt(8)
	ds_write_b128 v232, v[146:149] offset:8448
	v_med3_i32 v34, v34, 0, v233
	v_add_f32_e32 v51, v76, v38
	v_mul_u32_u24_e32 v38, 0xc00, v34
	ds_read_b128 v[34:37], v177
	v_or_b32_e32 v38, v38, v176
	global_load_dwordx4 v[74:77], v38, s[8:9] offset:1024
	global_load_dwordx4 v[78:81], v38, s[8:9] offset:2048
	v_add_u32_e32 v38, s10, v190
	v_med3_i32 v38, v38, 0, v233
	v_mul_u32_u24_e32 v38, 0xc00, v38
	ds_read_b128 v[54:57], v177 offset:32
	v_mfma_f32_32x32x16_bf16 v[18:33], v[42:45], v[154:157], v[18:33]
	v_or_b32_e32 v86, v38, v176
	global_load_dwordx4 v[82:85], v86, s[8:9] offset:1024
	s_nop 0
	global_load_dwordx4 v[86:89], v86, s[8:9] offset:2048
	v_add_f32_e32 v51, v153, v51
	v_add_f32_e32 v51, v164, v51
	v_add_f32_e32 v51, v165, v51
	v_add_f32_e32 v51, v171, v51
	v_add_f32_e32 v51, v172, v51
	s_waitcnt lgkmcnt(1)
	v_mfma_f32_32x32x16_bf16 v[34:49], v[34:37], v[66:69], 0
	v_add_u32_e32 v66, s10, v191
	v_med3_i32 v66, v66, 0, v233
	v_mul_u32_u24_e32 v66, 0xc00, v66
	v_or_b32_e32 v94, v66, v176
	ds_read_b128 v[138:141], v177 offset:96
	ds_read_b128 v[66:69], v177 offset:64
	global_load_dwordx4 v[90:93], v94, s[8:9] offset:1024
	s_nop 0
	global_load_dwordx4 v[94:97], v94, s[8:9] offset:2048
	v_add_f32_e32 v51, v173, v51
	s_waitcnt lgkmcnt(2)
	v_mfma_f32_32x32x16_bf16 v[34:49], v[54:57], v[62:65], v[34:49]
	v_add_u32_e32 v54, s10, v192
	v_med3_i32 v54, v54, 0, v233
	v_mul_u32_u24_e32 v54, 0xc00, v54
	v_or_b32_e32 v54, v54, v176
	global_load_dwordx4 v[98:101], v54, s[8:9] offset:1024
	global_load_dwordx4 v[102:105], v54, s[8:9] offset:2048
	v_add_f32_e32 v142, v237, v51
	s_waitcnt lgkmcnt(0)
	v_mfma_f32_32x32x16_bf16 v[34:49], v[66:69], v[58:61], v[34:49]
	global_load_dwordx4 v[66:69], v[162:163], off
	global_load_dwordx4 v[62:65], v[162:163], off offset:32
	global_load_dwordx4 v[58:61], v[162:163], off offset:64
	global_load_dwordx4 v[54:57], v[162:163], off offset:96
	v_mfma_f32_32x32x16_bf16 v[34:49], v[138:141], v[70:73], v[34:49]
	v_mfma_f32_32x32x16_bf16 v[2:17], v[158:161], v[154:157], v[2:17]
	s_nop 9
	v_sub_u32_e32 v253, v151, v152
	v_subrev_u32_e32 v253, 0x80, v253
	v_cmp_le_i32_e32 vcc, 0, v253
	v_cmp_le_i32_e64 s[98:99], 1, v253
	v_cmp_le_i32_e64 s[100:101], 2, v253
	v_cndmask_b32_e32 v51, v234, v34, vcc
	v_cmp_le_i32_e32 vcc, 3, v253
	v_cndmask_b32_e64 v35, v234, v35, s[98:99]
	v_max3_f32 v34, v51, s31, v35
	v_cmp_le_i32_e64 s[98:99], 8, v253
	v_cndmask_b32_e64 v36, v234, v36, s[100:101]
	v_cmp_le_i32_e64 s[100:101], 9, v253
	v_cndmask_b32_e32 v37, v234, v37, vcc
	v_max3_f32 v34, v34, v36, v37
	v_cmp_le_i32_e32 vcc, 10, v253
	v_cndmask_b32_e64 v38, v234, v38, s[98:99]
	v_cmp_le_i32_e64 s[98:99], 11, v253
	v_cndmask_b32_e64 v39, v234, v39, s[100:101]
	v_max3_f32 v34, v34, v38, v39
	v_cmp_le_i32_e64 s[100:101], 16, v253
	v_cndmask_b32_e32 v40, v234, v40, vcc
	v_cmp_le_i32_e32 vcc, 17, v253
	v_cndmask_b32_e64 v41, v234, v41, s[98:99]
	v_max3_f32 v34, v34, v40, v41
	v_cmp_le_i32_e64 s[98:99], 18, v253
	v_cndmask_b32_e64 v42, v234, v42, s[100:101]
	v_cmp_le_i32_e64 s[100:101], 19, v253
	v_cndmask_b32_e32 v43, v234, v43, vcc
	v_max3_f32 v34, v34, v42, v43
	v_cmp_le_i32_e32 vcc, 24, v253
	v_cndmask_b32_e64 v44, v234, v44, s[98:99]
	v_cmp_le_i32_e64 s[98:99], 25, v253
	v_cndmask_b32_e64 v45, v234, v45, s[100:101]
	v_max3_f32 v34, v34, v44, v45
	v_cmp_le_i32_e64 s[100:101], 26, v253
	v_cndmask_b32_e32 v46, v234, v46, vcc
	v_cmp_le_i32_e32 vcc, 27, v253
	v_cndmask_b32_e64 v47, v234, v47, s[98:99]
	v_max3_f32 v34, v34, v46, v47
	v_cndmask_b32_e64 v48, v234, v48, s[100:101]
	v_cndmask_b32_e32 v49, v234, v49, vcc
	v_max3_f32 v70, v34, v48, v49
	ds_bpermute_b32 v71, v179, v70
	v_add_f32_e32 v34, v238, v142
	v_add_f32_e32 v34, v50, v34
	s_waitcnt lgkmcnt(0)
	v_max_f32_e32 v50, v71, v71
	v_max_f32_e32 v50, v70, v50
	v_cmp_gt_f32_e32 vcc, v50, v150
	s_cbranch_vccz .LBB0_378
	v_max_f32_e32 v50, v50, v50
	v_max_f32_e32 v70, v150, v150
	v_max_f32_e32 v70, v70, v50
	v_sub_f32_e32 v50, v150, v70
	v_exp_f32_e32 v50, v50
	v_mov_b32_e32 v150, v70
	v_pk_mul_f32 v[32:33], v[32:33], v[50:51] op_sel_hi:[1,0]
	v_pk_mul_f32 v[30:31], v[30:31], v[50:51] op_sel_hi:[1,0]
	v_pk_mul_f32 v[28:29], v[28:29], v[50:51] op_sel_hi:[1,0]
	v_pk_mul_f32 v[26:27], v[26:27], v[50:51] op_sel_hi:[1,0]
	v_pk_mul_f32 v[24:25], v[24:25], v[50:51] op_sel_hi:[1,0]
	v_pk_mul_f32 v[22:23], v[22:23], v[50:51] op_sel_hi:[1,0]
	v_pk_mul_f32 v[20:21], v[20:21], v[50:51] op_sel_hi:[1,0]
	v_pk_mul_f32 v[18:19], v[18:19], v[50:51] op_sel_hi:[1,0]
	v_pk_mul_f32 v[16:17], v[16:17], v[50:51] op_sel_hi:[1,0]
	v_pk_mul_f32 v[14:15], v[14:15], v[50:51] op_sel_hi:[1,0]
	v_pk_mul_f32 v[12:13], v[12:13], v[50:51] op_sel_hi:[1,0]
	v_pk_mul_f32 v[10:11], v[10:11], v[50:51] op_sel_hi:[1,0]
	v_pk_mul_f32 v[8:9], v[8:9], v[50:51] op_sel_hi:[1,0]
	v_pk_mul_f32 v[6:7], v[6:7], v[50:51] op_sel_hi:[1,0]
	v_pk_mul_f32 v[4:5], v[4:5], v[50:51] op_sel_hi:[1,0]
	v_pk_mul_f32 v[2:3], v[2:3], v[50:51] op_sel_hi:[1,0]
	v_mul_f32_e32 v34, v34, v50

; __device__ __forceinline__ float bf_lo(unsigned w) { return __uint_as_float(w << 16); }
; template <int STAGE, int OFF> __device__ __forceinline__ void attn32_unit(const bf16* base, bf16* yrow0, int blk0, int u, LAS unsigned char* xtab, LAS unsigned char* kbuf, LAS unsigned char* vbuf, int lane, ...
;     ...
;     } else {
; #pragma unroll
;         for (int mb = 0; mb < 2; ++mb)
; #pragma unroll
;             for (int gq = 0; gq < 4; ++gq) { const v2u w = *(const LAS v2u*)(xrow + 2 * (32 * mb + 8 * gq + 4 * h)); o[mb][4 * gq] = bf_lo(w.x); o[mb][4 * gq + 1] = bf_hi(w.x); o[mb][4 * gq + 2] = bf_lo(w.y); o[mb][4 * gq + 3] = bf_hi(w.y); }
;         m = *(const LAS float*)(xrow + 128); l = h == 0 ? *(const LAS float*)(xrow + 132) : 0.f;
;     }
;     const int hi = qi, lo = max(qi - 128, -(t0 >> SH));
;     const unsigned mspan = (unsigned)(hi - lo);
; #pragma unroll
;     for (int pp = 0; pp < 5; ++pp) {
;         constexpr int dummy = 0; (void)dummy;
;         const int set = (pp + OFF) % 2, n0 = -128 + 32 * pp;
; #pragma unroll
;         for (int c = 0; c < 4; ++c) { *(LAS v4u*)(kbuf + (8 * c + lrow) * 144 + lch * 16) = kr[set][c]; *(LAS v4u*)(vbuf + (8 * c + lrow) * 160 + lch * 16) = vr[set][c]; }
;         if (pp + 2 < 5) { ATT32_LOAD(set, pp + 2, t0, SH); }
;         else { const bf16* base_ = base; { const bf16* base = nbase; ATT32_LOAD(set, pp + 2 - 5, nt0, nsh); } (void)base_; }
;         f32x16 sc;
; #pragma unroll
;         for (int i = 0; i < 16; ++i) sc[i] = 0.f;
; #pragma unroll
;         for (int ks = 0; ks < 4; ++ks) { const bf16x8 ka = *(const LAS bf16x8*)(kbuf + qi * 144 + 32 * ks + 16 * h); sc = MFMA32(ka, qb[ks], sc); }
;         if (pp == 4) {
; #pragma unroll
;             for (int ks = 0; ks < 4; ++ks) qb[ks] = *(const bf16x8*)(nbase + (size_t)min(nt0 + (qi << nsh), SEQ - 1) * 1536 + 16 * ks + 8 * h);
;         }
;         const int mbase = n0 + 4 * h - lo; float mx = -INFINITY;
; #pragma unroll
;         for (int rg = 0; rg < 16; ++rg) { sc[rg] = ((unsigned)(mbase + (rg & 3) + 8 * (rg >> 2)) <= mspan) ? sc[rg] : -INFINITY; mx = fmaxf(mx, sc[rg]); }
;         mx = fmaxf(mx, __shfl_xor(mx, 32));
;         if (__any(mx > m)) {
;             const float mn = fmaxf(m, mx), alpha = __builtin_amdgcn_exp2f(m - mn); m = mn; l *= alpha;
; #pragma unroll
;             for (int i = 0; i < 16; ++i) { o[0][i] *= alpha; o[1][i] *= alpha; }
;         }
.LBB0_380:
	s_or_b64 exec, exec, s[14:15]
	v_add_u32_e32 v51, v194, v166
	s_waitcnt lgkmcnt(0)
	s_barrier
	ds_read2_b64 v[10:13], v51 offset1:2
	ds_read2_b64 v[2:5], v51 offset0:4 offset1:6
	ds_read2_b64 v[6:9], v51 offset0:8 offset1:10
	ds_read2_b64 v[14:17], v51 offset0:12 offset1:14
	ds_read_b32 v50, v194 offset:128
	v_mov_b32_e32 v138, 0
	s_and_saveexec_b64 s[14:15], s[4:5]
	ds_read_b32 v138, v194 offset:132
	s_or_b64 exec, exec, s[14:15]
	s_waitcnt vmcnt(19)
	ds_write_b128 v231, v[106:109]
	s_waitcnt vmcnt(18)
	ds_write_b128 v232, v[110:113] offset:4608
	s_waitcnt vmcnt(17)
	ds_write_b128 v231, v[114:117] offset:1152
	s_waitcnt vmcnt(16)
	ds_write_b128 v232, v[118:121] offset:5888
	s_waitcnt vmcnt(15)
	ds_write_b128 v231, v[122:125] offset:2304
	s_waitcnt vmcnt(14)
	ds_write_b128 v232, v[126:129] offset:7168
	s_waitcnt vmcnt(13)
	ds_write_b128 v231, v[130:133] offset:3456
	s_waitcnt vmcnt(12)
	ds_write_b128 v232, v[134:137] offset:8448
	ds_read_b128 v[34:37], v177
	s_waitcnt lgkmcnt(13)
	v_lshlrev_b32_e32 v22, 16, v12
	v_and_b32_e32 v23, 0xffff0000, v12
	v_add_u32_e32 v12, s10, v195
	v_med3_i32 v12, v12, 0, v233
	v_mul_u32_u24_e32 v12, 0xc00, v12
	v_or_b32_e32 v12, v12, v176
	global_load_dwordx4 v[70:73], v12, s[8:9] offset:1024
	global_load_dwordx4 v[106:109], v12, s[8:9] offset:2048
	ds_read_b128 v[118:121], v177 offset:32
	v_add_u32_e32 v12, s10, v196
	s_waitcnt vmcnt(5) lgkmcnt(1)
	v_mfma_f32_32x32x16_bf16 v[34:49], v[34:37], v[66:69], 0
	v_med3_i32 v12, v12, 0, v233
	v_mul_u32_u24_e32 v12, 0xc00, v12
	v_or_b32_e32 v12, v12, v176
	global_load_dwordx4 v[110:113], v12, s[8:9] offset:1024
	global_load_dwordx4 v[114:117], v12, s[8:9] offset:2048
	v_add_u32_e32 v12, s10, v197
	v_med3_i32 v12, v12, 0, v233
	v_mul_u32_u24_e32 v12, 0xc00, v12
	v_or_b32_e32 v12, v12, v176
	ds_read_b128 v[134:137], v177 offset:96
	ds_read_b128 v[140:143], v177 offset:64
	s_waitcnt vmcnt(6) lgkmcnt(2)
	v_mfma_f32_32x32x16_bf16 v[34:49], v[118:121], v[62:65], v[34:49]
	global_load_dwordx4 v[118:121], v12, s[8:9] offset:1024
	global_load_dwordx4 v[122:125], v12, s[8:9] offset:2048
	v_add_u32_e32 v12, s10, v198
	v_med3_i32 v12, v12, 0, v233
	v_mul_u32_u24_e32 v12, 0xc00, v12
	v_or_b32_e32 v12, v12, v176
	global_load_dwordx4 v[126:129], v12, s[8:9] offset:1024
	global_load_dwordx4 v[130:133], v12, s[8:9] offset:2048
	s_ashr_i32 s0, s10, 2
	s_waitcnt vmcnt(9) lgkmcnt(0)
	v_mfma_f32_32x32x16_bf16 v[34:49], v[140:143], v[58:61], v[34:49]
	s_sub_i32 s0, 0, s0
	v_lshlrev_b32_e32 v18, 16, v10
	v_and_b32_e32 v19, 0xffff0000, v10
	v_lshlrev_b32_e32 v20, 16, v11
	v_and_b32_e32 v21, 0xffff0000, v11
	v_lshlrev_b32_e32 v10, 16, v14
	v_and_b32_e32 v11, 0xffff0000, v14
	s_waitcnt vmcnt(8)
	v_mfma_f32_32x32x16_bf16 v[34:49], v[134:137], v[54:57], v[34:49]
	v_max_i32_e32 v14, s0, v175
	v_sub_u32_e32 v162, v1, v14
	v_sub_u32_e32 v163, v178, v14
	v_lshlrev_b32_e32 v24, 16, v13
	v_and_b32_e32 v25, 0xffff0000, v13
	v_lshlrev_b32_e32 v12, 16, v15
	v_and_b32_e32 v13, 0xffff0000, v15
	s_nop 2
	v_add_u32_e32 v253, 27, v163
	v_cmp_le_i32_e32 vcc, 27, v253
	v_cmp_le_i32_e64 s[98:99], 26, v253
	v_cmp_le_i32_e64 s[100:101], 25, v253
	v_cndmask_b32_e32 v34, v234, v34, vcc
	v_lshlrev_b32_e32 v26, 16, v2
	v_cmp_le_i32_e32 vcc, 24, v253
	v_cndmask_b32_e64 v35, v234, v35, s[98:99]
	v_max3_f32 v14, v34, s31, v35
	v_cmp_le_i32_e64 s[98:99], 19, v253
	v_cndmask_b32_e64 v36, v234, v36, s[100:101]
	v_and_b32_e32 v27, 0xffff0000, v2
	v_cmp_le_i32_e64 s[100:101], 18, v253
	v_cndmask_b32_e32 v37, v234, v37, vcc
	v_max3_f32 v14, v14, v36, v37
	v_cmp_le_i32_e32 vcc, 17, v253
	v_cndmask_b32_e64 v38, v234, v38, s[98:99]
	v_lshlrev_b32_e32 v28, 16, v3
	v_cmp_le_i32_e64 s[98:99], 16, v253
	v_cndmask_b32_e64 v39, v234, v39, s[100:101]
	v_max3_f32 v14, v14, v38, v39
	v_cmp_le_i32_e64 s[100:101], 11, v253
	v_cndmask_b32_e32 v40, v234, v40, vcc
	v_and_b32_e32 v29, 0xffff0000, v3
	v_cmp_le_i32_e32 vcc, 10, v253
	v_cndmask_b32_e64 v41, v234, v41, s[98:99]
	v_max3_f32 v14, v14, v40, v41
	v_cmp_le_i32_e64 s[98:99], 9, v253
	v_cndmask_b32_e64 v42, v234, v42, s[100:101]
	v_lshlrev_b32_e32 v30, 16, v4
	v_cmp_le_i32_e64 s[100:101], 8, v253
	v_cndmask_b32_e32 v43, v234, v43, vcc
	v_max3_f32 v14, v14, v42, v43
	v_cmp_le_i32_e32 vcc, 3, v253
	v_cndmask_b32_e64 v44, v234, v44, s[98:99]
	v_and_b32_e32 v31, 0xffff0000, v4
	v_cmp_le_i32_e64 s[98:99], 2, v253
	v_cndmask_b32_e64 v45, v234, v45, s[100:101]
	v_max3_f32 v14, v14, v44, v45
	v_cmp_le_i32_e64 s[100:101], 1, v253
	v_cndmask_b32_e32 v46, v234, v46, vcc
	v_lshlrev_b32_e32 v32, 16, v5
	v_cmp_le_i32_e32 vcc, 0, v253
	v_cndmask_b32_e64 v47, v234, v47, s[98:99]
	v_max3_f32 v14, v14, v46, v47
	v_cndmask_b32_e64 v48, v234, v48, s[100:101]
	v_and_b32_e32 v33, 0xffff0000, v5
	v_lshlrev_b32_e32 v2, 16, v6
	v_cndmask_b32_e32 v49, v234, v49, vcc
	v_max3_f32 v134, v14, v48, v49
	ds_bpermute_b32 v135, v179, v134
	v_and_b32_e32 v3, 0xffff0000, v6
	v_lshlrev_b32_e32 v4, 16, v7
	v_and_b32_e32 v5, 0xffff0000, v7
	v_lshlrev_b32_e32 v6, 16, v8
	s_waitcnt lgkmcnt(0)
	v_max_f32_e32 v135, v135, v135
	v_max_f32_e32 v134, v134, v135
	v_and_b32_e32 v7, 0xffff0000, v8
	v_lshlrev_b32_e32 v8, 16, v9
	v_and_b32_e32 v9, 0xffff0000, v9
	v_lshlrev_b32_e32 v14, 16, v16
	v_and_b32_e32 v15, 0xffff0000, v16
	v_lshlrev_b32_e32 v16, 16, v17
	v_and_b32_e32 v17, 0xffff0000, v17
	v_cmp_gt_f32_e32 vcc, v134, v50
	s_cbranch_vccz .LBB0_384
	v_max_f32_e32 v134, v134, v134
	v_max_f32_e32 v135, v50, v50
	v_max_f32_e32 v134, v135, v134
	v_sub_f32_e32 v50, v50, v134
	v_exp_f32_e32 v50, v50
	s_nop 0
	v_pk_mul_f32 v[16:17], v[50:51], v[16:17] op_sel_hi:[0,1]
	v_pk_mul_f32 v[14:15], v[50:51], v[14:15] op_sel_hi:[0,1]
	v_pk_mul_f32 v[12:13], v[50:51], v[12:13] op_sel_hi:[0,1]
	v_pk_mul_f32 v[10:11], v[50:51], v[10:11] op_sel_hi:[0,1]
	v_pk_mul_f32 v[8:9], v[50:51], v[8:9] op_sel_hi:[0,1]
	v_pk_mul_f32 v[6:7], v[50:51], v[6:7] op_sel_hi:[0,1]
	v_pk_mul_f32 v[4:5], v[50:51], v[4:5] op_sel_hi:[0,1]
	v_pk_mul_f32 v[2:3], v[50:51], v[2:3] op_sel_hi:[0,1]
	v_pk_mul_f32 v[32:33], v[50:51], v[32:33] op_sel_hi:[0,1]
	v_pk_mul_f32 v[30:31], v[50:51], v[30:31] op_sel_hi:[0,1]
	v_pk_mul_f32 v[28:29], v[50:51], v[28:29] op_sel_hi:[0,1]
	v_pk_mul_f32 v[26:27], v[50:51], v[26:27] op_sel_hi:[0,1]
	v_pk_mul_f32 v[24:25], v[50:51], v[24:25] op_sel_hi:[0,1]
	v_pk_mul_f32 v[22:23], v[50:51], v[22:23] op_sel_hi:[0,1]
	v_pk_mul_f32 v[20:21], v[50:51], v[20:21] op_sel_hi:[0,1]
	v_pk_mul_f32 v[18:19], v[50:51], v[18:19] op_sel_hi:[0,1]
	v_mul_f32_e32 v138, v138, v50
	v_mov_b32_e32 v50, v134
; #define LAS __attribute__((address_space(3)))
; template <int STAGE, int OFF> __device__ __forceinline__ void attn32_unit(const bf16* base, bf16* yrow0, int blk0, int u, LAS unsigned char* xtab, LAS unsigned char* kbuf, LAS unsigned char* vbuf, int lane, ...
;     ...
;         for (int c = 0; c < 4; ++c) { *(LAS v4u*)(kbuf + (8 * c + lrow) * 144 + lch * 16) = kr[set][c]; *(LAS v4u*)(vbuf + (8 * c + lrow) * 160 + lch * 16) = vr[set][c]; }
;         if (pp + 2 < 5) { ATT32_LOAD(set, pp + 2, t0, SH); }
;         else { const bf16* base_ = base; { const bf16* base = nbase; ATT32_LOAD(set, pp + 2 - 5, nt0, nsh); } (void)base_; }
;         f32x16 sc;
; #pragma unroll
;         for (int i = 0; i < 16; ++i) sc[i] = 0.f;
; #pragma unroll
;         for (int ks = 0; ks < 4; ++ks) { const bf16x8 ka = *(const LAS bf16x8*)(kbuf + qi * 144 + 32 * ks + 16 * h); sc = MFMA32(ka, qb[ks], sc); }
;         if (pp == 4) {
; #pragma unroll
;             for (int ks = 0; ks < 4; ++ks) qb[ks] = *(const bf16x8*)(nbase + (size_t)min(nt0 + (qi << nsh), SEQ - 1) * 1536 + 16 * ks + 8 * h);
;         }
;         const int mbase = n0 + 4 * h - lo; float mx = -INFINITY;
; #pragma unroll
;         for (int rg = 0; rg < 16; ++rg) { sc[rg] = ((unsigned)(mbase + (rg & 3) + 8 * (rg >> 2)) <= mspan) ? sc[rg] : -INFINITY; mx = fmaxf(mx, sc[rg]); }
;         mx = fmaxf(mx, __shfl_xor(mx, 32));
;         if (__any(mx > m)) {
;             const float mn = fmaxf(m, mx), alpha = __builtin_amdgcn_exp2f(m - mn); m = mn; l *= alpha;
; #pragma unroll
;             for (int i = 0; i < 16; ++i) { o[0][i] *= alpha; o[1][i] *= alpha; }
;         }
;         float ps = 0.f;
; #pragma unroll
;         for (int rg = 0; rg < 16; ++rg) { sc[rg] = __builtin_amdgcn_exp2f(sc[rg] - m); ps += sc[rg]; }
;         l += ps;
;         bf16x8 pb[2];
; #pragma unroll
;         for (int s2 = 0; s2 < 2; ++s2) { v4u w; w.x = pg8::cvt_pk_bf16(sc[8 * s2], sc[8 * s2 + 1]); w.y = pg8::cvt_pk_bf16(sc[8 * s2 + 2], sc[8 * s2 + 3]); w.z = pg8::cvt_pk_bf16(sc[8 * s2 + 4], sc[8 * s2 + 5]); w.w = pg8::cvt_pk_bf16(sc[8 * s2 + 6], sc[8 * s2 + 7]); pb[s2] = __builtin_bit_cast(bf16x8, w); }
; #pragma unroll
;         for (int mb = 0; mb < 2; ++mb)
; #pragma unroll
;             for (int s2 = 0; s2 < 2; ++s2) {
;                 LAS unsigned char* vp = vbuf + tr_off + (16 * s2) * 160 + 64 * mb;
.LBB0_384:
	v_sub_f32_e32 v34, v34, v50
	v_exp_f32_e32 v134, v34
	v_sub_f32_e32 v34, v35, v50
	v_exp_f32_e32 v135, v34
	v_sub_f32_e32 v34, v36, v50
	v_exp_f32_e32 v136, v34
	v_sub_f32_e32 v34, v37, v50
	v_exp_f32_e32 v137, v34
	v_sub_f32_e32 v34, v38, v50
	v_exp_f32_e32 v139, v34
	v_sub_f32_e32 v34, v39, v50
	v_exp_f32_e32 v140, v34
	v_sub_f32_e32 v34, v40, v50
	v_exp_f32_e32 v141, v34
	v_sub_f32_e32 v34, v41, v50
	v_exp_f32_e32 v142, v34
	v_sub_f32_e32 v34, v42, v50
	v_exp_f32_e32 v164, v34
	v_sub_f32_e32 v34, v43, v50
	v_exp_f32_e32 v165, v34
	v_sub_f32_e32 v34, v44, v50
	v_exp_f32_e32 v171, v34
	v_sub_f32_e32 v34, v45, v50
	v_exp_f32_e32 v172, v34
	v_sub_f32_e32 v34, v46, v50
	v_exp_f32_e32 v173, v34
	v_sub_f32_e32 v34, v47, v50
	v_exp_f32_e32 v237, v34
	v_sub_f32_e32 v34, v48, v50
	v_exp_f32_e32 v246, v34
	v_sub_f32_e32 v34, v49, v50
	v_exp_f32_e32 v247, v34
	v_cvt_pk_bf16_f32 v34, v134, v135
	v_cvt_pk_bf16_f32 v35, v136, v137
	v_cvt_pk_bf16_f32 v36, v139, v140
	v_cvt_pk_bf16_f32 v37, v141, v142
	v_cvt_pk_bf16_f32 v238, v164, v165
	v_cvt_pk_bf16_f32 v239, v171, v172
	v_cvt_pk_bf16_f32 v240, v173, v237
	v_cvt_pk_bf16_f32 v241, v246, v247
	ds_read_b64_tr_b16 v[38:39], v181 offset:4608
	ds_read_b64_tr_b16 v[40:41], v181 offset:5888
	ds_read_b64_tr_b16 v[44:45], v181 offset:5952
	ds_read_b64_tr_b16 v[42:43], v181 offset:4672
	s_waitcnt lgkmcnt(2)
	v_mfma_f32_32x32x16_bf16 v[18:33], v[38:41], v[34:37], v[18:33]
	ds_read_b64_tr_b16 v[38:39], v181 offset:7168
	ds_read_b64_tr_b16 v[40:41], v181 offset:8448
	v_add_f32_e32 v46, 0, v134
	ds_read_b64_tr_b16 v[244:245], v181 offset:8512
	ds_read_b64_tr_b16 v[242:243], v181 offset:7232
	ds_write_b128 v231, v[74:77]
	ds_write_b128 v232, v[78:81] offset:4608
	ds_write_b128 v231, v[82:85] offset:1152
	ds_write_b128 v232, v[86:89] offset:5888
	ds_write_b128 v231, v[90:93] offset:2304
	ds_write_b128 v232, v[94:97] offset:7168
	ds_write_b128 v231, v[98:101] offset:3456
	ds_write_b128 v232, v[102:105] offset:8448
	s_waitcnt lgkmcnt(10)
	v_mfma_f32_32x32x16_bf16 v[18:33], v[38:41], v[238:241], v[18:33]
	v_add_f32_e32 v38, v135, v46
	v_add_f32_e32 v38, v136, v38
	v_add_f32_e32 v38, v137, v38
	v_add_f32_e32 v38, v139, v38
	v_add_f32_e32 v38, v140, v38
	v_add_f32_e32 v38, v141, v38
	v_add_f32_e32 v139, v142, v38
	v_mfma_f32_32x32x16_bf16 v[2:17], v[42:45], v[34:37], v[2:17]
	v_add_u32_e32 v34, s10, v199
	v_med3_i32 v34, v34, 0, v233
	v_mul_u32_u24_e32 v38, 0xc00, v34
	ds_read_b128 v[34:37], v177
	v_or_b32_e32 v38, v38, v176
	global_load_dwordx4 v[86:89], v38, s[8:9] offset:1024
	global_load_dwordx4 v[90:93], v38, s[8:9] offset:2048
	v_add_u32_e32 v38, s10, v200
	v_med3_i32 v38, v38, 0, v233
	v_mul_u32_u24_e32 v38, 0xc00, v38
	ds_read_b128 v[74:77], v177 offset:32
	v_or_b32_e32 v78, v38, v176
	s_waitcnt lgkmcnt(1)
	v_mfma_f32_32x32x16_bf16 v[34:49], v[34:37], v[66:69], 0
	global_load_dwordx4 v[134:137], v78, s[8:9] offset:1024
	global_load_dwordx4 v[142:145], v78, s[8:9] offset:2048
	v_add_u32_e32 v78, s10, v201
	v_med3_i32 v78, v78, 0, v233
	v_mul_u32_u24_e32 v78, 0xc00, v78
	v_or_b32_e32 v94, v78, v176
	ds_read_b128 v[78:81], v177 offset:96
	ds_read_b128 v[82:85], v177 offset:64
	global_load_dwordx4 v[146:149], v94, s[8:9] offset:1024
	global_load_dwordx4 v[150:153], v94, s[8:9] offset:2048
	s_waitcnt lgkmcnt(2)
	v_mfma_f32_32x32x16_bf16 v[34:49], v[74:77], v[62:65], v[34:49]
	v_add_u32_e32 v74, s10, v202
	v_med3_i32 v74, v74, 0, v233
	v_mul_u32_u24_e32 v74, 0xc00, v74
	v_or_b32_e32 v74, v74, v176
	global_load_dwordx4 v[154:157], v74, s[8:9] offset:1024
	global_load_dwordx4 v[158:161], v74, s[8:9] offset:2048
	s_waitcnt lgkmcnt(0)
	v_mfma_f32_32x32x16_bf16 v[34:49], v[82:85], v[58:61], v[34:49]
	v_add_f32_e32 v74, v164, v139
	v_add_f32_e32 v74, v165, v74
	v_add_f32_e32 v74, v171, v74
	v_add_f32_e32 v74, v172, v74
	v_add_f32_e32 v74, v173, v74
	v_mfma_f32_32x32x16_bf16 v[34:49], v[78:81], v[54:57], v[34:49]
	v_add_f32_e32 v74, v237, v74
	v_add_f32_e32 v74, v246, v74
	v_add_f32_e32 v74, v247, v74
	v_add_f32_e32 v164, v138, v74
	v_mfma_f32_32x32x16_bf16 v[2:17], v[242:245], v[238:241], v[2:17]
	s_nop 6
	v_add_u32_e32 v253, 59, v163
	v_cmp_le_i32_e32 vcc, 27, v253
	v_cmp_le_i32_e64 s[98:99], 26, v253
	v_cmp_le_i32_e64 s[100:101], 25, v253
	v_cndmask_b32_e32 v34, v234, v34, vcc
	v_cmp_le_i32_e32 vcc, 24, v253
	v_cndmask_b32_e64 v35, v234, v35, s[98:99]
	v_max3_f32 v75, v34, s31, v35
	v_cmp_le_i32_e64 s[98:99], 19, v253
	v_cndmask_b32_e64 v36, v234, v36, s[100:101]
	v_cmp_le_i32_e64 s[100:101], 18, v253
	v_cndmask_b32_e32 v37, v234, v37, vcc
	v_max3_f32 v75, v75, v36, v37
	v_cmp_le_i32_e32 vcc, 17, v253
	v_cndmask_b32_e64 v38, v234, v38, s[98:99]
	v_cmp_le_i32_e64 s[98:99], 16, v253
	v_cndmask_b32_e64 v39, v234, v39, s[100:101]
	v_max3_f32 v75, v75, v38, v39
	v_cmp_le_i32_e64 s[100:101], 11, v253
	v_cndmask_b32_e32 v40, v234, v40, vcc
	v_cmp_le_i32_e32 vcc, 10, v253
	v_cndmask_b32_e64 v41, v234, v41, s[98:99]
	v_max3_f32 v75, v75, v40, v41
	v_cmp_le_i32_e64 s[98:99], 9, v253
	v_cndmask_b32_e64 v42, v234, v42, s[100:101]
	v_cmp_le_i32_e64 s[100:101], 8, v253
	v_cndmask_b32_e32 v43, v234, v43, vcc
	v_max3_f32 v75, v75, v42, v43
	v_cmp_le_i32_e32 vcc, 3, v253
	v_cndmask_b32_e64 v44, v234, v44, s[98:99]
	v_cmp_le_i32_e64 s[98:99], 2, v253
	v_cndmask_b32_e64 v45, v234, v45, s[100:101]
	v_max3_f32 v75, v75, v44, v45
	v_cmp_le_i32_e64 s[100:101], 1, v253
	v_cndmask_b32_e32 v46, v234, v46, vcc
	v_cmp_le_i32_e32 vcc, 0, v253
	v_cndmask_b32_e64 v47, v234, v47, s[98:99]
	v_max3_f32 v75, v75, v46, v47
	v_cndmask_b32_e64 v48, v234, v48, s[100:101]
	v_cndmask_b32_e32 v49, v234, v49, vcc
	v_max3_f32 v75, v75, v48, v49
	ds_bpermute_b32 v76, v179, v75
	s_waitcnt lgkmcnt(0)
	v_max_f32_e32 v74, v76, v76
	v_max_f32_e32 v74, v75, v74
	v_cmp_gt_f32_e32 vcc, v74, v50
	s_cbranch_vccz .LBB0_386
	v_max_f32_e32 v74, v74, v74
	v_max_f32_e32 v75, v50, v50
	v_max_f32_e32 v74, v75, v74
	v_sub_f32_e32 v50, v50, v74
	v_exp_f32_e32 v50, v50
	s_nop 0
	v_pk_mul_f32 v[32:33], v[32:33], v[50:51] op_sel_hi:[1,0]
	v_pk_mul_f32 v[30:31], v[30:31], v[50:51] op_sel_hi:[1,0]
	v_pk_mul_f32 v[28:29], v[28:29], v[50:51] op_sel_hi:[1,0]
	v_pk_mul_f32 v[26:27], v[26:27], v[50:51] op_sel_hi:[1,0]
	v_pk_mul_f32 v[24:25], v[24:25], v[50:51] op_sel_hi:[1,0]
	v_pk_mul_f32 v[22:23], v[22:23], v[50:51] op_sel_hi:[1,0]
	v_pk_mul_f32 v[20:21], v[20:21], v[50:51] op_sel_hi:[1,0]
	v_pk_mul_f32 v[18:19], v[18:19], v[50:51] op_sel_hi:[1,0]
	v_pk_mul_f32 v[16:17], v[16:17], v[50:51] op_sel_hi:[1,0]
	v_pk_mul_f32 v[14:15], v[14:15], v[50:51] op_sel_hi:[1,0]
	v_pk_mul_f32 v[12:13], v[12:13], v[50:51] op_sel_hi:[1,0]
	v_pk_mul_f32 v[10:11], v[10:11], v[50:51] op_sel_hi:[1,0]
	v_pk_mul_f32 v[8:9], v[8:9], v[50:51] op_sel_hi:[1,0]
	v_pk_mul_f32 v[6:7], v[6:7], v[50:51] op_sel_hi:[1,0]
	v_pk_mul_f32 v[4:5], v[4:5], v[50:51] op_sel_hi:[1,0]
	v_pk_mul_f32 v[2:3], v[2:3], v[50:51] op_sel_hi:[1,0]
	v_mul_f32_e32 v164, v164, v50
	v_mov_b32_e32 v50, v74
; #define LAS __attribute__((address_space(3)))
; template <int STAGE, int OFF> __device__ __forceinline__ void attn32_unit(const bf16* base, bf16* yrow0, int blk0, int u, LAS unsigned char* xtab, LAS unsigned char* kbuf, LAS unsigned char* vbuf, int lane, ...
;     ...
;         for (int c = 0; c < 4; ++c) { *(LAS v4u*)(kbuf + (8 * c + lrow) * 144 + lch * 16) = kr[set][c]; *(LAS v4u*)(vbuf + (8 * c + lrow) * 160 + lch * 16) = vr[set][c]; }
;         if (pp + 2 < 5) { ATT32_LOAD(set, pp + 2, t0, SH); }
;         else { const bf16* base_ = base; { const bf16* base = nbase; ATT32_LOAD(set, pp + 2 - 5, nt0, nsh); } (void)base_; }
;         f32x16 sc;
; #pragma unroll
;         for (int i = 0; i < 16; ++i) sc[i] = 0.f;
; #pragma unroll
;         for (int ks = 0; ks < 4; ++ks) { const bf16x8 ka = *(const LAS bf16x8*)(kbuf + qi * 144 + 32 * ks + 16 * h); sc = MFMA32(ka, qb[ks], sc); }
;         if (pp == 4) {
; #pragma unroll
;             for (int ks = 0; ks < 4; ++ks) qb[ks] = *(const bf16x8*)(nbase + (size_t)min(nt0 + (qi << nsh), SEQ - 1) * 1536 + 16 * ks + 8 * h);
;         }
;         const int mbase = n0 + 4 * h - lo; float mx = -INFINITY;
; #pragma unroll
;         for (int rg = 0; rg < 16; ++rg) { sc[rg] = ((unsigned)(mbase + (rg & 3) + 8 * (rg >> 2)) <= mspan) ? sc[rg] : -INFINITY; mx = fmaxf(mx, sc[rg]); }
;         mx = fmaxf(mx, __shfl_xor(mx, 32));
;         if (__any(mx > m)) {
;             const float mn = fmaxf(m, mx), alpha = __builtin_amdgcn_exp2f(m - mn); m = mn; l *= alpha;
; #pragma unroll
;             for (int i = 0; i < 16; ++i) { o[0][i] *= alpha; o[1][i] *= alpha; }
;         }
;         float ps = 0.f;
; #pragma unroll
;         for (int rg = 0; rg < 16; ++rg) { sc[rg] = __builtin_amdgcn_exp2f(sc[rg] - m); ps += sc[rg]; }
;         l += ps;
;         bf16x8 pb[2];
; #pragma unroll
;         for (int s2 = 0; s2 < 2; ++s2) { v4u w; w.x = pg8::cvt_pk_bf16(sc[8 * s2], sc[8 * s2 + 1]); w.y = pg8::cvt_pk_bf16(sc[8 * s2 + 2], sc[8 * s2 + 3]); w.z = pg8::cvt_pk_bf16(sc[8 * s2 + 4], sc[8 * s2 + 5]); w.w = pg8::cvt_pk_bf16(sc[8 * s2 + 6], sc[8 * s2 + 7]); pb[s2] = __builtin_bit_cast(bf16x8, w); }
; #pragma unroll
;         for (int mb = 0; mb < 2; ++mb)
; #pragma unroll
;             for (int s2 = 0; s2 < 2; ++s2) {
;                 LAS unsigned char* vp = vbuf + tr_off + (16 * s2) * 160 + 64 * mb;
.LBB0_386:
	v_sub_f32_e32 v34, v34, v50
	v_exp_f32_e32 v74, v34
	v_sub_f32_e32 v34, v35, v50
	v_exp_f32_e32 v75, v34
	v_sub_f32_e32 v34, v36, v50
	v_exp_f32_e32 v76, v34
	v_sub_f32_e32 v34, v37, v50
	v_exp_f32_e32 v77, v34
	v_sub_f32_e32 v34, v38, v50
	v_exp_f32_e32 v78, v34
	v_sub_f32_e32 v34, v39, v50
	v_exp_f32_e32 v79, v34
	v_sub_f32_e32 v34, v40, v50
	v_exp_f32_e32 v80, v34
	v_sub_f32_e32 v34, v41, v50
	v_exp_f32_e32 v81, v34
	v_sub_f32_e32 v34, v42, v50
	v_exp_f32_e32 v165, v34
	v_sub_f32_e32 v34, v43, v50
	v_exp_f32_e32 v171, v34
	v_sub_f32_e32 v34, v44, v50
	v_exp_f32_e32 v172, v34
	v_sub_f32_e32 v34, v45, v50
	v_exp_f32_e32 v173, v34
	v_sub_f32_e32 v34, v46, v50
	v_exp_f32_e32 v237, v34
	v_sub_f32_e32 v34, v47, v50
	v_exp_f32_e32 v246, v34
	v_sub_f32_e32 v34, v48, v50
	v_exp_f32_e32 v247, v34
	v_sub_f32_e32 v34, v49, v50
	v_exp_f32_e32 v248, v34
	v_cvt_pk_bf16_f32 v34, v74, v75
	v_cvt_pk_bf16_f32 v35, v76, v77
	v_cvt_pk_bf16_f32 v36, v78, v79
	v_cvt_pk_bf16_f32 v37, v80, v81
	v_cvt_pk_bf16_f32 v238, v165, v171
	v_cvt_pk_bf16_f32 v239, v172, v173
	v_cvt_pk_bf16_f32 v240, v237, v246
	v_cvt_pk_bf16_f32 v241, v247, v248
	ds_read_b64_tr_b16 v[38:39], v181 offset:4608
	ds_read_b64_tr_b16 v[40:41], v181 offset:5888
	ds_read_b64_tr_b16 v[44:45], v181 offset:5952
	ds_read_b64_tr_b16 v[42:43], v181 offset:4672
	s_waitcnt lgkmcnt(2)
	v_mfma_f32_32x32x16_bf16 v[18:33], v[38:41], v[34:37], v[18:33]
	ds_read_b64_tr_b16 v[38:39], v181 offset:7168
	ds_read_b64_tr_b16 v[40:41], v181 offset:8448
	v_add_f32_e32 v46, 0, v74
	ds_read_b64_tr_b16 v[244:245], v181 offset:8512
	ds_read_b64_tr_b16 v[242:243], v181 offset:7232
	s_waitcnt vmcnt(15)
	ds_write_b128 v231, v[70:73]
	s_waitcnt vmcnt(14)
	ds_write_b128 v232, v[106:109] offset:4608
	s_waitcnt vmcnt(13)
	ds_write_b128 v231, v[110:113] offset:1152
	s_waitcnt vmcnt(12)
	ds_write_b128 v232, v[114:117] offset:5888
	s_waitcnt vmcnt(11)
	ds_write_b128 v231, v[118:121] offset:2304
	s_waitcnt vmcnt(10)
	ds_write_b128 v232, v[122:125] offset:7168
	s_waitcnt vmcnt(9)
	ds_write_b128 v231, v[126:129] offset:3456
	s_waitcnt vmcnt(8)
	ds_write_b128 v232, v[130:133] offset:8448
	v_or_b32_e32 v98, s10, v204
	v_or_b32_e32 v102, s10, v205
	s_waitcnt lgkmcnt(10)
	v_mfma_f32_32x32x16_bf16 v[18:33], v[38:41], v[238:241], v[18:33]
	v_add_f32_e32 v38, v75, v46
	v_add_f32_e32 v38, v76, v38
	v_add_f32_e32 v38, v77, v38
	v_add_f32_e32 v38, v78, v38
	v_add_f32_e32 v38, v79, v38
	v_add_f32_e32 v38, v80, v38
	v_add_f32_e32 v249, v81, v38
	v_mfma_f32_32x32x16_bf16 v[2:17], v[42:45], v[34:37], v[2:17]
	v_or_b32_e32 v34, s10, v184
	v_min_u32_e32 v34, 0x3fff, v34
	v_mul_u32_u24_e32 v38, 0xc00, v34
	ds_read_b128 v[34:37], v177
	v_or_b32_e32 v38, v38, v176
	global_load_dwordx4 v[70:73], v38, s[8:9] offset:1024
	global_load_dwordx4 v[74:77], v38, s[8:9] offset:2048
	v_or_b32_e32 v38, s10, v203
	v_min_u32_e32 v38, 0x3fff, v38
	v_mul_u32_u24_e32 v38, 0xc00, v38
	ds_read_b128 v[94:97], v177 offset:32
	v_or_b32_e32 v82, v38, v176
	s_waitcnt lgkmcnt(1)
	v_mfma_f32_32x32x16_bf16 v[34:49], v[34:37], v[66:69], 0
	v_min_u32_e32 v98, 0x3fff, v98
	v_min_u32_e32 v102, 0x3fff, v102
	v_mul_u32_u24_e32 v98, 0xc00, v98
	v_mul_u32_u24_e32 v102, 0xc00, v102
	v_or_b32_e32 v98, v98, v176
	v_or_b32_e32 v114, v102, v176
	global_load_dwordx4 v[78:81], v82, s[8:9] offset:1024
	s_nop 0
	global_load_dwordx4 v[82:85], v82, s[8:9] offset:2048
	ds_read_b128 v[106:109], v177 offset:96
	ds_read_b128 v[110:113], v177 offset:64
	s_waitcnt lgkmcnt(2)
	v_mfma_f32_32x32x16_bf16 v[34:49], v[94:97], v[62:65], v[34:49]
	global_load_dwordx4 v[94:97], v98, s[8:9] offset:1024
	s_nop 0
	global_load_dwordx4 v[98:101], v98, s[8:9] offset:2048
	s_nop 0
	global_load_dwordx4 v[102:105], v114, s[8:9] offset:1024
	global_load_dwordx4 v[138:141], v114, s[8:9] offset:2048
	s_waitcnt lgkmcnt(0)
	v_mfma_f32_32x32x16_bf16 v[34:49], v[110:113], v[58:61], v[34:49]
	v_add_f32_e32 v110, v165, v249
	v_add_f32_e32 v110, v171, v110
	v_add_f32_e32 v110, v172, v110
	v_add_f32_e32 v110, v173, v110
	v_add_f32_e32 v110, v237, v110
	v_add_f32_e32 v110, v246, v110
	v_add_f32_e32 v110, v247, v110
	v_mfma_f32_32x32x16_bf16 v[34:49], v[106:109], v[54:57], v[34:49]
	v_add_f32_e32 v108, v248, v110
	v_add_f32_e32 v164, v164, v108
	s_nop 5
	v_add_u32_e32 v253, 91, v163
	v_cmp_le_i32_e32 vcc, 27, v253
	v_cmp_le_i32_e64 s[98:99], 26, v253
	v_cmp_le_i32_e64 s[100:101], 25, v253
	v_cndmask_b32_e32 v34, v234, v34, vcc
	v_mfma_f32_32x32x16_bf16 v[2:17], v[242:245], v[238:241], v[2:17]
	v_cmp_le_i32_e32 vcc, 24, v253
	v_cndmask_b32_e64 v35, v234, v35, s[98:99]
	v_max3_f32 v106, v34, s31, v35
	v_cmp_le_i32_e64 s[98:99], 19, v253
	v_cndmask_b32_e64 v36, v234, v36, s[100:101]
	v_cmp_le_i32_e64 s[100:101], 18, v253
	v_cndmask_b32_e32 v37, v234, v37, vcc
	v_max3_f32 v106, v106, v36, v37
	v_cmp_le_i32_e32 vcc, 17, v253
	v_cndmask_b32_e64 v38, v234, v38, s[98:99]
	v_cmp_le_i32_e64 s[98:99], 16, v253
	v_cndmask_b32_e64 v39, v234, v39, s[100:101]
	v_max3_f32 v106, v106, v38, v39
	v_cmp_le_i32_e64 s[100:101], 11, v253
	v_cndmask_b32_e32 v40, v234, v40, vcc
	v_cmp_le_i32_e32 vcc, 10, v253
	v_cndmask_b32_e64 v41, v234, v41, s[98:99]
	v_max3_f32 v106, v106, v40, v41
	v_cmp_le_i32_e64 s[98:99], 9, v253
	v_cndmask_b32_e64 v42, v234, v42, s[100:101]
	v_cmp_le_i32_e64 s[100:101], 8, v253
	v_cndmask_b32_e32 v43, v234, v43, vcc
	v_max3_f32 v106, v106, v42, v43
	v_cmp_le_i32_e32 vcc, 3, v253
	v_cndmask_b32_e64 v44, v234, v44, s[98:99]
	v_cmp_le_i32_e64 s[98:99], 2, v253
	v_cndmask_b32_e64 v45, v234, v45, s[100:101]
	v_max3_f32 v106, v106, v44, v45
	v_cmp_le_i32_e64 s[100:101], 1, v253
	v_cndmask_b32_e32 v46, v234, v46, vcc
	v_cmp_le_i32_e32 vcc, 0, v253
	v_cndmask_b32_e64 v47, v234, v47, s[98:99]
	v_max3_f32 v106, v106, v46, v47
	v_cndmask_b32_e64 v48, v234, v48, s[100:101]
	v_cndmask_b32_e32 v49, v234, v49, vcc
	v_max3_f32 v106, v106, v48, v49
	ds_bpermute_b32 v107, v179, v106
	s_waitcnt lgkmcnt(0)
	v_max_f32_e32 v107, v107, v107
	v_max_f32_e32 v106, v106, v107
	v_cmp_gt_f32_e32 vcc, v106, v50
	s_cbranch_vccz .LBB0_388
; #define LAS __attribute__((address_space(3)))
; template <int STAGE, int OFF> __device__ __forceinline__ void attn32_unit(const bf16* base, bf16* yrow0, int blk0, int u, LAS unsigned char* xtab, LAS unsigned char* kbuf, LAS unsigned char* vbuf, int lane, ...
;     ...
;         for (int c = 0; c < 4; ++c) { *(LAS v4u*)(kbuf + (8 * c + lrow) * 144 + lch * 16) = kr[set][c]; *(LAS v4u*)(vbuf + (8 * c + lrow) * 160 + lch * 16) = vr[set][c]; }
;         if (pp + 2 < 5) { ATT32_LOAD(set, pp + 2, t0, SH); }
;         else { const bf16* base_ = base; { const bf16* base = nbase; ATT32_LOAD(set, pp + 2 - 5, nt0, nsh); } (void)base_; }
;         f32x16 sc;
; #pragma unroll
;         for (int i = 0; i < 16; ++i) sc[i] = 0.f;
; #pragma unroll
;         for (int ks = 0; ks < 4; ++ks) { const bf16x8 ka = *(const LAS bf16x8*)(kbuf + qi * 144 + 32 * ks + 16 * h); sc = MFMA32(ka, qb[ks], sc); }
;         if (pp == 4) {
; #pragma unroll
;             for (int ks = 0; ks < 4; ++ks) qb[ks] = *(const bf16x8*)(nbase + (size_t)min(nt0 + (qi << nsh), SEQ - 1) * 1536 + 16 * ks + 8 * h);
;         }
;         const int mbase = n0 + 4 * h - lo; float mx = -INFINITY;
; #pragma unroll
;         for (int rg = 0; rg < 16; ++rg) { sc[rg] = ((unsigned)(mbase + (rg & 3) + 8 * (rg >> 2)) <= mspan) ? sc[rg] : -INFINITY; mx = fmaxf(mx, sc[rg]); }
;         mx = fmaxf(mx, __shfl_xor(mx, 32));
;         if (__any(mx > m)) {
;             const float mn = fmaxf(m, mx), alpha = __builtin_amdgcn_exp2f(m - mn); m = mn; l *= alpha;
; #pragma unroll
;             for (int i = 0; i < 16; ++i) { o[0][i] *= alpha; o[1][i] *= alpha; }
;         }
;         float ps = 0.f;
; #pragma unroll
;         for (int rg = 0; rg < 16; ++rg) { sc[rg] = __builtin_amdgcn_exp2f(sc[rg] - m); ps += sc[rg]; }
;         l += ps;
;         bf16x8 pb[2];
; #pragma unroll
;         for (int s2 = 0; s2 < 2; ++s2) { v4u w; w.x = pg8::cvt_pk_bf16(sc[8 * s2], sc[8 * s2 + 1]); w.y = pg8::cvt_pk_bf16(sc[8 * s2 + 2], sc[8 * s2 + 3]); w.z = pg8::cvt_pk_bf16(sc[8 * s2 + 4], sc[8 * s2 + 5]); w.w = pg8::cvt_pk_bf16(sc[8 * s2 + 6], sc[8 * s2 + 7]); pb[s2] = __builtin_bit_cast(bf16x8, w); }
; #pragma unroll
;         for (int mb = 0; mb < 2; ++mb)
; #pragma unroll
;             for (int s2 = 0; s2 < 2; ++s2) {
;                 LAS unsigned char* vp = vbuf + tr_off + (16 * s2) * 160 + 64 * mb;
	v_max_f32_e32 v106, v106, v106
	v_max_f32_e32 v107, v50, v50
	v_max_f32_e32 v106, v107, v106
	v_sub_f32_e32 v50, v50, v106
	v_exp_f32_e32 v50, v50
	s_nop 0
	v_pk_mul_f32 v[32:33], v[32:33], v[50:51] op_sel_hi:[1,0]
	v_pk_mul_f32 v[30:31], v[30:31], v[50:51] op_sel_hi:[1,0]
	v_pk_mul_f32 v[28:29], v[28:29], v[50:51] op_sel_hi:[1,0]
	v_pk_mul_f32 v[26:27], v[26:27], v[50:51] op_sel_hi:[1,0]
	v_pk_mul_f32 v[24:25], v[24:25], v[50:51] op_sel_hi:[1,0]
	v_pk_mul_f32 v[22:23], v[22:23], v[50:51] op_sel_hi:[1,0]
	v_pk_mul_f32 v[20:21], v[20:21], v[50:51] op_sel_hi:[1,0]
	v_pk_mul_f32 v[18:19], v[18:19], v[50:51] op_sel_hi:[1,0]
	v_pk_mul_f32 v[16:17], v[16:17], v[50:51] op_sel_hi:[1,0]
	v_pk_mul_f32 v[14:15], v[14:15], v[50:51] op_sel_hi:[1,0]
	v_pk_mul_f32 v[12:13], v[12:13], v[50:51] op_sel_hi:[1,0]
	v_pk_mul_f32 v[10:11], v[10:11], v[50:51] op_sel_hi:[1,0]
	v_pk_mul_f32 v[8:9], v[8:9], v[50:51] op_sel_hi:[1,0]
	v_pk_mul_f32 v[6:7], v[6:7], v[50:51] op_sel_hi:[1,0]
	v_pk_mul_f32 v[4:5], v[4:5], v[50:51] op_sel_hi:[1,0]
	v_pk_mul_f32 v[2:3], v[2:3], v[50:51] op_sel_hi:[1,0]
	v_mul_f32_e32 v164, v164, v50
	v_mov_b32_e32 v50, v106
.LBB0_388:
	v_sub_f32_e32 v34, v34, v50
	v_exp_f32_e32 v106, v34
	v_sub_f32_e32 v34, v35, v50
	v_exp_f32_e32 v107, v34
	v_sub_f32_e32 v34, v36, v50
	v_exp_f32_e32 v108, v34
	v_sub_f32_e32 v34, v37, v50
	v_exp_f32_e32 v109, v34
	v_sub_f32_e32 v34, v38, v50
	v_exp_f32_e32 v110, v34
	v_sub_f32_e32 v34, v39, v50
	v_exp_f32_e32 v111, v34
	v_sub_f32_e32 v34, v40, v50
	v_exp_f32_e32 v112, v34
	v_sub_f32_e32 v34, v41, v50
	v_exp_f32_e32 v113, v34
	v_sub_f32_e32 v34, v42, v50
	v_exp_f32_e32 v165, v34
	v_sub_f32_e32 v34, v43, v50
	v_exp_f32_e32 v171, v34
	v_sub_f32_e32 v34, v44, v50
	v_exp_f32_e32 v172, v34
	v_sub_f32_e32 v34, v45, v50
	v_exp_f32_e32 v173, v34
	v_sub_f32_e32 v34, v46, v50
	v_exp_f32_e32 v237, v34
	v_sub_f32_e32 v34, v47, v50
	v_exp_f32_e32 v246, v34
	v_sub_f32_e32 v34, v48, v50
	v_exp_f32_e32 v247, v34
	v_sub_f32_e32 v34, v49, v50
	v_exp_f32_e32 v248, v34
	v_cvt_pk_bf16_f32 v34, v106, v107
	v_cvt_pk_bf16_f32 v35, v108, v109
	v_cvt_pk_bf16_f32 v36, v110, v111
	v_cvt_pk_bf16_f32 v37, v112, v113
	v_cvt_pk_bf16_f32 v238, v165, v171
	v_cvt_pk_bf16_f32 v239, v172, v173
	v_cvt_pk_bf16_f32 v240, v237, v246
	v_cvt_pk_bf16_f32 v241, v247, v248
	ds_read_b64_tr_b16 v[38:39], v181 offset:4608
	ds_read_b64_tr_b16 v[40:41], v181 offset:5888
	ds_read_b64_tr_b16 v[44:45], v181 offset:5952
	ds_read_b64_tr_b16 v[42:43], v181 offset:4672
	s_waitcnt lgkmcnt(2)
	v_mfma_f32_32x32x16_bf16 v[18:33], v[38:41], v[34:37], v[18:33]
	ds_read_b64_tr_b16 v[38:39], v181 offset:7168
	ds_read_b64_tr_b16 v[40:41], v181 offset:8448
	v_add_f32_e32 v46, 0, v106
	s_add_i32 s10, s13, s25
	ds_read_b64_tr_b16 v[244:245], v181 offset:8512
	ds_read_b64_tr_b16 v[242:243], v181 offset:7232
	s_waitcnt vmcnt(15)
	ds_write_b128 v231, v[86:89]
	s_waitcnt vmcnt(14)
	ds_write_b128 v232, v[90:93] offset:4608
	s_waitcnt vmcnt(13)
	ds_write_b128 v231, v[134:137] offset:1152
	s_waitcnt vmcnt(12)
	ds_write_b128 v232, v[142:145] offset:5888
	s_waitcnt vmcnt(11)
	ds_write_b128 v231, v[146:149] offset:2304
	s_waitcnt vmcnt(10)
	ds_write_b128 v232, v[150:153] offset:7168
	s_waitcnt vmcnt(9)
	ds_write_b128 v231, v[154:157] offset:3456
	s_waitcnt vmcnt(8)
	ds_write_b128 v232, v[158:161] offset:8448
	s_waitcnt lgkmcnt(10)
	v_mfma_f32_32x32x16_bf16 v[18:33], v[38:41], v[238:241], v[18:33]
	v_add_f32_e32 v38, v107, v46
	v_add_f32_e32 v38, v108, v38
	v_add_f32_e32 v38, v109, v38
	v_add_f32_e32 v38, v110, v38
	v_add_f32_e32 v38, v111, v38
	v_add_f32_e32 v38, v112, v38
	v_add_f32_e32 v249, v113, v38
	v_mfma_f32_32x32x16_bf16 v[2:17], v[42:45], v[34:37], v[2:17]
	v_add_u32_e32 v34, s10, v185
	v_med3_i32 v34, v34, 0, v233
	v_mul_u32_u24_e32 v38, 0xc00, v34
	ds_read_b128 v[34:37], v177
	v_or_b32_e32 v38, v38, v176
	global_load_dwordx4 v[106:109], v38, s[8:9] offset:1024
	global_load_dwordx4 v[110:113], v38, s[8:9] offset:2048
	v_add_u32_e32 v38, s10, v186
	v_med3_i32 v38, v38, 0, v233
	v_mul_u32_u24_e32 v38, 0xc00, v38
	ds_read_b128 v[86:89], v177 offset:32
	v_or_b32_e32 v90, v38, v176
	s_waitcnt lgkmcnt(1)
	v_mfma_f32_32x32x16_bf16 v[34:49], v[34:37], v[66:69], 0
	global_load_dwordx4 v[114:117], v90, s[8:9] offset:1024
	global_load_dwordx4 v[118:121], v90, s[8:9] offset:2048
	v_add_u32_e32 v90, s10, v187
	v_med3_i32 v90, v90, 0, v233
	v_mul_u32_u24_e32 v90, 0xc00, v90
	v_or_b32_e32 v126, v90, v176
	ds_read_b128 v[90:93], v177 offset:96
	ds_read_b128 v[142:145], v177 offset:64
	global_load_dwordx4 v[122:125], v126, s[8:9] offset:1024
	s_nop 0
	global_load_dwordx4 v[126:129], v126, s[8:9] offset:2048
	s_waitcnt lgkmcnt(2)
	v_mfma_f32_32x32x16_bf16 v[34:49], v[86:89], v[62:65], v[34:49]
	v_add_u32_e32 v86, s10, v188
	v_med3_i32 v86, v86, 0, v233
	v_mul_u32_u24_e32 v86, 0xc00, v86
	v_or_b32_e32 v86, v86, v176
	global_load_dwordx4 v[130:133], v86, s[8:9] offset:1024
	global_load_dwordx4 v[134:137], v86, s[8:9] offset:2048
	s_waitcnt lgkmcnt(0)
; __device__ __forceinline__ unsigned cvt_pk_bf16(float lo, float hi) { unsigned r; asm volatile("v_cvt_pk_bf16_f32 %0, %1, %2" : "=v"(r) : "v"(lo), "v"(hi)); return r; }
; #define LAS __attribute__((address_space(3)))
; #define MFMA32(a, b, c) __builtin_amdgcn_mfma_f32_32x32x16_bf16((a), (b), (c), 0, 0, 0)
; template <int STAGE, int OFF> __device__ __forceinline__ void attn32_unit(const bf16* base, bf16* yrow0, int blk0, int u, LAS unsigned char* xtab, LAS unsigned char* kbuf, LAS unsigned char* vbuf, int lane, ...
;     ...
;         const int mbase = n0 + 4 * h - lo; float mx = -INFINITY;
; #pragma unroll
;         for (int rg = 0; rg < 16; ++rg) { sc[rg] = ((unsigned)(mbase + (rg & 3) + 8 * (rg >> 2)) <= mspan) ? sc[rg] : -INFINITY; mx = fmaxf(mx, sc[rg]); }
;         mx = fmaxf(mx, __shfl_xor(mx, 32));
;         if (__any(mx > m)) {
;             const float mn = fmaxf(m, mx), alpha = __builtin_amdgcn_exp2f(m - mn); m = mn; l *= alpha;
; #pragma unroll
;             for (int i = 0; i < 16; ++i) { o[0][i] *= alpha; o[1][i] *= alpha; }
;         }
;         float ps = 0.f;
; #pragma unroll
;         for (int rg = 0; rg < 16; ++rg) { sc[rg] = __builtin_amdgcn_exp2f(sc[rg] - m); ps += sc[rg]; }
;         l += ps;
;         bf16x8 pb[2];
; #pragma unroll
;         for (int s2 = 0; s2 < 2; ++s2) { v4u w; w.x = pg8::cvt_pk_bf16(sc[8 * s2], sc[8 * s2 + 1]); w.y = pg8::cvt_pk_bf16(sc[8 * s2 + 2], sc[8 * s2 + 3]); w.z = pg8::cvt_pk_bf16(sc[8 * s2 + 4], sc[8 * s2 + 5]); w.w = pg8::cvt_pk_bf16(sc[8 * s2 + 6], sc[8 * s2 + 7]); pb[s2] = __builtin_bit_cast(bf16x8, w); }
; #pragma unroll
;         for (int mb = 0; mb < 2; ++mb)
; #pragma unroll
;             for (int s2 = 0; s2 < 2; ++s2) {
;                 LAS unsigned char* vp = vbuf + tr_off + (16 * s2) * 160 + 64 * mb;
;                 const v4i16 a0 = __builtin_amdgcn_ds_read_tr16_b64_v4i16((LAS v4i16*)vp), a1 = __builtin_amdgcn_ds_read_tr16_b64_v4i16((LAS v4i16*)(vp + 8 * 160));
;                 const bf16x8 va = __builtin_shufflevector(a0, a1, 0, 1, 2, 3, 4, 5, 6, 7);
;                 o[mb] = MFMA32(va, pb[s2], o[mb]);
	v_mfma_f32_32x32x16_bf16 v[34:49], v[142:145], v[58:61], v[34:49]
	v_add_f32_e32 v86, v165, v249
	v_add_f32_e32 v86, v171, v86
	v_add_f32_e32 v86, v172, v86
	v_add_f32_e32 v86, v173, v86
	v_add_f32_e32 v86, v237, v86
	v_mfma_f32_32x32x16_bf16 v[34:49], v[90:93], v[54:57], v[34:49]
	v_add_f32_e32 v86, v246, v86
	v_add_f32_e32 v86, v247, v86
	v_add_f32_e32 v86, v248, v86
	v_add_f32_e32 v142, v164, v86
	v_mfma_f32_32x32x16_bf16 v[2:17], v[242:245], v[238:241], v[2:17]
	s_nop 6
	v_add_u32_e32 v253, 123, v163
	v_cmp_le_i32_e32 vcc, 27, v253
	v_cmp_le_i32_e64 s[98:99], 26, v253
	v_cmp_le_i32_e64 s[100:101], 25, v253
	v_cndmask_b32_e32 v34, v234, v34, vcc
	v_cmp_le_i32_e32 vcc, 24, v253
	v_cndmask_b32_e64 v35, v234, v35, s[98:99]
	v_max3_f32 v87, v34, s31, v35
	v_cmp_le_i32_e64 s[98:99], 19, v253
	v_cndmask_b32_e64 v36, v234, v36, s[100:101]
	v_cmp_le_i32_e64 s[100:101], 18, v253
	v_cndmask_b32_e32 v37, v234, v37, vcc
	v_max3_f32 v87, v87, v36, v37
	v_cmp_le_i32_e32 vcc, 17, v253
	v_cndmask_b32_e64 v38, v234, v38, s[98:99]
	v_cmp_le_i32_e64 s[98:99], 16, v253
	v_cndmask_b32_e64 v39, v234, v39, s[100:101]
	v_max3_f32 v87, v87, v38, v39
	v_cmp_le_i32_e64 s[100:101], 11, v253
	v_cndmask_b32_e32 v40, v234, v40, vcc
	v_cmp_le_i32_e32 vcc, 10, v253
	v_cndmask_b32_e64 v41, v234, v41, s[98:99]
	v_max3_f32 v87, v87, v40, v41
	v_cmp_le_i32_e64 s[98:99], 9, v253
	v_cndmask_b32_e64 v42, v234, v42, s[100:101]
	v_cmp_le_i32_e64 s[100:101], 8, v253
	v_cndmask_b32_e32 v43, v234, v43, vcc
	v_max3_f32 v87, v87, v42, v43
	v_cmp_le_i32_e32 vcc, 3, v253
	v_cndmask_b32_e64 v44, v234, v44, s[98:99]
	v_cmp_le_i32_e64 s[98:99], 2, v253
	v_cndmask_b32_e64 v45, v234, v45, s[100:101]
	v_max3_f32 v87, v87, v44, v45
	v_cmp_le_i32_e64 s[100:101], 1, v253
	v_cndmask_b32_e32 v46, v234, v46, vcc
	v_cmp_le_i32_e32 vcc, 0, v253
	v_cndmask_b32_e64 v47, v234, v47, s[98:99]
	v_max3_f32 v87, v87, v46, v47
	v_cndmask_b32_e64 v48, v234, v48, s[100:101]
	v_cndmask_b32_e32 v49, v234, v49, vcc
	v_max3_f32 v87, v87, v48, v49
	ds_bpermute_b32 v88, v179, v87
	s_waitcnt lgkmcnt(0)
	v_max_f32_e32 v86, v88, v88
	v_max_f32_e32 v86, v87, v86
	v_cmp_gt_f32_e32 vcc, v86, v50
	s_cbranch_vccz .LBB0_390
	v_max_f32_e32 v86, v86, v86
	v_max_f32_e32 v87, v50, v50
	v_max_f32_e32 v86, v87, v86
	v_sub_f32_e32 v50, v50, v86
	v_exp_f32_e32 v50, v50
	s_nop 0
	v_pk_mul_f32 v[32:33], v[32:33], v[50:51] op_sel_hi:[1,0]
	v_pk_mul_f32 v[30:31], v[30:31], v[50:51] op_sel_hi:[1,0]
	v_pk_mul_f32 v[28:29], v[28:29], v[50:51] op_sel_hi:[1,0]
	v_pk_mul_f32 v[26:27], v[26:27], v[50:51] op_sel_hi:[1,0]
	v_pk_mul_f32 v[24:25], v[24:25], v[50:51] op_sel_hi:[1,0]
	v_pk_mul_f32 v[22:23], v[22:23], v[50:51] op_sel_hi:[1,0]
	v_pk_mul_f32 v[20:21], v[20:21], v[50:51] op_sel_hi:[1,0]
	v_pk_mul_f32 v[18:19], v[18:19], v[50:51] op_sel_hi:[1,0]
	v_pk_mul_f32 v[16:17], v[16:17], v[50:51] op_sel_hi:[1,0]
	v_pk_mul_f32 v[14:15], v[14:15], v[50:51] op_sel_hi:[1,0]
	v_pk_mul_f32 v[12:13], v[12:13], v[50:51] op_sel_hi:[1,0]
	v_pk_mul_f32 v[10:11], v[10:11], v[50:51] op_sel_hi:[1,0]
	v_pk_mul_f32 v[8:9], v[8:9], v[50:51] op_sel_hi:[1,0]
	v_pk_mul_f32 v[6:7], v[6:7], v[50:51] op_sel_hi:[1,0]
	v_pk_mul_f32 v[4:5], v[4:5], v[50:51] op_sel_hi:[1,0]
	v_pk_mul_f32 v[2:3], v[2:3], v[50:51] op_sel_hi:[1,0]
	v_mul_f32_e32 v142, v142, v50
	v_mov_b32_e32 v50, v86
.LBB0_390:
	v_sub_f32_e32 v34, v34, v50
	v_exp_f32_e32 v86, v34
	v_sub_f32_e32 v34, v35, v50
	v_exp_f32_e32 v87, v34
	v_sub_f32_e32 v34, v36, v50
	v_exp_f32_e32 v88, v34
	v_sub_f32_e32 v34, v37, v50
	v_exp_f32_e32 v89, v34
	v_sub_f32_e32 v34, v38, v50
	v_exp_f32_e32 v90, v34
	v_sub_f32_e32 v34, v39, v50
	v_exp_f32_e32 v91, v34
	v_sub_f32_e32 v34, v40, v50
	v_exp_f32_e32 v92, v34
	v_sub_f32_e32 v34, v41, v50
	v_exp_f32_e32 v93, v34
	v_sub_f32_e32 v34, v42, v50
	v_exp_f32_e32 v143, v34
	v_sub_f32_e32 v34, v43, v50
	v_exp_f32_e32 v154, v34
	v_sub_f32_e32 v34, v44, v50
	v_exp_f32_e32 v155, v34
	v_sub_f32_e32 v34, v45, v50
	v_exp_f32_e32 v156, v34
	v_sub_f32_e32 v34, v46, v50
	v_exp_f32_e32 v157, v34
	v_sub_f32_e32 v34, v47, v50
	v_exp_f32_e32 v158, v34
	v_sub_f32_e32 v34, v48, v50
	v_exp_f32_e32 v159, v34
	v_sub_f32_e32 v34, v49, v50
	v_exp_f32_e32 v160, v34
	v_cvt_pk_bf16_f32 v34, v86, v87
	v_cvt_pk_bf16_f32 v35, v88, v89
	v_cvt_pk_bf16_f32 v36, v90, v91
	v_cvt_pk_bf16_f32 v37, v92, v93
	v_cvt_pk_bf16_f32 v144, v143, v154
	v_cvt_pk_bf16_f32 v145, v155, v156
	v_cvt_pk_bf16_f32 v146, v157, v158
	v_cvt_pk_bf16_f32 v147, v159, v160
	ds_read_b64_tr_b16 v[38:39], v181 offset:4608
	ds_read_b64_tr_b16 v[40:41], v181 offset:5888
	v_or_b32_e32 v42, s10, v183
	v_min_i32_e32 v148, 0x3fff, v42
	s_waitcnt lgkmcnt(0)
	v_mfma_f32_32x32x16_bf16 v[18:33], v[38:41], v[34:37], v[18:33]
	v_mul_u32_u24_e32 v38, 0xc00, v148
	v_mov_b32_e32 v39, v169
	v_lshl_add_u64 v[38:39], s[8:9], 0, v[38:39]
	ds_read_b64_tr_b16 v[42:43], v181 offset:7168
	ds_read_b64_tr_b16 v[44:45], v181 offset:8448
	ds_read_b64_tr_b16 v[48:49], v181 offset:5952
	ds_read_b64_tr_b16 v[46:47], v181 offset:4672
	v_lshl_add_u64 v[152:153], v[38:39], 0, v[168:169]
	v_add_f32_e32 v38, 0, v86
	v_add_f32_e32 v38, v87, v38
	v_add_f32_e32 v38, v88, v38
	v_add_f32_e32 v38, v89, v38
	v_add_f32_e32 v38, v90, v38
	v_add_f32_e32 v38, v91, v38
	s_waitcnt lgkmcnt(0)
	v_mfma_f32_32x32x16_bf16 v[2:17], v[46:49], v[34:37], v[2:17]
	v_add_u32_e32 v34, s10, v189
	ds_read_b64_tr_b16 v[150:151], v181 offset:8512
	ds_read_b64_tr_b16 v[148:149], v181 offset:7232
	v_add_f32_e32 v38, v92, v38
	s_waitcnt vmcnt(15)
; #define LAS __attribute__((address_space(3)))
; #define MFMA32(a, b, c) __builtin_amdgcn_mfma_f32_32x32x16_bf16((a), (b), (c), 0, 0, 0)
; template <int STAGE, int OFF> __device__ __forceinline__ void attn32_unit(const bf16* base, bf16* yrow0, int blk0, int u, LAS unsigned char* xtab, LAS unsigned char* kbuf, LAS unsigned char* vbuf, int lane, ...
;     ...
;         for (int c = 0; c < 4; ++c) { *(LAS v4u*)(kbuf + (8 * c + lrow) * 144 + lch * 16) = kr[set][c]; *(LAS v4u*)(vbuf + (8 * c + lrow) * 160 + lch * 16) = vr[set][c]; }
;         if (pp + 2 < 5) { ATT32_LOAD(set, pp + 2, t0, SH); }
;         else { const bf16* base_ = base; { const bf16* base = nbase; ATT32_LOAD(set, pp + 2 - 5, nt0, nsh); } (void)base_; }
;         f32x16 sc;
; #pragma unroll
;         for (int i = 0; i < 16; ++i) sc[i] = 0.f;
; #pragma unroll
;         for (int ks = 0; ks < 4; ++ks) { const bf16x8 ka = *(const LAS bf16x8*)(kbuf + qi * 144 + 32 * ks + 16 * h); sc = MFMA32(ka, qb[ks], sc); }
;         if (pp == 4) {
; #pragma unroll
;             for (int ks = 0; ks < 4; ++ks) qb[ks] = *(const bf16x8*)(nbase + (size_t)min(nt0 + (qi << nsh), SEQ - 1) * 1536 + 16 * ks + 8 * h);
;         }
;         const int mbase = n0 + 4 * h - lo; float mx = -INFINITY;
; #pragma unroll
;         for (int rg = 0; rg < 16; ++rg) { sc[rg] = ((unsigned)(mbase + (rg & 3) + 8 * (rg >> 2)) <= mspan) ? sc[rg] : -INFINITY; mx = fmaxf(mx, sc[rg]); }
;         mx = fmaxf(mx, __shfl_xor(mx, 32));
;         if (__any(mx > m)) {
;             const float mn = fmaxf(m, mx), alpha = __builtin_amdgcn_exp2f(m - mn); m = mn; l *= alpha;
; #pragma unroll
;             for (int i = 0; i < 16; ++i) { o[0][i] *= alpha; o[1][i] *= alpha; }
;         }
	ds_write_b128 v231, v[70:73]
	s_waitcnt vmcnt(14)
	ds_write_b128 v232, v[74:77] offset:4608
	s_waitcnt vmcnt(13)
	ds_write_b128 v231, v[78:81] offset:1152
	s_waitcnt vmcnt(12)
	ds_write_b128 v232, v[82:85] offset:5888
	s_waitcnt vmcnt(11)
	ds_write_b128 v231, v[94:97] offset:2304
	s_waitcnt vmcnt(10)
	ds_write_b128 v232, v[98:101] offset:7168
	s_waitcnt vmcnt(9)
	ds_write_b128 v231, v[102:105] offset:3456
	s_waitcnt vmcnt(8)
	ds_write_b128 v232, v[138:141] offset:8448
	v_med3_i32 v34, v34, 0, v233
	v_add_f32_e32 v161, v93, v38
	v_mul_u32_u24_e32 v38, 0xc00, v34
	ds_read_b128 v[34:37], v177
	v_or_b32_e32 v38, v38, v176
	global_load_dwordx4 v[74:77], v38, s[8:9] offset:1024
	global_load_dwordx4 v[78:81], v38, s[8:9] offset:2048
	v_add_u32_e32 v38, s10, v190
	v_med3_i32 v38, v38, 0, v233
	v_mul_u32_u24_e32 v38, 0xc00, v38
	ds_read_b128 v[70:73], v177 offset:32
	v_mfma_f32_32x32x16_bf16 v[18:33], v[42:45], v[144:147], v[18:33]
	v_or_b32_e32 v86, v38, v176
	global_load_dwordx4 v[82:85], v86, s[8:9] offset:1024
	s_nop 0
	global_load_dwordx4 v[86:89], v86, s[8:9] offset:2048
	v_add_f32_e32 v143, v143, v161
	v_add_f32_e32 v143, v154, v143
	v_add_f32_e32 v143, v155, v143
	v_add_f32_e32 v143, v156, v143
	v_add_f32_e32 v143, v157, v143
	s_waitcnt lgkmcnt(1)
	v_mfma_f32_32x32x16_bf16 v[34:49], v[34:37], v[66:69], 0
	v_add_u32_e32 v66, s10, v191
	v_med3_i32 v66, v66, 0, v233
	v_mul_u32_u24_e32 v66, 0xc00, v66
	v_or_b32_e32 v94, v66, v176
	ds_read_b128 v[138:141], v177 offset:96
	ds_read_b128 v[66:69], v177 offset:64
	global_load_dwordx4 v[90:93], v94, s[8:9] offset:1024
	s_nop 0
	global_load_dwordx4 v[94:97], v94, s[8:9] offset:2048
	v_add_f32_e32 v143, v158, v143
	s_waitcnt lgkmcnt(2)
	v_mfma_f32_32x32x16_bf16 v[34:49], v[70:73], v[62:65], v[34:49]
	v_add_u32_e32 v62, s10, v192
	v_med3_i32 v62, v62, 0, v233
	v_mul_u32_u24_e32 v62, 0xc00, v62
	v_or_b32_e32 v62, v62, v176
	global_load_dwordx4 v[98:101], v62, s[8:9] offset:1024
	global_load_dwordx4 v[102:105], v62, s[8:9] offset:2048
	v_add_f32_e32 v143, v159, v143
	s_waitcnt lgkmcnt(0)
	v_mfma_f32_32x32x16_bf16 v[34:49], v[66:69], v[58:61], v[34:49]
	global_load_dwordx4 v[70:73], v[152:153], off
	global_load_dwordx4 v[66:69], v[152:153], off offset:32
	global_load_dwordx4 v[62:65], v[152:153], off offset:64
	global_load_dwordx4 v[58:61], v[152:153], off offset:96
	v_mfma_f32_32x32x16_bf16 v[34:49], v[138:141], v[54:57], v[34:49]
	v_mfma_f32_32x32x16_bf16 v[2:17], v[148:151], v[144:147], v[2:17]
	s_nop 7
	v_sub_u32_e32 v253, v162, v163
	v_subrev_u32_e32 v253, 0x80, v253
	v_cmp_le_i32_e32 vcc, 0, v253
	v_cmp_le_i32_e64 s[98:99], 1, v253
	v_cmp_le_i32_e64 s[100:101], 2, v253
	v_cndmask_b32_e32 v54, v234, v34, vcc
	v_cmp_le_i32_e32 vcc, 3, v253
	v_cndmask_b32_e64 v35, v234, v35, s[98:99]
	v_max3_f32 v34, v54, s31, v35
	v_cmp_le_i32_e64 s[98:99], 8, v253
	v_cndmask_b32_e64 v36, v234, v36, s[100:101]
	v_cmp_le_i32_e64 s[100:101], 9, v253
	v_cndmask_b32_e32 v37, v234, v37, vcc
	v_max3_f32 v34, v34, v36, v37
	v_cmp_le_i32_e32 vcc, 10, v253
	v_cndmask_b32_e64 v38, v234, v38, s[98:99]
	v_cmp_le_i32_e64 s[98:99], 11, v253
	v_cndmask_b32_e64 v39, v234, v39, s[100:101]
	v_max3_f32 v34, v34, v38, v39
	v_cmp_le_i32_e64 s[100:101], 16, v253
	v_cndmask_b32_e32 v40, v234, v40, vcc
	v_cmp_le_i32_e32 vcc, 17, v253
	v_cndmask_b32_e64 v41, v234, v41, s[98:99]
	v_max3_f32 v34, v34, v40, v41
	v_cmp_le_i32_e64 s[98:99], 18, v253
	v_cndmask_b32_e64 v42, v234, v42, s[100:101]
	v_cmp_le_i32_e64 s[100:101], 19, v253
	v_cndmask_b32_e32 v43, v234, v43, vcc
	v_max3_f32 v34, v34, v42, v43
	v_cmp_le_i32_e32 vcc, 24, v253
	v_cndmask_b32_e64 v44, v234, v44, s[98:99]
	v_cmp_le_i32_e64 s[98:99], 25, v253
	v_cndmask_b32_e64 v45, v234, v45, s[100:101]
	v_max3_f32 v34, v34, v44, v45
	v_cmp_le_i32_e64 s[100:101], 26, v253
	v_cndmask_b32_e32 v46, v234, v46, vcc
	v_cmp_le_i32_e32 vcc, 27, v253
	v_cndmask_b32_e64 v47, v234, v47, s[98:99]
	v_max3_f32 v34, v34, v46, v47
	v_cndmask_b32_e64 v48, v234, v48, s[100:101]
	v_cndmask_b32_e32 v49, v234, v49, vcc
	v_max3_f32 v55, v34, v48, v49
	ds_bpermute_b32 v56, v179, v55
	v_add_f32_e32 v34, v160, v143
	v_add_f32_e32 v34, v142, v34
	s_waitcnt lgkmcnt(0)
	v_max_f32_e32 v56, v56, v56
	v_max_f32_e32 v55, v55, v56
	v_cmp_gt_f32_e32 vcc, v55, v50
	s_cbranch_vccz .LBB0_392
	v_max_f32_e32 v55, v55, v55
	v_max_f32_e32 v56, v50, v50
	v_max_f32_e32 v55, v56, v55
	v_sub_f32_e32 v50, v50, v55
	v_exp_f32_e32 v50, v50
	s_nop 0
	v_pk_mul_f32 v[32:33], v[32:33], v[50:51] op_sel_hi:[1,0]
	v_pk_mul_f32 v[30:31], v[30:31], v[50:51] op_sel_hi:[1,0]
	v_pk_mul_f32 v[28:29], v[28:29], v[50:51] op_sel_hi:[1,0]
	v_pk_mul_f32 v[26:27], v[26:27], v[50:51] op_sel_hi:[1,0]
	v_pk_mul_f32 v[24:25], v[24:25], v[50:51] op_sel_hi:[1,0]
	v_pk_mul_f32 v[22:23], v[22:23], v[50:51] op_sel_hi:[1,0]
	v_pk_mul_f32 v[20:21], v[20:21], v[50:51] op_sel_hi:[1,0]
	v_pk_mul_f32 v[18:19], v[18:19], v[50:51] op_sel_hi:[1,0]
	v_pk_mul_f32 v[16:17], v[16:17], v[50:51] op_sel_hi:[1,0]
	v_pk_mul_f32 v[14:15], v[14:15], v[50:51] op_sel_hi:[1,0]
	v_pk_mul_f32 v[12:13], v[12:13], v[50:51] op_sel_hi:[1,0]
	v_pk_mul_f32 v[10:11], v[10:11], v[50:51] op_sel_hi:[1,0]
	v_pk_mul_f32 v[8:9], v[8:9], v[50:51] op_sel_hi:[1,0]
	v_pk_mul_f32 v[6:7], v[6:7], v[50:51] op_sel_hi:[1,0]
	v_pk_mul_f32 v[4:5], v[4:5], v[50:51] op_sel_hi:[1,0]
	v_pk_mul_f32 v[2:3], v[2:3], v[50:51] op_sel_hi:[1,0]
	v_mul_f32_e32 v34, v34, v50
	v_mov_b32_e32 v50, v55

; __device__ __forceinline__ float bf_lo(unsigned w) { return __uint_as_float(w << 16); }
; template <int STAGE, int OFF> __device__ __forceinline__ void attn32_unit(const bf16* base, bf16* yrow0, int blk0, int u, LAS unsigned char* xtab, LAS unsigned char* kbuf, LAS unsigned char* vbuf, int lane, ...
;     ...
;     } else {
; #pragma unroll
;         for (int mb = 0; mb < 2; ++mb)
; #pragma unroll
;             for (int gq = 0; gq < 4; ++gq) { const v2u w = *(const LAS v2u*)(xrow + 2 * (32 * mb + 8 * gq + 4 * h)); o[mb][4 * gq] = bf_lo(w.x); o[mb][4 * gq + 1] = bf_hi(w.x); o[mb][4 * gq + 2] = bf_lo(w.y); o[mb][4 * gq + 3] = bf_hi(w.y); }
;         m = *(const LAS float*)(xrow + 128); l = h == 0 ? *(const LAS float*)(xrow + 132) : 0.f;
;     }
;     const int hi = qi, lo = max(qi - 128, -(t0 >> SH));
;     const unsigned mspan = (unsigned)(hi - lo);
; #pragma unroll
;     for (int pp = 0; pp < 5; ++pp) {
;         constexpr int dummy = 0; (void)dummy;
;         const int set = (pp + OFF) % 2, n0 = -128 + 32 * pp;
; #pragma unroll
;         for (int c = 0; c < 4; ++c) { *(LAS v4u*)(kbuf + (8 * c + lrow) * 144 + lch * 16) = kr[set][c]; *(LAS v4u*)(vbuf + (8 * c + lrow) * 160 + lch * 16) = vr[set][c]; }
;         if (pp + 2 < 5) { ATT32_LOAD(set, pp + 2, t0, SH); }
;         else { const bf16* base_ = base; { const bf16* base = nbase; ATT32_LOAD(set, pp + 2 - 5, nt0, nsh); } (void)base_; }
;         f32x16 sc;
; #pragma unroll
;         for (int i = 0; i < 16; ++i) sc[i] = 0.f;
; #pragma unroll
;         for (int ks = 0; ks < 4; ++ks) { const bf16x8 ka = *(const LAS bf16x8*)(kbuf + qi * 144 + 32 * ks + 16 * h); sc = MFMA32(ka, qb[ks], sc); }
;         if (pp == 4) {
; #pragma unroll
;             for (int ks = 0; ks < 4; ++ks) qb[ks] = *(const bf16x8*)(nbase + (size_t)min(nt0 + (qi << nsh), SEQ - 1) * 1536 + 16 * ks + 8 * h);
;         }
;         const int mbase = n0 + 4 * h - lo; float mx = -INFINITY;
; #pragma unroll
;         for (int rg = 0; rg < 16; ++rg) { sc[rg] = ((unsigned)(mbase + (rg & 3) + 8 * (rg >> 2)) <= mspan) ? sc[rg] : -INFINITY; mx = fmaxf(mx, sc[rg]); }
;         mx = fmaxf(mx, __shfl_xor(mx, 32));
;         if (__any(mx > m)) {
;             const float mn = fmaxf(m, mx), alpha = __builtin_amdgcn_exp2f(m - mn); m = mn; l *= alpha;
; #pragma unroll
;             for (int i = 0; i < 16; ++i) { o[0][i] *= alpha; o[1][i] *= alpha; }
;         }
.LBB0_394:
	s_or_b64 exec, exec, s[14:15]
	v_add_u32_e32 v51, v206, v166
	ds_read2_b64 v[10:13], v51 offset1:2
	ds_read2_b64 v[2:5], v51 offset0:4 offset1:6
	ds_read2_b64 v[6:9], v51 offset0:8 offset1:10
	ds_read2_b64 v[14:17], v51 offset0:12 offset1:14
	ds_read_b32 v50, v206 offset:128
	v_mov_b32_e32 v138, 0
	s_and_saveexec_b64 s[14:15], s[4:5]
	ds_read_b32 v138, v206 offset:132
	s_or_b64 exec, exec, s[14:15]
	s_waitcnt vmcnt(19)
	ds_write_b128 v231, v[106:109]
	s_waitcnt vmcnt(18)
	ds_write_b128 v232, v[110:113] offset:4608
	s_waitcnt vmcnt(17)
	ds_write_b128 v231, v[114:117] offset:1152
	s_waitcnt vmcnt(16)
	ds_write_b128 v232, v[118:121] offset:5888
	s_waitcnt vmcnt(15)
	ds_write_b128 v231, v[122:125] offset:2304
	s_waitcnt vmcnt(14)
	ds_write_b128 v232, v[126:129] offset:7168
	s_waitcnt vmcnt(13)
	ds_write_b128 v231, v[130:133] offset:3456
	s_waitcnt vmcnt(12)
	ds_write_b128 v232, v[134:137] offset:8448
	s_waitcnt lgkmcnt(14)
	ds_read_b128 v[34:37], v177
	s_waitcnt lgkmcnt(13)
	v_lshlrev_b32_e32 v22, 16, v12
	v_and_b32_e32 v23, 0xffff0000, v12
	v_add_u32_e32 v12, s10, v195
	v_med3_i32 v12, v12, 0, v233
	v_mul_u32_u24_e32 v12, 0xc00, v12
	v_or_b32_e32 v12, v12, v176
	global_load_dwordx4 v[54:57], v12, s[8:9] offset:1024
	global_load_dwordx4 v[106:109], v12, s[8:9] offset:2048
	ds_read_b128 v[118:121], v177 offset:32
	v_add_u32_e32 v12, s10, v196
	s_waitcnt vmcnt(5) lgkmcnt(1)
	v_mfma_f32_32x32x16_bf16 v[34:49], v[34:37], v[70:73], 0
	v_med3_i32 v12, v12, 0, v233
	v_mul_u32_u24_e32 v12, 0xc00, v12
	v_or_b32_e32 v12, v12, v176
	global_load_dwordx4 v[110:113], v12, s[8:9] offset:1024
	global_load_dwordx4 v[114:117], v12, s[8:9] offset:2048
	v_add_u32_e32 v12, s10, v197
	v_med3_i32 v12, v12, 0, v233
	v_mul_u32_u24_e32 v12, 0xc00, v12
	v_or_b32_e32 v12, v12, v176
	ds_read_b128 v[134:137], v177 offset:96
	ds_read_b128 v[140:143], v177 offset:64
	s_waitcnt vmcnt(6) lgkmcnt(2)
	v_mfma_f32_32x32x16_bf16 v[34:49], v[118:121], v[66:69], v[34:49]
	global_load_dwordx4 v[118:121], v12, s[8:9] offset:1024
	global_load_dwordx4 v[122:125], v12, s[8:9] offset:2048
	v_add_u32_e32 v12, s10, v198
	v_med3_i32 v12, v12, 0, v233
	v_mul_u32_u24_e32 v12, 0xc00, v12
	v_or_b32_e32 v12, v12, v176
	global_load_dwordx4 v[126:129], v12, s[8:9] offset:1024
	global_load_dwordx4 v[130:133], v12, s[8:9] offset:2048
	s_lshr_b32 s0, s10, 2
	s_waitcnt vmcnt(9) lgkmcnt(0)
	v_mfma_f32_32x32x16_bf16 v[34:49], v[140:143], v[62:65], v[34:49]
	s_sub_i32 s0, 0, s0
	v_lshlrev_b32_e32 v18, 16, v10
	v_and_b32_e32 v19, 0xffff0000, v10
	v_lshlrev_b32_e32 v20, 16, v11
	v_and_b32_e32 v21, 0xffff0000, v11
	v_lshlrev_b32_e32 v10, 16, v14
	v_and_b32_e32 v11, 0xffff0000, v14
	s_waitcnt vmcnt(8)
	v_mfma_f32_32x32x16_bf16 v[34:49], v[134:137], v[58:61], v[34:49]
	v_max_i32_e32 v14, s0, v175
	v_sub_u32_e32 v163, v1, v14
	v_sub_u32_e32 v164, v178, v14
	v_lshlrev_b32_e32 v24, 16, v13
	v_and_b32_e32 v25, 0xffff0000, v13
	v_lshlrev_b32_e32 v12, 16, v15
	v_and_b32_e32 v13, 0xffff0000, v15
	s_nop 2
	v_add_u32_e32 v253, 27, v164
	v_cmp_le_i32_e32 vcc, 27, v253
	v_cmp_le_i32_e64 s[98:99], 26, v253
	v_cmp_le_i32_e64 s[100:101], 25, v253
	v_cndmask_b32_e32 v34, v234, v34, vcc
	v_lshlrev_b32_e32 v26, 16, v2
	v_cmp_le_i32_e32 vcc, 24, v253
	v_cndmask_b32_e64 v35, v234, v35, s[98:99]
	v_max3_f32 v14, v34, s31, v35
	v_cmp_le_i32_e64 s[98:99], 19, v253
	v_cndmask_b32_e64 v36, v234, v36, s[100:101]
	v_and_b32_e32 v27, 0xffff0000, v2
	v_cmp_le_i32_e64 s[100:101], 18, v253
	v_cndmask_b32_e32 v37, v234, v37, vcc
	v_max3_f32 v14, v14, v36, v37
	v_cmp_le_i32_e32 vcc, 17, v253
	v_cndmask_b32_e64 v38, v234, v38, s[98:99]
	v_lshlrev_b32_e32 v28, 16, v3
	v_cmp_le_i32_e64 s[98:99], 16, v253
	v_cndmask_b32_e64 v39, v234, v39, s[100:101]
	v_max3_f32 v14, v14, v38, v39
	v_cmp_le_i32_e64 s[100:101], 11, v253
	v_cndmask_b32_e32 v40, v234, v40, vcc
	v_and_b32_e32 v29, 0xffff0000, v3
	v_cmp_le_i32_e32 vcc, 10, v253
	v_cndmask_b32_e64 v41, v234, v41, s[98:99]
	v_max3_f32 v14, v14, v40, v41
	v_cmp_le_i32_e64 s[98:99], 9, v253
	v_cndmask_b32_e64 v42, v234, v42, s[100:101]
	v_lshlrev_b32_e32 v30, 16, v4
	v_cmp_le_i32_e64 s[100:101], 8, v253
	v_cndmask_b32_e32 v43, v234, v43, vcc
	v_max3_f32 v14, v14, v42, v43
	v_cmp_le_i32_e32 vcc, 3, v253
	v_cndmask_b32_e64 v44, v234, v44, s[98:99]
	v_and_b32_e32 v31, 0xffff0000, v4
	v_cmp_le_i32_e64 s[98:99], 2, v253
	v_cndmask_b32_e64 v45, v234, v45, s[100:101]
	v_max3_f32 v14, v14, v44, v45
	v_cmp_le_i32_e64 s[100:101], 1, v253
	v_cndmask_b32_e32 v46, v234, v46, vcc
	v_lshlrev_b32_e32 v32, 16, v5
	v_cmp_le_i32_e32 vcc, 0, v253
	v_cndmask_b32_e64 v47, v234, v47, s[98:99]
	v_max3_f32 v14, v14, v46, v47
	v_cndmask_b32_e64 v48, v234, v48, s[100:101]
	v_and_b32_e32 v33, 0xffff0000, v5
	v_lshlrev_b32_e32 v2, 16, v6
	v_cndmask_b32_e32 v49, v234, v49, vcc
	v_max3_f32 v134, v14, v48, v49
	ds_bpermute_b32 v135, v179, v134
	v_and_b32_e32 v3, 0xffff0000, v6
	v_lshlrev_b32_e32 v4, 16, v7
	v_and_b32_e32 v5, 0xffff0000, v7
	v_lshlrev_b32_e32 v6, 16, v8
	s_waitcnt lgkmcnt(0)
	v_max_f32_e32 v135, v135, v135
	v_max_f32_e32 v134, v134, v135
	v_and_b32_e32 v7, 0xffff0000, v8
	v_lshlrev_b32_e32 v8, 16, v9
	v_and_b32_e32 v9, 0xffff0000, v9
	v_lshlrev_b32_e32 v14, 16, v16
	v_and_b32_e32 v15, 0xffff0000, v16
	v_lshlrev_b32_e32 v16, 16, v17
	v_and_b32_e32 v17, 0xffff0000, v17
	v_cmp_gt_f32_e32 vcc, v134, v50
	s_cbranch_vccz .LBB0_398
	v_max_f32_e32 v134, v134, v134
	v_max_f32_e32 v135, v50, v50
	v_max_f32_e32 v134, v135, v134
	v_sub_f32_e32 v50, v50, v134
	v_exp_f32_e32 v50, v50
	s_nop 0
	v_pk_mul_f32 v[16:17], v[50:51], v[16:17] op_sel_hi:[0,1]
	v_pk_mul_f32 v[14:15], v[50:51], v[14:15] op_sel_hi:[0,1]
	v_pk_mul_f32 v[12:13], v[50:51], v[12:13] op_sel_hi:[0,1]
	v_pk_mul_f32 v[10:11], v[50:51], v[10:11] op_sel_hi:[0,1]
	v_pk_mul_f32 v[8:9], v[50:51], v[8:9] op_sel_hi:[0,1]
	v_pk_mul_f32 v[6:7], v[50:51], v[6:7] op_sel_hi:[0,1]
	v_pk_mul_f32 v[4:5], v[50:51], v[4:5] op_sel_hi:[0,1]
	v_pk_mul_f32 v[2:3], v[50:51], v[2:3] op_sel_hi:[0,1]
	v_pk_mul_f32 v[32:33], v[50:51], v[32:33] op_sel_hi:[0,1]
	v_pk_mul_f32 v[30:31], v[50:51], v[30:31] op_sel_hi:[0,1]
	v_pk_mul_f32 v[28:29], v[50:51], v[28:29] op_sel_hi:[0,1]
	v_pk_mul_f32 v[26:27], v[50:51], v[26:27] op_sel_hi:[0,1]
	v_pk_mul_f32 v[24:25], v[50:51], v[24:25] op_sel_hi:[0,1]
	v_pk_mul_f32 v[22:23], v[50:51], v[22:23] op_sel_hi:[0,1]
	v_pk_mul_f32 v[20:21], v[50:51], v[20:21] op_sel_hi:[0,1]
	v_pk_mul_f32 v[18:19], v[50:51], v[18:19] op_sel_hi:[0,1]
	v_mul_f32_e32 v138, v138, v50
	v_mov_b32_e32 v50, v134
; #define LAS __attribute__((address_space(3)))
; template <int STAGE, int OFF> __device__ __forceinline__ void attn32_unit(const bf16* base, bf16* yrow0, int blk0, int u, LAS unsigned char* xtab, LAS unsigned char* kbuf, LAS unsigned char* vbuf, int lane, ...
;     ...
;         for (int c = 0; c < 4; ++c) { *(LAS v4u*)(kbuf + (8 * c + lrow) * 144 + lch * 16) = kr[set][c]; *(LAS v4u*)(vbuf + (8 * c + lrow) * 160 + lch * 16) = vr[set][c]; }
;         if (pp + 2 < 5) { ATT32_LOAD(set, pp + 2, t0, SH); }
;         else { const bf16* base_ = base; { const bf16* base = nbase; ATT32_LOAD(set, pp + 2 - 5, nt0, nsh); } (void)base_; }
;         f32x16 sc;
; #pragma unroll
;         for (int i = 0; i < 16; ++i) sc[i] = 0.f;
; #pragma unroll
;         for (int ks = 0; ks < 4; ++ks) { const bf16x8 ka = *(const LAS bf16x8*)(kbuf + qi * 144 + 32 * ks + 16 * h); sc = MFMA32(ka, qb[ks], sc); }
;         if (pp == 4) {
; #pragma unroll
;             for (int ks = 0; ks < 4; ++ks) qb[ks] = *(const bf16x8*)(nbase + (size_t)min(nt0 + (qi << nsh), SEQ - 1) * 1536 + 16 * ks + 8 * h);
;         }
;         const int mbase = n0 + 4 * h - lo; float mx = -INFINITY;
; #pragma unroll
;         for (int rg = 0; rg < 16; ++rg) { sc[rg] = ((unsigned)(mbase + (rg & 3) + 8 * (rg >> 2)) <= mspan) ? sc[rg] : -INFINITY; mx = fmaxf(mx, sc[rg]); }
;         mx = fmaxf(mx, __shfl_xor(mx, 32));
;         if (__any(mx > m)) {
;             const float mn = fmaxf(m, mx), alpha = __builtin_amdgcn_exp2f(m - mn); m = mn; l *= alpha;
; #pragma unroll
;             for (int i = 0; i < 16; ++i) { o[0][i] *= alpha; o[1][i] *= alpha; }
;         }
;         float ps = 0.f;
; #pragma unroll
;         for (int rg = 0; rg < 16; ++rg) { sc[rg] = __builtin_amdgcn_exp2f(sc[rg] - m); ps += sc[rg]; }
;         l += ps;
;         bf16x8 pb[2];
; #pragma unroll
;         for (int s2 = 0; s2 < 2; ++s2) { v4u w; w.x = pg8::cvt_pk_bf16(sc[8 * s2], sc[8 * s2 + 1]); w.y = pg8::cvt_pk_bf16(sc[8 * s2 + 2], sc[8 * s2 + 3]); w.z = pg8::cvt_pk_bf16(sc[8 * s2 + 4], sc[8 * s2 + 5]); w.w = pg8::cvt_pk_bf16(sc[8 * s2 + 6], sc[8 * s2 + 7]); pb[s2] = __builtin_bit_cast(bf16x8, w); }
; #pragma unroll
;         for (int mb = 0; mb < 2; ++mb)
; #pragma unroll
;             for (int s2 = 0; s2 < 2; ++s2) {
;                 LAS unsigned char* vp = vbuf + tr_off + (16 * s2) * 160 + 64 * mb;
.LBB0_398:
	v_sub_f32_e32 v34, v34, v50
	v_exp_f32_e32 v134, v34
	v_sub_f32_e32 v34, v35, v50
	v_exp_f32_e32 v135, v34
	v_sub_f32_e32 v34, v36, v50
	v_exp_f32_e32 v136, v34
	v_sub_f32_e32 v34, v37, v50
	v_exp_f32_e32 v137, v34
	v_sub_f32_e32 v34, v38, v50
	v_exp_f32_e32 v139, v34
	v_sub_f32_e32 v34, v39, v50
	v_exp_f32_e32 v140, v34
	v_sub_f32_e32 v34, v40, v50
	v_exp_f32_e32 v141, v34
	v_sub_f32_e32 v34, v41, v50
	v_exp_f32_e32 v142, v34
	v_sub_f32_e32 v34, v42, v50
	v_exp_f32_e32 v162, v34
	v_sub_f32_e32 v34, v43, v50
	v_exp_f32_e32 v165, v34
	v_sub_f32_e32 v34, v44, v50
	v_exp_f32_e32 v171, v34
	v_sub_f32_e32 v34, v45, v50
	v_exp_f32_e32 v172, v34
	v_sub_f32_e32 v34, v46, v50
	v_exp_f32_e32 v173, v34
	v_sub_f32_e32 v34, v47, v50
	v_exp_f32_e32 v237, v34
	v_sub_f32_e32 v34, v48, v50
	v_exp_f32_e32 v246, v34
	v_sub_f32_e32 v34, v49, v50
	v_exp_f32_e32 v247, v34
	v_cvt_pk_bf16_f32 v34, v134, v135
	v_cvt_pk_bf16_f32 v35, v136, v137
	v_cvt_pk_bf16_f32 v36, v139, v140
	v_cvt_pk_bf16_f32 v37, v141, v142
	v_cvt_pk_bf16_f32 v238, v162, v165
	v_cvt_pk_bf16_f32 v239, v171, v172
	v_cvt_pk_bf16_f32 v240, v173, v237
	v_cvt_pk_bf16_f32 v241, v246, v247
	ds_read_b64_tr_b16 v[38:39], v181 offset:4608
	ds_read_b64_tr_b16 v[40:41], v181 offset:5888
	ds_read_b64_tr_b16 v[44:45], v181 offset:5952
	ds_read_b64_tr_b16 v[42:43], v181 offset:4672
	s_waitcnt lgkmcnt(2)
	v_mfma_f32_32x32x16_bf16 v[18:33], v[38:41], v[34:37], v[18:33]
	ds_read_b64_tr_b16 v[38:39], v181 offset:7168
	ds_read_b64_tr_b16 v[40:41], v181 offset:8448
	v_add_f32_e32 v46, 0, v134
	ds_read_b64_tr_b16 v[244:245], v181 offset:8512
	ds_read_b64_tr_b16 v[242:243], v181 offset:7232
	ds_write_b128 v231, v[74:77]
	ds_write_b128 v232, v[78:81] offset:4608
	ds_write_b128 v231, v[82:85] offset:1152
	ds_write_b128 v232, v[86:89] offset:5888
	ds_write_b128 v231, v[90:93] offset:2304
	ds_write_b128 v232, v[94:97] offset:7168
	ds_write_b128 v231, v[98:101] offset:3456
	ds_write_b128 v232, v[102:105] offset:8448
	s_waitcnt lgkmcnt(10)
	v_mfma_f32_32x32x16_bf16 v[18:33], v[38:41], v[238:241], v[18:33]
	v_add_f32_e32 v38, v135, v46
	v_add_f32_e32 v38, v136, v38
	v_add_f32_e32 v38, v137, v38
	v_add_f32_e32 v38, v139, v38
	v_add_f32_e32 v38, v140, v38
	v_add_f32_e32 v38, v141, v38
	v_add_f32_e32 v139, v142, v38
	v_mfma_f32_32x32x16_bf16 v[2:17], v[42:45], v[34:37], v[2:17]
	v_add_u32_e32 v34, s10, v199
	v_med3_i32 v34, v34, 0, v233
	v_mul_u32_u24_e32 v38, 0xc00, v34
	ds_read_b128 v[34:37], v177
	v_or_b32_e32 v38, v38, v176
	global_load_dwordx4 v[86:89], v38, s[8:9] offset:1024
	global_load_dwordx4 v[90:93], v38, s[8:9] offset:2048
	v_add_u32_e32 v38, s10, v200
	v_med3_i32 v38, v38, 0, v233
	v_mul_u32_u24_e32 v38, 0xc00, v38
	ds_read_b128 v[74:77], v177 offset:32
	v_or_b32_e32 v78, v38, v176
	s_waitcnt lgkmcnt(1)
	v_mfma_f32_32x32x16_bf16 v[34:49], v[34:37], v[70:73], 0
	global_load_dwordx4 v[134:137], v78, s[8:9] offset:1024
	global_load_dwordx4 v[142:145], v78, s[8:9] offset:2048
	v_add_u32_e32 v78, s10, v201
	v_med3_i32 v78, v78, 0, v233
	v_mul_u32_u24_e32 v78, 0xc00, v78
	v_or_b32_e32 v94, v78, v176
	ds_read_b128 v[78:81], v177 offset:96
	ds_read_b128 v[82:85], v177 offset:64
	global_load_dwordx4 v[146:149], v94, s[8:9] offset:1024
	global_load_dwordx4 v[150:153], v94, s[8:9] offset:2048
	s_waitcnt lgkmcnt(2)
	v_mfma_f32_32x32x16_bf16 v[34:49], v[74:77], v[66:69], v[34:49]
	v_add_u32_e32 v74, s10, v202
	v_med3_i32 v74, v74, 0, v233
	v_mul_u32_u24_e32 v74, 0xc00, v74
	v_or_b32_e32 v74, v74, v176
	global_load_dwordx4 v[154:157], v74, s[8:9] offset:1024
	global_load_dwordx4 v[158:161], v74, s[8:9] offset:2048
	s_waitcnt lgkmcnt(0)
	v_mfma_f32_32x32x16_bf16 v[34:49], v[82:85], v[62:65], v[34:49]
	v_add_f32_e32 v74, v162, v139
	v_add_f32_e32 v74, v165, v74
	v_add_f32_e32 v74, v171, v74
	v_add_f32_e32 v74, v172, v74
	v_add_f32_e32 v74, v173, v74
	v_mfma_f32_32x32x16_bf16 v[34:49], v[78:81], v[58:61], v[34:49]
	v_add_f32_e32 v74, v237, v74
	v_add_f32_e32 v74, v246, v74
	v_add_f32_e32 v74, v247, v74
	v_add_f32_e32 v162, v138, v74
	v_mfma_f32_32x32x16_bf16 v[2:17], v[242:245], v[238:241], v[2:17]
	s_nop 6
	v_add_u32_e32 v253, 59, v164
	v_cmp_le_i32_e32 vcc, 27, v253
	v_cmp_le_i32_e64 s[98:99], 26, v253
	v_cmp_le_i32_e64 s[100:101], 25, v253
	v_cndmask_b32_e32 v34, v234, v34, vcc
	v_cmp_le_i32_e32 vcc, 24, v253
	v_cndmask_b32_e64 v35, v234, v35, s[98:99]
	v_max3_f32 v75, v34, s31, v35
	v_cmp_le_i32_e64 s[98:99], 19, v253
	v_cndmask_b32_e64 v36, v234, v36, s[100:101]
	v_cmp_le_i32_e64 s[100:101], 18, v253
	v_cndmask_b32_e32 v37, v234, v37, vcc
	v_max3_f32 v75, v75, v36, v37
	v_cmp_le_i32_e32 vcc, 17, v253
	v_cndmask_b32_e64 v38, v234, v38, s[98:99]
	v_cmp_le_i32_e64 s[98:99], 16, v253
	v_cndmask_b32_e64 v39, v234, v39, s[100:101]
	v_max3_f32 v75, v75, v38, v39
	v_cmp_le_i32_e64 s[100:101], 11, v253
	v_cndmask_b32_e32 v40, v234, v40, vcc
	v_cmp_le_i32_e32 vcc, 10, v253
	v_cndmask_b32_e64 v41, v234, v41, s[98:99]
	v_max3_f32 v75, v75, v40, v41
	v_cmp_le_i32_e64 s[98:99], 9, v253
	v_cndmask_b32_e64 v42, v234, v42, s[100:101]
	v_cmp_le_i32_e64 s[100:101], 8, v253
	v_cndmask_b32_e32 v43, v234, v43, vcc
	v_max3_f32 v75, v75, v42, v43
	v_cmp_le_i32_e32 vcc, 3, v253
	v_cndmask_b32_e64 v44, v234, v44, s[98:99]
	v_cmp_le_i32_e64 s[98:99], 2, v253
	v_cndmask_b32_e64 v45, v234, v45, s[100:101]
	v_max3_f32 v75, v75, v44, v45
	v_cmp_le_i32_e64 s[100:101], 1, v253
	v_cndmask_b32_e32 v46, v234, v46, vcc
	v_cmp_le_i32_e32 vcc, 0, v253
	v_cndmask_b32_e64 v47, v234, v47, s[98:99]
	v_max3_f32 v75, v75, v46, v47
	v_cndmask_b32_e64 v48, v234, v48, s[100:101]
	v_cndmask_b32_e32 v49, v234, v49, vcc
	v_max3_f32 v75, v75, v48, v49
	ds_bpermute_b32 v76, v179, v75
	s_waitcnt lgkmcnt(0)
	v_max_f32_e32 v74, v76, v76
	v_max_f32_e32 v74, v75, v74
	v_cmp_gt_f32_e32 vcc, v74, v50
	s_cbranch_vccz .LBB0_400
	v_max_f32_e32 v74, v74, v74
	v_max_f32_e32 v75, v50, v50
	v_max_f32_e32 v74, v75, v74
	v_sub_f32_e32 v50, v50, v74
	v_exp_f32_e32 v50, v50
	s_nop 0
	v_pk_mul_f32 v[32:33], v[32:33], v[50:51] op_sel_hi:[1,0]
	v_pk_mul_f32 v[30:31], v[30:31], v[50:51] op_sel_hi:[1,0]
	v_pk_mul_f32 v[28:29], v[28:29], v[50:51] op_sel_hi:[1,0]
	v_pk_mul_f32 v[26:27], v[26:27], v[50:51] op_sel_hi:[1,0]
	v_pk_mul_f32 v[24:25], v[24:25], v[50:51] op_sel_hi:[1,0]
	v_pk_mul_f32 v[22:23], v[22:23], v[50:51] op_sel_hi:[1,0]
	v_pk_mul_f32 v[20:21], v[20:21], v[50:51] op_sel_hi:[1,0]
	v_pk_mul_f32 v[18:19], v[18:19], v[50:51] op_sel_hi:[1,0]
	v_pk_mul_f32 v[16:17], v[16:17], v[50:51] op_sel_hi:[1,0]
	v_pk_mul_f32 v[14:15], v[14:15], v[50:51] op_sel_hi:[1,0]
	v_pk_mul_f32 v[12:13], v[12:13], v[50:51] op_sel_hi:[1,0]
	v_pk_mul_f32 v[10:11], v[10:11], v[50:51] op_sel_hi:[1,0]
	v_pk_mul_f32 v[8:9], v[8:9], v[50:51] op_sel_hi:[1,0]
	v_pk_mul_f32 v[6:7], v[6:7], v[50:51] op_sel_hi:[1,0]
	v_pk_mul_f32 v[4:5], v[4:5], v[50:51] op_sel_hi:[1,0]
	v_pk_mul_f32 v[2:3], v[2:3], v[50:51] op_sel_hi:[1,0]
	v_mul_f32_e32 v162, v162, v50
	v_mov_b32_e32 v50, v74
; #define LAS __attribute__((address_space(3)))
; template <int STAGE, int OFF> __device__ __forceinline__ void attn32_unit(const bf16* base, bf16* yrow0, int blk0, int u, LAS unsigned char* xtab, LAS unsigned char* kbuf, LAS unsigned char* vbuf, int lane, ...
;     ...
;         for (int c = 0; c < 4; ++c) { *(LAS v4u*)(kbuf + (8 * c + lrow) * 144 + lch * 16) = kr[set][c]; *(LAS v4u*)(vbuf + (8 * c + lrow) * 160 + lch * 16) = vr[set][c]; }
;         if (pp + 2 < 5) { ATT32_LOAD(set, pp + 2, t0, SH); }
;         else { const bf16* base_ = base; { const bf16* base = nbase; ATT32_LOAD(set, pp + 2 - 5, nt0, nsh); } (void)base_; }
;         f32x16 sc;
; #pragma unroll
;         for (int i = 0; i < 16; ++i) sc[i] = 0.f;
; #pragma unroll
;         for (int ks = 0; ks < 4; ++ks) { const bf16x8 ka = *(const LAS bf16x8*)(kbuf + qi * 144 + 32 * ks + 16 * h); sc = MFMA32(ka, qb[ks], sc); }
;         if (pp == 4) {
; #pragma unroll
;             for (int ks = 0; ks < 4; ++ks) qb[ks] = *(const bf16x8*)(nbase + (size_t)min(nt0 + (qi << nsh), SEQ - 1) * 1536 + 16 * ks + 8 * h);
;         }
;         const int mbase = n0 + 4 * h - lo; float mx = -INFINITY;
; #pragma unroll
;         for (int rg = 0; rg < 16; ++rg) { sc[rg] = ((unsigned)(mbase + (rg & 3) + 8 * (rg >> 2)) <= mspan) ? sc[rg] : -INFINITY; mx = fmaxf(mx, sc[rg]); }
;         mx = fmaxf(mx, __shfl_xor(mx, 32));
;         if (__any(mx > m)) {
;             const float mn = fmaxf(m, mx), alpha = __builtin_amdgcn_exp2f(m - mn); m = mn; l *= alpha;
; #pragma unroll
;             for (int i = 0; i < 16; ++i) { o[0][i] *= alpha; o[1][i] *= alpha; }
;         }
;         float ps = 0.f;
; #pragma unroll
;         for (int rg = 0; rg < 16; ++rg) { sc[rg] = __builtin_amdgcn_exp2f(sc[rg] - m); ps += sc[rg]; }
;         l += ps;
;         bf16x8 pb[2];
; #pragma unroll
;         for (int s2 = 0; s2 < 2; ++s2) { v4u w; w.x = pg8::cvt_pk_bf16(sc[8 * s2], sc[8 * s2 + 1]); w.y = pg8::cvt_pk_bf16(sc[8 * s2 + 2], sc[8 * s2 + 3]); w.z = pg8::cvt_pk_bf16(sc[8 * s2 + 4], sc[8 * s2 + 5]); w.w = pg8::cvt_pk_bf16(sc[8 * s2 + 6], sc[8 * s2 + 7]); pb[s2] = __builtin_bit_cast(bf16x8, w); }
; #pragma unroll
;         for (int mb = 0; mb < 2; ++mb)
; #pragma unroll
;             for (int s2 = 0; s2 < 2; ++s2) {
;                 LAS unsigned char* vp = vbuf + tr_off + (16 * s2) * 160 + 64 * mb;
.LBB0_400:
	v_sub_f32_e32 v34, v34, v50
	v_exp_f32_e32 v74, v34
	v_sub_f32_e32 v34, v35, v50
	v_exp_f32_e32 v75, v34
	v_sub_f32_e32 v34, v36, v50
	v_exp_f32_e32 v76, v34
	v_sub_f32_e32 v34, v37, v50
	v_exp_f32_e32 v77, v34
	v_sub_f32_e32 v34, v38, v50
	v_exp_f32_e32 v78, v34
	v_sub_f32_e32 v34, v39, v50
	v_exp_f32_e32 v79, v34
	v_sub_f32_e32 v34, v40, v50
	v_exp_f32_e32 v80, v34
	v_sub_f32_e32 v34, v41, v50
	v_exp_f32_e32 v81, v34
	v_sub_f32_e32 v34, v42, v50
	v_exp_f32_e32 v165, v34
	v_sub_f32_e32 v34, v43, v50
	v_exp_f32_e32 v171, v34
	v_sub_f32_e32 v34, v44, v50
	v_exp_f32_e32 v172, v34
	v_sub_f32_e32 v34, v45, v50
	v_exp_f32_e32 v173, v34
	v_sub_f32_e32 v34, v46, v50
	v_exp_f32_e32 v237, v34
	v_sub_f32_e32 v34, v47, v50
	v_exp_f32_e32 v246, v34
	v_sub_f32_e32 v34, v48, v50
	v_exp_f32_e32 v247, v34
	v_sub_f32_e32 v34, v49, v50
	v_exp_f32_e32 v248, v34
	v_cvt_pk_bf16_f32 v34, v74, v75
	v_cvt_pk_bf16_f32 v35, v76, v77
	v_cvt_pk_bf16_f32 v36, v78, v79
	v_cvt_pk_bf16_f32 v37, v80, v81
	v_cvt_pk_bf16_f32 v238, v165, v171
	v_cvt_pk_bf16_f32 v239, v172, v173
	v_cvt_pk_bf16_f32 v240, v237, v246
	v_cvt_pk_bf16_f32 v241, v247, v248
	ds_read_b64_tr_b16 v[38:39], v181 offset:4608
	ds_read_b64_tr_b16 v[40:41], v181 offset:5888
	ds_read_b64_tr_b16 v[44:45], v181 offset:5952
	ds_read_b64_tr_b16 v[42:43], v181 offset:4672
	s_waitcnt lgkmcnt(2)
	v_mfma_f32_32x32x16_bf16 v[18:33], v[38:41], v[34:37], v[18:33]
	ds_read_b64_tr_b16 v[38:39], v181 offset:7168
	ds_read_b64_tr_b16 v[40:41], v181 offset:8448
	v_add_f32_e32 v46, 0, v74
	ds_read_b64_tr_b16 v[244:245], v181 offset:8512
	ds_read_b64_tr_b16 v[242:243], v181 offset:7232
	s_waitcnt vmcnt(15)
	ds_write_b128 v231, v[54:57]
	s_waitcnt vmcnt(14)
	ds_write_b128 v232, v[106:109] offset:4608
	s_waitcnt vmcnt(13)
	ds_write_b128 v231, v[110:113] offset:1152
	s_waitcnt vmcnt(12)
	ds_write_b128 v232, v[114:117] offset:5888
	s_waitcnt vmcnt(11)
	ds_write_b128 v231, v[118:121] offset:2304
	s_waitcnt vmcnt(10)
	ds_write_b128 v232, v[122:125] offset:7168
	s_waitcnt vmcnt(9)
	ds_write_b128 v231, v[126:129] offset:3456
	s_waitcnt vmcnt(8)
	ds_write_b128 v232, v[130:133] offset:8448
	v_or_b32_e32 v98, s10, v204
	v_or_b32_e32 v102, s10, v205
	s_waitcnt lgkmcnt(10)
	v_mfma_f32_32x32x16_bf16 v[18:33], v[38:41], v[238:241], v[18:33]
	v_add_f32_e32 v38, v75, v46
	v_add_f32_e32 v38, v76, v38
	v_add_f32_e32 v38, v77, v38
	v_add_f32_e32 v38, v78, v38
	v_add_f32_e32 v38, v79, v38
	v_add_f32_e32 v38, v80, v38
	v_add_f32_e32 v249, v81, v38
	v_mfma_f32_32x32x16_bf16 v[2:17], v[42:45], v[34:37], v[2:17]
	v_or_b32_e32 v34, s10, v184
	v_min_u32_e32 v34, 0x3fff, v34
	v_mul_u32_u24_e32 v38, 0xc00, v34
	ds_read_b128 v[34:37], v177
	v_or_b32_e32 v38, v38, v176
	global_load_dwordx4 v[54:57], v38, s[8:9] offset:1024
	global_load_dwordx4 v[74:77], v38, s[8:9] offset:2048
	v_or_b32_e32 v38, s10, v203
	v_min_u32_e32 v38, 0x3fff, v38
	v_mul_u32_u24_e32 v38, 0xc00, v38
	ds_read_b128 v[94:97], v177 offset:32
	v_or_b32_e32 v82, v38, v176
	s_waitcnt lgkmcnt(1)
	v_mfma_f32_32x32x16_bf16 v[34:49], v[34:37], v[70:73], 0
	v_min_u32_e32 v98, 0x3fff, v98
	v_min_u32_e32 v102, 0x3fff, v102
	v_mul_u32_u24_e32 v98, 0xc00, v98
	v_mul_u32_u24_e32 v102, 0xc00, v102
	v_or_b32_e32 v98, v98, v176
	v_or_b32_e32 v114, v102, v176
	global_load_dwordx4 v[78:81], v82, s[8:9] offset:1024
	s_nop 0
	global_load_dwordx4 v[82:85], v82, s[8:9] offset:2048
	ds_read_b128 v[106:109], v177 offset:96
	ds_read_b128 v[110:113], v177 offset:64
	s_waitcnt lgkmcnt(2)
	v_mfma_f32_32x32x16_bf16 v[34:49], v[94:97], v[66:69], v[34:49]
	global_load_dwordx4 v[94:97], v98, s[8:9] offset:1024
	s_nop 0
	global_load_dwordx4 v[98:101], v98, s[8:9] offset:2048
	s_nop 0
	global_load_dwordx4 v[102:105], v114, s[8:9] offset:1024
	global_load_dwordx4 v[138:141], v114, s[8:9] offset:2048
	s_waitcnt lgkmcnt(0)
	v_mfma_f32_32x32x16_bf16 v[34:49], v[110:113], v[62:65], v[34:49]
	v_add_f32_e32 v110, v165, v249
	v_add_f32_e32 v110, v171, v110
	v_add_f32_e32 v110, v172, v110
	v_add_f32_e32 v110, v173, v110
	v_add_f32_e32 v110, v237, v110
	v_add_f32_e32 v110, v246, v110
	v_add_f32_e32 v110, v247, v110
	v_mfma_f32_32x32x16_bf16 v[34:49], v[106:109], v[58:61], v[34:49]
	v_add_f32_e32 v108, v248, v110
	v_add_f32_e32 v162, v162, v108
	s_nop 5
	v_add_u32_e32 v253, 91, v164
	v_cmp_le_i32_e32 vcc, 27, v253
	v_cmp_le_i32_e64 s[98:99], 26, v253
	v_cmp_le_i32_e64 s[100:101], 25, v253
	v_cndmask_b32_e32 v34, v234, v34, vcc
	v_mfma_f32_32x32x16_bf16 v[2:17], v[242:245], v[238:241], v[2:17]
	v_cmp_le_i32_e32 vcc, 24, v253
	v_cndmask_b32_e64 v35, v234, v35, s[98:99]
	v_max3_f32 v106, v34, s31, v35
	v_cmp_le_i32_e64 s[98:99], 19, v253
	v_cndmask_b32_e64 v36, v234, v36, s[100:101]
	v_cmp_le_i32_e64 s[100:101], 18, v253
	v_cndmask_b32_e32 v37, v234, v37, vcc
	v_max3_f32 v106, v106, v36, v37
	v_cmp_le_i32_e32 vcc, 17, v253
	v_cndmask_b32_e64 v38, v234, v38, s[98:99]
	v_cmp_le_i32_e64 s[98:99], 16, v253
	v_cndmask_b32_e64 v39, v234, v39, s[100:101]
	v_max3_f32 v106, v106, v38, v39
	v_cmp_le_i32_e64 s[100:101], 11, v253
	v_cndmask_b32_e32 v40, v234, v40, vcc
	v_cmp_le_i32_e32 vcc, 10, v253
	v_cndmask_b32_e64 v41, v234, v41, s[98:99]
	v_max3_f32 v106, v106, v40, v41
	v_cmp_le_i32_e64 s[98:99], 9, v253
	v_cndmask_b32_e64 v42, v234, v42, s[100:101]
	v_cmp_le_i32_e64 s[100:101], 8, v253
	v_cndmask_b32_e32 v43, v234, v43, vcc
	v_max3_f32 v106, v106, v42, v43
	v_cmp_le_i32_e32 vcc, 3, v253
	v_cndmask_b32_e64 v44, v234, v44, s[98:99]
	v_cmp_le_i32_e64 s[98:99], 2, v253
	v_cndmask_b32_e64 v45, v234, v45, s[100:101]
	v_max3_f32 v106, v106, v44, v45
	v_cmp_le_i32_e64 s[100:101], 1, v253
	v_cndmask_b32_e32 v46, v234, v46, vcc
	v_cmp_le_i32_e32 vcc, 0, v253
	v_cndmask_b32_e64 v47, v234, v47, s[98:99]
	v_max3_f32 v106, v106, v46, v47
	v_cndmask_b32_e64 v48, v234, v48, s[100:101]
	v_cndmask_b32_e32 v49, v234, v49, vcc
	v_max3_f32 v106, v106, v48, v49
	ds_bpermute_b32 v107, v179, v106
	s_waitcnt lgkmcnt(0)
	v_max_f32_e32 v107, v107, v107
	v_max_f32_e32 v106, v106, v107
	v_cmp_gt_f32_e32 vcc, v106, v50
	s_cbranch_vccz .LBB0_402
; __device__ __forceinline__ unsigned cvt_pk_bf16(float lo, float hi) { unsigned r; asm volatile("v_cvt_pk_bf16_f32 %0, %1, %2" : "=v"(r) : "v"(lo), "v"(hi)); return r; }
; #define LAS __attribute__((address_space(3)))
; #define MFMA32(a, b, c) __builtin_amdgcn_mfma_f32_32x32x16_bf16((a), (b), (c), 0, 0, 0)
; template <int STAGE, int OFF> __device__ __forceinline__ void attn32_unit(const bf16* base, bf16* yrow0, int blk0, int u, LAS unsigned char* xtab, LAS unsigned char* kbuf, LAS unsigned char* vbuf, int lane, ...
;     ...
;         if (__any(mx > m)) {
;             const float mn = fmaxf(m, mx), alpha = __builtin_amdgcn_exp2f(m - mn); m = mn; l *= alpha;
; #pragma unroll
;             for (int i = 0; i < 16; ++i) { o[0][i] *= alpha; o[1][i] *= alpha; }
;         }
;         float ps = 0.f;
; #pragma unroll
;         for (int rg = 0; rg < 16; ++rg) { sc[rg] = __builtin_amdgcn_exp2f(sc[rg] - m); ps += sc[rg]; }
;         l += ps;
;         bf16x8 pb[2];
; #pragma unroll
;         for (int s2 = 0; s2 < 2; ++s2) { v4u w; w.x = pg8::cvt_pk_bf16(sc[8 * s2], sc[8 * s2 + 1]); w.y = pg8::cvt_pk_bf16(sc[8 * s2 + 2], sc[8 * s2 + 3]); w.z = pg8::cvt_pk_bf16(sc[8 * s2 + 4], sc[8 * s2 + 5]); w.w = pg8::cvt_pk_bf16(sc[8 * s2 + 6], sc[8 * s2 + 7]); pb[s2] = __builtin_bit_cast(bf16x8, w); }
; #pragma unroll
;         for (int mb = 0; mb < 2; ++mb)
; #pragma unroll
;             for (int s2 = 0; s2 < 2; ++s2) {
;                 LAS unsigned char* vp = vbuf + tr_off + (16 * s2) * 160 + 64 * mb;
;                 const v4i16 a0 = __builtin_amdgcn_ds_read_tr16_b64_v4i16((LAS v4i16*)vp), a1 = __builtin_amdgcn_ds_read_tr16_b64_v4i16((LAS v4i16*)(vp + 8 * 160));
;                 const bf16x8 va = __builtin_shufflevector(a0, a1, 0, 1, 2, 3, 4, 5, 6, 7);
;                 o[mb] = MFMA32(va, pb[s2], o[mb]);
	v_max_f32_e32 v106, v106, v106
	v_max_f32_e32 v107, v50, v50
	v_max_f32_e32 v106, v107, v106
	v_sub_f32_e32 v50, v50, v106
	v_exp_f32_e32 v50, v50
	s_nop 0
	v_pk_mul_f32 v[32:33], v[32:33], v[50:51] op_sel_hi:[1,0]
	v_pk_mul_f32 v[30:31], v[30:31], v[50:51] op_sel_hi:[1,0]
	v_pk_mul_f32 v[28:29], v[28:29], v[50:51] op_sel_hi:[1,0]
	v_pk_mul_f32 v[26:27], v[26:27], v[50:51] op_sel_hi:[1,0]
	v_pk_mul_f32 v[24:25], v[24:25], v[50:51] op_sel_hi:[1,0]
	v_pk_mul_f32 v[22:23], v[22:23], v[50:51] op_sel_hi:[1,0]
	v_pk_mul_f32 v[20:21], v[20:21], v[50:51] op_sel_hi:[1,0]
	v_pk_mul_f32 v[18:19], v[18:19], v[50:51] op_sel_hi:[1,0]
	v_pk_mul_f32 v[16:17], v[16:17], v[50:51] op_sel_hi:[1,0]
	v_pk_mul_f32 v[14:15], v[14:15], v[50:51] op_sel_hi:[1,0]
	v_pk_mul_f32 v[12:13], v[12:13], v[50:51] op_sel_hi:[1,0]
	v_pk_mul_f32 v[10:11], v[10:11], v[50:51] op_sel_hi:[1,0]
	v_pk_mul_f32 v[8:9], v[8:9], v[50:51] op_sel_hi:[1,0]
	v_pk_mul_f32 v[6:7], v[6:7], v[50:51] op_sel_hi:[1,0]
	v_pk_mul_f32 v[4:5], v[4:5], v[50:51] op_sel_hi:[1,0]
	v_pk_mul_f32 v[2:3], v[2:3], v[50:51] op_sel_hi:[1,0]
	v_mul_f32_e32 v162, v162, v50
	v_mov_b32_e32 v50, v106
.LBB0_402:
	v_sub_f32_e32 v34, v34, v50
	v_exp_f32_e32 v106, v34
	v_sub_f32_e32 v34, v35, v50
	v_exp_f32_e32 v107, v34
	v_sub_f32_e32 v34, v36, v50
	v_exp_f32_e32 v108, v34
	v_sub_f32_e32 v34, v37, v50
	v_exp_f32_e32 v109, v34
	v_sub_f32_e32 v34, v38, v50
	v_exp_f32_e32 v110, v34
	v_sub_f32_e32 v34, v39, v50
	v_exp_f32_e32 v111, v34
	v_sub_f32_e32 v34, v40, v50
	v_exp_f32_e32 v112, v34
	v_sub_f32_e32 v34, v41, v50
	v_exp_f32_e32 v113, v34
	v_sub_f32_e32 v34, v42, v50
	v_exp_f32_e32 v165, v34
	v_sub_f32_e32 v34, v43, v50
	v_exp_f32_e32 v171, v34
	v_sub_f32_e32 v34, v44, v50
	v_exp_f32_e32 v172, v34
	v_sub_f32_e32 v34, v45, v50
	v_exp_f32_e32 v173, v34
	v_sub_f32_e32 v34, v46, v50
	v_exp_f32_e32 v237, v34
	v_sub_f32_e32 v34, v47, v50
	v_exp_f32_e32 v246, v34
	v_sub_f32_e32 v34, v48, v50
	v_exp_f32_e32 v247, v34
	v_sub_f32_e32 v34, v49, v50
	v_exp_f32_e32 v248, v34
	v_cvt_pk_bf16_f32 v34, v106, v107
	v_cvt_pk_bf16_f32 v35, v108, v109
	v_cvt_pk_bf16_f32 v36, v110, v111
	v_cvt_pk_bf16_f32 v37, v112, v113
	v_cvt_pk_bf16_f32 v238, v165, v171
	v_cvt_pk_bf16_f32 v239, v172, v173
	v_cvt_pk_bf16_f32 v240, v237, v246
	v_cvt_pk_bf16_f32 v241, v247, v248
	ds_read_b64_tr_b16 v[38:39], v181 offset:4608
	ds_read_b64_tr_b16 v[40:41], v181 offset:5888
	ds_read_b64_tr_b16 v[44:45], v181 offset:5952
	ds_read_b64_tr_b16 v[42:43], v181 offset:4672
	s_waitcnt lgkmcnt(2)
	v_mfma_f32_32x32x16_bf16 v[18:33], v[38:41], v[34:37], v[18:33]
	ds_read_b64_tr_b16 v[38:39], v181 offset:7168
	ds_read_b64_tr_b16 v[40:41], v181 offset:8448
	v_add_f32_e32 v46, 0, v106
	s_add_i32 s10, s13, s20
	ds_read_b64_tr_b16 v[244:245], v181 offset:8512
	ds_read_b64_tr_b16 v[242:243], v181 offset:7232
	s_waitcnt vmcnt(15)
	ds_write_b128 v231, v[86:89]
	s_waitcnt vmcnt(14)
	ds_write_b128 v232, v[90:93] offset:4608
	s_waitcnt vmcnt(13)
	ds_write_b128 v231, v[134:137] offset:1152
	s_waitcnt vmcnt(12)
	ds_write_b128 v232, v[142:145] offset:5888
	s_waitcnt vmcnt(11)
	ds_write_b128 v231, v[146:149] offset:2304
	s_waitcnt vmcnt(10)
	ds_write_b128 v232, v[150:153] offset:7168
	s_waitcnt vmcnt(9)
	ds_write_b128 v231, v[154:157] offset:3456
	s_waitcnt vmcnt(8)
	ds_write_b128 v232, v[158:161] offset:8448
	s_waitcnt lgkmcnt(10)
	v_mfma_f32_32x32x16_bf16 v[18:33], v[38:41], v[238:241], v[18:33]
	v_add_f32_e32 v38, v107, v46
	v_add_f32_e32 v38, v108, v38
	v_add_f32_e32 v38, v109, v38
	v_add_f32_e32 v38, v110, v38
	v_add_f32_e32 v38, v111, v38
	v_add_f32_e32 v38, v112, v38
	v_add_f32_e32 v249, v113, v38
	v_mfma_f32_32x32x16_bf16 v[2:17], v[42:45], v[34:37], v[2:17]
	v_add_u32_e32 v34, s10, v208
	v_med3_i32 v34, v34, 0, v233
	v_mul_u32_u24_e32 v38, 0xc00, v34
	ds_read_b128 v[34:37], v177
	v_or_b32_e32 v38, v38, v176
	global_load_dwordx4 v[106:109], v38, s[8:9] offset:1024
	global_load_dwordx4 v[110:113], v38, s[8:9] offset:2048
	v_add_u32_e32 v38, s10, v209
	v_med3_i32 v38, v38, 0, v233
	v_mul_u32_u24_e32 v38, 0xc00, v38
	ds_read_b128 v[86:89], v177 offset:32
	v_or_b32_e32 v90, v38, v176
	s_waitcnt lgkmcnt(1)
	v_mfma_f32_32x32x16_bf16 v[34:49], v[34:37], v[70:73], 0
	global_load_dwordx4 v[114:117], v90, s[8:9] offset:1024
	global_load_dwordx4 v[118:121], v90, s[8:9] offset:2048
	v_add_u32_e32 v90, s10, v211
	v_med3_i32 v90, v90, 0, v233
	v_mul_u32_u24_e32 v90, 0xc00, v90
	v_or_b32_e32 v126, v90, v176
	ds_read_b128 v[90:93], v177 offset:96
	ds_read_b128 v[142:145], v177 offset:64
	global_load_dwordx4 v[122:125], v126, s[8:9] offset:1024
	s_nop 0
	global_load_dwordx4 v[126:129], v126, s[8:9] offset:2048
	s_waitcnt lgkmcnt(2)
	v_mfma_f32_32x32x16_bf16 v[34:49], v[86:89], v[66:69], v[34:49]
	v_add_u32_e32 v86, s10, v212
	v_med3_i32 v86, v86, 0, v233
	v_mul_u32_u24_e32 v86, 0xc00, v86
	v_or_b32_e32 v86, v86, v176
	global_load_dwordx4 v[130:133], v86, s[8:9] offset:1024
	global_load_dwordx4 v[134:137], v86, s[8:9] offset:2048
	s_waitcnt lgkmcnt(0)
; __device__ __forceinline__ unsigned cvt_pk_bf16(float lo, float hi) { unsigned r; asm volatile("v_cvt_pk_bf16_f32 %0, %1, %2" : "=v"(r) : "v"(lo), "v"(hi)); return r; }
; #define LAS __attribute__((address_space(3)))
; #define MFMA32(a, b, c) __builtin_amdgcn_mfma_f32_32x32x16_bf16((a), (b), (c), 0, 0, 0)
; template <int STAGE, int OFF> __device__ __forceinline__ void attn32_unit(const bf16* base, bf16* yrow0, int blk0, int u, LAS unsigned char* xtab, LAS unsigned char* kbuf, LAS unsigned char* vbuf, int lane, ...
;     ...
;         const int mbase = n0 + 4 * h - lo; float mx = -INFINITY;
; #pragma unroll
;         for (int rg = 0; rg < 16; ++rg) { sc[rg] = ((unsigned)(mbase + (rg & 3) + 8 * (rg >> 2)) <= mspan) ? sc[rg] : -INFINITY; mx = fmaxf(mx, sc[rg]); }
;         mx = fmaxf(mx, __shfl_xor(mx, 32));
;         if (__any(mx > m)) {
;             const float mn = fmaxf(m, mx), alpha = __builtin_amdgcn_exp2f(m - mn); m = mn; l *= alpha;
; #pragma unroll
;             for (int i = 0; i < 16; ++i) { o[0][i] *= alpha; o[1][i] *= alpha; }
;         }
;         float ps = 0.f;
; #pragma unroll
;         for (int rg = 0; rg < 16; ++rg) { sc[rg] = __builtin_amdgcn_exp2f(sc[rg] - m); ps += sc[rg]; }
;         l += ps;
;         bf16x8 pb[2];
; #pragma unroll
;         for (int s2 = 0; s2 < 2; ++s2) { v4u w; w.x = pg8::cvt_pk_bf16(sc[8 * s2], sc[8 * s2 + 1]); w.y = pg8::cvt_pk_bf16(sc[8 * s2 + 2], sc[8 * s2 + 3]); w.z = pg8::cvt_pk_bf16(sc[8 * s2 + 4], sc[8 * s2 + 5]); w.w = pg8::cvt_pk_bf16(sc[8 * s2 + 6], sc[8 * s2 + 7]); pb[s2] = __builtin_bit_cast(bf16x8, w); }
; #pragma unroll
;         for (int mb = 0; mb < 2; ++mb)
; #pragma unroll
;             for (int s2 = 0; s2 < 2; ++s2) {
;                 LAS unsigned char* vp = vbuf + tr_off + (16 * s2) * 160 + 64 * mb;
;                 const v4i16 a0 = __builtin_amdgcn_ds_read_tr16_b64_v4i16((LAS v4i16*)vp), a1 = __builtin_amdgcn_ds_read_tr16_b64_v4i16((LAS v4i16*)(vp + 8 * 160));
;                 const bf16x8 va = __builtin_shufflevector(a0, a1, 0, 1, 2, 3, 4, 5, 6, 7);
;                 o[mb] = MFMA32(va, pb[s2], o[mb]);
	v_mfma_f32_32x32x16_bf16 v[34:49], v[142:145], v[62:65], v[34:49]
	v_add_f32_e32 v86, v165, v249
	v_add_f32_e32 v86, v171, v86
	v_add_f32_e32 v86, v172, v86
	v_add_f32_e32 v86, v173, v86
	v_add_f32_e32 v86, v237, v86
	v_mfma_f32_32x32x16_bf16 v[34:49], v[90:93], v[58:61], v[34:49]
	v_add_f32_e32 v86, v246, v86
	v_add_f32_e32 v86, v247, v86
	v_add_f32_e32 v86, v248, v86
	v_add_f32_e32 v142, v162, v86
	v_mfma_f32_32x32x16_bf16 v[2:17], v[242:245], v[238:241], v[2:17]
	s_nop 6
	v_add_u32_e32 v253, 123, v164
	v_cmp_le_i32_e32 vcc, 27, v253
	v_cmp_le_i32_e64 s[98:99], 26, v253
	v_cmp_le_i32_e64 s[100:101], 25, v253
	v_cndmask_b32_e32 v34, v234, v34, vcc
	v_cmp_le_i32_e32 vcc, 24, v253
	v_cndmask_b32_e64 v35, v234, v35, s[98:99]
	v_max3_f32 v87, v34, s31, v35
	v_cmp_le_i32_e64 s[98:99], 19, v253
	v_cndmask_b32_e64 v36, v234, v36, s[100:101]
	v_cmp_le_i32_e64 s[100:101], 18, v253
	v_cndmask_b32_e32 v37, v234, v37, vcc
	v_max3_f32 v87, v87, v36, v37
	v_cmp_le_i32_e32 vcc, 17, v253
	v_cndmask_b32_e64 v38, v234, v38, s[98:99]
	v_cmp_le_i32_e64 s[98:99], 16, v253
	v_cndmask_b32_e64 v39, v234, v39, s[100:101]
	v_max3_f32 v87, v87, v38, v39
	v_cmp_le_i32_e64 s[100:101], 11, v253
	v_cndmask_b32_e32 v40, v234, v40, vcc
	v_cmp_le_i32_e32 vcc, 10, v253
	v_cndmask_b32_e64 v41, v234, v41, s[98:99]
	v_max3_f32 v87, v87, v40, v41
	v_cmp_le_i32_e64 s[98:99], 9, v253
	v_cndmask_b32_e64 v42, v234, v42, s[100:101]
	v_cmp_le_i32_e64 s[100:101], 8, v253
	v_cndmask_b32_e32 v43, v234, v43, vcc
	v_max3_f32 v87, v87, v42, v43
	v_cmp_le_i32_e32 vcc, 3, v253
	v_cndmask_b32_e64 v44, v234, v44, s[98:99]
	v_cmp_le_i32_e64 s[98:99], 2, v253
	v_cndmask_b32_e64 v45, v234, v45, s[100:101]
	v_max3_f32 v87, v87, v44, v45
	v_cmp_le_i32_e64 s[100:101], 1, v253
	v_cndmask_b32_e32 v46, v234, v46, vcc
	v_cmp_le_i32_e32 vcc, 0, v253
	v_cndmask_b32_e64 v47, v234, v47, s[98:99]
	v_max3_f32 v87, v87, v46, v47
	v_cndmask_b32_e64 v48, v234, v48, s[100:101]
	v_cndmask_b32_e32 v49, v234, v49, vcc
	v_max3_f32 v87, v87, v48, v49
	ds_bpermute_b32 v88, v179, v87
	s_waitcnt lgkmcnt(0)
	v_max_f32_e32 v86, v88, v88
	v_max_f32_e32 v86, v87, v86
	v_cmp_gt_f32_e32 vcc, v86, v50
	s_cbranch_vccz .LBB0_404
	v_max_f32_e32 v86, v86, v86
	v_max_f32_e32 v87, v50, v50
	v_max_f32_e32 v86, v87, v86
	v_sub_f32_e32 v50, v50, v86
	v_exp_f32_e32 v50, v50
	s_nop 0
	v_pk_mul_f32 v[32:33], v[32:33], v[50:51] op_sel_hi:[1,0]
	v_pk_mul_f32 v[30:31], v[30:31], v[50:51] op_sel_hi:[1,0]
	v_pk_mul_f32 v[28:29], v[28:29], v[50:51] op_sel_hi:[1,0]
	v_pk_mul_f32 v[26:27], v[26:27], v[50:51] op_sel_hi:[1,0]
	v_pk_mul_f32 v[24:25], v[24:25], v[50:51] op_sel_hi:[1,0]
	v_pk_mul_f32 v[22:23], v[22:23], v[50:51] op_sel_hi:[1,0]
	v_pk_mul_f32 v[20:21], v[20:21], v[50:51] op_sel_hi:[1,0]
	v_pk_mul_f32 v[18:19], v[18:19], v[50:51] op_sel_hi:[1,0]
	v_pk_mul_f32 v[16:17], v[16:17], v[50:51] op_sel_hi:[1,0]
	v_pk_mul_f32 v[14:15], v[14:15], v[50:51] op_sel_hi:[1,0]
	v_pk_mul_f32 v[12:13], v[12:13], v[50:51] op_sel_hi:[1,0]
	v_pk_mul_f32 v[10:11], v[10:11], v[50:51] op_sel_hi:[1,0]
	v_pk_mul_f32 v[8:9], v[8:9], v[50:51] op_sel_hi:[1,0]
	v_pk_mul_f32 v[6:7], v[6:7], v[50:51] op_sel_hi:[1,0]
	v_pk_mul_f32 v[4:5], v[4:5], v[50:51] op_sel_hi:[1,0]
	v_pk_mul_f32 v[2:3], v[2:3], v[50:51] op_sel_hi:[1,0]
	v_mul_f32_e32 v142, v142, v50
	v_mov_b32_e32 v50, v86
.LBB0_404:
	v_sub_f32_e32 v34, v34, v50
	v_exp_f32_e32 v86, v34
	v_sub_f32_e32 v34, v35, v50
	v_exp_f32_e32 v87, v34
	v_sub_f32_e32 v34, v36, v50
	v_exp_f32_e32 v88, v34
	v_sub_f32_e32 v34, v37, v50
	v_exp_f32_e32 v89, v34
	v_sub_f32_e32 v34, v38, v50
	v_exp_f32_e32 v90, v34
	v_sub_f32_e32 v34, v39, v50
	v_exp_f32_e32 v91, v34
	v_sub_f32_e32 v34, v40, v50
	v_exp_f32_e32 v92, v34
	v_sub_f32_e32 v34, v41, v50
	v_exp_f32_e32 v93, v34
	v_sub_f32_e32 v34, v42, v50
	v_exp_f32_e32 v143, v34
	v_sub_f32_e32 v34, v43, v50
	v_exp_f32_e32 v154, v34
	v_sub_f32_e32 v34, v44, v50
	v_exp_f32_e32 v155, v34
	v_sub_f32_e32 v34, v45, v50
	v_exp_f32_e32 v156, v34
	v_sub_f32_e32 v34, v46, v50
	v_exp_f32_e32 v157, v34
	v_sub_f32_e32 v34, v47, v50
	v_exp_f32_e32 v158, v34
	v_sub_f32_e32 v34, v48, v50
	v_exp_f32_e32 v159, v34
	v_sub_f32_e32 v34, v49, v50
	v_exp_f32_e32 v160, v34
	v_cvt_pk_bf16_f32 v34, v86, v87
	v_cvt_pk_bf16_f32 v35, v88, v89
	v_cvt_pk_bf16_f32 v36, v90, v91
	v_cvt_pk_bf16_f32 v37, v92, v93
	v_cvt_pk_bf16_f32 v144, v143, v154
	v_cvt_pk_bf16_f32 v145, v155, v156
	v_cvt_pk_bf16_f32 v146, v157, v158
	v_cvt_pk_bf16_f32 v147, v159, v160
	ds_read_b64_tr_b16 v[38:39], v181 offset:4608
	ds_read_b64_tr_b16 v[40:41], v181 offset:5888
	v_add_u32_e32 v162, s10, v52
	v_min_i32_e32 v148, 0x3fff, v162
	s_waitcnt lgkmcnt(0)
	v_mfma_f32_32x32x16_bf16 v[18:33], v[38:41], v[34:37], v[18:33]
	v_mul_u32_u24_e32 v38, 0xc00, v148
	v_mov_b32_e32 v39, v169
	v_lshl_add_u64 v[38:39], s[8:9], 0, v[38:39]
	ds_read_b64_tr_b16 v[42:43], v181 offset:7168
	ds_read_b64_tr_b16 v[44:45], v181 offset:8448
	ds_read_b64_tr_b16 v[48:49], v181 offset:5952
	ds_read_b64_tr_b16 v[46:47], v181 offset:4672
	v_lshl_add_u64 v[152:153], v[38:39], 0, v[168:169]
	v_add_f32_e32 v38, 0, v86
	v_add_f32_e32 v38, v87, v38
	v_add_f32_e32 v38, v88, v38
	v_add_f32_e32 v38, v89, v38
	v_add_f32_e32 v38, v90, v38
	v_add_f32_e32 v38, v91, v38
	s_waitcnt lgkmcnt(0)
	v_mfma_f32_32x32x16_bf16 v[2:17], v[46:49], v[34:37], v[2:17]
	v_add_u32_e32 v34, s10, v213
	ds_read_b64_tr_b16 v[150:151], v181 offset:8512
	ds_read_b64_tr_b16 v[148:149], v181 offset:7232
	v_add_f32_e32 v38, v92, v38
	s_waitcnt vmcnt(15)
; #define LAS __attribute__((address_space(3)))
; #define MFMA32(a, b, c) __builtin_amdgcn_mfma_f32_32x32x16_bf16((a), (b), (c), 0, 0, 0)
; template <int STAGE, int OFF> __device__ __forceinline__ void attn32_unit(const bf16* base, bf16* yrow0, int blk0, int u, LAS unsigned char* xtab, LAS unsigned char* kbuf, LAS unsigned char* vbuf, int lane, ...
;     ...
;         for (int c = 0; c < 4; ++c) { *(LAS v4u*)(kbuf + (8 * c + lrow) * 144 + lch * 16) = kr[set][c]; *(LAS v4u*)(vbuf + (8 * c + lrow) * 160 + lch * 16) = vr[set][c]; }
;         if (pp + 2 < 5) { ATT32_LOAD(set, pp + 2, t0, SH); }
;         else { const bf16* base_ = base; { const bf16* base = nbase; ATT32_LOAD(set, pp + 2 - 5, nt0, nsh); } (void)base_; }
;         f32x16 sc;
; #pragma unroll
;         for (int i = 0; i < 16; ++i) sc[i] = 0.f;
; #pragma unroll
;         for (int ks = 0; ks < 4; ++ks) { const bf16x8 ka = *(const LAS bf16x8*)(kbuf + qi * 144 + 32 * ks + 16 * h); sc = MFMA32(ka, qb[ks], sc); }
;         if (pp == 4) {
; #pragma unroll
;             for (int ks = 0; ks < 4; ++ks) qb[ks] = *(const bf16x8*)(nbase + (size_t)min(nt0 + (qi << nsh), SEQ - 1) * 1536 + 16 * ks + 8 * h);
;         }
;         const int mbase = n0 + 4 * h - lo; float mx = -INFINITY;
; #pragma unroll
;         for (int rg = 0; rg < 16; ++rg) { sc[rg] = ((unsigned)(mbase + (rg & 3) + 8 * (rg >> 2)) <= mspan) ? sc[rg] : -INFINITY; mx = fmaxf(mx, sc[rg]); }
;         mx = fmaxf(mx, __shfl_xor(mx, 32));
;         if (__any(mx > m)) {
;             const float mn = fmaxf(m, mx), alpha = __builtin_amdgcn_exp2f(m - mn); m = mn; l *= alpha;
; #pragma unroll
;             for (int i = 0; i < 16; ++i) { o[0][i] *= alpha; o[1][i] *= alpha; }
;         }
	ds_write_b128 v231, v[54:57]
	s_waitcnt vmcnt(14)
	ds_write_b128 v232, v[74:77] offset:4608
	s_waitcnt vmcnt(13)
	ds_write_b128 v231, v[78:81] offset:1152
	s_waitcnt vmcnt(12)
	ds_write_b128 v232, v[82:85] offset:5888
	s_waitcnt vmcnt(11)
	ds_write_b128 v231, v[94:97] offset:2304
	s_waitcnt vmcnt(10)
	ds_write_b128 v232, v[98:101] offset:7168
	s_waitcnt vmcnt(9)
	ds_write_b128 v231, v[102:105] offset:3456
	s_waitcnt vmcnt(8)
	ds_write_b128 v232, v[138:141] offset:8448
	v_med3_i32 v34, v34, 0, v233
	v_add_f32_e32 v161, v93, v38
	v_mul_u32_u24_e32 v38, 0xc00, v34
	ds_read_b128 v[34:37], v177
	v_or_b32_e32 v38, v38, v176
	global_load_dwordx4 v[74:77], v38, s[8:9] offset:1024
	global_load_dwordx4 v[78:81], v38, s[8:9] offset:2048
	v_add_u32_e32 v38, s10, v214
	v_med3_i32 v38, v38, 0, v233
	v_mul_u32_u24_e32 v38, 0xc00, v38
	ds_read_b128 v[54:57], v177 offset:32
	v_mfma_f32_32x32x16_bf16 v[18:33], v[42:45], v[144:147], v[18:33]
	v_or_b32_e32 v86, v38, v176
	global_load_dwordx4 v[82:85], v86, s[8:9] offset:1024
	s_nop 0
	global_load_dwordx4 v[86:89], v86, s[8:9] offset:2048
	v_add_f32_e32 v143, v143, v161
	v_add_f32_e32 v143, v154, v143
	v_add_f32_e32 v143, v155, v143
	v_add_f32_e32 v143, v156, v143
	v_add_f32_e32 v143, v157, v143
	s_waitcnt lgkmcnt(1)
	v_mfma_f32_32x32x16_bf16 v[34:49], v[34:37], v[70:73], 0
	v_add_u32_e32 v70, s10, v215
	v_med3_i32 v70, v70, 0, v233
	v_mul_u32_u24_e32 v70, 0xc00, v70
	v_or_b32_e32 v94, v70, v176
	ds_read_b128 v[138:141], v177 offset:96
	ds_read_b128 v[70:73], v177 offset:64
	global_load_dwordx4 v[90:93], v94, s[8:9] offset:1024
	s_nop 0
	global_load_dwordx4 v[94:97], v94, s[8:9] offset:2048
	v_add_f32_e32 v143, v158, v143
	s_waitcnt lgkmcnt(2)
	v_mfma_f32_32x32x16_bf16 v[34:49], v[54:57], v[66:69], v[34:49]
	v_add_u32_e32 v54, s10, v216
	v_med3_i32 v54, v54, 0, v233
	v_mul_u32_u24_e32 v54, 0xc00, v54
	v_or_b32_e32 v54, v54, v176
	global_load_dwordx4 v[98:101], v54, s[8:9] offset:1024
	global_load_dwordx4 v[102:105], v54, s[8:9] offset:2048
	v_add_f32_e32 v143, v159, v143
	s_waitcnt lgkmcnt(0)
	v_mfma_f32_32x32x16_bf16 v[34:49], v[70:73], v[62:65], v[34:49]
	global_load_dwordx4 v[70:73], v[152:153], off
	global_load_dwordx4 v[62:65], v[152:153], off offset:32
	global_load_dwordx4 v[54:57], v[152:153], off offset:64
	global_load_dwordx4 v[66:69], v[152:153], off offset:96
	v_mfma_f32_32x32x16_bf16 v[34:49], v[138:141], v[58:61], v[34:49]
	v_mfma_f32_32x32x16_bf16 v[2:17], v[148:151], v[144:147], v[2:17]
	s_nop 7
	v_sub_u32_e32 v253, v163, v164
	v_subrev_u32_e32 v253, 0x80, v253
	v_cmp_le_i32_e32 vcc, 0, v253
	v_cmp_le_i32_e64 s[98:99], 1, v253
	v_cmp_le_i32_e64 s[100:101], 2, v253
	v_cndmask_b32_e32 v58, v234, v34, vcc
	v_cmp_le_i32_e32 vcc, 3, v253
	v_cndmask_b32_e64 v35, v234, v35, s[98:99]
	v_max3_f32 v34, v58, s31, v35
	v_cmp_le_i32_e64 s[98:99], 8, v253
	v_cndmask_b32_e64 v36, v234, v36, s[100:101]
	v_cmp_le_i32_e64 s[100:101], 9, v253
	v_cndmask_b32_e32 v37, v234, v37, vcc
	v_max3_f32 v34, v34, v36, v37
	v_cmp_le_i32_e32 vcc, 10, v253
	v_cndmask_b32_e64 v38, v234, v38, s[98:99]
	v_cmp_le_i32_e64 s[98:99], 11, v253
	v_cndmask_b32_e64 v39, v234, v39, s[100:101]
	v_max3_f32 v34, v34, v38, v39
	v_cmp_le_i32_e64 s[100:101], 16, v253
	v_cndmask_b32_e32 v40, v234, v40, vcc
	v_cmp_le_i32_e32 vcc, 17, v253
	v_cndmask_b32_e64 v41, v234, v41, s[98:99]
	v_max3_f32 v34, v34, v40, v41
	v_cmp_le_i32_e64 s[98:99], 18, v253
	v_cndmask_b32_e64 v42, v234, v42, s[100:101]
	v_cmp_le_i32_e64 s[100:101], 19, v253
	v_cndmask_b32_e32 v43, v234, v43, vcc
	v_max3_f32 v34, v34, v42, v43
	v_cmp_le_i32_e32 vcc, 24, v253
	v_cndmask_b32_e64 v44, v234, v44, s[98:99]
	v_cmp_le_i32_e64 s[98:99], 25, v253
	v_cndmask_b32_e64 v45, v234, v45, s[100:101]
	v_max3_f32 v34, v34, v44, v45
	v_cmp_le_i32_e64 s[100:101], 26, v253
	v_cndmask_b32_e32 v46, v234, v46, vcc
	v_cmp_le_i32_e32 vcc, 27, v253
	v_cndmask_b32_e64 v47, v234, v47, s[98:99]
	v_max3_f32 v34, v34, v46, v47
	v_cndmask_b32_e64 v48, v234, v48, s[100:101]
	v_cndmask_b32_e32 v49, v234, v49, vcc
	v_max3_f32 v59, v34, v48, v49
	ds_bpermute_b32 v60, v179, v59
	v_add_f32_e32 v34, v160, v143
	v_add_f32_e32 v34, v142, v34
	s_waitcnt lgkmcnt(0)
	v_max_f32_e32 v60, v60, v60
	v_max_f32_e32 v59, v59, v60
	v_cmp_gt_f32_e32 vcc, v59, v50
	s_cbranch_vccz .LBB0_406
	v_max_f32_e32 v59, v59, v59
	v_max_f32_e32 v60, v50, v50
	v_max_f32_e32 v59, v60, v59
	v_sub_f32_e32 v50, v50, v59
	v_exp_f32_e32 v50, v50
	s_nop 0
	v_pk_mul_f32 v[32:33], v[32:33], v[50:51] op_sel_hi:[1,0]
	v_pk_mul_f32 v[30:31], v[30:31], v[50:51] op_sel_hi:[1,0]
	v_pk_mul_f32 v[28:29], v[28:29], v[50:51] op_sel_hi:[1,0]
	v_pk_mul_f32 v[26:27], v[26:27], v[50:51] op_sel_hi:[1,0]
	v_pk_mul_f32 v[24:25], v[24:25], v[50:51] op_sel_hi:[1,0]
	v_pk_mul_f32 v[22:23], v[22:23], v[50:51] op_sel_hi:[1,0]
	v_pk_mul_f32 v[20:21], v[20:21], v[50:51] op_sel_hi:[1,0]
	v_pk_mul_f32 v[18:19], v[18:19], v[50:51] op_sel_hi:[1,0]
	v_pk_mul_f32 v[16:17], v[16:17], v[50:51] op_sel_hi:[1,0]
	v_pk_mul_f32 v[14:15], v[14:15], v[50:51] op_sel_hi:[1,0]
	v_pk_mul_f32 v[12:13], v[12:13], v[50:51] op_sel_hi:[1,0]
	v_pk_mul_f32 v[10:11], v[10:11], v[50:51] op_sel_hi:[1,0]
	v_pk_mul_f32 v[8:9], v[8:9], v[50:51] op_sel_hi:[1,0]
	v_pk_mul_f32 v[6:7], v[6:7], v[50:51] op_sel_hi:[1,0]
	v_pk_mul_f32 v[4:5], v[4:5], v[50:51] op_sel_hi:[1,0]
	v_pk_mul_f32 v[2:3], v[2:3], v[50:51] op_sel_hi:[1,0]
	v_mul_f32_e32 v34, v34, v50
	v_mov_b32_e32 v50, v59

; __device__ __forceinline__ float bf_lo(unsigned w) { return __uint_as_float(w << 16); }
; template <int STAGE, int OFF> __device__ __forceinline__ void attn32_unit(const bf16* base, bf16* yrow0, int blk0, int u, LAS unsigned char* xtab, LAS unsigned char* kbuf, LAS unsigned char* vbuf, int lane, ...
;     ...
;     } else {
; #pragma unroll
;         for (int mb = 0; mb < 2; ++mb)
; #pragma unroll
;             for (int gq = 0; gq < 4; ++gq) { const v2u w = *(const LAS v2u*)(xrow + 2 * (32 * mb + 8 * gq + 4 * h)); o[mb][4 * gq] = bf_lo(w.x); o[mb][4 * gq + 1] = bf_hi(w.x); o[mb][4 * gq + 2] = bf_lo(w.y); o[mb][4 * gq + 3] = bf_hi(w.y); }
;         m = *(const LAS float*)(xrow + 128); l = h == 0 ? *(const LAS float*)(xrow + 132) : 0.f;
;     }
;     const int hi = qi, lo = max(qi - 128, -(t0 >> SH));
;     const unsigned mspan = (unsigned)(hi - lo);
; #pragma unroll
;     for (int pp = 0; pp < 5; ++pp) {
;         constexpr int dummy = 0; (void)dummy;
;         const int set = (pp + OFF) % 2, n0 = -128 + 32 * pp;
; #pragma unroll
;         for (int c = 0; c < 4; ++c) { *(LAS v4u*)(kbuf + (8 * c + lrow) * 144 + lch * 16) = kr[set][c]; *(LAS v4u*)(vbuf + (8 * c + lrow) * 160 + lch * 16) = vr[set][c]; }
;         if (pp + 2 < 5) { ATT32_LOAD(set, pp + 2, t0, SH); }
;         else { const bf16* base_ = base; { const bf16* base = nbase; ATT32_LOAD(set, pp + 2 - 5, nt0, nsh); } (void)base_; }
;         f32x16 sc;
; #pragma unroll
;         for (int i = 0; i < 16; ++i) sc[i] = 0.f;
; #pragma unroll
;         for (int ks = 0; ks < 4; ++ks) { const bf16x8 ka = *(const LAS bf16x8*)(kbuf + qi * 144 + 32 * ks + 16 * h); sc = MFMA32(ka, qb[ks], sc); }
;         if (pp == 4) {
; #pragma unroll
;             for (int ks = 0; ks < 4; ++ks) qb[ks] = *(const bf16x8*)(nbase + (size_t)min(nt0 + (qi << nsh), SEQ - 1) * 1536 + 16 * ks + 8 * h);
;         }
;         const int mbase = n0 + 4 * h - lo; float mx = -INFINITY;
; #pragma unroll
;         for (int rg = 0; rg < 16; ++rg) { sc[rg] = ((unsigned)(mbase + (rg & 3) + 8 * (rg >> 2)) <= mspan) ? sc[rg] : -INFINITY; mx = fmaxf(mx, sc[rg]); }
;         mx = fmaxf(mx, __shfl_xor(mx, 32));
;         if (__any(mx > m)) {
;             const float mn = fmaxf(m, mx), alpha = __builtin_amdgcn_exp2f(m - mn); m = mn; l *= alpha;
; #pragma unroll
;             for (int i = 0; i < 16; ++i) { o[0][i] *= alpha; o[1][i] *= alpha; }
;         }
.LBB0_408:
	s_or_b64 exec, exec, s[14:15]
	v_add_u32_e32 v14, v217, v166
	s_waitcnt lgkmcnt(0)
	s_barrier
	ds_read2_b64 v[10:13], v14 offset1:2
	ds_read2_b64 v[2:5], v14 offset0:4 offset1:6
	ds_read2_b64 v[6:9], v14 offset0:8 offset1:10
	ds_read2_b64 v[14:17], v14 offset0:12 offset1:14
	ds_read_b32 v164, v217 offset:128
	v_mov_b32_e32 v50, 0
	s_and_saveexec_b64 s[14:15], s[4:5]
	ds_read_b32 v50, v217 offset:132
	s_or_b64 exec, exec, s[14:15]
	s_waitcnt vmcnt(19)
	ds_write_b128 v231, v[106:109]
	s_waitcnt vmcnt(18)
	ds_write_b128 v232, v[110:113] offset:4608
	s_waitcnt vmcnt(17)
	ds_write_b128 v231, v[114:117] offset:1152
	s_waitcnt vmcnt(16)
	ds_write_b128 v232, v[118:121] offset:5888
	s_waitcnt vmcnt(15)
	ds_write_b128 v231, v[122:125] offset:2304
	s_waitcnt vmcnt(14)
	ds_write_b128 v232, v[126:129] offset:7168
	s_waitcnt vmcnt(13)
	ds_write_b128 v231, v[130:133] offset:3456
	s_waitcnt vmcnt(12)
	ds_write_b128 v232, v[134:137] offset:8448
	ds_read_b128 v[34:37], v177
	s_waitcnt lgkmcnt(13)
	v_lshlrev_b32_e32 v22, 16, v12
	v_and_b32_e32 v23, 0xffff0000, v12
	v_add_u32_e32 v12, s10, v218
	v_med3_i32 v12, v12, 0, v233
	v_mul_u32_u24_e32 v12, 0xc00, v12
	v_or_b32_e32 v12, v12, v176
	global_load_dwordx4 v[58:61], v12, s[8:9] offset:1024
	global_load_dwordx4 v[106:109], v12, s[8:9] offset:2048
	ds_read_b128 v[118:121], v177 offset:32
	v_add_u32_e32 v12, s10, v219
	s_waitcnt vmcnt(5) lgkmcnt(1)
	v_mfma_f32_32x32x16_bf16 v[34:49], v[34:37], v[70:73], 0
	v_med3_i32 v12, v12, 0, v233
	v_mul_u32_u24_e32 v12, 0xc00, v12
	v_or_b32_e32 v12, v12, v176
	global_load_dwordx4 v[110:113], v12, s[8:9] offset:1024
	global_load_dwordx4 v[114:117], v12, s[8:9] offset:2048
	v_add_u32_e32 v12, s10, v220
	v_med3_i32 v12, v12, 0, v233
	v_mul_u32_u24_e32 v12, 0xc00, v12
	v_or_b32_e32 v12, v12, v176
	ds_read_b128 v[134:137], v177 offset:96
	ds_read_b128 v[138:141], v177 offset:64
	s_waitcnt vmcnt(6) lgkmcnt(2)
	v_mfma_f32_32x32x16_bf16 v[34:49], v[118:121], v[62:65], v[34:49]
	global_load_dwordx4 v[118:121], v12, s[8:9] offset:1024
	global_load_dwordx4 v[122:125], v12, s[8:9] offset:2048
	v_add_u32_e32 v12, s10, v221
	v_med3_i32 v12, v12, 0, v233
	v_mul_u32_u24_e32 v12, 0xc00, v12
	v_or_b32_e32 v12, v12, v176
	global_load_dwordx4 v[126:129], v12, s[8:9] offset:1024
	global_load_dwordx4 v[130:133], v12, s[8:9] offset:2048
	s_lshr_b32 s0, s10, 4
	s_waitcnt vmcnt(9) lgkmcnt(0)
	v_mfma_f32_32x32x16_bf16 v[34:49], v[138:141], v[54:57], v[34:49]
	s_sub_i32 s0, 0, s0
	v_lshlrev_b32_e32 v18, 16, v10
	v_and_b32_e32 v19, 0xffff0000, v10
	v_lshlrev_b32_e32 v20, 16, v11
	v_and_b32_e32 v21, 0xffff0000, v11
	v_lshlrev_b32_e32 v10, 16, v14
	v_and_b32_e32 v11, 0xffff0000, v14
	s_waitcnt vmcnt(8)
	v_mfma_f32_32x32x16_bf16 v[34:49], v[134:137], v[66:69], v[34:49]
	v_max_i32_e32 v14, s0, v175
	v_sub_u32_e32 v51, v1, v14
	v_sub_u32_e32 v163, v178, v14
	v_lshlrev_b32_e32 v24, 16, v13
	v_and_b32_e32 v25, 0xffff0000, v13
	v_lshlrev_b32_e32 v12, 16, v15
	v_and_b32_e32 v13, 0xffff0000, v15
	s_nop 2
	v_add_u32_e32 v253, 27, v163
	v_cmp_le_i32_e32 vcc, 27, v253
	v_cmp_le_i32_e64 s[98:99], 26, v253
	v_cmp_le_i32_e64 s[100:101], 25, v253
	v_cndmask_b32_e32 v34, v234, v34, vcc
	v_lshlrev_b32_e32 v26, 16, v2
	v_cmp_le_i32_e32 vcc, 24, v253
	v_cndmask_b32_e64 v35, v234, v35, s[98:99]
	v_max3_f32 v14, v34, s31, v35
	v_cmp_le_i32_e64 s[98:99], 19, v253
	v_cndmask_b32_e64 v36, v234, v36, s[100:101]
	v_and_b32_e32 v27, 0xffff0000, v2
	v_cmp_le_i32_e64 s[100:101], 18, v253
	v_cndmask_b32_e32 v37, v234, v37, vcc
	v_max3_f32 v14, v14, v36, v37
	v_cmp_le_i32_e32 vcc, 17, v253
	v_cndmask_b32_e64 v38, v234, v38, s[98:99]
	v_lshlrev_b32_e32 v28, 16, v3
	v_cmp_le_i32_e64 s[98:99], 16, v253
	v_cndmask_b32_e64 v39, v234, v39, s[100:101]
	v_max3_f32 v14, v14, v38, v39
	v_cmp_le_i32_e64 s[100:101], 11, v253
	v_cndmask_b32_e32 v40, v234, v40, vcc
	v_and_b32_e32 v29, 0xffff0000, v3
	v_cmp_le_i32_e32 vcc, 10, v253
	v_cndmask_b32_e64 v41, v234, v41, s[98:99]
	v_max3_f32 v14, v14, v40, v41
	v_cmp_le_i32_e64 s[98:99], 9, v253
	v_cndmask_b32_e64 v42, v234, v42, s[100:101]
	v_lshlrev_b32_e32 v30, 16, v4
	v_cmp_le_i32_e64 s[100:101], 8, v253
	v_cndmask_b32_e32 v43, v234, v43, vcc
	v_max3_f32 v14, v14, v42, v43
	v_cmp_le_i32_e32 vcc, 3, v253
	v_cndmask_b32_e64 v44, v234, v44, s[98:99]
	v_and_b32_e32 v31, 0xffff0000, v4
	v_cmp_le_i32_e64 s[98:99], 2, v253
	v_cndmask_b32_e64 v45, v234, v45, s[100:101]
	v_max3_f32 v14, v14, v44, v45
	v_cmp_le_i32_e64 s[100:101], 1, v253
	v_cndmask_b32_e32 v46, v234, v46, vcc
	v_lshlrev_b32_e32 v32, 16, v5
	v_cmp_le_i32_e32 vcc, 0, v253
	v_cndmask_b32_e64 v47, v234, v47, s[98:99]
	v_max3_f32 v14, v14, v46, v47
	v_cndmask_b32_e64 v48, v234, v48, s[100:101]
	v_and_b32_e32 v33, 0xffff0000, v5
	v_lshlrev_b32_e32 v2, 16, v6
	v_cndmask_b32_e32 v49, v234, v49, vcc
	v_max3_f32 v134, v14, v48, v49
	ds_bpermute_b32 v135, v179, v134
	v_and_b32_e32 v3, 0xffff0000, v6
	v_lshlrev_b32_e32 v4, 16, v7
	v_and_b32_e32 v5, 0xffff0000, v7
	v_lshlrev_b32_e32 v6, 16, v8
	s_waitcnt lgkmcnt(0)
	v_max_f32_e32 v135, v135, v135
	v_max_f32_e32 v134, v134, v135
	v_and_b32_e32 v7, 0xffff0000, v8
	v_lshlrev_b32_e32 v8, 16, v9
	v_and_b32_e32 v9, 0xffff0000, v9
	v_lshlrev_b32_e32 v14, 16, v16
	v_and_b32_e32 v15, 0xffff0000, v16
	v_lshlrev_b32_e32 v16, 16, v17
	v_and_b32_e32 v17, 0xffff0000, v17
	v_cmp_gt_f32_e32 vcc, v134, v164
	s_cbranch_vccz .LBB0_412
	v_max_f32_e32 v134, v134, v134
	v_max_f32_e32 v135, v164, v164
	v_max_f32_e32 v135, v135, v134
	v_sub_f32_e32 v134, v164, v135
	v_exp_f32_e32 v134, v134
	v_mov_b32_e32 v164, v135
	v_pk_mul_f32 v[16:17], v[134:135], v[16:17] op_sel_hi:[0,1]
	v_pk_mul_f32 v[14:15], v[134:135], v[14:15] op_sel_hi:[0,1]
	v_pk_mul_f32 v[12:13], v[134:135], v[12:13] op_sel_hi:[0,1]
	v_pk_mul_f32 v[10:11], v[134:135], v[10:11] op_sel_hi:[0,1]
	v_pk_mul_f32 v[8:9], v[134:135], v[8:9] op_sel_hi:[0,1]
	v_pk_mul_f32 v[6:7], v[134:135], v[6:7] op_sel_hi:[0,1]
	v_pk_mul_f32 v[4:5], v[134:135], v[4:5] op_sel_hi:[0,1]
	v_pk_mul_f32 v[2:3], v[134:135], v[2:3] op_sel_hi:[0,1]
	v_pk_mul_f32 v[32:33], v[134:135], v[32:33] op_sel_hi:[0,1]
	v_pk_mul_f32 v[30:31], v[134:135], v[30:31] op_sel_hi:[0,1]
	v_pk_mul_f32 v[28:29], v[134:135], v[28:29] op_sel_hi:[0,1]
	v_pk_mul_f32 v[26:27], v[134:135], v[26:27] op_sel_hi:[0,1]
	v_pk_mul_f32 v[24:25], v[134:135], v[24:25] op_sel_hi:[0,1]
	v_pk_mul_f32 v[22:23], v[134:135], v[22:23] op_sel_hi:[0,1]
	v_pk_mul_f32 v[20:21], v[134:135], v[20:21] op_sel_hi:[0,1]
	v_pk_mul_f32 v[18:19], v[134:135], v[18:19] op_sel_hi:[0,1]
	v_mul_f32_e32 v50, v50, v134
; #define LAS __attribute__((address_space(3)))
; template <int STAGE, int OFF> __device__ __forceinline__ void attn32_unit(const bf16* base, bf16* yrow0, int blk0, int u, LAS unsigned char* xtab, LAS unsigned char* kbuf, LAS unsigned char* vbuf, int lane, ...
;     ...
;         for (int c = 0; c < 4; ++c) { *(LAS v4u*)(kbuf + (8 * c + lrow) * 144 + lch * 16) = kr[set][c]; *(LAS v4u*)(vbuf + (8 * c + lrow) * 160 + lch * 16) = vr[set][c]; }
;         if (pp + 2 < 5) { ATT32_LOAD(set, pp + 2, t0, SH); }
;         else { const bf16* base_ = base; { const bf16* base = nbase; ATT32_LOAD(set, pp + 2 - 5, nt0, nsh); } (void)base_; }
;         f32x16 sc;
; #pragma unroll
;         for (int i = 0; i < 16; ++i) sc[i] = 0.f;
; #pragma unroll
;         for (int ks = 0; ks < 4; ++ks) { const bf16x8 ka = *(const LAS bf16x8*)(kbuf + qi * 144 + 32 * ks + 16 * h); sc = MFMA32(ka, qb[ks], sc); }
;         if (pp == 4) {
; #pragma unroll
;             for (int ks = 0; ks < 4; ++ks) qb[ks] = *(const bf16x8*)(nbase + (size_t)min(nt0 + (qi << nsh), SEQ - 1) * 1536 + 16 * ks + 8 * h);
;         }
;         const int mbase = n0 + 4 * h - lo; float mx = -INFINITY;
; #pragma unroll
;         for (int rg = 0; rg < 16; ++rg) { sc[rg] = ((unsigned)(mbase + (rg & 3) + 8 * (rg >> 2)) <= mspan) ? sc[rg] : -INFINITY; mx = fmaxf(mx, sc[rg]); }
;         mx = fmaxf(mx, __shfl_xor(mx, 32));
;         if (__any(mx > m)) {
;             const float mn = fmaxf(m, mx), alpha = __builtin_amdgcn_exp2f(m - mn); m = mn; l *= alpha;
; #pragma unroll
;             for (int i = 0; i < 16; ++i) { o[0][i] *= alpha; o[1][i] *= alpha; }
;         }
;         float ps = 0.f;
; #pragma unroll
;         for (int rg = 0; rg < 16; ++rg) { sc[rg] = __builtin_amdgcn_exp2f(sc[rg] - m); ps += sc[rg]; }
;         l += ps;
;         bf16x8 pb[2];
; #pragma unroll
;         for (int s2 = 0; s2 < 2; ++s2) { v4u w; w.x = pg8::cvt_pk_bf16(sc[8 * s2], sc[8 * s2 + 1]); w.y = pg8::cvt_pk_bf16(sc[8 * s2 + 2], sc[8 * s2 + 3]); w.z = pg8::cvt_pk_bf16(sc[8 * s2 + 4], sc[8 * s2 + 5]); w.w = pg8::cvt_pk_bf16(sc[8 * s2 + 6], sc[8 * s2 + 7]); pb[s2] = __builtin_bit_cast(bf16x8, w); }
; #pragma unroll
;         for (int mb = 0; mb < 2; ++mb)
; #pragma unroll
;             for (int s2 = 0; s2 < 2; ++s2) {
;                 LAS unsigned char* vp = vbuf + tr_off + (16 * s2) * 160 + 64 * mb;
.LBB0_412:
	v_sub_f32_e32 v34, v34, v164
	v_exp_f32_e32 v134, v34
	v_sub_f32_e32 v34, v35, v164
	v_exp_f32_e32 v135, v34
	v_sub_f32_e32 v34, v36, v164
	v_exp_f32_e32 v136, v34
	v_sub_f32_e32 v34, v37, v164
	v_exp_f32_e32 v137, v34
	v_sub_f32_e32 v34, v38, v164
	v_exp_f32_e32 v142, v34
	v_sub_f32_e32 v34, v39, v164
	v_exp_f32_e32 v143, v34
	v_sub_f32_e32 v34, v40, v164
	v_exp_f32_e32 v144, v34
	v_sub_f32_e32 v34, v41, v164
	v_exp_f32_e32 v145, v34
	v_sub_f32_e32 v34, v42, v164
	v_exp_f32_e32 v165, v34
	v_sub_f32_e32 v34, v43, v164
	v_exp_f32_e32 v171, v34
	v_sub_f32_e32 v34, v44, v164
	v_exp_f32_e32 v172, v34
	v_sub_f32_e32 v34, v45, v164
	v_exp_f32_e32 v173, v34
	v_sub_f32_e32 v34, v46, v164
	v_exp_f32_e32 v237, v34
	v_sub_f32_e32 v34, v47, v164
	v_exp_f32_e32 v242, v34
	v_sub_f32_e32 v34, v48, v164
	v_exp_f32_e32 v243, v34
	v_sub_f32_e32 v34, v49, v164
	v_exp_f32_e32 v244, v34
	v_cvt_pk_bf16_f32 v34, v134, v135
	v_cvt_pk_bf16_f32 v35, v136, v137
	v_cvt_pk_bf16_f32 v36, v142, v143
	v_cvt_pk_bf16_f32 v37, v144, v145
	v_cvt_pk_bf16_f32 v138, v165, v171
	v_cvt_pk_bf16_f32 v139, v172, v173
	v_cvt_pk_bf16_f32 v140, v237, v242
	v_cvt_pk_bf16_f32 v141, v243, v244
	ds_read_b64_tr_b16 v[38:39], v181 offset:4608
	ds_read_b64_tr_b16 v[40:41], v181 offset:5888
	ds_read_b64_tr_b16 v[44:45], v181 offset:5952
	ds_read_b64_tr_b16 v[42:43], v181 offset:4672
	s_waitcnt lgkmcnt(2)
	v_mfma_f32_32x32x16_bf16 v[18:33], v[38:41], v[34:37], v[18:33]
	ds_read_b64_tr_b16 v[38:39], v181 offset:7168
	ds_read_b64_tr_b16 v[40:41], v181 offset:8448
	v_add_f32_e32 v46, 0, v134
	ds_read_b64_tr_b16 v[240:241], v181 offset:8512
	ds_read_b64_tr_b16 v[238:239], v181 offset:7232
	ds_write_b128 v231, v[74:77]
	ds_write_b128 v232, v[78:81] offset:4608
	ds_write_b128 v231, v[82:85] offset:1152
	ds_write_b128 v232, v[86:89] offset:5888
	ds_write_b128 v231, v[90:93] offset:2304
	ds_write_b128 v232, v[94:97] offset:7168
	ds_write_b128 v231, v[98:101] offset:3456
	ds_write_b128 v232, v[102:105] offset:8448
	s_waitcnt lgkmcnt(10)
	v_mfma_f32_32x32x16_bf16 v[18:33], v[38:41], v[138:141], v[18:33]
	v_add_f32_e32 v38, v135, v46
	v_add_f32_e32 v38, v136, v38
	v_add_f32_e32 v38, v137, v38
	v_add_f32_e32 v38, v142, v38
	v_add_f32_e32 v38, v143, v38
	v_add_f32_e32 v38, v144, v38
	v_add_f32_e32 v245, v145, v38
	v_mfma_f32_32x32x16_bf16 v[2:17], v[42:45], v[34:37], v[2:17]
	v_add_u32_e32 v34, s10, v222
	v_med3_i32 v34, v34, 0, v233
	v_mul_u32_u24_e32 v38, 0xc00, v34
	ds_read_b128 v[34:37], v177
	v_or_b32_e32 v38, v38, v176
	global_load_dwordx4 v[86:89], v38, s[8:9] offset:1024
	global_load_dwordx4 v[90:93], v38, s[8:9] offset:2048
	v_add_u32_e32 v38, s10, v223
	v_med3_i32 v38, v38, 0, v233
	v_mul_u32_u24_e32 v38, 0xc00, v38
	ds_read_b128 v[74:77], v177 offset:32
	v_or_b32_e32 v78, v38, v176
	s_waitcnt lgkmcnt(1)
	v_mfma_f32_32x32x16_bf16 v[34:49], v[34:37], v[70:73], 0
	global_load_dwordx4 v[134:137], v78, s[8:9] offset:1024
	global_load_dwordx4 v[142:145], v78, s[8:9] offset:2048
	v_add_u32_e32 v78, s10, v224
	v_med3_i32 v78, v78, 0, v233
	v_mul_u32_u24_e32 v78, 0xc00, v78
	v_or_b32_e32 v94, v78, v176
	ds_read_b128 v[78:81], v177 offset:96
	ds_read_b128 v[82:85], v177 offset:64
	global_load_dwordx4 v[146:149], v94, s[8:9] offset:1024
	global_load_dwordx4 v[150:153], v94, s[8:9] offset:2048
	s_waitcnt lgkmcnt(2)
	v_mfma_f32_32x32x16_bf16 v[34:49], v[74:77], v[62:65], v[34:49]
	v_add_u32_e32 v74, s10, v225
	v_med3_i32 v74, v74, 0, v233
	v_mul_u32_u24_e32 v74, 0xc00, v74
	v_or_b32_e32 v74, v74, v176
	global_load_dwordx4 v[154:157], v74, s[8:9] offset:1024
	global_load_dwordx4 v[158:161], v74, s[8:9] offset:2048
	s_waitcnt lgkmcnt(0)
	v_mfma_f32_32x32x16_bf16 v[34:49], v[82:85], v[54:57], v[34:49]
	v_add_f32_e32 v74, v165, v245
	v_add_f32_e32 v74, v171, v74
	v_add_f32_e32 v74, v172, v74
	v_add_f32_e32 v74, v173, v74
	v_add_f32_e32 v74, v237, v74
	v_mfma_f32_32x32x16_bf16 v[34:49], v[78:81], v[66:69], v[34:49]
	v_add_f32_e32 v74, v242, v74
	v_add_f32_e32 v74, v243, v74
	v_add_f32_e32 v74, v244, v74
	v_add_f32_e32 v50, v50, v74
	v_mfma_f32_32x32x16_bf16 v[2:17], v[238:241], v[138:141], v[2:17]
	s_nop 6
	v_add_u32_e32 v253, 59, v163
	v_cmp_le_i32_e32 vcc, 27, v253
	v_cmp_le_i32_e64 s[98:99], 26, v253
	v_cmp_le_i32_e64 s[100:101], 25, v253
	v_cndmask_b32_e32 v34, v234, v34, vcc
	v_cmp_le_i32_e32 vcc, 24, v253
	v_cndmask_b32_e64 v35, v234, v35, s[98:99]
	v_max3_f32 v75, v34, s31, v35
	v_cmp_le_i32_e64 s[98:99], 19, v253
	v_cndmask_b32_e64 v36, v234, v36, s[100:101]
	v_cmp_le_i32_e64 s[100:101], 18, v253
	v_cndmask_b32_e32 v37, v234, v37, vcc
	v_max3_f32 v75, v75, v36, v37
	v_cmp_le_i32_e32 vcc, 17, v253
	v_cndmask_b32_e64 v38, v234, v38, s[98:99]
	v_cmp_le_i32_e64 s[98:99], 16, v253
	v_cndmask_b32_e64 v39, v234, v39, s[100:101]
	v_max3_f32 v75, v75, v38, v39
	v_cmp_le_i32_e64 s[100:101], 11, v253
	v_cndmask_b32_e32 v40, v234, v40, vcc
	v_cmp_le_i32_e32 vcc, 10, v253
	v_cndmask_b32_e64 v41, v234, v41, s[98:99]
	v_max3_f32 v75, v75, v40, v41
	v_cmp_le_i32_e64 s[98:99], 9, v253
	v_cndmask_b32_e64 v42, v234, v42, s[100:101]
	v_cmp_le_i32_e64 s[100:101], 8, v253
	v_cndmask_b32_e32 v43, v234, v43, vcc
	v_max3_f32 v75, v75, v42, v43
	v_cmp_le_i32_e32 vcc, 3, v253
	v_cndmask_b32_e64 v44, v234, v44, s[98:99]
	v_cmp_le_i32_e64 s[98:99], 2, v253
	v_cndmask_b32_e64 v45, v234, v45, s[100:101]
	v_max3_f32 v75, v75, v44, v45
	v_cmp_le_i32_e64 s[100:101], 1, v253
	v_cndmask_b32_e32 v46, v234, v46, vcc
	v_cmp_le_i32_e32 vcc, 0, v253
	v_cndmask_b32_e64 v47, v234, v47, s[98:99]
	v_max3_f32 v75, v75, v46, v47
	v_cndmask_b32_e64 v48, v234, v48, s[100:101]
	v_cndmask_b32_e32 v49, v234, v49, vcc
	v_max3_f32 v75, v75, v48, v49
	ds_bpermute_b32 v76, v179, v75
	s_waitcnt lgkmcnt(0)
	v_max_f32_e32 v74, v76, v76
	v_max_f32_e32 v74, v75, v74
	v_cmp_gt_f32_e32 vcc, v74, v164
	s_cbranch_vccz .LBB0_414
	v_max_f32_e32 v74, v74, v74
	v_max_f32_e32 v75, v164, v164
	v_max_f32_e32 v75, v75, v74
	v_sub_f32_e32 v74, v164, v75
	v_exp_f32_e32 v74, v74
	v_mov_b32_e32 v164, v75
	v_pk_mul_f32 v[32:33], v[32:33], v[74:75] op_sel_hi:[1,0]
	v_pk_mul_f32 v[30:31], v[30:31], v[74:75] op_sel_hi:[1,0]
	v_pk_mul_f32 v[28:29], v[28:29], v[74:75] op_sel_hi:[1,0]
	v_pk_mul_f32 v[26:27], v[26:27], v[74:75] op_sel_hi:[1,0]
	v_pk_mul_f32 v[24:25], v[24:25], v[74:75] op_sel_hi:[1,0]
	v_pk_mul_f32 v[22:23], v[22:23], v[74:75] op_sel_hi:[1,0]
	v_pk_mul_f32 v[20:21], v[20:21], v[74:75] op_sel_hi:[1,0]
	v_pk_mul_f32 v[18:19], v[18:19], v[74:75] op_sel_hi:[1,0]
	v_pk_mul_f32 v[16:17], v[16:17], v[74:75] op_sel_hi:[1,0]
	v_pk_mul_f32 v[14:15], v[14:15], v[74:75] op_sel_hi:[1,0]
	v_pk_mul_f32 v[12:13], v[12:13], v[74:75] op_sel_hi:[1,0]
	v_pk_mul_f32 v[10:11], v[10:11], v[74:75] op_sel_hi:[1,0]
	v_pk_mul_f32 v[8:9], v[8:9], v[74:75] op_sel_hi:[1,0]
	v_pk_mul_f32 v[6:7], v[6:7], v[74:75] op_sel_hi:[1,0]
	v_pk_mul_f32 v[4:5], v[4:5], v[74:75] op_sel_hi:[1,0]
	v_pk_mul_f32 v[2:3], v[2:3], v[74:75] op_sel_hi:[1,0]
	v_mul_f32_e32 v50, v50, v74
; #define LAS __attribute__((address_space(3)))
; template <int STAGE, int OFF> __device__ __forceinline__ void attn32_unit(const bf16* base, bf16* yrow0, int blk0, int u, LAS unsigned char* xtab, LAS unsigned char* kbuf, LAS unsigned char* vbuf, int lane, ...
;     ...
;         for (int c = 0; c < 4; ++c) { *(LAS v4u*)(kbuf + (8 * c + lrow) * 144 + lch * 16) = kr[set][c]; *(LAS v4u*)(vbuf + (8 * c + lrow) * 160 + lch * 16) = vr[set][c]; }
;         if (pp + 2 < 5) { ATT32_LOAD(set, pp + 2, t0, SH); }
;         else { const bf16* base_ = base; { const bf16* base = nbase; ATT32_LOAD(set, pp + 2 - 5, nt0, nsh); } (void)base_; }
;         f32x16 sc;
; #pragma unroll
;         for (int i = 0; i < 16; ++i) sc[i] = 0.f;
; #pragma unroll
;         for (int ks = 0; ks < 4; ++ks) { const bf16x8 ka = *(const LAS bf16x8*)(kbuf + qi * 144 + 32 * ks + 16 * h); sc = MFMA32(ka, qb[ks], sc); }
;         if (pp == 4) {
; #pragma unroll
;             for (int ks = 0; ks < 4; ++ks) qb[ks] = *(const bf16x8*)(nbase + (size_t)min(nt0 + (qi << nsh), SEQ - 1) * 1536 + 16 * ks + 8 * h);
;         }
;         const int mbase = n0 + 4 * h - lo; float mx = -INFINITY;
; #pragma unroll
;         for (int rg = 0; rg < 16; ++rg) { sc[rg] = ((unsigned)(mbase + (rg & 3) + 8 * (rg >> 2)) <= mspan) ? sc[rg] : -INFINITY; mx = fmaxf(mx, sc[rg]); }
;         mx = fmaxf(mx, __shfl_xor(mx, 32));
;         if (__any(mx > m)) {
;             const float mn = fmaxf(m, mx), alpha = __builtin_amdgcn_exp2f(m - mn); m = mn; l *= alpha;
; #pragma unroll
;             for (int i = 0; i < 16; ++i) { o[0][i] *= alpha; o[1][i] *= alpha; }
;         }
;         float ps = 0.f;
; #pragma unroll
;         for (int rg = 0; rg < 16; ++rg) { sc[rg] = __builtin_amdgcn_exp2f(sc[rg] - m); ps += sc[rg]; }
;         l += ps;
;         bf16x8 pb[2];
; #pragma unroll
;         for (int s2 = 0; s2 < 2; ++s2) { v4u w; w.x = pg8::cvt_pk_bf16(sc[8 * s2], sc[8 * s2 + 1]); w.y = pg8::cvt_pk_bf16(sc[8 * s2 + 2], sc[8 * s2 + 3]); w.z = pg8::cvt_pk_bf16(sc[8 * s2 + 4], sc[8 * s2 + 5]); w.w = pg8::cvt_pk_bf16(sc[8 * s2 + 6], sc[8 * s2 + 7]); pb[s2] = __builtin_bit_cast(bf16x8, w); }
; #pragma unroll
;         for (int mb = 0; mb < 2; ++mb)
; #pragma unroll
;             for (int s2 = 0; s2 < 2; ++s2) {
;                 LAS unsigned char* vp = vbuf + tr_off + (16 * s2) * 160 + 64 * mb;
.LBB0_414:
	v_sub_f32_e32 v34, v34, v164
	v_exp_f32_e32 v74, v34
	v_sub_f32_e32 v34, v35, v164
	v_exp_f32_e32 v75, v34
	v_sub_f32_e32 v34, v36, v164
	v_exp_f32_e32 v76, v34
	v_sub_f32_e32 v34, v37, v164
	v_exp_f32_e32 v77, v34
	v_sub_f32_e32 v34, v38, v164
	v_exp_f32_e32 v78, v34
	v_sub_f32_e32 v34, v39, v164
	v_exp_f32_e32 v79, v34
	v_sub_f32_e32 v34, v40, v164
	v_exp_f32_e32 v80, v34
	v_sub_f32_e32 v34, v41, v164
	v_exp_f32_e32 v81, v34
	v_sub_f32_e32 v34, v42, v164
	v_exp_f32_e32 v165, v34
	v_sub_f32_e32 v34, v43, v164
	v_exp_f32_e32 v171, v34
	v_sub_f32_e32 v34, v44, v164
	v_exp_f32_e32 v172, v34
	v_sub_f32_e32 v34, v45, v164
	v_exp_f32_e32 v173, v34
	v_sub_f32_e32 v34, v46, v164
	v_exp_f32_e32 v237, v34
	v_sub_f32_e32 v34, v47, v164
	v_exp_f32_e32 v246, v34
	v_sub_f32_e32 v34, v48, v164
	v_exp_f32_e32 v247, v34
	v_sub_f32_e32 v34, v49, v164
	v_exp_f32_e32 v248, v34
	v_cvt_pk_bf16_f32 v34, v74, v75
	v_cvt_pk_bf16_f32 v35, v76, v77
	v_cvt_pk_bf16_f32 v36, v78, v79
	v_cvt_pk_bf16_f32 v37, v80, v81
	v_cvt_pk_bf16_f32 v238, v165, v171
	v_cvt_pk_bf16_f32 v239, v172, v173
	v_cvt_pk_bf16_f32 v240, v237, v246
	v_cvt_pk_bf16_f32 v241, v247, v248
	ds_read_b64_tr_b16 v[38:39], v181 offset:4608
	ds_read_b64_tr_b16 v[40:41], v181 offset:5888
	ds_read_b64_tr_b16 v[44:45], v181 offset:5952
	ds_read_b64_tr_b16 v[42:43], v181 offset:4672
	s_waitcnt lgkmcnt(2)
	v_mfma_f32_32x32x16_bf16 v[18:33], v[38:41], v[34:37], v[18:33]
	ds_read_b64_tr_b16 v[38:39], v181 offset:7168
	ds_read_b64_tr_b16 v[40:41], v181 offset:8448
	v_add_f32_e32 v46, 0, v74
	ds_read_b64_tr_b16 v[244:245], v181 offset:8512
	ds_read_b64_tr_b16 v[242:243], v181 offset:7232
	s_waitcnt vmcnt(15)
	ds_write_b128 v231, v[58:61]
	s_waitcnt vmcnt(14)
	ds_write_b128 v232, v[106:109] offset:4608
	s_waitcnt vmcnt(13)
	ds_write_b128 v231, v[110:113] offset:1152
	s_waitcnt vmcnt(12)
	ds_write_b128 v232, v[114:117] offset:5888
	s_waitcnt vmcnt(11)
	ds_write_b128 v231, v[118:121] offset:2304
	s_waitcnt vmcnt(10)
	ds_write_b128 v232, v[122:125] offset:7168
	s_waitcnt vmcnt(9)
	ds_write_b128 v231, v[126:129] offset:3456
	s_waitcnt vmcnt(8)
	ds_write_b128 v232, v[130:133] offset:8448
	v_add_u32_e32 v98, s10, v227
	v_add_u32_e32 v102, s10, v228
	s_waitcnt lgkmcnt(10)
	v_mfma_f32_32x32x16_bf16 v[18:33], v[38:41], v[238:241], v[18:33]
	v_add_f32_e32 v38, v75, v46
	v_add_f32_e32 v38, v76, v38
	v_add_f32_e32 v38, v77, v38
	v_add_f32_e32 v38, v78, v38
	v_add_f32_e32 v38, v79, v38
	v_add_f32_e32 v38, v80, v38
	v_add_f32_e32 v249, v81, v38
	v_mfma_f32_32x32x16_bf16 v[2:17], v[42:45], v[34:37], v[2:17]
	v_add_u32_e32 v34, s10, v207
	v_min_u32_e32 v34, 0x3fff, v34
	v_mul_u32_u24_e32 v38, 0xc00, v34
	ds_read_b128 v[34:37], v177
	v_or_b32_e32 v38, v38, v176
	global_load_dwordx4 v[58:61], v38, s[8:9] offset:1024
	global_load_dwordx4 v[74:77], v38, s[8:9] offset:2048
	v_add_u32_e32 v38, s10, v226
	v_min_u32_e32 v38, 0x3fff, v38
	v_mul_u32_u24_e32 v38, 0xc00, v38
	ds_read_b128 v[94:97], v177 offset:32
	v_or_b32_e32 v82, v38, v176
	s_waitcnt lgkmcnt(1)
	v_mfma_f32_32x32x16_bf16 v[34:49], v[34:37], v[70:73], 0
	v_min_u32_e32 v98, 0x3fff, v98
	v_min_u32_e32 v102, 0x3fff, v102
	v_mul_u32_u24_e32 v98, 0xc00, v98
	v_mul_u32_u24_e32 v102, 0xc00, v102
	v_or_b32_e32 v98, v98, v176
	v_or_b32_e32 v114, v102, v176
	global_load_dwordx4 v[78:81], v82, s[8:9] offset:1024
	s_nop 0
	global_load_dwordx4 v[82:85], v82, s[8:9] offset:2048
	ds_read_b128 v[106:109], v177 offset:96
	ds_read_b128 v[110:113], v177 offset:64
	s_waitcnt lgkmcnt(2)
	v_mfma_f32_32x32x16_bf16 v[34:49], v[94:97], v[62:65], v[34:49]
	global_load_dwordx4 v[94:97], v98, s[8:9] offset:1024
	s_nop 0
	global_load_dwordx4 v[98:101], v98, s[8:9] offset:2048
	s_nop 0
	global_load_dwordx4 v[102:105], v114, s[8:9] offset:1024
	global_load_dwordx4 v[138:141], v114, s[8:9] offset:2048
	s_waitcnt lgkmcnt(0)
	v_mfma_f32_32x32x16_bf16 v[34:49], v[110:113], v[54:57], v[34:49]
	v_add_f32_e32 v110, v165, v249
	v_add_f32_e32 v110, v171, v110
	v_add_f32_e32 v110, v172, v110
	v_add_f32_e32 v110, v173, v110
	v_add_f32_e32 v110, v237, v110
	v_add_f32_e32 v110, v246, v110
	v_add_f32_e32 v110, v247, v110
	v_mfma_f32_32x32x16_bf16 v[34:49], v[106:109], v[66:69], v[34:49]
	v_add_f32_e32 v108, v248, v110
	v_add_f32_e32 v50, v50, v108
	s_nop 5
	v_add_u32_e32 v253, 91, v163
	v_cmp_le_i32_e32 vcc, 27, v253
	v_cmp_le_i32_e64 s[98:99], 26, v253
	v_cmp_le_i32_e64 s[100:101], 25, v253
	v_cndmask_b32_e32 v34, v234, v34, vcc
	v_mfma_f32_32x32x16_bf16 v[2:17], v[242:245], v[238:241], v[2:17]
	v_cmp_le_i32_e32 vcc, 24, v253
	v_cndmask_b32_e64 v35, v234, v35, s[98:99]
	v_max3_f32 v106, v34, s31, v35
	v_cmp_le_i32_e64 s[98:99], 19, v253
	v_cndmask_b32_e64 v36, v234, v36, s[100:101]
	v_cmp_le_i32_e64 s[100:101], 18, v253
	v_cndmask_b32_e32 v37, v234, v37, vcc
	v_max3_f32 v106, v106, v36, v37
	v_cmp_le_i32_e32 vcc, 17, v253
	v_cndmask_b32_e64 v38, v234, v38, s[98:99]
	v_cmp_le_i32_e64 s[98:99], 16, v253
	v_cndmask_b32_e64 v39, v234, v39, s[100:101]
	v_max3_f32 v106, v106, v38, v39
	v_cmp_le_i32_e64 s[100:101], 11, v253
	v_cndmask_b32_e32 v40, v234, v40, vcc
	v_cmp_le_i32_e32 vcc, 10, v253
	v_cndmask_b32_e64 v41, v234, v41, s[98:99]
	v_max3_f32 v106, v106, v40, v41
	v_cmp_le_i32_e64 s[98:99], 9, v253
	v_cndmask_b32_e64 v42, v234, v42, s[100:101]
	v_cmp_le_i32_e64 s[100:101], 8, v253
	v_cndmask_b32_e32 v43, v234, v43, vcc
	v_max3_f32 v106, v106, v42, v43
	v_cmp_le_i32_e32 vcc, 3, v253
	v_cndmask_b32_e64 v44, v234, v44, s[98:99]
	v_cmp_le_i32_e64 s[98:99], 2, v253
	v_cndmask_b32_e64 v45, v234, v45, s[100:101]
	v_max3_f32 v106, v106, v44, v45
	v_cmp_le_i32_e64 s[100:101], 1, v253
	v_cndmask_b32_e32 v46, v234, v46, vcc
	v_cmp_le_i32_e32 vcc, 0, v253
	v_cndmask_b32_e64 v47, v234, v47, s[98:99]
	v_max3_f32 v106, v106, v46, v47
	v_cndmask_b32_e64 v48, v234, v48, s[100:101]
	v_cndmask_b32_e32 v49, v234, v49, vcc
	v_max3_f32 v106, v106, v48, v49
	ds_bpermute_b32 v107, v179, v106
	s_waitcnt lgkmcnt(0)
	v_max_f32_e32 v107, v107, v107
	v_max_f32_e32 v106, v106, v107
	v_cmp_gt_f32_e32 vcc, v106, v164
	s_cbranch_vccz .LBB0_416
; __device__ __forceinline__ unsigned cvt_pk_bf16(float lo, float hi) { unsigned r; asm volatile("v_cvt_pk_bf16_f32 %0, %1, %2" : "=v"(r) : "v"(lo), "v"(hi)); return r; }
; #define LAS __attribute__((address_space(3)))
; #define MFMA32(a, b, c) __builtin_amdgcn_mfma_f32_32x32x16_bf16((a), (b), (c), 0, 0, 0)
; template <int STAGE, int OFF> __device__ __forceinline__ void attn32_unit(const bf16* base, bf16* yrow0, int blk0, int u, LAS unsigned char* xtab, LAS unsigned char* kbuf, LAS unsigned char* vbuf, int lane, ...
;     ...
;         if (__any(mx > m)) {
;             const float mn = fmaxf(m, mx), alpha = __builtin_amdgcn_exp2f(m - mn); m = mn; l *= alpha;
; #pragma unroll
;             for (int i = 0; i < 16; ++i) { o[0][i] *= alpha; o[1][i] *= alpha; }
;         }
;         float ps = 0.f;
; #pragma unroll
;         for (int rg = 0; rg < 16; ++rg) { sc[rg] = __builtin_amdgcn_exp2f(sc[rg] - m); ps += sc[rg]; }
;         l += ps;
;         bf16x8 pb[2];
; #pragma unroll
;         for (int s2 = 0; s2 < 2; ++s2) { v4u w; w.x = pg8::cvt_pk_bf16(sc[8 * s2], sc[8 * s2 + 1]); w.y = pg8::cvt_pk_bf16(sc[8 * s2 + 2], sc[8 * s2 + 3]); w.z = pg8::cvt_pk_bf16(sc[8 * s2 + 4], sc[8 * s2 + 5]); w.w = pg8::cvt_pk_bf16(sc[8 * s2 + 6], sc[8 * s2 + 7]); pb[s2] = __builtin_bit_cast(bf16x8, w); }
; #pragma unroll
;         for (int mb = 0; mb < 2; ++mb)
; #pragma unroll
;             for (int s2 = 0; s2 < 2; ++s2) {
;                 LAS unsigned char* vp = vbuf + tr_off + (16 * s2) * 160 + 64 * mb;
;                 const v4i16 a0 = __builtin_amdgcn_ds_read_tr16_b64_v4i16((LAS v4i16*)vp), a1 = __builtin_amdgcn_ds_read_tr16_b64_v4i16((LAS v4i16*)(vp + 8 * 160));
;                 const bf16x8 va = __builtin_shufflevector(a0, a1, 0, 1, 2, 3, 4, 5, 6, 7);
;                 o[mb] = MFMA32(va, pb[s2], o[mb]);
	v_max_f32_e32 v106, v106, v106
	v_max_f32_e32 v107, v164, v164
	v_max_f32_e32 v107, v107, v106
	v_sub_f32_e32 v106, v164, v107
	v_exp_f32_e32 v106, v106
	v_mov_b32_e32 v164, v107
	v_pk_mul_f32 v[32:33], v[32:33], v[106:107] op_sel_hi:[1,0]
	v_pk_mul_f32 v[30:31], v[30:31], v[106:107] op_sel_hi:[1,0]
	v_pk_mul_f32 v[28:29], v[28:29], v[106:107] op_sel_hi:[1,0]
	v_pk_mul_f32 v[26:27], v[26:27], v[106:107] op_sel_hi:[1,0]
	v_pk_mul_f32 v[24:25], v[24:25], v[106:107] op_sel_hi:[1,0]
	v_pk_mul_f32 v[22:23], v[22:23], v[106:107] op_sel_hi:[1,0]
	v_pk_mul_f32 v[20:21], v[20:21], v[106:107] op_sel_hi:[1,0]
	v_pk_mul_f32 v[18:19], v[18:19], v[106:107] op_sel_hi:[1,0]
	v_pk_mul_f32 v[16:17], v[16:17], v[106:107] op_sel_hi:[1,0]
	v_pk_mul_f32 v[14:15], v[14:15], v[106:107] op_sel_hi:[1,0]
	v_pk_mul_f32 v[12:13], v[12:13], v[106:107] op_sel_hi:[1,0]
	v_pk_mul_f32 v[10:11], v[10:11], v[106:107] op_sel_hi:[1,0]
	v_pk_mul_f32 v[8:9], v[8:9], v[106:107] op_sel_hi:[1,0]
	v_pk_mul_f32 v[6:7], v[6:7], v[106:107] op_sel_hi:[1,0]
	v_pk_mul_f32 v[4:5], v[4:5], v[106:107] op_sel_hi:[1,0]
	v_pk_mul_f32 v[2:3], v[2:3], v[106:107] op_sel_hi:[1,0]
	v_mul_f32_e32 v50, v50, v106
.LBB0_416:
	v_sub_f32_e32 v34, v34, v164
	v_exp_f32_e32 v106, v34
	v_sub_f32_e32 v34, v35, v164
	v_exp_f32_e32 v107, v34
	v_sub_f32_e32 v34, v36, v164
	v_exp_f32_e32 v108, v34
	v_sub_f32_e32 v34, v37, v164
	v_exp_f32_e32 v109, v34
	v_sub_f32_e32 v34, v38, v164
	v_exp_f32_e32 v110, v34
	v_sub_f32_e32 v34, v39, v164
	v_exp_f32_e32 v111, v34
	v_sub_f32_e32 v34, v40, v164
	v_exp_f32_e32 v112, v34
	v_sub_f32_e32 v34, v41, v164
	v_exp_f32_e32 v113, v34
	v_sub_f32_e32 v34, v42, v164
	v_exp_f32_e32 v165, v34
	v_sub_f32_e32 v34, v43, v164
	v_exp_f32_e32 v171, v34
	v_sub_f32_e32 v34, v44, v164
	v_exp_f32_e32 v172, v34
	v_sub_f32_e32 v34, v45, v164
	v_exp_f32_e32 v173, v34
	v_sub_f32_e32 v34, v46, v164
	v_exp_f32_e32 v237, v34
	v_sub_f32_e32 v34, v47, v164
	v_exp_f32_e32 v246, v34
	v_sub_f32_e32 v34, v48, v164
	v_exp_f32_e32 v247, v34
	v_sub_f32_e32 v34, v49, v164
	v_exp_f32_e32 v248, v34
	v_cvt_pk_bf16_f32 v34, v106, v107
	v_cvt_pk_bf16_f32 v35, v108, v109
	v_cvt_pk_bf16_f32 v36, v110, v111
	v_cvt_pk_bf16_f32 v37, v112, v113
	v_cvt_pk_bf16_f32 v238, v165, v171
	v_cvt_pk_bf16_f32 v239, v172, v173
	v_cvt_pk_bf16_f32 v240, v237, v246
	v_cvt_pk_bf16_f32 v241, v247, v248
	ds_read_b64_tr_b16 v[38:39], v181 offset:4608
	ds_read_b64_tr_b16 v[40:41], v181 offset:5888
	ds_read_b64_tr_b16 v[44:45], v181 offset:5952
	ds_read_b64_tr_b16 v[42:43], v181 offset:4672
	s_waitcnt lgkmcnt(2)
	v_mfma_f32_32x32x16_bf16 v[18:33], v[38:41], v[34:37], v[18:33]
	ds_read_b64_tr_b16 v[38:39], v181 offset:7168
	ds_read_b64_tr_b16 v[40:41], v181 offset:8448
	v_add_f32_e32 v46, 0, v106
	s_add_i32 s10, s13, s21
	ds_read_b64_tr_b16 v[244:245], v181 offset:8512
	ds_read_b64_tr_b16 v[242:243], v181 offset:7232
	s_waitcnt vmcnt(15)
	ds_write_b128 v231, v[86:89]
	s_waitcnt vmcnt(14)
	ds_write_b128 v232, v[90:93] offset:4608
	s_waitcnt vmcnt(13)
	ds_write_b128 v231, v[134:137] offset:1152
	s_waitcnt vmcnt(12)
	ds_write_b128 v232, v[142:145] offset:5888
	s_waitcnt vmcnt(11)
	ds_write_b128 v231, v[146:149] offset:2304
	s_waitcnt vmcnt(10)
	ds_write_b128 v232, v[150:153] offset:7168
	s_waitcnt vmcnt(9)
	ds_write_b128 v231, v[154:157] offset:3456
	s_waitcnt vmcnt(8)
	ds_write_b128 v232, v[158:161] offset:8448
	s_waitcnt lgkmcnt(10)
	v_mfma_f32_32x32x16_bf16 v[18:33], v[38:41], v[238:241], v[18:33]
	v_add_f32_e32 v38, v107, v46
	v_add_f32_e32 v38, v108, v38
	v_add_f32_e32 v38, v109, v38
	v_add_f32_e32 v38, v110, v38
	v_add_f32_e32 v38, v111, v38
	v_add_f32_e32 v38, v112, v38
	v_add_f32_e32 v249, v113, v38
	v_mfma_f32_32x32x16_bf16 v[2:17], v[42:45], v[34:37], v[2:17]
	v_add_u32_e32 v34, s10, v208
	v_med3_i32 v34, v34, 0, v233
	v_mul_u32_u24_e32 v38, 0xc00, v34
	ds_read_b128 v[34:37], v177
	v_or_b32_e32 v38, v38, v176
	global_load_dwordx4 v[106:109], v38, s[8:9] offset:1024
	global_load_dwordx4 v[110:113], v38, s[8:9] offset:2048
	v_add_u32_e32 v38, s10, v209
	v_med3_i32 v38, v38, 0, v233
	v_mul_u32_u24_e32 v38, 0xc00, v38
	ds_read_b128 v[86:89], v177 offset:32
	v_or_b32_e32 v90, v38, v176
	s_waitcnt lgkmcnt(1)
	v_mfma_f32_32x32x16_bf16 v[34:49], v[34:37], v[70:73], 0
	global_load_dwordx4 v[114:117], v90, s[8:9] offset:1024
	global_load_dwordx4 v[118:121], v90, s[8:9] offset:2048
	v_add_u32_e32 v90, s10, v211
	v_med3_i32 v90, v90, 0, v233
	v_mul_u32_u24_e32 v90, 0xc00, v90
	v_or_b32_e32 v126, v90, v176
	ds_read_b128 v[90:93], v177 offset:96
	ds_read_b128 v[142:145], v177 offset:64
	global_load_dwordx4 v[122:125], v126, s[8:9] offset:1024
	s_nop 0
	global_load_dwordx4 v[126:129], v126, s[8:9] offset:2048
	s_waitcnt lgkmcnt(2)
	v_mfma_f32_32x32x16_bf16 v[34:49], v[86:89], v[62:65], v[34:49]
	v_add_u32_e32 v86, s10, v212
	v_med3_i32 v86, v86, 0, v233
	v_mul_u32_u24_e32 v86, 0xc00, v86
	v_or_b32_e32 v86, v86, v176
	global_load_dwordx4 v[130:133], v86, s[8:9] offset:1024
	global_load_dwordx4 v[134:137], v86, s[8:9] offset:2048
	s_waitcnt lgkmcnt(0)
; __device__ __forceinline__ unsigned cvt_pk_bf16(float lo, float hi) { unsigned r; asm volatile("v_cvt_pk_bf16_f32 %0, %1, %2" : "=v"(r) : "v"(lo), "v"(hi)); return r; }
; #define LAS __attribute__((address_space(3)))
; #define MFMA32(a, b, c) __builtin_amdgcn_mfma_f32_32x32x16_bf16((a), (b), (c), 0, 0, 0)
; template <int STAGE, int OFF> __device__ __forceinline__ void attn32_unit(const bf16* base, bf16* yrow0, int blk0, int u, LAS unsigned char* xtab, LAS unsigned char* kbuf, LAS unsigned char* vbuf, int lane, ...
;     ...
;         const int mbase = n0 + 4 * h - lo; float mx = -INFINITY;
; #pragma unroll
;         for (int rg = 0; rg < 16; ++rg) { sc[rg] = ((unsigned)(mbase + (rg & 3) + 8 * (rg >> 2)) <= mspan) ? sc[rg] : -INFINITY; mx = fmaxf(mx, sc[rg]); }
;         mx = fmaxf(mx, __shfl_xor(mx, 32));
;         if (__any(mx > m)) {
;             const float mn = fmaxf(m, mx), alpha = __builtin_amdgcn_exp2f(m - mn); m = mn; l *= alpha;
; #pragma unroll
;             for (int i = 0; i < 16; ++i) { o[0][i] *= alpha; o[1][i] *= alpha; }
;         }
;         float ps = 0.f;
; #pragma unroll
;         for (int rg = 0; rg < 16; ++rg) { sc[rg] = __builtin_amdgcn_exp2f(sc[rg] - m); ps += sc[rg]; }
;         l += ps;
;         bf16x8 pb[2];
; #pragma unroll
;         for (int s2 = 0; s2 < 2; ++s2) { v4u w; w.x = pg8::cvt_pk_bf16(sc[8 * s2], sc[8 * s2 + 1]); w.y = pg8::cvt_pk_bf16(sc[8 * s2 + 2], sc[8 * s2 + 3]); w.z = pg8::cvt_pk_bf16(sc[8 * s2 + 4], sc[8 * s2 + 5]); w.w = pg8::cvt_pk_bf16(sc[8 * s2 + 6], sc[8 * s2 + 7]); pb[s2] = __builtin_bit_cast(bf16x8, w); }
; #pragma unroll
;         for (int mb = 0; mb < 2; ++mb)
; #pragma unroll
;             for (int s2 = 0; s2 < 2; ++s2) {
;                 LAS unsigned char* vp = vbuf + tr_off + (16 * s2) * 160 + 64 * mb;
;                 const v4i16 a0 = __builtin_amdgcn_ds_read_tr16_b64_v4i16((LAS v4i16*)vp), a1 = __builtin_amdgcn_ds_read_tr16_b64_v4i16((LAS v4i16*)(vp + 8 * 160));
;                 const bf16x8 va = __builtin_shufflevector(a0, a1, 0, 1, 2, 3, 4, 5, 6, 7);
;                 o[mb] = MFMA32(va, pb[s2], o[mb]);
	v_mfma_f32_32x32x16_bf16 v[34:49], v[142:145], v[54:57], v[34:49]
	v_add_f32_e32 v86, v165, v249
	v_add_f32_e32 v86, v171, v86
	v_add_f32_e32 v86, v172, v86
	v_add_f32_e32 v86, v173, v86
	v_add_f32_e32 v86, v237, v86
	v_mfma_f32_32x32x16_bf16 v[34:49], v[90:93], v[66:69], v[34:49]
	v_add_f32_e32 v86, v246, v86
	v_add_f32_e32 v86, v247, v86
	v_add_f32_e32 v86, v248, v86
	v_add_f32_e32 v142, v50, v86
	v_mfma_f32_32x32x16_bf16 v[2:17], v[242:245], v[238:241], v[2:17]
	s_nop 6
	v_add_u32_e32 v253, 123, v163
	v_cmp_le_i32_e32 vcc, 27, v253
	v_cmp_le_i32_e64 s[98:99], 26, v253
	v_cmp_le_i32_e64 s[100:101], 25, v253
	v_cndmask_b32_e32 v34, v234, v34, vcc
	v_cmp_le_i32_e32 vcc, 24, v253
	v_cndmask_b32_e64 v35, v234, v35, s[98:99]
	v_max3_f32 v87, v34, s31, v35
	v_cmp_le_i32_e64 s[98:99], 19, v253
	v_cndmask_b32_e64 v36, v234, v36, s[100:101]
	v_cmp_le_i32_e64 s[100:101], 18, v253
	v_cndmask_b32_e32 v37, v234, v37, vcc
	v_max3_f32 v87, v87, v36, v37
	v_cmp_le_i32_e32 vcc, 17, v253
	v_cndmask_b32_e64 v38, v234, v38, s[98:99]
	v_cmp_le_i32_e64 s[98:99], 16, v253
	v_cndmask_b32_e64 v39, v234, v39, s[100:101]
	v_max3_f32 v87, v87, v38, v39
	v_cmp_le_i32_e64 s[100:101], 11, v253
	v_cndmask_b32_e32 v40, v234, v40, vcc
	v_cmp_le_i32_e32 vcc, 10, v253
	v_cndmask_b32_e64 v41, v234, v41, s[98:99]
	v_max3_f32 v87, v87, v40, v41
	v_cmp_le_i32_e64 s[98:99], 9, v253
	v_cndmask_b32_e64 v42, v234, v42, s[100:101]
	v_cmp_le_i32_e64 s[100:101], 8, v253
	v_cndmask_b32_e32 v43, v234, v43, vcc
	v_max3_f32 v87, v87, v42, v43
	v_cmp_le_i32_e32 vcc, 3, v253
	v_cndmask_b32_e64 v44, v234, v44, s[98:99]
	v_cmp_le_i32_e64 s[98:99], 2, v253
	v_cndmask_b32_e64 v45, v234, v45, s[100:101]
	v_max3_f32 v87, v87, v44, v45
	v_cmp_le_i32_e64 s[100:101], 1, v253
	v_cndmask_b32_e32 v46, v234, v46, vcc
	v_cmp_le_i32_e32 vcc, 0, v253
	v_cndmask_b32_e64 v47, v234, v47, s[98:99]
	v_max3_f32 v87, v87, v46, v47
	v_cndmask_b32_e64 v48, v234, v48, s[100:101]
	v_cndmask_b32_e32 v49, v234, v49, vcc
	v_max3_f32 v87, v87, v48, v49
	ds_bpermute_b32 v88, v179, v87
	s_waitcnt lgkmcnt(0)
	v_max_f32_e32 v50, v88, v88
	v_max_f32_e32 v50, v87, v50
	v_cmp_gt_f32_e32 vcc, v50, v164
	s_cbranch_vccz .LBB0_418
	v_max_f32_e32 v50, v50, v50
	v_max_f32_e32 v86, v164, v164
	v_max_f32_e32 v86, v86, v50
	v_sub_f32_e32 v50, v164, v86
	v_exp_f32_e32 v50, v50
	v_mov_b32_e32 v164, v86
	v_pk_mul_f32 v[32:33], v[32:33], v[50:51] op_sel_hi:[1,0]
	v_pk_mul_f32 v[30:31], v[30:31], v[50:51] op_sel_hi:[1,0]
	v_pk_mul_f32 v[28:29], v[28:29], v[50:51] op_sel_hi:[1,0]
	v_pk_mul_f32 v[26:27], v[26:27], v[50:51] op_sel_hi:[1,0]
	v_pk_mul_f32 v[24:25], v[24:25], v[50:51] op_sel_hi:[1,0]
	v_pk_mul_f32 v[22:23], v[22:23], v[50:51] op_sel_hi:[1,0]
	v_pk_mul_f32 v[20:21], v[20:21], v[50:51] op_sel_hi:[1,0]
	v_pk_mul_f32 v[18:19], v[18:19], v[50:51] op_sel_hi:[1,0]
	v_pk_mul_f32 v[16:17], v[16:17], v[50:51] op_sel_hi:[1,0]
	v_pk_mul_f32 v[14:15], v[14:15], v[50:51] op_sel_hi:[1,0]
	v_pk_mul_f32 v[12:13], v[12:13], v[50:51] op_sel_hi:[1,0]
	v_pk_mul_f32 v[10:11], v[10:11], v[50:51] op_sel_hi:[1,0]
	v_pk_mul_f32 v[8:9], v[8:9], v[50:51] op_sel_hi:[1,0]
	v_pk_mul_f32 v[6:7], v[6:7], v[50:51] op_sel_hi:[1,0]
	v_pk_mul_f32 v[4:5], v[4:5], v[50:51] op_sel_hi:[1,0]
	v_pk_mul_f32 v[2:3], v[2:3], v[50:51] op_sel_hi:[1,0]
	v_mul_f32_e32 v142, v142, v50
.LBB0_418:
	v_sub_f32_e32 v34, v34, v164
	v_exp_f32_e32 v86, v34
	v_sub_f32_e32 v34, v35, v164
	v_exp_f32_e32 v87, v34
	v_sub_f32_e32 v34, v36, v164
	v_exp_f32_e32 v88, v34
	v_sub_f32_e32 v34, v37, v164
	v_exp_f32_e32 v89, v34
	v_sub_f32_e32 v34, v38, v164
	v_exp_f32_e32 v90, v34
	v_sub_f32_e32 v34, v39, v164
	v_exp_f32_e32 v91, v34
	v_sub_f32_e32 v34, v40, v164
	v_exp_f32_e32 v92, v34
	v_sub_f32_e32 v34, v41, v164
	v_exp_f32_e32 v93, v34
	v_sub_f32_e32 v34, v42, v164
	v_exp_f32_e32 v143, v34
	v_sub_f32_e32 v34, v43, v164
	v_exp_f32_e32 v154, v34
	v_sub_f32_e32 v34, v44, v164
	v_exp_f32_e32 v155, v34
	v_sub_f32_e32 v34, v45, v164
	v_exp_f32_e32 v156, v34
	v_sub_f32_e32 v34, v46, v164
	v_exp_f32_e32 v157, v34
	v_sub_f32_e32 v34, v47, v164
	v_exp_f32_e32 v158, v34
	v_sub_f32_e32 v34, v48, v164
	v_exp_f32_e32 v159, v34
	v_sub_f32_e32 v34, v49, v164
	v_exp_f32_e32 v160, v34
	v_cvt_pk_bf16_f32 v34, v86, v87
	v_cvt_pk_bf16_f32 v35, v88, v89
	v_cvt_pk_bf16_f32 v36, v90, v91
	v_cvt_pk_bf16_f32 v37, v92, v93
	v_cvt_pk_bf16_f32 v144, v143, v154
	v_cvt_pk_bf16_f32 v145, v155, v156
	v_cvt_pk_bf16_f32 v146, v157, v158
	v_cvt_pk_bf16_f32 v147, v159, v160
	ds_read_b64_tr_b16 v[38:39], v181 offset:4608
	ds_read_b64_tr_b16 v[40:41], v181 offset:5888
	v_add_u32_e32 v50, s10, v52
	v_min_i32_e32 v148, 0x3fff, v50
	s_waitcnt lgkmcnt(0)
	v_mfma_f32_32x32x16_bf16 v[18:33], v[38:41], v[34:37], v[18:33]
	v_mul_u32_u24_e32 v38, 0xc00, v148
	v_mov_b32_e32 v39, v169
	v_lshl_add_u64 v[38:39], s[8:9], 0, v[38:39]
	ds_read_b64_tr_b16 v[42:43], v181 offset:7168
	ds_read_b64_tr_b16 v[44:45], v181 offset:8448
	ds_read_b64_tr_b16 v[48:49], v181 offset:5952
	ds_read_b64_tr_b16 v[46:47], v181 offset:4672
	v_lshl_add_u64 v[152:153], v[38:39], 0, v[168:169]
	v_add_f32_e32 v38, 0, v86
	v_add_f32_e32 v38, v87, v38
	v_add_f32_e32 v38, v88, v38
	v_add_f32_e32 v38, v89, v38
	v_add_f32_e32 v38, v90, v38
	v_add_f32_e32 v38, v91, v38
	s_waitcnt lgkmcnt(0)
	v_mfma_f32_32x32x16_bf16 v[2:17], v[46:49], v[34:37], v[2:17]
	v_add_u32_e32 v34, s10, v213
	ds_read_b64_tr_b16 v[150:151], v181 offset:8512
	ds_read_b64_tr_b16 v[148:149], v181 offset:7232
	v_add_f32_e32 v38, v92, v38
	s_waitcnt vmcnt(15)
	ds_write_b128 v231, v[58:61]
	s_waitcnt vmcnt(14)
	ds_write_b128 v232, v[74:77] offset:4608
	s_waitcnt vmcnt(13)
	ds_write_b128 v231, v[78:81] offset:1152
	s_waitcnt vmcnt(12)
; #define LAS __attribute__((address_space(3)))
; #define MFMA32(a, b, c) __builtin_amdgcn_mfma_f32_32x32x16_bf16((a), (b), (c), 0, 0, 0)
; template <int STAGE, int OFF> __device__ __forceinline__ void attn32_unit(const bf16* base, bf16* yrow0, int blk0, int u, LAS unsigned char* xtab, LAS unsigned char* kbuf, LAS unsigned char* vbuf, int lane, ...
;     ...
;         for (int c = 0; c < 4; ++c) { *(LAS v4u*)(kbuf + (8 * c + lrow) * 144 + lch * 16) = kr[set][c]; *(LAS v4u*)(vbuf + (8 * c + lrow) * 160 + lch * 16) = vr[set][c]; }
;         if (pp + 2 < 5) { ATT32_LOAD(set, pp + 2, t0, SH); }
;         else { const bf16* base_ = base; { const bf16* base = nbase; ATT32_LOAD(set, pp + 2 - 5, nt0, nsh); } (void)base_; }
;         f32x16 sc;
; #pragma unroll
;         for (int i = 0; i < 16; ++i) sc[i] = 0.f;
; #pragma unroll
;         for (int ks = 0; ks < 4; ++ks) { const bf16x8 ka = *(const LAS bf16x8*)(kbuf + qi * 144 + 32 * ks + 16 * h); sc = MFMA32(ka, qb[ks], sc); }
;         if (pp == 4) {
; #pragma unroll
;             for (int ks = 0; ks < 4; ++ks) qb[ks] = *(const bf16x8*)(nbase + (size_t)min(nt0 + (qi << nsh), SEQ - 1) * 1536 + 16 * ks + 8 * h);
;         }
;         const int mbase = n0 + 4 * h - lo; float mx = -INFINITY;
; #pragma unroll
;         for (int rg = 0; rg < 16; ++rg) { sc[rg] = ((unsigned)(mbase + (rg & 3) + 8 * (rg >> 2)) <= mspan) ? sc[rg] : -INFINITY; mx = fmaxf(mx, sc[rg]); }
;         mx = fmaxf(mx, __shfl_xor(mx, 32));
;         if (__any(mx > m)) {
;             const float mn = fmaxf(m, mx), alpha = __builtin_amdgcn_exp2f(m - mn); m = mn; l *= alpha;
; #pragma unroll
;             for (int i = 0; i < 16; ++i) { o[0][i] *= alpha; o[1][i] *= alpha; }
;         }
	ds_write_b128 v232, v[82:85] offset:5888
	s_waitcnt vmcnt(11)
	ds_write_b128 v231, v[94:97] offset:2304
	s_waitcnt vmcnt(10)
	ds_write_b128 v232, v[98:101] offset:7168
	s_waitcnt vmcnt(9)
	ds_write_b128 v231, v[102:105] offset:3456
	s_waitcnt vmcnt(8)
	ds_write_b128 v232, v[138:141] offset:8448
	v_med3_i32 v34, v34, 0, v233
	v_add_f32_e32 v161, v93, v38
	v_mul_u32_u24_e32 v38, 0xc00, v34
	ds_read_b128 v[34:37], v177
	v_or_b32_e32 v38, v38, v176
	global_load_dwordx4 v[74:77], v38, s[8:9] offset:1024
	global_load_dwordx4 v[78:81], v38, s[8:9] offset:2048
	v_add_u32_e32 v38, s10, v214
	v_med3_i32 v38, v38, 0, v233
	v_mul_u32_u24_e32 v38, 0xc00, v38
	ds_read_b128 v[58:61], v177 offset:32
	v_mfma_f32_32x32x16_bf16 v[18:33], v[42:45], v[144:147], v[18:33]
	v_or_b32_e32 v86, v38, v176
	global_load_dwordx4 v[82:85], v86, s[8:9] offset:1024
	s_nop 0
	global_load_dwordx4 v[86:89], v86, s[8:9] offset:2048
	v_add_f32_e32 v143, v143, v161
	v_add_f32_e32 v143, v154, v143
	v_add_f32_e32 v143, v155, v143
	v_add_f32_e32 v143, v156, v143
	v_add_f32_e32 v143, v157, v143
	s_waitcnt lgkmcnt(1)
	v_mfma_f32_32x32x16_bf16 v[34:49], v[34:37], v[70:73], 0
	v_add_u32_e32 v70, s10, v215
	v_med3_i32 v70, v70, 0, v233
	v_mul_u32_u24_e32 v70, 0xc00, v70
	v_or_b32_e32 v94, v70, v176
	ds_read_b128 v[138:141], v177 offset:96
	ds_read_b128 v[70:73], v177 offset:64
	global_load_dwordx4 v[90:93], v94, s[8:9] offset:1024
	s_nop 0
	global_load_dwordx4 v[94:97], v94, s[8:9] offset:2048
	v_add_f32_e32 v143, v158, v143
	s_waitcnt lgkmcnt(2)
	v_mfma_f32_32x32x16_bf16 v[34:49], v[58:61], v[62:65], v[34:49]
	v_add_u32_e32 v58, s10, v216
	v_med3_i32 v58, v58, 0, v233
	v_mul_u32_u24_e32 v58, 0xc00, v58
	v_or_b32_e32 v58, v58, v176
	global_load_dwordx4 v[98:101], v58, s[8:9] offset:1024
	global_load_dwordx4 v[102:105], v58, s[8:9] offset:2048
	v_add_f32_e32 v143, v159, v143
	s_waitcnt lgkmcnt(0)
	v_mfma_f32_32x32x16_bf16 v[34:49], v[70:73], v[54:57], v[34:49]
	global_load_dwordx4 v[62:65], v[152:153], off
	global_load_dwordx4 v[58:61], v[152:153], off offset:32
	global_load_dwordx4 v[54:57], v[152:153], off offset:64
	global_load_dwordx4 v[70:73], v[152:153], off offset:96
	v_mfma_f32_32x32x16_bf16 v[34:49], v[138:141], v[66:69], v[34:49]
	v_mfma_f32_32x32x16_bf16 v[2:17], v[148:151], v[144:147], v[2:17]
	s_nop 7
	v_sub_u32_e32 v253, v51, v163
	v_subrev_u32_e32 v253, 0x80, v253
	v_cmp_le_i32_e32 vcc, 0, v253
	v_cmp_le_i32_e64 s[98:99], 1, v253
	v_cmp_le_i32_e64 s[100:101], 2, v253
	v_cndmask_b32_e32 v66, v234, v34, vcc
	v_cmp_le_i32_e32 vcc, 3, v253
	v_cndmask_b32_e64 v35, v234, v35, s[98:99]
	v_max3_f32 v34, v66, s31, v35
	v_cmp_le_i32_e64 s[98:99], 8, v253
	v_cndmask_b32_e64 v36, v234, v36, s[100:101]
	v_cmp_le_i32_e64 s[100:101], 9, v253
	v_cndmask_b32_e32 v37, v234, v37, vcc
	v_max3_f32 v34, v34, v36, v37
	v_cmp_le_i32_e32 vcc, 10, v253
	v_cndmask_b32_e64 v38, v234, v38, s[98:99]
	v_cmp_le_i32_e64 s[98:99], 11, v253
	v_cndmask_b32_e64 v39, v234, v39, s[100:101]
	v_max3_f32 v34, v34, v38, v39
	v_cmp_le_i32_e64 s[100:101], 16, v253
	v_cndmask_b32_e32 v40, v234, v40, vcc
	v_cmp_le_i32_e32 vcc, 17, v253
	v_cndmask_b32_e64 v41, v234, v41, s[98:99]
	v_max3_f32 v34, v34, v40, v41
	v_cmp_le_i32_e64 s[98:99], 18, v253
	v_cndmask_b32_e64 v42, v234, v42, s[100:101]
	v_cmp_le_i32_e64 s[100:101], 19, v253
	v_cndmask_b32_e32 v43, v234, v43, vcc
	v_max3_f32 v34, v34, v42, v43
	v_cmp_le_i32_e32 vcc, 24, v253
	v_cndmask_b32_e64 v44, v234, v44, s[98:99]
	v_cmp_le_i32_e64 s[98:99], 25, v253
	v_cndmask_b32_e64 v45, v234, v45, s[100:101]
	v_max3_f32 v34, v34, v44, v45
	v_cmp_le_i32_e64 s[100:101], 26, v253
	v_cndmask_b32_e32 v46, v234, v46, vcc
	v_cmp_le_i32_e32 vcc, 27, v253
	v_cndmask_b32_e64 v47, v234, v47, s[98:99]
	v_max3_f32 v34, v34, v46, v47
	v_cndmask_b32_e64 v48, v234, v48, s[100:101]
	v_cndmask_b32_e32 v49, v234, v49, vcc
	v_max3_f32 v51, v34, v48, v49
	ds_bpermute_b32 v67, v179, v51
	v_add_f32_e32 v34, v160, v143
	v_add_f32_e32 v34, v142, v34
	s_waitcnt lgkmcnt(0)
	v_max_f32_e32 v67, v67, v67
	v_max_f32_e32 v51, v51, v67
	v_cmp_gt_f32_e32 vcc, v51, v164
	s_cbranch_vccz .LBB0_420
	v_max_f32_e32 v51, v51, v51
	v_max_f32_e32 v67, v164, v164
	v_max_f32_e32 v51, v67, v51
	v_sub_f32_e32 v67, v164, v51
	v_exp_f32_e32 v68, v67
	v_mov_b32_e32 v164, v51
	v_pk_mul_f32 v[32:33], v[32:33], v[68:69] op_sel_hi:[1,0]
	v_pk_mul_f32 v[30:31], v[30:31], v[68:69] op_sel_hi:[1,0]
	v_pk_mul_f32 v[28:29], v[28:29], v[68:69] op_sel_hi:[1,0]
	v_pk_mul_f32 v[26:27], v[26:27], v[68:69] op_sel_hi:[1,0]
	v_pk_mul_f32 v[24:25], v[24:25], v[68:69] op_sel_hi:[1,0]
	v_pk_mul_f32 v[22:23], v[22:23], v[68:69] op_sel_hi:[1,0]
	v_pk_mul_f32 v[20:21], v[20:21], v[68:69] op_sel_hi:[1,0]
	v_pk_mul_f32 v[18:19], v[18:19], v[68:69] op_sel_hi:[1,0]
	v_pk_mul_f32 v[16:17], v[16:17], v[68:69] op_sel_hi:[1,0]
	v_pk_mul_f32 v[14:15], v[14:15], v[68:69] op_sel_hi:[1,0]
	v_pk_mul_f32 v[12:13], v[12:13], v[68:69] op_sel_hi:[1,0]
	v_pk_mul_f32 v[10:11], v[10:11], v[68:69] op_sel_hi:[1,0]
	v_pk_mul_f32 v[8:9], v[8:9], v[68:69] op_sel_hi:[1,0]
	v_pk_mul_f32 v[6:7], v[6:7], v[68:69] op_sel_hi:[1,0]
	v_pk_mul_f32 v[4:5], v[4:5], v[68:69] op_sel_hi:[1,0]
	v_pk_mul_f32 v[2:3], v[2:3], v[68:69] op_sel_hi:[1,0]
	v_mul_f32_e32 v34, v34, v68
; __device__ __forceinline__ unsigned cvt_pk_bf16(float lo, float hi) { unsigned r; asm volatile("v_cvt_pk_bf16_f32 %0, %1, %2" : "=v"(r) : "v"(lo), "v"(hi)); return r; }
; #define LAS __attribute__((address_space(3)))
; template <int STAGE, int OFF> __device__ __forceinline__ void attn32_unit(const bf16* base, bf16* yrow0, int blk0, int u, LAS unsigned char* xtab, LAS unsigned char* kbuf, LAS unsigned char* vbuf, int lane, ...
;     ...
;         for (int rg = 0; rg < 16; ++rg) { sc[rg] = __builtin_amdgcn_exp2f(sc[rg] - m); ps += sc[rg]; }
;         l += ps;
;         bf16x8 pb[2];
; #pragma unroll
;         for (int s2 = 0; s2 < 2; ++s2) { v4u w; w.x = pg8::cvt_pk_bf16(sc[8 * s2], sc[8 * s2 + 1]); w.y = pg8::cvt_pk_bf16(sc[8 * s2 + 2], sc[8 * s2 + 3]); w.z = pg8::cvt_pk_bf16(sc[8 * s2 + 4], sc[8 * s2 + 5]); w.w = pg8::cvt_pk_bf16(sc[8 * s2 + 6], sc[8 * s2 + 7]); pb[s2] = __builtin_bit_cast(bf16x8, w); }
; #pragma unroll
;         for (int mb = 0; mb < 2; ++mb)
; #pragma unroll
;             for (int s2 = 0; s2 < 2; ++s2) {
;                 LAS unsigned char* vp = vbuf + tr_off + (16 * s2) * 160 + 64 * mb;
;                 const v4i16 a0 = __builtin_amdgcn_ds_read_tr16_b64_v4i16((LAS v4i16*)vp), a1 = __builtin_amdgcn_ds_read_tr16_b64_v4i16((LAS v4i16*)(vp + 8 * 160));
;                 const bf16x8 va = __builtin_shufflevector(a0, a1, 0, 1, 2, 3, 4, 5, 6, 7);
;                 o[mb] = MFMA32(va, pb[s2], o[mb]);
;             }
;         asm volatile("" ::: "memory");
;     }
;     l += __shfl_xor(l, 32);
;     if (STAGE < 2) {
; #pragma unroll
;         for (int mb = 0; mb < 2; ++mb)
; #pragma unroll
;             for (int gq = 0; gq < 4; ++gq) { v2u w; w.x = pk2(o[mb][4 * gq], o[mb][4 * gq + 1]); w.y = pk2(o[mb][4 * gq + 2], o[mb][4 * gq + 3]); *(LAS v2u*)(xrow + 2 * (32 * mb + 8 * gq + 4 * h)) = w; }
;         if (h == 0) { *(LAS float*)(xrow + 128) = m; *(LAS float*)(xrow + 132) = l; }
;     } else {
;         const float inv = __builtin_amdgcn_rcpf(l);
;         bf16* yo = yrow0 + (size_t)tq * 1024 + 4 * h;
; #pragma unroll
;         for (int mb = 0; mb < 2; ++mb)
; #pragma unroll
;             for (int gq = 0; gq < 4; ++gq) { uint2 w; w.x = pk2(o[mb][4 * gq] * inv, o[mb][4 * gq + 1] * inv); w.y = pk2(o[mb][4 * gq + 2] * inv, o[mb][4 * gq + 3] * inv); *(uint2*)(yo + 32 * mb + 8 * gq) = w; }
;     }
.LBB0_420:
	v_sub_f32_e32 v36, v36, v164
	v_exp_f32_e32 v142, v36
	v_sub_f32_e32 v36, v37, v164
	v_exp_f32_e32 v143, v36
	v_sub_f32_e32 v36, v38, v164
	v_exp_f32_e32 v144, v36
	v_sub_f32_e32 v36, v39, v164
	v_exp_f32_e32 v145, v36
	v_sub_f32_e32 v36, v40, v164
	v_exp_f32_e32 v146, v36
	v_sub_f32_e32 v36, v41, v164
	v_exp_f32_e32 v147, v36
	v_sub_f32_e32 v36, v42, v164
	v_exp_f32_e32 v148, v36
	v_sub_f32_e32 v36, v43, v164
	v_exp_f32_e32 v149, v36
	v_sub_f32_e32 v36, v44, v164
	v_sub_f32_e32 v51, v66, v164
	v_exp_f32_e32 v150, v36
	v_sub_f32_e32 v36, v45, v164
	v_exp_f32_e32 v51, v51
	v_sub_f32_e32 v35, v35, v164
	v_exp_f32_e32 v151, v36
	v_sub_f32_e32 v36, v46, v164
	v_exp_f32_e32 v35, v35
	v_exp_f32_e32 v152, v36
	v_sub_f32_e32 v36, v47, v164
	v_exp_f32_e32 v153, v36
	v_sub_f32_e32 v36, v48, v164
	v_exp_f32_e32 v48, v36
	v_sub_f32_e32 v36, v49, v164
	v_exp_f32_e32 v49, v36
	v_cvt_pk_bf16_f32 v36, v51, v35
	v_add_f32_e32 v51, 0, v51
	v_add_f32_e32 v35, v35, v51
	v_add_f32_e32 v35, v142, v35
	v_add_f32_e32 v35, v143, v35
	v_add_f32_e32 v35, v144, v35
	v_cvt_pk_bf16_f32 v37, v142, v143
	v_cvt_pk_bf16_f32 v38, v144, v145
	v_cvt_pk_bf16_f32 v39, v146, v147
	v_cvt_pk_bf16_f32 v40, v148, v149
	v_cvt_pk_bf16_f32 v41, v150, v151
	v_cvt_pk_bf16_f32 v42, v152, v153
	v_cvt_pk_bf16_f32 v43, v48, v49
	ds_read_b64_tr_b16 v[44:45], v181 offset:4608
	ds_read_b64_tr_b16 v[46:47], v181 offset:5888
	v_add_f32_e32 v35, v145, v35
	v_add_f32_e32 v35, v146, v35
	v_add_f32_e32 v35, v147, v35
	v_add_f32_e32 v35, v148, v35
	v_add_f32_e32 v35, v149, v35
	s_waitcnt lgkmcnt(0)
	v_mfma_f32_32x32x16_bf16 v[18:33], v[44:47], v[36:39], v[18:33]
	v_add_f32_e32 v35, v150, v35
	v_add_f32_e32 v35, v151, v35
	v_add_f32_e32 v35, v152, v35
	v_add_f32_e32 v35, v153, v35
	v_add_f32_e32 v35, v48, v35
	ds_read_b64_tr_b16 v[66:67], v181 offset:7168
	ds_read_b64_tr_b16 v[68:69], v181 offset:8448
	ds_read_b64_tr_b16 v[140:141], v181 offset:5952
	ds_read_b64_tr_b16 v[138:139], v181 offset:4672
	v_add_f32_e32 v35, v49, v35
	v_add_f32_e32 v34, v34, v35
	ds_bpermute_b32 v35, v179, v34
	s_waitcnt lgkmcnt(3)
	v_mfma_f32_32x32x16_bf16 v[18:33], v[66:69], v[40:43], v[18:33]
	s_ashr_i32 s13, s12, 31
	s_lshl_b64 s[12:13], s[12:13], 25
	s_add_u32 s0, s18, s12
	s_waitcnt lgkmcnt(0)
	v_add_f32_e32 v34, v34, v35
	v_rcp_f32_e32 v34, v34
	s_addc_u32 s1, s19, s13
	s_add_u32 s12, s0, s39
	v_mfma_f32_32x32x16_bf16 v[2:17], v[138:141], v[36:39], v[2:17]
	s_nop 2
	v_mov_b32_e32 v38, v18
	v_mov_b32_e32 v39, v20
	v_mul_f32_e64 v38, v38, v34
	v_mul_f32_e64 v39, v39, v34
	v_mov_b32_e32 v20, v19
	v_pk_mul_f32 v[18:19], v[20:21], v[34:35] op_sel_hi:[1,0]
	v_and_b32_sdwa v21, v38, v236 dst_sel:DWORD dst_unused:UNUSED_PAD src0_sel:WORD_1 src1_sel:DWORD
	v_mov_b32_e32 v163, v169
	v_add3_u32 v21, v38, v21, s35
	v_and_b32_sdwa v35, v19, v236 dst_sel:DWORD dst_unused:UNUSED_PAD src0_sel:WORD_1 src1_sel:DWORD
	v_and_b32_sdwa v38, v18, v236 dst_sel:DWORD dst_unused:UNUSED_PAD src0_sel:WORD_1 src1_sel:DWORD
	s_addc_u32 s13, s1, 0
	v_lshlrev_b64 v[36:37], 11, v[162:163]
	v_and_b32_sdwa v20, v39, v236 dst_sel:DWORD dst_unused:UNUSED_PAD src0_sel:WORD_1 src1_sel:DWORD
	v_add3_u32 v19, v19, v35, s35
	v_add3_u32 v18, v18, v38, s35
	v_lshl_add_u64 v[36:37], s[12:13], 0, v[36:37]
	v_mov_b32_e32 v171, v169
	v_add3_u32 v20, v39, v20, s35
	v_and_b32_e32 v19, 0xffff0000, v19
	v_and_b32_e32 v18, 0xffff0000, v18
	v_lshl_add_u64 v[36:37], v[36:37], 0, v[170:171]
	v_or_b32_sdwa v19, v19, v20 dst_sel:DWORD dst_unused:UNUSED_PAD src0_sel:DWORD src1_sel:WORD_1
	v_or_b32_sdwa v18, v18, v21 dst_sel:DWORD dst_unused:UNUSED_PAD src0_sel:DWORD src1_sel:WORD_1
	ds_read_b64_tr_b16 v[46:47], v181 offset:8512
	ds_read_b64_tr_b16 v[44:45], v181 offset:7232
	global_store_dwordx2 v[36:37], v[18:19], off
	v_mov_b32_e32 v18, v22
	v_mov_b32_e32 v19, v24
	v_pk_mul_f32 v[18:19], v[18:19], v[34:35] op_sel_hi:[1,0]
	v_mov_b32_e32 v24, v23
	v_pk_mul_f32 v[20:21], v[24:25], v[34:35] op_sel_hi:[1,0]
	v_and_b32_sdwa v22, v19, v236 dst_sel:DWORD dst_unused:UNUSED_PAD src0_sel:WORD_1 src1_sel:DWORD
	v_and_b32_sdwa v23, v18, v236 dst_sel:DWORD dst_unused:UNUSED_PAD src0_sel:WORD_1 src1_sel:DWORD
	v_add3_u32 v18, v18, v23, s35
	v_add3_u32 v19, v19, v22, s35
	v_and_b32_sdwa v22, v21, v236 dst_sel:DWORD dst_unused:UNUSED_PAD src0_sel:WORD_1 src1_sel:DWORD
	v_and_b32_sdwa v23, v20, v236 dst_sel:DWORD dst_unused:UNUSED_PAD src0_sel:WORD_1 src1_sel:DWORD
	v_add3_u32 v21, v21, v22, s35
	v_add3_u32 v20, v20, v23, s35
	v_and_b32_e32 v21, 0xffff0000, v21
	v_and_b32_e32 v20, 0xffff0000, v20
	v_or_b32_sdwa v19, v21, v19 dst_sel:DWORD dst_unused:UNUSED_PAD src0_sel:DWORD src1_sel:WORD_1
	v_or_b32_sdwa v18, v20, v18 dst_sel:DWORD dst_unused:UNUSED_PAD src0_sel:DWORD src1_sel:WORD_1
	global_store_dwordx2 v[36:37], v[18:19], off offset:16
	v_mov_b32_e32 v18, v26
	v_mov_b32_e32 v19, v28
	v_pk_mul_f32 v[18:19], v[18:19], v[34:35] op_sel_hi:[1,0]
	v_mov_b32_e32 v28, v27
	v_pk_mul_f32 v[20:21], v[28:29], v[34:35] op_sel_hi:[1,0]
	v_and_b32_sdwa v22, v19, v236 dst_sel:DWORD dst_unused:UNUSED_PAD src0_sel:WORD_1 src1_sel:DWORD
	v_and_b32_sdwa v23, v18, v236 dst_sel:DWORD dst_unused:UNUSED_PAD src0_sel:WORD_1 src1_sel:DWORD
	v_add3_u32 v18, v18, v23, s35
	v_add3_u32 v19, v19, v22, s35
	v_and_b32_sdwa v22, v21, v236 dst_sel:DWORD dst_unused:UNUSED_PAD src0_sel:WORD_1 src1_sel:DWORD
	v_and_b32_sdwa v23, v20, v236 dst_sel:DWORD dst_unused:UNUSED_PAD src0_sel:WORD_1 src1_sel:DWORD
	v_add3_u32 v21, v21, v22, s35
	v_add3_u32 v20, v20, v23, s35
	v_and_b32_e32 v21, 0xffff0000, v21
	v_and_b32_e32 v20, 0xffff0000, v20
	s_waitcnt lgkmcnt(0)
; __device__ __forceinline__ float bf_lo(unsigned w) { return __uint_as_float(w << 16); }
; __device__ __forceinline__ float bf_hi(unsigned w) { return __uint_as_float(w & 0xffff0000u); }
; #define LAS __attribute__((address_space(3)))
; __device__ __forceinline__ unsigned pk2(float lo, float hi) { return f2bf(lo) | (f2bf(hi) << 16); }
; template <int STAGE, int OFF> __device__ __forceinline__ void attn32_unit(const bf16* base, bf16* yrow0, int blk0, int u, LAS unsigned char* xtab, LAS unsigned char* kbuf, LAS unsigned char* vbuf, int lane, ...
;     ...
;     } else {
; #pragma unroll
;         for (int mb = 0; mb < 2; ++mb)
; #pragma unroll
;             for (int gq = 0; gq < 4; ++gq) { const v2u w = *(const LAS v2u*)(xrow + 2 * (32 * mb + 8 * gq + 4 * h)); o[mb][4 * gq] = bf_lo(w.x); o[mb][4 * gq + 1] = bf_hi(w.x); o[mb][4 * gq + 2] = bf_lo(w.y); o[mb][4 * gq + 3] = bf_hi(w.y); }
;         m = *(const LAS float*)(xrow + 128); l = h == 0 ? *(const LAS float*)(xrow + 132) : 0.f;
;     ...
;         const float inv = __builtin_amdgcn_rcpf(l);
;         bf16* yo = yrow0 + (size_t)tq * 1024 + 4 * h;
; #pragma unroll
;         for (int mb = 0; mb < 2; ++mb)
; #pragma unroll
;             for (int gq = 0; gq < 4; ++gq) { uint2 w; w.x = pk2(o[mb][4 * gq] * inv, o[mb][4 * gq + 1] * inv); w.y = pk2(o[mb][4 * gq + 2] * inv, o[mb][4 * gq + 3] * inv); *(uint2*)(yo + 32 * mb + 8 * gq) = w; }
;     }
	v_mfma_f32_32x32x16_bf16 v[2:17], v[44:47], v[40:43], v[2:17]
	v_or_b32_sdwa v19, v21, v19 dst_sel:DWORD dst_unused:UNUSED_PAD src0_sel:DWORD src1_sel:WORD_1
	v_or_b32_sdwa v18, v20, v18 dst_sel:DWORD dst_unused:UNUSED_PAD src0_sel:DWORD src1_sel:WORD_1
	global_store_dwordx2 v[36:37], v[18:19], off offset:32
	v_mov_b32_e32 v18, v30
	v_mov_b32_e32 v19, v32
	v_pk_mul_f32 v[18:19], v[18:19], v[34:35] op_sel_hi:[1,0]
	v_mov_b32_e32 v32, v31
	v_pk_mul_f32 v[20:21], v[32:33], v[34:35] op_sel_hi:[1,0]
	v_and_b32_sdwa v22, v19, v236 dst_sel:DWORD dst_unused:UNUSED_PAD src0_sel:WORD_1 src1_sel:DWORD
	v_and_b32_sdwa v23, v18, v236 dst_sel:DWORD dst_unused:UNUSED_PAD src0_sel:WORD_1 src1_sel:DWORD
	v_add3_u32 v18, v18, v23, s35
	v_add3_u32 v19, v19, v22, s35
	v_and_b32_sdwa v22, v21, v236 dst_sel:DWORD dst_unused:UNUSED_PAD src0_sel:WORD_1 src1_sel:DWORD
	v_and_b32_sdwa v23, v20, v236 dst_sel:DWORD dst_unused:UNUSED_PAD src0_sel:WORD_1 src1_sel:DWORD
	v_add3_u32 v21, v21, v22, s35
	v_add3_u32 v20, v20, v23, s35
	v_and_b32_e32 v21, 0xffff0000, v21
	v_and_b32_e32 v20, 0xffff0000, v20
	v_or_b32_sdwa v19, v21, v19 dst_sel:DWORD dst_unused:UNUSED_PAD src0_sel:DWORD src1_sel:WORD_1
	v_or_b32_sdwa v18, v20, v18 dst_sel:DWORD dst_unused:UNUSED_PAD src0_sel:DWORD src1_sel:WORD_1
	global_store_dwordx2 v[36:37], v[18:19], off offset:48
	v_mov_b32_e32 v18, v2
	v_mov_b32_e32 v19, v4
	v_pk_mul_f32 v[18:19], v[18:19], v[34:35] op_sel_hi:[1,0]
	v_mov_b32_e32 v4, v3
	v_pk_mul_f32 v[2:3], v[4:5], v[34:35] op_sel_hi:[1,0]
	v_and_b32_sdwa v4, v19, v236 dst_sel:DWORD dst_unused:UNUSED_PAD src0_sel:WORD_1 src1_sel:DWORD
	v_and_b32_sdwa v5, v18, v236 dst_sel:DWORD dst_unused:UNUSED_PAD src0_sel:WORD_1 src1_sel:DWORD
	v_add3_u32 v5, v18, v5, s35
	v_add3_u32 v4, v19, v4, s35
	v_and_b32_sdwa v18, v3, v236 dst_sel:DWORD dst_unused:UNUSED_PAD src0_sel:WORD_1 src1_sel:DWORD
	v_and_b32_sdwa v19, v2, v236 dst_sel:DWORD dst_unused:UNUSED_PAD src0_sel:WORD_1 src1_sel:DWORD
	v_add3_u32 v3, v3, v18, s35
	v_add3_u32 v2, v2, v19, s35
	v_and_b32_e32 v3, 0xffff0000, v3
	v_and_b32_e32 v2, 0xffff0000, v2
	v_or_b32_sdwa v3, v3, v4 dst_sel:DWORD dst_unused:UNUSED_PAD src0_sel:DWORD src1_sel:WORD_1
	v_or_b32_sdwa v2, v2, v5 dst_sel:DWORD dst_unused:UNUSED_PAD src0_sel:DWORD src1_sel:WORD_1
	global_store_dwordx2 v[36:37], v[2:3], off offset:64
	v_mov_b32_e32 v2, v6
	v_mov_b32_e32 v3, v8
	v_pk_mul_f32 v[2:3], v[2:3], v[34:35] op_sel_hi:[1,0]
	v_mov_b32_e32 v8, v7
	v_pk_mul_f32 v[4:5], v[8:9], v[34:35] op_sel_hi:[1,0]
	v_and_b32_sdwa v6, v3, v236 dst_sel:DWORD dst_unused:UNUSED_PAD src0_sel:WORD_1 src1_sel:DWORD
	v_and_b32_sdwa v7, v2, v236 dst_sel:DWORD dst_unused:UNUSED_PAD src0_sel:WORD_1 src1_sel:DWORD
	v_add3_u32 v2, v2, v7, s35
	v_add3_u32 v3, v3, v6, s35
	v_and_b32_sdwa v6, v5, v236 dst_sel:DWORD dst_unused:UNUSED_PAD src0_sel:WORD_1 src1_sel:DWORD
	v_and_b32_sdwa v7, v4, v236 dst_sel:DWORD dst_unused:UNUSED_PAD src0_sel:WORD_1 src1_sel:DWORD
	v_add3_u32 v5, v5, v6, s35
	v_add3_u32 v4, v4, v7, s35
	v_and_b32_e32 v5, 0xffff0000, v5
	v_and_b32_e32 v4, 0xffff0000, v4
	v_or_b32_sdwa v3, v5, v3 dst_sel:DWORD dst_unused:UNUSED_PAD src0_sel:DWORD src1_sel:WORD_1
	v_or_b32_sdwa v2, v4, v2 dst_sel:DWORD dst_unused:UNUSED_PAD src0_sel:DWORD src1_sel:WORD_1
	global_store_dwordx2 v[36:37], v[2:3], off offset:80
	v_mov_b32_e32 v2, v10
	v_mov_b32_e32 v3, v12
	v_pk_mul_f32 v[2:3], v[2:3], v[34:35] op_sel_hi:[1,0]
	v_mov_b32_e32 v12, v11
	v_pk_mul_f32 v[4:5], v[12:13], v[34:35] op_sel_hi:[1,0]
	v_and_b32_sdwa v6, v3, v236 dst_sel:DWORD dst_unused:UNUSED_PAD src0_sel:WORD_1 src1_sel:DWORD
	v_and_b32_sdwa v7, v2, v236 dst_sel:DWORD dst_unused:UNUSED_PAD src0_sel:WORD_1 src1_sel:DWORD
	v_add3_u32 v2, v2, v7, s35
	v_add3_u32 v3, v3, v6, s35
	v_and_b32_sdwa v6, v5, v236 dst_sel:DWORD dst_unused:UNUSED_PAD src0_sel:WORD_1 src1_sel:DWORD
	v_and_b32_sdwa v7, v4, v236 dst_sel:DWORD dst_unused:UNUSED_PAD src0_sel:WORD_1 src1_sel:DWORD
	v_add3_u32 v5, v5, v6, s35
	v_add3_u32 v4, v4, v7, s35
	v_and_b32_e32 v5, 0xffff0000, v5
	v_and_b32_e32 v4, 0xffff0000, v4
	v_or_b32_sdwa v3, v5, v3 dst_sel:DWORD dst_unused:UNUSED_PAD src0_sel:DWORD src1_sel:WORD_1
	v_or_b32_sdwa v2, v4, v2 dst_sel:DWORD dst_unused:UNUSED_PAD src0_sel:DWORD src1_sel:WORD_1
	global_store_dwordx2 v[36:37], v[2:3], off offset:96
	v_mov_b32_e32 v2, v14
	v_mov_b32_e32 v3, v16
	v_pk_mul_f32 v[2:3], v[2:3], v[34:35] op_sel_hi:[1,0]
	v_mov_b32_e32 v16, v15
	v_pk_mul_f32 v[4:5], v[16:17], v[34:35] op_sel_hi:[1,0]
	v_and_b32_sdwa v7, v2, v236 dst_sel:DWORD dst_unused:UNUSED_PAD src0_sel:WORD_1 src1_sel:DWORD
	v_and_b32_sdwa v6, v3, v236 dst_sel:DWORD dst_unused:UNUSED_PAD src0_sel:WORD_1 src1_sel:DWORD
	v_add3_u32 v18, v2, v7, s35
	v_and_b32_sdwa v2, v5, v236 dst_sel:DWORD dst_unused:UNUSED_PAD src0_sel:WORD_1 src1_sel:DWORD
	v_add3_u32 v19, v3, v6, s35
	v_and_b32_sdwa v3, v4, v236 dst_sel:DWORD dst_unused:UNUSED_PAD src0_sel:WORD_1 src1_sel:DWORD
	v_add3_u32 v2, v5, v2, s35
	v_add_u32_e32 v14, v229, v166
	v_add3_u32 v20, v4, v3, s35
	v_and_b32_e32 v21, 0xffff0000, v2
	ds_read2_b64 v[10:13], v14 offset1:2
	ds_read2_b64 v[2:5], v14 offset0:4 offset1:6
	ds_read2_b64 v[6:9], v14 offset0:8 offset1:10
	ds_read2_b64 v[14:17], v14 offset0:12 offset1:14
	ds_read_b32 v139, v229 offset:128
	v_and_b32_e32 v20, 0xffff0000, v20
	v_mov_b32_e32 v140, 0
	v_or_b32_sdwa v19, v21, v19 dst_sel:DWORD dst_unused:UNUSED_PAD src0_sel:DWORD src1_sel:WORD_1
	v_or_b32_sdwa v18, v20, v18 dst_sel:DWORD dst_unused:UNUSED_PAD src0_sel:DWORD src1_sel:WORD_1
	global_store_dwordx2 v[36:37], v[18:19], off offset:112
	s_and_saveexec_b64 s[14:15], s[4:5]
	ds_read_b32 v140, v229 offset:132
	s_or_b64 exec, exec, s[14:15]
	s_waitcnt vmcnt(27)
; __device__ __forceinline__ float bf_lo(unsigned w) { return __uint_as_float(w << 16); }
; template <int STAGE, int OFF> __device__ __forceinline__ void attn32_unit(const bf16* base, bf16* yrow0, int blk0, int u, LAS unsigned char* xtab, LAS unsigned char* kbuf, LAS unsigned char* vbuf, int lane, ...
;     ...
;     } else {
; #pragma unroll
;         for (int mb = 0; mb < 2; ++mb)
; #pragma unroll
;             for (int gq = 0; gq < 4; ++gq) { const v2u w = *(const LAS v2u*)(xrow + 2 * (32 * mb + 8 * gq + 4 * h)); o[mb][4 * gq] = bf_lo(w.x); o[mb][4 * gq + 1] = bf_hi(w.x); o[mb][4 * gq + 2] = bf_lo(w.y); o[mb][4 * gq + 3] = bf_hi(w.y); }
;         m = *(const LAS float*)(xrow + 128); l = h == 0 ? *(const LAS float*)(xrow + 132) : 0.f;
;     }
;     const int hi = qi, lo = max(qi - 128, -(t0 >> SH));
;     const unsigned mspan = (unsigned)(hi - lo);
; #pragma unroll
;     for (int pp = 0; pp < 5; ++pp) {
;         constexpr int dummy = 0; (void)dummy;
;         const int set = (pp + OFF) % 2, n0 = -128 + 32 * pp;
; #pragma unroll
;         for (int c = 0; c < 4; ++c) { *(LAS v4u*)(kbuf + (8 * c + lrow) * 144 + lch * 16) = kr[set][c]; *(LAS v4u*)(vbuf + (8 * c + lrow) * 160 + lch * 16) = vr[set][c]; }
;         if (pp + 2 < 5) { ATT32_LOAD(set, pp + 2, t0, SH); }
;         else { const bf16* base_ = base; { const bf16* base = nbase; ATT32_LOAD(set, pp + 2 - 5, nt0, nsh); } (void)base_; }
;         f32x16 sc;
; #pragma unroll
;         for (int i = 0; i < 16; ++i) sc[i] = 0.f;
; #pragma unroll
;         for (int ks = 0; ks < 4; ++ks) { const bf16x8 ka = *(const LAS bf16x8*)(kbuf + qi * 144 + 32 * ks + 16 * h); sc = MFMA32(ka, qb[ks], sc); }
;         if (pp == 4) {
; #pragma unroll
;             for (int ks = 0; ks < 4; ++ks) qb[ks] = *(const bf16x8*)(nbase + (size_t)min(nt0 + (qi << nsh), SEQ - 1) * 1536 + 16 * ks + 8 * h);
;         }
;         const int mbase = n0 + 4 * h - lo; float mx = -INFINITY;
; #pragma unroll
;         for (int rg = 0; rg < 16; ++rg) { sc[rg] = ((unsigned)(mbase + (rg & 3) + 8 * (rg >> 2)) <= mspan) ? sc[rg] : -INFINITY; mx = fmaxf(mx, sc[rg]); }
;         mx = fmaxf(mx, __shfl_xor(mx, 32));
;         if (__any(mx > m)) {
;             const float mn = fmaxf(m, mx), alpha = __builtin_amdgcn_exp2f(m - mn); m = mn; l *= alpha;
; #pragma unroll
;             for (int i = 0; i < 16; ++i) { o[0][i] *= alpha; o[1][i] *= alpha; }
;         }
	ds_write_b128 v231, v[106:109]
	s_waitcnt vmcnt(26)
	ds_write_b128 v232, v[110:113] offset:4608
	s_waitcnt vmcnt(25)
	ds_write_b128 v231, v[114:117] offset:1152
	s_waitcnt vmcnt(24)
	ds_write_b128 v232, v[118:121] offset:5888
	s_waitcnt vmcnt(23)
	ds_write_b128 v231, v[122:125] offset:2304
	s_waitcnt vmcnt(22)
	ds_write_b128 v232, v[126:129] offset:7168
	s_waitcnt vmcnt(21)
	ds_write_b128 v231, v[130:133] offset:3456
	s_waitcnt vmcnt(20)
	ds_write_b128 v232, v[134:137] offset:8448
	ds_read_b128 v[34:37], v177
	s_waitcnt lgkmcnt(13)
	v_lshlrev_b32_e32 v22, 16, v12
	v_and_b32_e32 v23, 0xffff0000, v12
	v_add_u32_e32 v12, s10, v218
	v_med3_i32 v12, v12, 0, v233
	v_mul_u32_u24_e32 v12, 0xc00, v12
	v_or_b32_e32 v12, v12, v176
	global_load_dwordx4 v[66:69], v12, s[8:9] offset:1024
	global_load_dwordx4 v[106:109], v12, s[8:9] offset:2048
	ds_read_b128 v[118:121], v177 offset:32
	v_add_u32_e32 v12, s10, v219
	s_waitcnt vmcnt(13) lgkmcnt(1)
	v_mfma_f32_32x32x16_bf16 v[34:49], v[34:37], v[62:65], 0
	v_med3_i32 v12, v12, 0, v233
	v_mul_u32_u24_e32 v12, 0xc00, v12
	v_or_b32_e32 v12, v12, v176
	global_load_dwordx4 v[110:113], v12, s[8:9] offset:1024
	global_load_dwordx4 v[114:117], v12, s[8:9] offset:2048
	v_add_u32_e32 v12, s10, v220
	v_med3_i32 v12, v12, 0, v233
	v_mul_u32_u24_e32 v12, 0xc00, v12
	v_or_b32_e32 v12, v12, v176
	ds_read_b128 v[134:137], v177 offset:96
	ds_read_b128 v[142:145], v177 offset:64
	s_waitcnt vmcnt(14) lgkmcnt(2)
	v_mfma_f32_32x32x16_bf16 v[34:49], v[118:121], v[58:61], v[34:49]
	global_load_dwordx4 v[118:121], v12, s[8:9] offset:1024
	global_load_dwordx4 v[122:125], v12, s[8:9] offset:2048
	v_add_u32_e32 v12, s10, v221
	v_med3_i32 v12, v12, 0, v233
	v_mul_u32_u24_e32 v12, 0xc00, v12
	v_or_b32_e32 v12, v12, v176
	global_load_dwordx4 v[126:129], v12, s[8:9] offset:1024
	global_load_dwordx4 v[130:133], v12, s[8:9] offset:2048
	s_lshr_b32 s0, s10, 4
	s_waitcnt vmcnt(17) lgkmcnt(0)
	v_mfma_f32_32x32x16_bf16 v[34:49], v[142:145], v[54:57], v[34:49]
	s_sub_i32 s0, 0, s0
	v_lshlrev_b32_e32 v18, 16, v10
	v_and_b32_e32 v19, 0xffff0000, v10
	v_lshlrev_b32_e32 v20, 16, v11
	v_and_b32_e32 v21, 0xffff0000, v11
	v_lshlrev_b32_e32 v10, 16, v14
	v_and_b32_e32 v11, 0xffff0000, v14
	s_waitcnt vmcnt(16)
	v_mfma_f32_32x32x16_bf16 v[34:49], v[134:137], v[70:73], v[34:49]
	v_max_i32_e32 v14, s0, v175
	v_sub_u32_e32 v51, v1, v14
	v_sub_u32_e32 v138, v178, v14
	v_lshlrev_b32_e32 v24, 16, v13
	v_and_b32_e32 v25, 0xffff0000, v13
	v_lshlrev_b32_e32 v12, 16, v15
	v_and_b32_e32 v13, 0xffff0000, v15
	s_nop 2
	v_add_u32_e32 v253, 27, v138
	v_cmp_le_i32_e32 vcc, 27, v253
	v_cmp_le_i32_e64 s[98:99], 26, v253
	v_cmp_le_i32_e64 s[100:101], 25, v253
	v_cndmask_b32_e32 v34, v234, v34, vcc
	v_lshlrev_b32_e32 v26, 16, v2
	v_cmp_le_i32_e32 vcc, 24, v253
	v_cndmask_b32_e64 v35, v234, v35, s[98:99]
	v_max3_f32 v14, v34, s31, v35
	v_cmp_le_i32_e64 s[98:99], 19, v253
	v_cndmask_b32_e64 v36, v234, v36, s[100:101]
	v_and_b32_e32 v27, 0xffff0000, v2
	v_cmp_le_i32_e64 s[100:101], 18, v253
	v_cndmask_b32_e32 v37, v234, v37, vcc
	v_max3_f32 v14, v14, v36, v37
	v_cmp_le_i32_e32 vcc, 17, v253
	v_cndmask_b32_e64 v38, v234, v38, s[98:99]
	v_lshlrev_b32_e32 v28, 16, v3
	v_cmp_le_i32_e64 s[98:99], 16, v253
	v_cndmask_b32_e64 v39, v234, v39, s[100:101]
	v_max3_f32 v14, v14, v38, v39
	v_cmp_le_i32_e64 s[100:101], 11, v253
	v_cndmask_b32_e32 v40, v234, v40, vcc
	v_and_b32_e32 v29, 0xffff0000, v3
	v_cmp_le_i32_e32 vcc, 10, v253
	v_cndmask_b32_e64 v41, v234, v41, s[98:99]
	v_max3_f32 v14, v14, v40, v41
	v_cmp_le_i32_e64 s[98:99], 9, v253
	v_cndmask_b32_e64 v42, v234, v42, s[100:101]
	v_lshlrev_b32_e32 v30, 16, v4
	v_cmp_le_i32_e64 s[100:101], 8, v253
	v_cndmask_b32_e32 v43, v234, v43, vcc
	v_max3_f32 v14, v14, v42, v43
	v_cmp_le_i32_e32 vcc, 3, v253
	v_cndmask_b32_e64 v44, v234, v44, s[98:99]
	v_and_b32_e32 v31, 0xffff0000, v4
	v_cmp_le_i32_e64 s[98:99], 2, v253
	v_cndmask_b32_e64 v45, v234, v45, s[100:101]
	v_max3_f32 v14, v14, v44, v45
	v_cmp_le_i32_e64 s[100:101], 1, v253
	v_cndmask_b32_e32 v46, v234, v46, vcc
	v_lshlrev_b32_e32 v32, 16, v5
	v_cmp_le_i32_e32 vcc, 0, v253
	v_cndmask_b32_e64 v47, v234, v47, s[98:99]
	v_max3_f32 v14, v14, v46, v47
	v_cndmask_b32_e64 v48, v234, v48, s[100:101]
	v_and_b32_e32 v33, 0xffff0000, v5
	v_lshlrev_b32_e32 v2, 16, v6
	v_cndmask_b32_e32 v49, v234, v49, vcc
	v_max3_f32 v134, v14, v48, v49
	ds_bpermute_b32 v135, v179, v134
	v_and_b32_e32 v3, 0xffff0000, v6
	v_lshlrev_b32_e32 v4, 16, v7
	v_and_b32_e32 v5, 0xffff0000, v7
	v_lshlrev_b32_e32 v6, 16, v8
	s_waitcnt lgkmcnt(0)
	v_max_f32_e32 v135, v135, v135
	v_max_f32_e32 v134, v134, v135
	v_and_b32_e32 v7, 0xffff0000, v8
	v_lshlrev_b32_e32 v8, 16, v9
	v_and_b32_e32 v9, 0xffff0000, v9
	v_lshlrev_b32_e32 v14, 16, v16
	v_and_b32_e32 v15, 0xffff0000, v16
	v_lshlrev_b32_e32 v16, 16, v17
	v_and_b32_e32 v17, 0xffff0000, v17
	v_cmp_gt_f32_e32 vcc, v134, v139
	s_cbranch_vccz .LBB0_424
	v_max_f32_e32 v134, v134, v134
	v_max_f32_e32 v135, v139, v139
	v_max_f32_e32 v135, v135, v134
	v_sub_f32_e32 v134, v139, v135
	v_exp_f32_e32 v134, v134
	v_mov_b32_e32 v139, v135
	v_pk_mul_f32 v[16:17], v[134:135], v[16:17] op_sel_hi:[0,1]
	v_pk_mul_f32 v[14:15], v[134:135], v[14:15] op_sel_hi:[0,1]
	v_pk_mul_f32 v[12:13], v[134:135], v[12:13] op_sel_hi:[0,1]
	v_pk_mul_f32 v[10:11], v[134:135], v[10:11] op_sel_hi:[0,1]
	v_pk_mul_f32 v[8:9], v[134:135], v[8:9] op_sel_hi:[0,1]
	v_pk_mul_f32 v[6:7], v[134:135], v[6:7] op_sel_hi:[0,1]
	v_pk_mul_f32 v[4:5], v[134:135], v[4:5] op_sel_hi:[0,1]
	v_pk_mul_f32 v[2:3], v[134:135], v[2:3] op_sel_hi:[0,1]
	v_pk_mul_f32 v[32:33], v[134:135], v[32:33] op_sel_hi:[0,1]
	v_pk_mul_f32 v[30:31], v[134:135], v[30:31] op_sel_hi:[0,1]
	v_pk_mul_f32 v[28:29], v[134:135], v[28:29] op_sel_hi:[0,1]
	v_pk_mul_f32 v[26:27], v[134:135], v[26:27] op_sel_hi:[0,1]
	v_pk_mul_f32 v[24:25], v[134:135], v[24:25] op_sel_hi:[0,1]
	v_pk_mul_f32 v[22:23], v[134:135], v[22:23] op_sel_hi:[0,1]
	v_pk_mul_f32 v[20:21], v[134:135], v[20:21] op_sel_hi:[0,1]
	v_pk_mul_f32 v[18:19], v[134:135], v[18:19] op_sel_hi:[0,1]
	v_mul_f32_e32 v140, v140, v134
; #define LAS __attribute__((address_space(3)))
; template <int STAGE, int OFF> __device__ __forceinline__ void attn32_unit(const bf16* base, bf16* yrow0, int blk0, int u, LAS unsigned char* xtab, LAS unsigned char* kbuf, LAS unsigned char* vbuf, int lane, ...
;     ...
;         for (int c = 0; c < 4; ++c) { *(LAS v4u*)(kbuf + (8 * c + lrow) * 144 + lch * 16) = kr[set][c]; *(LAS v4u*)(vbuf + (8 * c + lrow) * 160 + lch * 16) = vr[set][c]; }
;         if (pp + 2 < 5) { ATT32_LOAD(set, pp + 2, t0, SH); }
;         else { const bf16* base_ = base; { const bf16* base = nbase; ATT32_LOAD(set, pp + 2 - 5, nt0, nsh); } (void)base_; }
;         f32x16 sc;
; #pragma unroll
;         for (int i = 0; i < 16; ++i) sc[i] = 0.f;
; #pragma unroll
;         for (int ks = 0; ks < 4; ++ks) { const bf16x8 ka = *(const LAS bf16x8*)(kbuf + qi * 144 + 32 * ks + 16 * h); sc = MFMA32(ka, qb[ks], sc); }
;         if (pp == 4) {
; #pragma unroll
;             for (int ks = 0; ks < 4; ++ks) qb[ks] = *(const bf16x8*)(nbase + (size_t)min(nt0 + (qi << nsh), SEQ - 1) * 1536 + 16 * ks + 8 * h);
;         }
;         const int mbase = n0 + 4 * h - lo; float mx = -INFINITY;
; #pragma unroll
;         for (int rg = 0; rg < 16; ++rg) { sc[rg] = ((unsigned)(mbase + (rg & 3) + 8 * (rg >> 2)) <= mspan) ? sc[rg] : -INFINITY; mx = fmaxf(mx, sc[rg]); }
;         mx = fmaxf(mx, __shfl_xor(mx, 32));
;         if (__any(mx > m)) {
;             const float mn = fmaxf(m, mx), alpha = __builtin_amdgcn_exp2f(m - mn); m = mn; l *= alpha;
; #pragma unroll
;             for (int i = 0; i < 16; ++i) { o[0][i] *= alpha; o[1][i] *= alpha; }
;         }
;         float ps = 0.f;
; #pragma unroll
;         for (int rg = 0; rg < 16; ++rg) { sc[rg] = __builtin_amdgcn_exp2f(sc[rg] - m); ps += sc[rg]; }
;         l += ps;
;         bf16x8 pb[2];
; #pragma unroll
;         for (int s2 = 0; s2 < 2; ++s2) { v4u w; w.x = pg8::cvt_pk_bf16(sc[8 * s2], sc[8 * s2 + 1]); w.y = pg8::cvt_pk_bf16(sc[8 * s2 + 2], sc[8 * s2 + 3]); w.z = pg8::cvt_pk_bf16(sc[8 * s2 + 4], sc[8 * s2 + 5]); w.w = pg8::cvt_pk_bf16(sc[8 * s2 + 6], sc[8 * s2 + 7]); pb[s2] = __builtin_bit_cast(bf16x8, w); }
; #pragma unroll
;         for (int mb = 0; mb < 2; ++mb)
; #pragma unroll
;             for (int s2 = 0; s2 < 2; ++s2) {
;                 LAS unsigned char* vp = vbuf + tr_off + (16 * s2) * 160 + 64 * mb;
.LBB0_424:
	v_sub_f32_e32 v34, v34, v139
	v_exp_f32_e32 v141, v34
	v_sub_f32_e32 v34, v35, v139
	v_exp_f32_e32 v146, v34
	v_sub_f32_e32 v34, v36, v139
	v_exp_f32_e32 v147, v34
	v_sub_f32_e32 v34, v37, v139
	v_exp_f32_e32 v148, v34
	v_sub_f32_e32 v34, v38, v139
	v_exp_f32_e32 v149, v34
	v_sub_f32_e32 v34, v39, v139
	v_exp_f32_e32 v150, v34
	v_sub_f32_e32 v34, v40, v139
	v_exp_f32_e32 v151, v34
	v_sub_f32_e32 v34, v41, v139
	v_exp_f32_e32 v152, v34
	v_sub_f32_e32 v34, v42, v139
	v_exp_f32_e32 v154, v34
	v_sub_f32_e32 v34, v43, v139
	v_exp_f32_e32 v155, v34
	v_sub_f32_e32 v34, v44, v139
	v_exp_f32_e32 v156, v34
	v_sub_f32_e32 v34, v45, v139
	v_exp_f32_e32 v157, v34
	v_sub_f32_e32 v34, v46, v139
	v_exp_f32_e32 v158, v34
	v_sub_f32_e32 v34, v47, v139
	v_exp_f32_e32 v159, v34
	v_sub_f32_e32 v34, v48, v139
	v_exp_f32_e32 v160, v34
	v_sub_f32_e32 v34, v49, v139
	v_exp_f32_e32 v161, v34
	v_cvt_pk_bf16_f32 v34, v141, v146
	v_cvt_pk_bf16_f32 v35, v147, v148
	v_cvt_pk_bf16_f32 v36, v149, v150
	v_cvt_pk_bf16_f32 v37, v151, v152
	v_cvt_pk_bf16_f32 v134, v154, v155
	v_cvt_pk_bf16_f32 v135, v156, v157
	v_cvt_pk_bf16_f32 v136, v158, v159
	v_cvt_pk_bf16_f32 v137, v160, v161
	ds_read_b64_tr_b16 v[38:39], v181 offset:4608
	ds_read_b64_tr_b16 v[40:41], v181 offset:5888
	ds_read_b64_tr_b16 v[44:45], v181 offset:5952
	ds_read_b64_tr_b16 v[42:43], v181 offset:4672
	s_waitcnt lgkmcnt(2)
	v_mfma_f32_32x32x16_bf16 v[18:33], v[38:41], v[34:37], v[18:33]
	ds_read_b64_tr_b16 v[38:39], v181 offset:7168
	ds_read_b64_tr_b16 v[40:41], v181 offset:8448
	v_add_f32_e32 v46, 0, v141
	ds_read_b64_tr_b16 v[144:145], v181 offset:8512
	ds_read_b64_tr_b16 v[142:143], v181 offset:7232
	ds_write_b128 v231, v[74:77]
	ds_write_b128 v232, v[78:81] offset:4608
	ds_write_b128 v231, v[82:85] offset:1152
	ds_write_b128 v232, v[86:89] offset:5888
	ds_write_b128 v231, v[90:93] offset:2304
	ds_write_b128 v232, v[94:97] offset:7168
	ds_write_b128 v231, v[98:101] offset:3456
	ds_write_b128 v232, v[102:105] offset:8448
	v_add_u32_e32 v94, s10, v224
	v_add_u32_e32 v98, s10, v225
	s_waitcnt lgkmcnt(10)
	v_mfma_f32_32x32x16_bf16 v[18:33], v[38:41], v[134:137], v[18:33]
	v_add_f32_e32 v38, v146, v46
	v_add_f32_e32 v38, v147, v38
	v_add_f32_e32 v38, v148, v38
	v_add_f32_e32 v38, v149, v38
	v_add_f32_e32 v38, v150, v38
	v_add_f32_e32 v38, v151, v38
	v_add_f32_e32 v141, v152, v38
	v_mfma_f32_32x32x16_bf16 v[2:17], v[42:45], v[34:37], v[2:17]
	v_add_u32_e32 v34, s10, v222
	v_med3_i32 v34, v34, 0, v233
	v_mul_u32_u24_e32 v38, 0xc00, v34
	ds_read_b128 v[34:37], v177
	v_or_b32_e32 v38, v38, v176
	global_load_dwordx4 v[74:77], v38, s[8:9] offset:1024
	global_load_dwordx4 v[78:81], v38, s[8:9] offset:2048
	v_add_u32_e32 v38, s10, v223
	v_med3_i32 v38, v38, 0, v233
	v_mul_u32_u24_e32 v38, 0xc00, v38
	ds_read_b128 v[90:93], v177 offset:32
	v_or_b32_e32 v86, v38, v176
	s_waitcnt lgkmcnt(1)
	v_mfma_f32_32x32x16_bf16 v[34:49], v[34:37], v[62:65], 0
	v_med3_i32 v94, v94, 0, v233
	v_med3_i32 v98, v98, 0, v233
	v_mul_u32_u24_e32 v94, 0xc00, v94
	v_mul_u32_u24_e32 v98, 0xc00, v98
	v_or_b32_e32 v94, v94, v176
	v_or_b32_e32 v102, v98, v176
	global_load_dwordx4 v[82:85], v86, s[8:9] offset:1024
	s_nop 0
	global_load_dwordx4 v[86:89], v86, s[8:9] offset:2048
	ds_read_b128 v[146:149], v177 offset:96
	ds_read_b128 v[150:153], v177 offset:64
	s_waitcnt lgkmcnt(2)
	v_mfma_f32_32x32x16_bf16 v[34:49], v[90:93], v[58:61], v[34:49]
	global_load_dwordx4 v[90:93], v94, s[8:9] offset:1024
	s_nop 0
	global_load_dwordx4 v[94:97], v94, s[8:9] offset:2048
	s_nop 0
	global_load_dwordx4 v[98:101], v102, s[8:9] offset:1024
	s_nop 0
	global_load_dwordx4 v[102:105], v102, s[8:9] offset:2048
	v_add_f32_e32 v141, v154, v141
	v_add_f32_e32 v141, v155, v141
	v_add_f32_e32 v141, v156, v141
	v_add_f32_e32 v141, v157, v141
	v_add_f32_e32 v141, v158, v141
	s_waitcnt lgkmcnt(0)
	v_mfma_f32_32x32x16_bf16 v[34:49], v[150:153], v[54:57], v[34:49]
	v_add_f32_e32 v141, v159, v141
	v_add_f32_e32 v141, v160, v141
	v_add_f32_e32 v141, v161, v141
	v_mfma_f32_32x32x16_bf16 v[34:49], v[146:149], v[70:73], v[34:49]
	v_mfma_f32_32x32x16_bf16 v[2:17], v[142:145], v[134:137], v[2:17]
	s_nop 6
	v_add_u32_e32 v253, 59, v138
	v_cmp_le_i32_e32 vcc, 27, v253
	v_cmp_le_i32_e64 s[98:99], 26, v253
	v_cmp_le_i32_e64 s[100:101], 25, v253
	v_cndmask_b32_e32 v34, v234, v34, vcc
	v_add_f32_e32 v134, v140, v141
	v_cmp_le_i32_e32 vcc, 24, v253
	v_cndmask_b32_e64 v35, v234, v35, s[98:99]
	v_max3_f32 v146, v34, s31, v35
	v_cmp_le_i32_e64 s[98:99], 19, v253
	v_cndmask_b32_e64 v36, v234, v36, s[100:101]
	v_cmp_le_i32_e64 s[100:101], 18, v253
	v_cndmask_b32_e32 v37, v234, v37, vcc
	v_max3_f32 v146, v146, v36, v37
	v_cmp_le_i32_e32 vcc, 17, v253
	v_cndmask_b32_e64 v38, v234, v38, s[98:99]
	v_cmp_le_i32_e64 s[98:99], 16, v253
	v_cndmask_b32_e64 v39, v234, v39, s[100:101]
	v_max3_f32 v146, v146, v38, v39
	v_cmp_le_i32_e64 s[100:101], 11, v253
	v_cndmask_b32_e32 v40, v234, v40, vcc
	v_cmp_le_i32_e32 vcc, 10, v253
	v_cndmask_b32_e64 v41, v234, v41, s[98:99]
	v_max3_f32 v146, v146, v40, v41
	v_cmp_le_i32_e64 s[98:99], 9, v253
	v_cndmask_b32_e64 v42, v234, v42, s[100:101]
	v_cmp_le_i32_e64 s[100:101], 8, v253
	v_cndmask_b32_e32 v43, v234, v43, vcc
	v_max3_f32 v146, v146, v42, v43
	v_cmp_le_i32_e32 vcc, 3, v253
	v_cndmask_b32_e64 v44, v234, v44, s[98:99]
	v_cmp_le_i32_e64 s[98:99], 2, v253
	v_cndmask_b32_e64 v45, v234, v45, s[100:101]
	v_max3_f32 v146, v146, v44, v45
	v_cmp_le_i32_e64 s[100:101], 1, v253
	v_cndmask_b32_e32 v46, v234, v46, vcc
	v_cmp_le_i32_e32 vcc, 0, v253
	v_cndmask_b32_e64 v47, v234, v47, s[98:99]
	v_max3_f32 v146, v146, v46, v47
	v_cndmask_b32_e64 v48, v234, v48, s[100:101]
	v_cndmask_b32_e32 v49, v234, v49, vcc
	v_max3_f32 v146, v146, v48, v49
	ds_bpermute_b32 v147, v179, v146
	s_waitcnt lgkmcnt(0)
	v_max_f32_e32 v135, v147, v147
	v_max_f32_e32 v135, v146, v135
	v_cmp_gt_f32_e32 vcc, v135, v139
	s_cbranch_vccz .LBB0_426
; #define LAS __attribute__((address_space(3)))
; template <int STAGE, int OFF> __device__ __forceinline__ void attn32_unit(const bf16* base, bf16* yrow0, int blk0, int u, LAS unsigned char* xtab, LAS unsigned char* kbuf, LAS unsigned char* vbuf, int lane, ...
;     ...
;         for (int c = 0; c < 4; ++c) { *(LAS v4u*)(kbuf + (8 * c + lrow) * 144 + lch * 16) = kr[set][c]; *(LAS v4u*)(vbuf + (8 * c + lrow) * 160 + lch * 16) = vr[set][c]; }
;         if (pp + 2 < 5) { ATT32_LOAD(set, pp + 2, t0, SH); }
;         else { const bf16* base_ = base; { const bf16* base = nbase; ATT32_LOAD(set, pp + 2 - 5, nt0, nsh); } (void)base_; }
;         f32x16 sc;
; #pragma unroll
;         for (int i = 0; i < 16; ++i) sc[i] = 0.f;
; #pragma unroll
;         for (int ks = 0; ks < 4; ++ks) { const bf16x8 ka = *(const LAS bf16x8*)(kbuf + qi * 144 + 32 * ks + 16 * h); sc = MFMA32(ka, qb[ks], sc); }
;         if (pp == 4) {
; #pragma unroll
;             for (int ks = 0; ks < 4; ++ks) qb[ks] = *(const bf16x8*)(nbase + (size_t)min(nt0 + (qi << nsh), SEQ - 1) * 1536 + 16 * ks + 8 * h);
;         }
;         const int mbase = n0 + 4 * h - lo; float mx = -INFINITY;
; #pragma unroll
;         for (int rg = 0; rg < 16; ++rg) { sc[rg] = ((unsigned)(mbase + (rg & 3) + 8 * (rg >> 2)) <= mspan) ? sc[rg] : -INFINITY; mx = fmaxf(mx, sc[rg]); }
;         mx = fmaxf(mx, __shfl_xor(mx, 32));
;         if (__any(mx > m)) {
;             const float mn = fmaxf(m, mx), alpha = __builtin_amdgcn_exp2f(m - mn); m = mn; l *= alpha;
; #pragma unroll
;             for (int i = 0; i < 16; ++i) { o[0][i] *= alpha; o[1][i] *= alpha; }
;         }
;         float ps = 0.f;
; #pragma unroll
;         for (int rg = 0; rg < 16; ++rg) { sc[rg] = __builtin_amdgcn_exp2f(sc[rg] - m); ps += sc[rg]; }
;         l += ps;
;         bf16x8 pb[2];
; #pragma unroll
;         for (int s2 = 0; s2 < 2; ++s2) { v4u w; w.x = pg8::cvt_pk_bf16(sc[8 * s2], sc[8 * s2 + 1]); w.y = pg8::cvt_pk_bf16(sc[8 * s2 + 2], sc[8 * s2 + 3]); w.z = pg8::cvt_pk_bf16(sc[8 * s2 + 4], sc[8 * s2 + 5]); w.w = pg8::cvt_pk_bf16(sc[8 * s2 + 6], sc[8 * s2 + 7]); pb[s2] = __builtin_bit_cast(bf16x8, w); }
; #pragma unroll
;         for (int mb = 0; mb < 2; ++mb)
; #pragma unroll
;             for (int s2 = 0; s2 < 2; ++s2) {
;                 LAS unsigned char* vp = vbuf + tr_off + (16 * s2) * 160 + 64 * mb;
	v_max_f32_e32 v135, v135, v135
	v_max_f32_e32 v136, v139, v139
	v_max_f32_e32 v135, v136, v135
	v_sub_f32_e32 v136, v139, v135
	v_exp_f32_e32 v136, v136
	v_mov_b32_e32 v139, v135
	v_pk_mul_f32 v[32:33], v[32:33], v[136:137] op_sel_hi:[1,0]
	v_pk_mul_f32 v[30:31], v[30:31], v[136:137] op_sel_hi:[1,0]
	v_pk_mul_f32 v[28:29], v[28:29], v[136:137] op_sel_hi:[1,0]
	v_pk_mul_f32 v[26:27], v[26:27], v[136:137] op_sel_hi:[1,0]
	v_pk_mul_f32 v[24:25], v[24:25], v[136:137] op_sel_hi:[1,0]
	v_pk_mul_f32 v[22:23], v[22:23], v[136:137] op_sel_hi:[1,0]
	v_pk_mul_f32 v[20:21], v[20:21], v[136:137] op_sel_hi:[1,0]
	v_pk_mul_f32 v[18:19], v[18:19], v[136:137] op_sel_hi:[1,0]
	v_pk_mul_f32 v[16:17], v[16:17], v[136:137] op_sel_hi:[1,0]
	v_pk_mul_f32 v[14:15], v[14:15], v[136:137] op_sel_hi:[1,0]
	v_pk_mul_f32 v[12:13], v[12:13], v[136:137] op_sel_hi:[1,0]
	v_pk_mul_f32 v[10:11], v[10:11], v[136:137] op_sel_hi:[1,0]
	v_pk_mul_f32 v[8:9], v[8:9], v[136:137] op_sel_hi:[1,0]
	v_pk_mul_f32 v[6:7], v[6:7], v[136:137] op_sel_hi:[1,0]
	v_pk_mul_f32 v[4:5], v[4:5], v[136:137] op_sel_hi:[1,0]
	v_pk_mul_f32 v[2:3], v[2:3], v[136:137] op_sel_hi:[1,0]
	v_mul_f32_e32 v134, v134, v136
.LBB0_426:
	v_sub_f32_e32 v34, v34, v139
	v_exp_f32_e32 v135, v34
	v_sub_f32_e32 v34, v35, v139
	v_exp_f32_e32 v136, v34
	v_sub_f32_e32 v34, v36, v139
	v_exp_f32_e32 v137, v34
	v_sub_f32_e32 v34, v37, v139
	v_exp_f32_e32 v148, v34
	v_sub_f32_e32 v34, v38, v139
	v_exp_f32_e32 v149, v34
	v_sub_f32_e32 v34, v39, v139
	v_exp_f32_e32 v150, v34
	v_sub_f32_e32 v34, v40, v139
	v_exp_f32_e32 v151, v34
	v_sub_f32_e32 v34, v41, v139
	v_exp_f32_e32 v152, v34
	v_sub_f32_e32 v34, v42, v139
	v_exp_f32_e32 v156, v34
	v_sub_f32_e32 v34, v43, v139
	v_exp_f32_e32 v157, v34
	v_sub_f32_e32 v34, v44, v139
	v_exp_f32_e32 v158, v34
	v_sub_f32_e32 v34, v45, v139
	v_exp_f32_e32 v159, v34
	v_sub_f32_e32 v34, v46, v139
	v_exp_f32_e32 v160, v34
	v_sub_f32_e32 v34, v47, v139
	v_exp_f32_e32 v161, v34
	v_sub_f32_e32 v34, v48, v139
	v_exp_f32_e32 v162, v34
	v_sub_f32_e32 v34, v49, v139
	v_exp_f32_e32 v163, v34
	v_cvt_pk_bf16_f32 v34, v135, v136
	v_cvt_pk_bf16_f32 v35, v137, v148
	v_cvt_pk_bf16_f32 v36, v149, v150
	v_cvt_pk_bf16_f32 v37, v151, v152
	v_cvt_pk_bf16_f32 v140, v156, v157
	v_cvt_pk_bf16_f32 v141, v158, v159
	v_cvt_pk_bf16_f32 v142, v160, v161
	v_cvt_pk_bf16_f32 v143, v162, v163
	ds_read_b64_tr_b16 v[38:39], v181 offset:4608
	ds_read_b64_tr_b16 v[40:41], v181 offset:5888
	ds_read_b64_tr_b16 v[44:45], v181 offset:5952
	ds_read_b64_tr_b16 v[42:43], v181 offset:4672
	s_waitcnt lgkmcnt(2)
	v_mfma_f32_32x32x16_bf16 v[18:33], v[38:41], v[34:37], v[18:33]
	ds_read_b64_tr_b16 v[38:39], v181 offset:7168
	ds_read_b64_tr_b16 v[40:41], v181 offset:8448
	v_add_f32_e32 v46, 0, v135
	ds_read_b64_tr_b16 v[146:147], v181 offset:8512
	ds_read_b64_tr_b16 v[144:145], v181 offset:7232
	s_waitcnt vmcnt(15)
	ds_write_b128 v231, v[66:69]
	s_waitcnt vmcnt(14)
	ds_write_b128 v232, v[106:109] offset:4608
	s_waitcnt vmcnt(13)
	ds_write_b128 v231, v[110:113] offset:1152
	s_waitcnt vmcnt(12)
	ds_write_b128 v232, v[114:117] offset:5888
	s_waitcnt vmcnt(11)
	ds_write_b128 v231, v[118:121] offset:2304
	s_waitcnt vmcnt(10)
	ds_write_b128 v232, v[122:125] offset:7168
	s_waitcnt vmcnt(9)
	ds_write_b128 v231, v[126:129] offset:3456
	s_waitcnt vmcnt(8)
	ds_write_b128 v232, v[130:133] offset:8448
	v_add_u32_e32 v122, s10, v227
	v_add_u32_e32 v126, s10, v228
	s_waitcnt lgkmcnt(10)
	v_mfma_f32_32x32x16_bf16 v[18:33], v[38:41], v[140:143], v[18:33]
	v_add_f32_e32 v38, v136, v46
	v_add_f32_e32 v38, v137, v38
	v_add_f32_e32 v38, v148, v38
	v_add_f32_e32 v38, v149, v38
	v_add_f32_e32 v38, v150, v38
	v_add_f32_e32 v38, v151, v38
	v_add_f32_e32 v135, v152, v38
	v_mfma_f32_32x32x16_bf16 v[2:17], v[42:45], v[34:37], v[2:17]
	v_add_u32_e32 v34, s10, v207
	v_min_u32_e32 v34, 0x3fff, v34
	v_mul_u32_u24_e32 v38, 0xc00, v34
	ds_read_b128 v[34:37], v177
	v_or_b32_e32 v38, v38, v176
	global_load_dwordx4 v[66:69], v38, s[8:9] offset:1024
	global_load_dwordx4 v[106:109], v38, s[8:9] offset:2048
	v_add_u32_e32 v38, s10, v226
	v_min_u32_e32 v38, 0x3fff, v38
	v_mul_u32_u24_e32 v38, 0xc00, v38
	ds_read_b128 v[118:121], v177 offset:32
	v_or_b32_e32 v114, v38, v176
	s_waitcnt lgkmcnt(1)
	v_mfma_f32_32x32x16_bf16 v[34:49], v[34:37], v[62:65], 0
	v_min_u32_e32 v122, 0x3fff, v122
	v_min_u32_e32 v126, 0x3fff, v126
	v_mul_u32_u24_e32 v122, 0xc00, v122
	v_mul_u32_u24_e32 v126, 0xc00, v126
	v_or_b32_e32 v122, v122, v176
	v_or_b32_e32 v130, v126, v176
	global_load_dwordx4 v[110:113], v114, s[8:9] offset:1024
	s_nop 0
	global_load_dwordx4 v[114:117], v114, s[8:9] offset:2048
	ds_read_b128 v[148:151], v177 offset:96
	ds_read_b128 v[152:155], v177 offset:64
	s_waitcnt lgkmcnt(2)
	v_mfma_f32_32x32x16_bf16 v[34:49], v[118:121], v[58:61], v[34:49]
	global_load_dwordx4 v[118:121], v122, s[8:9] offset:1024
	s_nop 0
	global_load_dwordx4 v[122:125], v122, s[8:9] offset:2048
	s_nop 0
	global_load_dwordx4 v[126:129], v130, s[8:9] offset:1024
	s_nop 0
	global_load_dwordx4 v[130:133], v130, s[8:9] offset:2048
	v_add_f32_e32 v135, v156, v135
	s_waitcnt lgkmcnt(0)
; #define LAS __attribute__((address_space(3)))
; template <int STAGE, int OFF> __device__ __forceinline__ void attn32_unit(const bf16* base, bf16* yrow0, int blk0, int u, LAS unsigned char* xtab, LAS unsigned char* kbuf, LAS unsigned char* vbuf, int lane, ...
;     ...
;         for (int c = 0; c < 4; ++c) { *(LAS v4u*)(kbuf + (8 * c + lrow) * 144 + lch * 16) = kr[set][c]; *(LAS v4u*)(vbuf + (8 * c + lrow) * 160 + lch * 16) = vr[set][c]; }
;         if (pp + 2 < 5) { ATT32_LOAD(set, pp + 2, t0, SH); }
;         else { const bf16* base_ = base; { const bf16* base = nbase; ATT32_LOAD(set, pp + 2 - 5, nt0, nsh); } (void)base_; }
;         f32x16 sc;
; #pragma unroll
;         for (int i = 0; i < 16; ++i) sc[i] = 0.f;
; #pragma unroll
;         for (int ks = 0; ks < 4; ++ks) { const bf16x8 ka = *(const LAS bf16x8*)(kbuf + qi * 144 + 32 * ks + 16 * h); sc = MFMA32(ka, qb[ks], sc); }
;         if (pp == 4) {
; #pragma unroll
;             for (int ks = 0; ks < 4; ++ks) qb[ks] = *(const bf16x8*)(nbase + (size_t)min(nt0 + (qi << nsh), SEQ - 1) * 1536 + 16 * ks + 8 * h);
;         }
;         const int mbase = n0 + 4 * h - lo; float mx = -INFINITY;
; #pragma unroll
;         for (int rg = 0; rg < 16; ++rg) { sc[rg] = ((unsigned)(mbase + (rg & 3) + 8 * (rg >> 2)) <= mspan) ? sc[rg] : -INFINITY; mx = fmaxf(mx, sc[rg]); }
;         mx = fmaxf(mx, __shfl_xor(mx, 32));
;         if (__any(mx > m)) {
;             const float mn = fmaxf(m, mx), alpha = __builtin_amdgcn_exp2f(m - mn); m = mn; l *= alpha;
; #pragma unroll
;             for (int i = 0; i < 16; ++i) { o[0][i] *= alpha; o[1][i] *= alpha; }
;         }
;         float ps = 0.f;
; #pragma unroll
;         for (int rg = 0; rg < 16; ++rg) { sc[rg] = __builtin_amdgcn_exp2f(sc[rg] - m); ps += sc[rg]; }
;         l += ps;
;         bf16x8 pb[2];
; #pragma unroll
;         for (int s2 = 0; s2 < 2; ++s2) { v4u w; w.x = pg8::cvt_pk_bf16(sc[8 * s2], sc[8 * s2 + 1]); w.y = pg8::cvt_pk_bf16(sc[8 * s2 + 2], sc[8 * s2 + 3]); w.z = pg8::cvt_pk_bf16(sc[8 * s2 + 4], sc[8 * s2 + 5]); w.w = pg8::cvt_pk_bf16(sc[8 * s2 + 6], sc[8 * s2 + 7]); pb[s2] = __builtin_bit_cast(bf16x8, w); }
; #pragma unroll
;         for (int mb = 0; mb < 2; ++mb)
; #pragma unroll
;             for (int s2 = 0; s2 < 2; ++s2) {
;                 LAS unsigned char* vp = vbuf + tr_off + (16 * s2) * 160 + 64 * mb;
	v_mfma_f32_32x32x16_bf16 v[34:49], v[152:155], v[54:57], v[34:49]
	v_add_f32_e32 v135, v157, v135
	v_add_f32_e32 v135, v158, v135
	v_add_f32_e32 v135, v159, v135
	v_add_f32_e32 v135, v160, v135
	v_add_f32_e32 v135, v161, v135
	v_add_f32_e32 v135, v162, v135
	v_add_f32_e32 v135, v163, v135
	v_mfma_f32_32x32x16_bf16 v[34:49], v[148:151], v[70:73], v[34:49]
	v_add_f32_e32 v135, v134, v135
	v_mfma_f32_32x32x16_bf16 v[2:17], v[144:147], v[140:143], v[2:17]
	s_nop 9
	v_add_u32_e32 v253, 91, v138
	v_cmp_le_i32_e32 vcc, 27, v253
	v_cmp_le_i32_e64 s[98:99], 26, v253
	v_cmp_le_i32_e64 s[100:101], 25, v253
	v_cndmask_b32_e32 v34, v234, v34, vcc
	v_cmp_le_i32_e32 vcc, 24, v253
	v_cndmask_b32_e64 v35, v234, v35, s[98:99]
	v_max3_f32 v136, v34, s31, v35
	v_cmp_le_i32_e64 s[98:99], 19, v253
	v_cndmask_b32_e64 v36, v234, v36, s[100:101]
	v_cmp_le_i32_e64 s[100:101], 18, v253
	v_cndmask_b32_e32 v37, v234, v37, vcc
	v_max3_f32 v136, v136, v36, v37
	v_cmp_le_i32_e32 vcc, 17, v253
	v_cndmask_b32_e64 v38, v234, v38, s[98:99]
	v_cmp_le_i32_e64 s[98:99], 16, v253
	v_cndmask_b32_e64 v39, v234, v39, s[100:101]
	v_max3_f32 v136, v136, v38, v39
	v_cmp_le_i32_e64 s[100:101], 11, v253
	v_cndmask_b32_e32 v40, v234, v40, vcc
	v_cmp_le_i32_e32 vcc, 10, v253
	v_cndmask_b32_e64 v41, v234, v41, s[98:99]
	v_max3_f32 v136, v136, v40, v41
	v_cmp_le_i32_e64 s[98:99], 9, v253
	v_cndmask_b32_e64 v42, v234, v42, s[100:101]
	v_cmp_le_i32_e64 s[100:101], 8, v253
	v_cndmask_b32_e32 v43, v234, v43, vcc
	v_max3_f32 v136, v136, v42, v43
	v_cmp_le_i32_e32 vcc, 3, v253
	v_cndmask_b32_e64 v44, v234, v44, s[98:99]
	v_cmp_le_i32_e64 s[98:99], 2, v253
	v_cndmask_b32_e64 v45, v234, v45, s[100:101]
	v_max3_f32 v136, v136, v44, v45
	v_cmp_le_i32_e64 s[100:101], 1, v253
	v_cndmask_b32_e32 v46, v234, v46, vcc
	v_cmp_le_i32_e32 vcc, 0, v253
	v_cndmask_b32_e64 v47, v234, v47, s[98:99]
	v_max3_f32 v136, v136, v46, v47
	v_cndmask_b32_e64 v48, v234, v48, s[100:101]
	v_cndmask_b32_e32 v49, v234, v49, vcc
	v_max3_f32 v136, v136, v48, v49
	ds_bpermute_b32 v137, v179, v136
	s_waitcnt lgkmcnt(0)
	v_max_f32_e32 v134, v137, v137
	v_max_f32_e32 v134, v136, v134
	v_cmp_gt_f32_e32 vcc, v134, v139
	s_cbranch_vccz .LBB0_428
	v_max_f32_e32 v134, v134, v134
	v_max_f32_e32 v136, v139, v139
	v_max_f32_e32 v136, v136, v134
	v_sub_f32_e32 v134, v139, v136
	v_exp_f32_e32 v134, v134
	v_mov_b32_e32 v139, v136
	v_pk_mul_f32 v[32:33], v[32:33], v[134:135] op_sel_hi:[1,0]
	v_pk_mul_f32 v[30:31], v[30:31], v[134:135] op_sel_hi:[1,0]
	v_pk_mul_f32 v[28:29], v[28:29], v[134:135] op_sel_hi:[1,0]
	v_pk_mul_f32 v[26:27], v[26:27], v[134:135] op_sel_hi:[1,0]
	v_pk_mul_f32 v[24:25], v[24:25], v[134:135] op_sel_hi:[1,0]
	v_pk_mul_f32 v[22:23], v[22:23], v[134:135] op_sel_hi:[1,0]
	v_pk_mul_f32 v[20:21], v[20:21], v[134:135] op_sel_hi:[1,0]
	v_pk_mul_f32 v[18:19], v[18:19], v[134:135] op_sel_hi:[1,0]
	v_pk_mul_f32 v[16:17], v[16:17], v[134:135] op_sel_hi:[1,0]
	v_pk_mul_f32 v[14:15], v[14:15], v[134:135] op_sel_hi:[1,0]
	v_pk_mul_f32 v[12:13], v[12:13], v[134:135] op_sel_hi:[1,0]
	v_pk_mul_f32 v[10:11], v[10:11], v[134:135] op_sel_hi:[1,0]
	v_pk_mul_f32 v[8:9], v[8:9], v[134:135] op_sel_hi:[1,0]
	v_pk_mul_f32 v[6:7], v[6:7], v[134:135] op_sel_hi:[1,0]
	v_pk_mul_f32 v[4:5], v[4:5], v[134:135] op_sel_hi:[1,0]
	v_pk_mul_f32 v[2:3], v[2:3], v[134:135] op_sel_hi:[1,0]
	v_mul_f32_e32 v135, v135, v134
.LBB0_428:
	v_sub_f32_e32 v34, v34, v139
	v_exp_f32_e32 v136, v34
	v_sub_f32_e32 v34, v35, v139
	v_exp_f32_e32 v137, v34
	v_sub_f32_e32 v34, v36, v139
	v_exp_f32_e32 v148, v34
	v_sub_f32_e32 v34, v37, v139
	v_exp_f32_e32 v149, v34
	v_sub_f32_e32 v34, v38, v139
	v_exp_f32_e32 v150, v34
	v_sub_f32_e32 v34, v39, v139
	v_exp_f32_e32 v151, v34
	v_sub_f32_e32 v34, v40, v139
	v_exp_f32_e32 v152, v34
	v_sub_f32_e32 v34, v41, v139
	v_exp_f32_e32 v153, v34
	v_sub_f32_e32 v34, v42, v139
	v_exp_f32_e32 v156, v34
	v_sub_f32_e32 v34, v43, v139
	v_exp_f32_e32 v157, v34
	v_sub_f32_e32 v34, v44, v139
	v_exp_f32_e32 v158, v34
	v_sub_f32_e32 v34, v45, v139
	v_exp_f32_e32 v159, v34
	v_sub_f32_e32 v34, v46, v139
	v_exp_f32_e32 v160, v34
	v_sub_f32_e32 v34, v47, v139
	v_exp_f32_e32 v161, v34
	v_sub_f32_e32 v34, v48, v139
	v_exp_f32_e32 v162, v34
	v_sub_f32_e32 v34, v49, v139
	v_exp_f32_e32 v163, v34
	v_cvt_pk_bf16_f32 v34, v136, v137
	v_cvt_pk_bf16_f32 v35, v148, v149
	v_cvt_pk_bf16_f32 v36, v150, v151
	v_cvt_pk_bf16_f32 v37, v152, v153
	v_cvt_pk_bf16_f32 v140, v156, v157
	v_cvt_pk_bf16_f32 v141, v158, v159
	v_cvt_pk_bf16_f32 v142, v160, v161
	v_cvt_pk_bf16_f32 v143, v162, v163
	ds_read_b64_tr_b16 v[38:39], v181 offset:4608
	ds_read_b64_tr_b16 v[40:41], v181 offset:5888
	ds_read_b64_tr_b16 v[42:43], v181 offset:7168
	ds_read_b64_tr_b16 v[44:45], v181 offset:8448
	ds_read_b64_tr_b16 v[48:49], v181 offset:5952
	ds_read_b64_tr_b16 v[46:47], v181 offset:4672
	s_waitcnt lgkmcnt(4)
	v_mfma_f32_32x32x16_bf16 v[18:33], v[38:41], v[34:37], v[18:33]
	v_add_f32_e32 v38, 0, v136
	s_lshl_b32 s0, s38, 9
	v_add_f32_e32 v38, v137, v38
	s_and_b32 s10, s0, 0x3e00
	v_add_f32_e32 v38, v148, v38
	s_add_i32 s10, s10, s23
	v_add_f32_e32 v38, v149, v38
	v_add_u32_e32 v134, s10, v180
	v_add_f32_e32 v38, v150, v38
	v_add_f32_e32 v38, v151, v38
	s_waitcnt lgkmcnt(0)
	v_mfma_f32_32x32x16_bf16 v[2:17], v[46:49], v[34:37], v[2:17]
	v_add_u32_e32 v34, 0x60, v134
	s_ashr_i32 s0, s38, 8
	ds_read_b64_tr_b16 v[146:147], v181 offset:8512
	ds_read_b64_tr_b16 v[144:145], v181 offset:7232
	v_add_f32_e32 v38, v152, v38
	s_waitcnt vmcnt(15)
	ds_write_b128 v231, v[74:77]
	s_waitcnt vmcnt(14)
	ds_write_b128 v232, v[78:81] offset:4608
	s_waitcnt vmcnt(13)
	ds_write_b128 v231, v[82:85] offset:1152
	s_waitcnt vmcnt(12)
; #define LAS __attribute__((address_space(3)))
; template <int STAGE, int OFF> __device__ __forceinline__ void attn32_unit(const bf16* base, bf16* yrow0, int blk0, int u, LAS unsigned char* xtab, LAS unsigned char* kbuf, LAS unsigned char* vbuf, int lane, ...
;     ...
;         for (int c = 0; c < 4; ++c) { *(LAS v4u*)(kbuf + (8 * c + lrow) * 144 + lch * 16) = kr[set][c]; *(LAS v4u*)(vbuf + (8 * c + lrow) * 160 + lch * 16) = vr[set][c]; }
;         if (pp + 2 < 5) { ATT32_LOAD(set, pp + 2, t0, SH); }
;         else { const bf16* base_ = base; { const bf16* base = nbase; ATT32_LOAD(set, pp + 2 - 5, nt0, nsh); } (void)base_; }
;         f32x16 sc;
; #pragma unroll
;         for (int i = 0; i < 16; ++i) sc[i] = 0.f;
; #pragma unroll
;         for (int ks = 0; ks < 4; ++ks) { const bf16x8 ka = *(const LAS bf16x8*)(kbuf + qi * 144 + 32 * ks + 16 * h); sc = MFMA32(ka, qb[ks], sc); }
;         if (pp == 4) {
; #pragma unroll
;             for (int ks = 0; ks < 4; ++ks) qb[ks] = *(const bf16x8*)(nbase + (size_t)min(nt0 + (qi << nsh), SEQ - 1) * 1536 + 16 * ks + 8 * h);
;         }
;         const int mbase = n0 + 4 * h - lo; float mx = -INFINITY;
; #pragma unroll
;         for (int rg = 0; rg < 16; ++rg) { sc[rg] = ((unsigned)(mbase + (rg & 3) + 8 * (rg >> 2)) <= mspan) ? sc[rg] : -INFINITY; mx = fmaxf(mx, sc[rg]); }
;         mx = fmaxf(mx, __shfl_xor(mx, 32));
;         if (__any(mx > m)) {
;             const float mn = fmaxf(m, mx), alpha = __builtin_amdgcn_exp2f(m - mn); m = mn; l *= alpha;
; #pragma unroll
;             for (int i = 0; i < 16; ++i) { o[0][i] *= alpha; o[1][i] *= alpha; }
;         }
;         float ps = 0.f;
; #pragma unroll
;         for (int rg = 0; rg < 16; ++rg) { sc[rg] = __builtin_amdgcn_exp2f(sc[rg] - m); ps += sc[rg]; }
;         l += ps;
;         bf16x8 pb[2];
; #pragma unroll
;         for (int s2 = 0; s2 < 2; ++s2) { v4u w; w.x = pg8::cvt_pk_bf16(sc[8 * s2], sc[8 * s2 + 1]); w.y = pg8::cvt_pk_bf16(sc[8 * s2 + 2], sc[8 * s2 + 3]); w.z = pg8::cvt_pk_bf16(sc[8 * s2 + 4], sc[8 * s2 + 5]); w.w = pg8::cvt_pk_bf16(sc[8 * s2 + 6], sc[8 * s2 + 7]); pb[s2] = __builtin_bit_cast(bf16x8, w); }
; #pragma unroll
;         for (int mb = 0; mb < 2; ++mb)
; #pragma unroll
;             for (int s2 = 0; s2 < 2; ++s2) {
;                 LAS unsigned char* vp = vbuf + tr_off + (16 * s2) * 160 + 64 * mb;
	ds_write_b128 v232, v[86:89] offset:5888
	s_waitcnt vmcnt(11)
	ds_write_b128 v231, v[90:93] offset:2304
	s_waitcnt vmcnt(10)
	ds_write_b128 v232, v[94:97] offset:7168
	s_waitcnt vmcnt(9)
	ds_write_b128 v231, v[98:101] offset:3456
	s_waitcnt vmcnt(8)
	ds_write_b128 v232, v[102:105] offset:8448
	v_med3_i32 v34, v34, 0, v233
	s_mul_hi_i32 s1, s0, 0x3000000
	s_mul_i32 s0, s0, 0x3000000
	v_add_f32_e32 v136, v153, v38
	v_mul_u32_u24_e32 v38, 0xc00, v34
	ds_read_b128 v[34:37], v177
	s_add_u32 s0, s16, s0
	s_addc_u32 s1, s17, s1
	s_lshl_b32 s8, s38, 2
	s_and_b32 s8, s8, 0x380
	s_add_u32 s8, s0, s8
	s_addc_u32 s9, s1, 0
	v_or_b32_e32 v38, v38, v176
	global_load_dwordx4 v[74:77], v38, s[8:9] offset:1024
	global_load_dwordx4 v[82:85], v38, s[8:9] offset:2048
	v_add_u32_e32 v38, 0x68, v134
	v_med3_i32 v38, v38, 0, v233
	v_mul_u32_u24_e32 v38, 0xc00, v38
	ds_read_b128 v[86:89], v177 offset:32
	v_mfma_f32_32x32x16_bf16 v[18:33], v[42:45], v[140:143], v[18:33]
	v_or_b32_e32 v90, v38, v176
	global_load_dwordx4 v[78:81], v90, s[8:9] offset:1024
	global_load_dwordx4 v[94:97], v90, s[8:9] offset:2048
	v_add_u32_e32 v90, 0x70, v134
	v_med3_i32 v90, v90, 0, v233
	v_mul_u32_u24_e32 v90, 0xc00, v90
	v_or_b32_e32 v90, v90, v176
	ds_read_b128 v[148:151], v177 offset:96
	ds_read_b128 v[152:155], v177 offset:64
	s_waitcnt lgkmcnt(3)
	v_mfma_f32_32x32x16_bf16 v[34:49], v[34:37], v[62:65], 0
	v_add_f32_e32 v136, v156, v136
	v_add_f32_e32 v136, v157, v136
	v_add_f32_e32 v136, v158, v136
	v_add_f32_e32 v136, v159, v136
	s_waitcnt lgkmcnt(2)
	v_mfma_f32_32x32x16_bf16 v[34:49], v[86:89], v[58:61], v[34:49]
	global_load_dwordx4 v[86:89], v90, s[8:9] offset:1024
	global_load_dwordx4 v[98:101], v90, s[8:9] offset:2048
	v_add_u32_e32 v90, 0x78, v134
	v_med3_i32 v90, v90, 0, v233
	v_mul_u32_u24_e32 v90, 0xc00, v90
	v_or_b32_e32 v102, v90, v176
	global_load_dwordx4 v[90:93], v102, s[8:9] offset:1024
	s_nop 0
	global_load_dwordx4 v[102:105], v102, s[8:9] offset:2048
	v_add_f32_e32 v136, v160, v136
	s_waitcnt lgkmcnt(0)
	v_mfma_f32_32x32x16_bf16 v[34:49], v[152:155], v[54:57], v[34:49]
	v_add_f32_e32 v136, v161, v136
	v_add_f32_e32 v136, v162, v136
	v_add_f32_e32 v136, v163, v136
	v_mfma_f32_32x32x16_bf16 v[34:49], v[148:151], v[70:73], v[34:49]
	v_mfma_f32_32x32x16_bf16 v[2:17], v[144:147], v[140:143], v[2:17]
	s_nop 9
	v_add_u32_e32 v253, 123, v138
	v_cmp_le_i32_e32 vcc, 27, v253
	v_cmp_le_i32_e64 s[98:99], 26, v253
	v_cmp_le_i32_e64 s[100:101], 25, v253
	v_cndmask_b32_e32 v34, v234, v34, vcc
	v_add_f32_e32 v140, v135, v136
	v_cmp_le_i32_e32 vcc, 24, v253
	v_cndmask_b32_e64 v35, v234, v35, s[98:99]
	v_max3_f32 v137, v34, s31, v35
	v_cmp_le_i32_e64 s[98:99], 19, v253
	v_cndmask_b32_e64 v36, v234, v36, s[100:101]
	v_cmp_le_i32_e64 s[100:101], 18, v253
	v_cndmask_b32_e32 v37, v234, v37, vcc
	v_max3_f32 v137, v137, v36, v37
	v_cmp_le_i32_e32 vcc, 17, v253
	v_cndmask_b32_e64 v38, v234, v38, s[98:99]
	v_cmp_le_i32_e64 s[98:99], 16, v253
	v_cndmask_b32_e64 v39, v234, v39, s[100:101]
	v_max3_f32 v137, v137, v38, v39
	v_cmp_le_i32_e64 s[100:101], 11, v253
	v_cndmask_b32_e32 v40, v234, v40, vcc
	v_cmp_le_i32_e32 vcc, 10, v253
	v_cndmask_b32_e64 v41, v234, v41, s[98:99]
	v_max3_f32 v137, v137, v40, v41
	v_cmp_le_i32_e64 s[98:99], 9, v253
	v_cndmask_b32_e64 v42, v234, v42, s[100:101]
	v_cmp_le_i32_e64 s[100:101], 8, v253
	v_cndmask_b32_e32 v43, v234, v43, vcc
	v_max3_f32 v137, v137, v42, v43
	v_cmp_le_i32_e32 vcc, 3, v253
	v_cndmask_b32_e64 v44, v234, v44, s[98:99]
	v_cmp_le_i32_e64 s[98:99], 2, v253
	v_cndmask_b32_e64 v45, v234, v45, s[100:101]
	v_max3_f32 v137, v137, v44, v45
	v_cmp_le_i32_e64 s[100:101], 1, v253
	v_cndmask_b32_e32 v46, v234, v46, vcc
	v_cmp_le_i32_e32 vcc, 0, v253
	v_cndmask_b32_e64 v47, v234, v47, s[98:99]
	v_max3_f32 v137, v137, v46, v47
	v_cndmask_b32_e64 v48, v234, v48, s[100:101]
	v_cndmask_b32_e32 v49, v234, v49, vcc
	v_max3_f32 v137, v137, v48, v49
	ds_bpermute_b32 v148, v179, v137
	s_waitcnt lgkmcnt(0)
	v_max_f32_e32 v135, v148, v148
	v_max_f32_e32 v135, v137, v135
	v_cmp_gt_f32_e32 vcc, v135, v139
	s_cbranch_vccz .LBB0_430
	v_max_f32_e32 v135, v135, v135
	v_max_f32_e32 v136, v139, v139
	v_max_f32_e32 v135, v136, v135
	v_sub_f32_e32 v136, v139, v135
	v_exp_f32_e32 v136, v136
	v_mov_b32_e32 v139, v135
	v_pk_mul_f32 v[32:33], v[32:33], v[136:137] op_sel_hi:[1,0]
	v_pk_mul_f32 v[30:31], v[30:31], v[136:137] op_sel_hi:[1,0]
	v_pk_mul_f32 v[28:29], v[28:29], v[136:137] op_sel_hi:[1,0]
	v_pk_mul_f32 v[26:27], v[26:27], v[136:137] op_sel_hi:[1,0]
	v_pk_mul_f32 v[24:25], v[24:25], v[136:137] op_sel_hi:[1,0]
	v_pk_mul_f32 v[22:23], v[22:23], v[136:137] op_sel_hi:[1,0]
	v_pk_mul_f32 v[20:21], v[20:21], v[136:137] op_sel_hi:[1,0]
	v_pk_mul_f32 v[18:19], v[18:19], v[136:137] op_sel_hi:[1,0]
	v_pk_mul_f32 v[16:17], v[16:17], v[136:137] op_sel_hi:[1,0]
	v_pk_mul_f32 v[14:15], v[14:15], v[136:137] op_sel_hi:[1,0]
	v_pk_mul_f32 v[12:13], v[12:13], v[136:137] op_sel_hi:[1,0]
	v_pk_mul_f32 v[10:11], v[10:11], v[136:137] op_sel_hi:[1,0]
	v_pk_mul_f32 v[8:9], v[8:9], v[136:137] op_sel_hi:[1,0]
	v_pk_mul_f32 v[6:7], v[6:7], v[136:137] op_sel_hi:[1,0]
	v_pk_mul_f32 v[4:5], v[4:5], v[136:137] op_sel_hi:[1,0]
	v_pk_mul_f32 v[2:3], v[2:3], v[136:137] op_sel_hi:[1,0]
	v_mul_f32_e32 v140, v140, v136
; #define LAS __attribute__((address_space(3)))
; template <int STAGE, int OFF> __device__ __forceinline__ void attn32_unit(const bf16* base, bf16* yrow0, int blk0, int u, LAS unsigned char* xtab, LAS unsigned char* kbuf, LAS unsigned char* vbuf, int lane, ...
;     ...
;         for (int c = 0; c < 4; ++c) { *(LAS v4u*)(kbuf + (8 * c + lrow) * 144 + lch * 16) = kr[set][c]; *(LAS v4u*)(vbuf + (8 * c + lrow) * 160 + lch * 16) = vr[set][c]; }
;         if (pp + 2 < 5) { ATT32_LOAD(set, pp + 2, t0, SH); }
;         else { const bf16* base_ = base; { const bf16* base = nbase; ATT32_LOAD(set, pp + 2 - 5, nt0, nsh); } (void)base_; }
;         f32x16 sc;
; #pragma unroll
;         for (int i = 0; i < 16; ++i) sc[i] = 0.f;
; #pragma unroll
;         for (int ks = 0; ks < 4; ++ks) { const bf16x8 ka = *(const LAS bf16x8*)(kbuf + qi * 144 + 32 * ks + 16 * h); sc = MFMA32(ka, qb[ks], sc); }
;         if (pp == 4) {
; #pragma unroll
;             for (int ks = 0; ks < 4; ++ks) qb[ks] = *(const bf16x8*)(nbase + (size_t)min(nt0 + (qi << nsh), SEQ - 1) * 1536 + 16 * ks + 8 * h);
;         }
;         const int mbase = n0 + 4 * h - lo; float mx = -INFINITY;
; #pragma unroll
;         for (int rg = 0; rg < 16; ++rg) { sc[rg] = ((unsigned)(mbase + (rg & 3) + 8 * (rg >> 2)) <= mspan) ? sc[rg] : -INFINITY; mx = fmaxf(mx, sc[rg]); }
;         mx = fmaxf(mx, __shfl_xor(mx, 32));
;         if (__any(mx > m)) {
;             const float mn = fmaxf(m, mx), alpha = __builtin_amdgcn_exp2f(m - mn); m = mn; l *= alpha;
; #pragma unroll
;             for (int i = 0; i < 16; ++i) { o[0][i] *= alpha; o[1][i] *= alpha; }
;         }
;         float ps = 0.f;
; #pragma unroll
;         for (int rg = 0; rg < 16; ++rg) { sc[rg] = __builtin_amdgcn_exp2f(sc[rg] - m); ps += sc[rg]; }
;         l += ps;
;         bf16x8 pb[2];
; #pragma unroll
;         for (int s2 = 0; s2 < 2; ++s2) { v4u w; w.x = pg8::cvt_pk_bf16(sc[8 * s2], sc[8 * s2 + 1]); w.y = pg8::cvt_pk_bf16(sc[8 * s2 + 2], sc[8 * s2 + 3]); w.z = pg8::cvt_pk_bf16(sc[8 * s2 + 4], sc[8 * s2 + 5]); w.w = pg8::cvt_pk_bf16(sc[8 * s2 + 6], sc[8 * s2 + 7]); pb[s2] = __builtin_bit_cast(bf16x8, w); }
; #pragma unroll
;         for (int mb = 0; mb < 2; ++mb)
; #pragma unroll
;             for (int s2 = 0; s2 < 2; ++s2) {
;                 LAS unsigned char* vp = vbuf + tr_off + (16 * s2) * 160 + 64 * mb;
.LBB0_430:
	v_sub_f32_e32 v34, v34, v139
	v_exp_f32_e32 v135, v34
	v_sub_f32_e32 v34, v35, v139
	v_exp_f32_e32 v136, v34
	v_sub_f32_e32 v34, v36, v139
	v_exp_f32_e32 v137, v34
	v_sub_f32_e32 v34, v37, v139
	v_exp_f32_e32 v141, v34
	v_sub_f32_e32 v34, v38, v139
	v_exp_f32_e32 v150, v34
	v_sub_f32_e32 v34, v39, v139
	v_exp_f32_e32 v151, v34
	v_sub_f32_e32 v34, v40, v139
	v_exp_f32_e32 v152, v34
	v_sub_f32_e32 v34, v41, v139
	v_exp_f32_e32 v153, v34
	v_sub_f32_e32 v34, v42, v139
	v_exp_f32_e32 v156, v34
	v_sub_f32_e32 v34, v43, v139
	v_exp_f32_e32 v157, v34
	v_sub_f32_e32 v34, v44, v139
	v_exp_f32_e32 v158, v34
	v_sub_f32_e32 v34, v45, v139
	v_exp_f32_e32 v159, v34
	v_sub_f32_e32 v34, v46, v139
	v_exp_f32_e32 v160, v34
	v_sub_f32_e32 v34, v47, v139
	v_exp_f32_e32 v161, v34
	v_sub_f32_e32 v34, v48, v139
	v_exp_f32_e32 v162, v34
	v_sub_f32_e32 v34, v49, v139
	v_exp_f32_e32 v163, v34
	v_cvt_pk_bf16_f32 v34, v135, v136
	v_cvt_pk_bf16_f32 v35, v137, v141
	v_cvt_pk_bf16_f32 v36, v150, v151
	v_cvt_pk_bf16_f32 v37, v152, v153
	v_cvt_pk_bf16_f32 v142, v156, v157
	v_cvt_pk_bf16_f32 v143, v158, v159
	v_cvt_pk_bf16_f32 v144, v160, v161
	v_cvt_pk_bf16_f32 v145, v162, v163
	ds_read_b64_tr_b16 v[38:39], v181 offset:4608
	ds_read_b64_tr_b16 v[40:41], v181 offset:5888
	v_or_b32_e32 v42, s10, v1
	v_min_i32_e32 v146, 0x3fff, v42
	s_waitcnt lgkmcnt(0)
	v_mfma_f32_32x32x16_bf16 v[18:33], v[38:41], v[34:37], v[18:33]
	v_mov_b64_e32 v[38:39], s[8:9]
	v_mad_i64_i32 v[38:39], s[10:11], v146, s30, v[38:39]
	ds_read_b64_tr_b16 v[42:43], v181 offset:7168
	ds_read_b64_tr_b16 v[44:45], v181 offset:8448
	ds_read_b64_tr_b16 v[48:49], v181 offset:5952
	ds_read_b64_tr_b16 v[46:47], v181 offset:4672
	v_lshl_add_u64 v[154:155], v[38:39], 0, v[168:169]
	v_add_f32_e32 v38, 0, v135
	v_add_f32_e32 v38, v136, v38
	v_add_f32_e32 v38, v137, v38
	v_add_f32_e32 v38, v141, v38
	v_add_f32_e32 v38, v150, v38
	v_add_f32_e32 v38, v151, v38
	s_waitcnt lgkmcnt(0)
	v_mfma_f32_32x32x16_bf16 v[2:17], v[46:49], v[34:37], v[2:17]
	v_add_u32_e32 v34, 0x80, v134
	ds_read_b64_tr_b16 v[148:149], v181 offset:8512
	ds_read_b64_tr_b16 v[146:147], v181 offset:7232
	v_add_f32_e32 v38, v152, v38
	s_waitcnt vmcnt(15)
	ds_write_b128 v231, v[66:69]
	s_waitcnt vmcnt(14)
	ds_write_b128 v232, v[106:109] offset:4608
	s_waitcnt vmcnt(13)
	ds_write_b128 v231, v[110:113] offset:1152
	s_waitcnt vmcnt(12)
	ds_write_b128 v232, v[114:117] offset:5888
	s_waitcnt vmcnt(11)
	ds_write_b128 v231, v[118:121] offset:2304
	s_waitcnt vmcnt(10)
	ds_write_b128 v232, v[122:125] offset:7168
	s_waitcnt vmcnt(9)
	ds_write_b128 v231, v[126:129] offset:3456
	s_waitcnt vmcnt(8)
	ds_write_b128 v232, v[130:133] offset:8448
	v_med3_i32 v34, v34, 0, v233
	v_add_f32_e32 v141, v153, v38
	v_mul_u32_u24_e32 v38, 0xc00, v34
	ds_read_b128 v[34:37], v177
	v_or_b32_e32 v38, v38, v176
	global_load_dwordx4 v[106:109], v38, s[8:9] offset:1024
	global_load_dwordx4 v[122:125], v38, s[8:9] offset:2048
	v_add_u32_e32 v38, 0x88, v134
	v_med3_i32 v38, v38, 0, v233
	v_mul_u32_u24_e32 v38, 0xc00, v38
	ds_read_b128 v[66:69], v177 offset:32
	v_mfma_f32_32x32x16_bf16 v[18:33], v[42:45], v[142:145], v[18:33]
	v_or_b32_e32 v114, v38, v176
	global_load_dwordx4 v[110:113], v114, s[8:9] offset:1024
	global_load_dwordx4 v[126:129], v114, s[8:9] offset:2048
	v_add_f32_e32 v141, v156, v141
	v_add_f32_e32 v141, v157, v141
	v_add_f32_e32 v141, v158, v141
	v_add_f32_e32 v141, v159, v141
	v_add_f32_e32 v141, v160, v141
	s_waitcnt lgkmcnt(1)
	v_mfma_f32_32x32x16_bf16 v[34:49], v[34:37], v[62:65], 0
	v_add_u32_e32 v62, 0x90, v134
	v_med3_i32 v62, v62, 0, v233
	v_mul_u32_u24_e32 v62, 0xc00, v62
	v_or_b32_e32 v118, v62, v176
	ds_read_b128 v[150:153], v177 offset:96
	ds_read_b128 v[62:65], v177 offset:64
	global_load_dwordx4 v[114:117], v118, s[8:9] offset:1024
	global_load_dwordx4 v[130:133], v118, s[8:9] offset:2048
	v_add_f32_e32 v141, v161, v141
	s_waitcnt lgkmcnt(2)
	v_mfma_f32_32x32x16_bf16 v[34:49], v[66:69], v[58:61], v[34:49]
	v_add_u32_e32 v58, 0x98, v134
	v_med3_i32 v58, v58, 0, v233
	v_mul_u32_u24_e32 v58, 0xc00, v58
	v_or_b32_e32 v58, v58, v176
	global_load_dwordx4 v[118:121], v58, s[8:9] offset:1024
	global_load_dwordx4 v[134:137], v58, s[8:9] offset:2048
	v_add_f32_e32 v141, v162, v141
	s_waitcnt lgkmcnt(0)
	v_mfma_f32_32x32x16_bf16 v[34:49], v[62:65], v[54:57], v[34:49]
	global_load_dwordx4 v[66:69], v[154:155], off
	global_load_dwordx4 v[62:65], v[154:155], off offset:32
	global_load_dwordx4 v[58:61], v[154:155], off offset:64
	global_load_dwordx4 v[54:57], v[154:155], off offset:96
	v_mfma_f32_32x32x16_bf16 v[34:49], v[150:153], v[70:73], v[34:49]
	v_mfma_f32_32x32x16_bf16 v[2:17], v[146:149], v[142:145], v[2:17]
	s_nop 7
	v_sub_u32_e32 v253, v51, v138
	v_subrev_u32_e32 v253, 0x80, v253
	v_cmp_le_i32_e32 vcc, 0, v253
	v_cmp_le_i32_e64 s[98:99], 1, v253
	v_cmp_le_i32_e64 s[100:101], 2, v253
	v_cndmask_b32_e32 v70, v234, v34, vcc
	v_cmp_le_i32_e32 vcc, 3, v253
	v_cndmask_b32_e64 v35, v234, v35, s[98:99]
	v_max3_f32 v34, v70, s31, v35
	v_cmp_le_i32_e64 s[98:99], 8, v253
	v_cndmask_b32_e64 v36, v234, v36, s[100:101]
	v_cmp_le_i32_e64 s[100:101], 9, v253
	v_cndmask_b32_e32 v37, v234, v37, vcc
	v_max3_f32 v34, v34, v36, v37
	v_cmp_le_i32_e32 vcc, 10, v253
	v_cndmask_b32_e64 v38, v234, v38, s[98:99]
	v_cmp_le_i32_e64 s[98:99], 11, v253
	v_cndmask_b32_e64 v39, v234, v39, s[100:101]
	v_max3_f32 v34, v34, v38, v39
	v_cmp_le_i32_e64 s[100:101], 16, v253
	v_cndmask_b32_e32 v40, v234, v40, vcc
	v_cmp_le_i32_e32 vcc, 17, v253
	v_cndmask_b32_e64 v41, v234, v41, s[98:99]
	v_max3_f32 v34, v34, v40, v41
	v_cmp_le_i32_e64 s[98:99], 18, v253
	v_cndmask_b32_e64 v42, v234, v42, s[100:101]
	v_cmp_le_i32_e64 s[100:101], 19, v253
	v_cndmask_b32_e32 v43, v234, v43, vcc
	v_max3_f32 v34, v34, v42, v43
	v_cmp_le_i32_e32 vcc, 24, v253
	v_cndmask_b32_e64 v44, v234, v44, s[98:99]
	v_cmp_le_i32_e64 s[98:99], 25, v253
	v_cndmask_b32_e64 v45, v234, v45, s[100:101]
	v_max3_f32 v34, v34, v44, v45
	v_cmp_le_i32_e64 s[100:101], 26, v253
	v_cndmask_b32_e32 v46, v234, v46, vcc
	v_cmp_le_i32_e32 vcc, 27, v253
	v_cndmask_b32_e64 v47, v234, v47, s[98:99]
	v_max3_f32 v34, v34, v46, v47
	v_cndmask_b32_e64 v48, v234, v48, s[100:101]
	v_cndmask_b32_e32 v49, v234, v49, vcc
	v_max3_f32 v51, v34, v48, v49
	ds_bpermute_b32 v71, v179, v51
	v_add_f32_e32 v34, v163, v141
	v_add_f32_e32 v34, v140, v34
	s_waitcnt lgkmcnt(0)
	v_max_f32_e32 v71, v71, v71
	v_max_f32_e32 v51, v51, v71
	v_cmp_gt_f32_e32 vcc, v51, v139
	s_cbranch_vccz .LBB0_355
; template <int STAGE, int OFF> __device__ __forceinline__ void attn32_unit(const bf16* base, bf16* yrow0, int blk0, int u, LAS unsigned char* xtab, LAS unsigned char* kbuf, LAS unsigned char* vbuf, int lane, ...
;     ...
;         if (__any(mx > m)) {
;             const float mn = fmaxf(m, mx), alpha = __builtin_amdgcn_exp2f(m - mn); m = mn; l *= alpha;
; #pragma unroll
;             for (int i = 0; i < 16; ++i) { o[0][i] *= alpha; o[1][i] *= alpha; }
;         }
	v_max_f32_e32 v51, v51, v51
	v_max_f32_e32 v71, v139, v139
	v_max_f32_e32 v51, v71, v51
	v_sub_f32_e32 v71, v139, v51
	v_exp_f32_e32 v72, v71
	v_mov_b32_e32 v139, v51
	v_pk_mul_f32 v[32:33], v[32:33], v[72:73] op_sel_hi:[1,0]
	v_pk_mul_f32 v[30:31], v[30:31], v[72:73] op_sel_hi:[1,0]
	v_pk_mul_f32 v[28:29], v[28:29], v[72:73] op_sel_hi:[1,0]
	v_pk_mul_f32 v[26:27], v[26:27], v[72:73] op_sel_hi:[1,0]
	v_pk_mul_f32 v[24:25], v[24:25], v[72:73] op_sel_hi:[1,0]
	v_pk_mul_f32 v[22:23], v[22:23], v[72:73] op_sel_hi:[1,0]
	v_pk_mul_f32 v[20:21], v[20:21], v[72:73] op_sel_hi:[1,0]
	v_pk_mul_f32 v[18:19], v[18:19], v[72:73] op_sel_hi:[1,0]
	v_pk_mul_f32 v[16:17], v[16:17], v[72:73] op_sel_hi:[1,0]
	v_pk_mul_f32 v[14:15], v[14:15], v[72:73] op_sel_hi:[1,0]
	v_pk_mul_f32 v[12:13], v[12:13], v[72:73] op_sel_hi:[1,0]
	v_pk_mul_f32 v[10:11], v[10:11], v[72:73] op_sel_hi:[1,0]
	v_pk_mul_f32 v[8:9], v[8:9], v[72:73] op_sel_hi:[1,0]
	v_pk_mul_f32 v[6:7], v[6:7], v[72:73] op_sel_hi:[1,0]
	v_pk_mul_f32 v[4:5], v[4:5], v[72:73] op_sel_hi:[1,0]
	v_pk_mul_f32 v[2:3], v[2:3], v[72:73] op_sel_hi:[1,0]
	v_mul_f32_e32 v34, v34, v72
	s_branch .LBB0_355

; __global__ void __launch_bounds__(512, 2) mk_fwd(Params P) {
	.amdhsa_kernel _Z6mk_fwd6Params
		.amdhsa_group_segment_fixed_size 0
		.amdhsa_private_segment_fixed_size 0
		.amdhsa_kernarg_size 440
		.amdhsa_user_sgpr_count 2
		.amdhsa_user_sgpr_dispatch_ptr 0
		.amdhsa_user_sgpr_queue_ptr 0
		.amdhsa_user_sgpr_kernarg_segment_ptr 1
		.amdhsa_user_sgpr_dispatch_id 0
		.amdhsa_user_sgpr_kernarg_preload_length 0
		.amdhsa_user_sgpr_kernarg_preload_offset 0
		.amdhsa_user_sgpr_private_segment_size 0
		.amdhsa_uses_dynamic_stack 0
		.amdhsa_enable_private_segment 0
		.amdhsa_system_sgpr_workgroup_id_x 1
		.amdhsa_system_sgpr_workgroup_id_y 0
		.amdhsa_system_sgpr_workgroup_id_z 0
		.amdhsa_system_sgpr_workgroup_info 0
		.amdhsa_system_vgpr_workitem_id 0
		.amdhsa_next_free_vgpr 255
		.amdhsa_next_free_sgpr 102
		.amdhsa_accum_offset 256
		.amdhsa_reserve_vcc 1
		.amdhsa_float_round_mode_32 0
		.amdhsa_float_round_mode_16_64 0
		.amdhsa_float_denorm_mode_32 3
		.amdhsa_float_denorm_mode_16_64 3
		.amdhsa_dx10_clamp 1
		.amdhsa_ieee_mode 1
		.amdhsa_fp16_overflow 0
		.amdhsa_tg_split 0
		.amdhsa_exception_fp_ieee_invalid_op 0
		.amdhsa_exception_fp_denorm_src 0
		.amdhsa_exception_fp_ieee_div_zero 0
		.amdhsa_exception_fp_ieee_overflow 0
		.amdhsa_exception_fp_ieee_underflow 0
		.amdhsa_exception_fp_ieee_inexact 0
		.amdhsa_exception_int_div_zero 0
	.end_amdhsa_kernel

; __global__ void __launch_bounds__(512, 2) mk_fwd(Params P) {
amdhsa.kernels:
  - .agpr_count:     0
    .args:
      - .offset:         0
        .size:           184
        .value_kind:     by_value
      - .offset:         184
        .size:           4
        .value_kind:     hidden_block_count_x
      - .offset:         188
        .size:           4
        .value_kind:     hidden_block_count_y
      - .offset:         192
        .size:           4
        .value_kind:     hidden_block_count_z
      - .offset:         196
        .size:           2
        .value_kind:     hidden_group_size_x
      - .offset:         198
        .size:           2
        .value_kind:     hidden_group_size_y
      - .offset:         200
        .size:           2
        .value_kind:     hidden_group_size_z
      - .offset:         202
        .size:           2
        .value_kind:     hidden_remainder_x
      - .offset:         204
        .size:           2
        .value_kind:     hidden_remainder_y
      - .offset:         206
        .size:           2
        .value_kind:     hidden_remainder_z
      - .offset:         224
        .size:           8
        .value_kind:     hidden_global_offset_x
      - .offset:         232
        .size:           8
        .value_kind:     hidden_global_offset_y
      - .offset:         240
        .size:           8
        .value_kind:     hidden_global_offset_z
      - .offset:         248
        .size:           2
        .value_kind:     hidden_grid_dims
      - .offset:         304
        .size:           4
        .value_kind:     hidden_dynamic_lds_size
    .group_segment_fixed_size: 0
    .kernarg_segment_align: 8
    .kernarg_segment_size: 440
    .language:       OpenCL C
    .language_version:
      - 2
      - 0
    .max_flat_workgroup_size: 512
    .name:           _Z6mk_fwd6Params
    .private_segment_fixed_size: 0
    .sgpr_count:     108
    .sgpr_spill_count: 15
    .symbol:         _Z6mk_fwd6Params.kd
    .uniform_work_group_size: 1
    .uses_dynamic_stack: false
    .vgpr_count:     255
    .vgpr_spill_count: 0
    .wavefront_size: 64
